# MoE-up: waves 4-7 run half a tile behind (k-step-1 MFMAs at start of next interval); unit setup loads batched; epilogue rstd preloaded
# speedup vs baseline: 1.0229x; 1.0118x over previous
;     __device__ __forceinline__ unsigned row(const Unit& u, int r) const { return (unsigned)slot_tok[u.pm * 256 + r]; }
; #define MOE_UNIT(idx_, x_, RMAX, CBN, e_, rb_, cb_, ok_) do { int b_ = 0; ok_ = false; for (int k_ = 0; k_ < 8; ++k_) { const int ee_ = (x_) + 8 * k_, n_ = ((ecnt[ee_] + (RMAX) - 1) / (RMAX)) * (CBN); \
;         if ((idx_) < b_ + n_) { e_ = ee_; rb_ = ((idx_) - b_) / (CBN); cb_ = ((idx_) - b_) % (CBN); ok_ = true; break; } b_ += n_; } } while (0)
; template <int MODE>
; __device__ __forceinline__ void moe_unit(PG8_LAS unsigned char* lds, int e, int cb, int slot0  , int nv  , const bf16_t* A, const int* slot_tok,
;                                          const float* W0, const float* W1, bf16_t* OUT, const float* slot_rs  , const int* slot_dst) {
;     ...
;     for (int i = 0; i < NMU; ++i) { const int R = 8 * (wid + 8 * i) + (lane >> 3), C = 8 * ((lane & 7) ^ ((R >> 1) & 7)); const int w4 = R / RWU, r = 4 * (R - RWU * w4) + w4;
;         const unsigned row = r < nv ? (MODE == 0 ? (unsigned)slot_tok[slot0 + r] : (unsigned)(slot0 + r)) : (MODE == 0 ? 0u : (unsigned)slot0); aoff[i] = (row * (unsigned)K + (unsigned)C) * 2u; }
; __global__ void __launch_bounds__(NTHREADS, 2) hymba_fwd(Args args) {
;     ...
;         for (int j = F.bid >> 3; ; j += F.G >> 3) { int e = 0, rb = 0, cb = 0; bool ok; MOE_UNIT(j, x, mu::MR, 8, e, rb, cb, ok); if (!ok) break;
;             const int n = ecnt[e], nrb = (n + mu::MR - 1) / mu::MR, base = n / nrb, rem = n % nrb, r0 = rb * base + (rb < rem ? rb : rem), nv = base + (rb < rem ? 1 : 0);
;             const long adj = (long)e * CAPS - eo[e];
;             mu::moe_unit<0>(F.lds, e, cb, eo[e] + r0, nv, (const bf16_t*)(F.ws + WS_HB), (const int*)(F.ws + WS_T2 + T2_TOK) + adj, F.wg, F.wu, (bf16_t*)(F.ws + WS_HID), (const float*)(F.ws + WS_T2 + T2_RS) + adj, nullptr); }
.LBB0_688:
	s_andn2_b64 vcc, exec, s[56:57]
	s_mov_b64 s[56:57], -1
	s_cbranch_vccnz .LBB0_682
	s_lshl_b32 s33, s54, 2
	s_add_i32 s33, s33, 0
	s_add_i32 s55, s33, 0x26d40
	v_mov_b32_e32 v1, s55
	ds_read_b32 v1, v1
	v_mov_b32_e32 v5, 0
	s_waitcnt lgkmcnt(0)
	v_readfirstlane_b32 s56, v1
	s_add_i32 s55, s56, 0x13f
	s_mul_hi_i32 s55, s55, 0x66666667
	s_lshr_b32 s57, s55, 31
	s_ashr_i32 s55, s55, 7
	s_add_i32 s57, s55, s57
	s_abs_i32 s58, s57
	v_cvt_f32_u32_e32 v1, s58
	s_sub_i32 s62, 0, s58
	s_abs_i32 s59, s56
	s_xor_b32 s61, s56, s57
	v_rcp_iflag_f32_e32 v1, v1
	s_ashr_i32 s55, s54, 31
	s_ashr_i32 s61, s61, 31
	v_mul_f32_e32 v1, 0x4f7ffffe, v1
	v_cvt_u32_f32_e32 v1, v1
	s_nop 0
	v_readfirstlane_b32 s63, v1
	s_mul_i32 s62, s62, s63
	s_mul_hi_u32 s62, s63, s62
	s_add_i32 s63, s63, s62
	s_mul_hi_u32 s62, s59, s63
	s_mul_i32 s63, s62, s58
	s_sub_i32 s59, s59, s63
	s_add_i32 s69, s62, 1
	s_sub_i32 s63, s59, s58
	s_cmp_ge_u32 s59, s58
	s_cselect_b32 s62, s69, s62
	s_cselect_b32 s59, s63, s59
	s_add_i32 s63, s62, 1
	s_cmp_ge_u32 s59, s58
	s_cselect_b32 s58, s63, s62
	s_xor_b32 s58, s58, s61
	s_sub_i32 s58, s58, s61
	s_mul_i32 s57, s58, s57
	s_sub_i32 s61, s56, s57
	s_cmp_lt_i32 s6, s61
	s_mul_i32 s59, s58, s6
	s_cselect_b64 s[56:57], -1, 0
	s_min_i32 s6, s6, s61
	s_add_i32 s6, s6, s59
	s_cmp_lg_u64 s[56:57], 0
	s_addc_u32 s69, s58, 0
	s_add_i32 s33, s33, 0x26c00
	v_mov_b32_e32 v1, s33
	ds_read_b32 v1, v1
	v_readfirstlane_b32 s58, v0
	s_lshr_b32 s62, s58, 6
	s_mul_hi_u32 s33, s58, 0xcccccccd
	s_lshl_b64 s[56:57], s[54:55], 14
	s_waitcnt lgkmcnt(0)
	v_add_u32_e32 v94, s6, v1
	s_lshl_b32 s6, s62, 3
	s_lshr_b32 s33, s33, 9
	v_mov_b32_e32 v3, s57
	v_ashrrev_i32_e32 v4, 31, v1
	v_sub_co_u32_e32 v2, vcc, s56, v1
	v_or_b32_e32 v1, s6, v130
	s_mul_i32 s56, s33, 0xffffffb0
	v_subb_co_u32_e32 v3, vcc, v3, v4, vcc
	v_add_u32_e32 v4, s56, v1
	v_lshlrev_b64 v[96:97], 2, v[2:3]
	v_lshl_add_u32 v6, v4, 2, s33
	v_lshl_add_u64 v[2:3], s[8:9], 0, v[96:97]
	v_cmp_gt_i32_e32 vcc, s69, v6
	v_mov_b32_e32 v4, 0
	s_and_saveexec_b64 s[56:57], vcc
	s_cbranch_execz .LBB0_691
	v_add_u32_e32 v6, v6, v94
	v_ashrrev_i32_e32 v7, 31, v6
	v_lshl_add_u64 v[6:7], v[6:7], 2, v[2:3]
	global_load_dword v5, v[6:7], off
.LBB0_691:
	s_or_b64 exec, exec, s[56:57]
	s_add_i32 s33, s6, 64
	v_or_b32_e32 v9, s33, v130
	s_mul_hi_u32 s33, s33, 0xccccccd
	s_lshr_b32 s33, s33, 2
	s_mul_i32 s56, s33, 0xffffffb0
	v_add_u32_e32 v6, s56, v9
	v_lshl_add_u32 v7, v6, 2, s33
	v_cmp_gt_i32_e32 vcc, s69, v7
	v_mov_b32_e32 v6, 0
	s_and_saveexec_b64 s[56:57], vcc
	s_cbranch_execz .LBB0_693
	v_add_u32_e32 v6, v7, v94
	v_ashrrev_i32_e32 v7, 31, v6
	v_lshl_add_u64 v[6:7], v[6:7], 2, v[2:3]
	global_load_dword v6, v[6:7], off
.LBB0_693:
	s_or_b64 exec, exec, s[56:57]
	s_add_i32 s33, s6, 0x80
	v_or_b32_e32 v10, s33, v130
	s_mul_hi_u32 s33, s33, 0xccccccd
	s_lshr_b32 s33, s33, 2
	s_mul_i32 s56, s33, 0xffffffb0
	v_add_u32_e32 v7, s56, v10
	v_lshl_add_u32 v7, v7, 2, s33
	v_cmp_gt_i32_e32 vcc, s69, v7
	s_and_saveexec_b64 s[56:57], vcc
	s_cbranch_execz .LBB0_695
	v_add_u32_e32 v12, v7, v94
	v_ashrrev_i32_e32 v13, 31, v12
	v_lshl_add_u64 v[12:13], v[12:13], 2, v[2:3]
	global_load_dword v4, v[12:13], off
.LBB0_695:
	s_or_b64 exec, exec, s[56:57]
	s_add_i32 s33, s6, 0xc0
	v_or_b32_e32 v11, s33, v130
	s_mul_hi_u32 s33, s33, 0xccccccd
	s_lshr_b32 s33, s33, 2
	s_mul_i32 s56, s33, 0xffffffb0
	v_add_u32_e32 v7, s56, v11
	v_lshl_add_u32 v12, v7, 2, s33
	v_cmp_gt_i32_e32 vcc, s69, v12
	v_mov_b32_e32 v7, 0
	v_mov_b32_e32 v8, 0
	s_and_saveexec_b64 s[56:57], vcc
	s_cbranch_execz .LBB0_697
	v_add_u32_e32 v12, v12, v94
	v_ashrrev_i32_e32 v13, 31, v12
	v_lshl_add_u64 v[12:13], v[12:13], 2, v[2:3]
	global_load_dword v8, v[12:13], off
.LBB0_697:
	s_or_b64 exec, exec, s[56:57]
	s_add_i32 s33, s6, 0x100
	v_or_b32_e32 v12, s33, v130
	s_mul_hi_u32 s33, s33, 0xccccccd
	s_lshr_b32 s33, s33, 2
	s_mul_i32 s56, s33, 0xffffffb0
	v_add_u32_e32 v13, s56, v12
	v_lshl_add_u32 v13, v13, 2, s33
	v_cmp_gt_i32_e32 vcc, s69, v13
	s_and_saveexec_b64 s[56:57], vcc
	s_cbranch_execz .LBB0_699
	v_add_u32_e32 v14, v13, v94
	v_ashrrev_i32_e32 v15, 31, v14
	v_lshl_add_u64 v[2:3], v[14:15], 2, v[2:3]
	global_load_dword v7, v[2:3], off
.LBB0_699:
	s_or_b64 exec, exec, s[56:57]
	s_waitcnt vmcnt(0)
; template <int MODE>
; __device__ __forceinline__ void moe_unit(PG8_LAS unsigned char* lds, int e, int cb, int slot0  , int nv  , const bf16_t* A, const int* slot_tok,
;                                          const float* W0, const float* W1, bf16_t* OUT, const float* slot_rs  , const int* slot_dst) {
;     ...
;     for (int i = 0; i < NMU; ++i) { const int R = 8 * (wid + 8 * i) + (lane >> 3), C = 8 * ((lane & 7) ^ ((R >> 1) & 7)); const int w4 = R / RWU, r = 4 * (R - RWU * w4) + w4;
;         const unsigned row = r < nv ? (MODE == 0 ? (unsigned)slot_tok[slot0 + r] : (unsigned)(slot0 + r)) : (MODE == 0 ? 0u : (unsigned)slot0); aoff[i] = (row * (unsigned)K + (unsigned)C) * 2u; }
;     const int jj0 = 2 * (lane & 31), typ = lane >> 5;
;     const int R0 = MODE == 0 ? 64 * (jj0 >> 5) + 32 * typ + 16 * ((jj0 >> 2) & 1) + 4 * ((jj0 >> 3) & 3) + (jj0 & 3) : 2 * lane;
;     const char* Bb = MODE == 0 ? (const char*)((typ ? W1 : W0) + (size_t)e * K * LDB + 64 * cb + jj0) + (size_t)(8 * wid) * RB
;                                : (const char*)(W0 + (size_t)e * K * LDB + 128 * cb + 2 * lane) + (size_t)(8 * wid) * RB;
;     const unsigned bw0 = (unsigned)(R0 * 128 + ((wid ^ ((R0 >> 1) & 7)) * 16)), bw1 = bw0 + 128u;
;     ...
;     MU_GLDS_A(0, 0); MU_B_ISSUE(s0, 0); MU_G_LOAD(g0, 0); MU_B_ISSUE(s1, 1);
;     MU_B_WAIT(s0, 8); MU_B_WRITE(s0, 0, g0); __builtin_amdgcn_sched_barrier(0); MU_B_ISSUE(s0, 2);
;     asm volatile("s_waitcnt vmcnt(16)" ::: "memory");
;     asm volatile("s_waitcnt lgkmcnt(0)" ::: "memory"); __builtin_amdgcn_s_barrier(); asm volatile("" ::: "memory");
; #pragma unroll 1
;     for (int t = 0; t < nt; t += 2) {
;         if (t + 2 < nt) MU_B_WAIT(s1, 8); else MU_B_WAIT(s1, 0);
;         MU_G_LOAD(g0, t + 1); MU_B_WRITE(s1, 1, g0); __builtin_amdgcn_sched_barrier(0); MU_GLDS_A(1, t + 1); __builtin_amdgcn_sched_barrier(0);
;         if (t + 3 < nt) { MU_B_ISSUE(s1, t + 3); }
;         MU_COMPUTE(0);
;         MU_END(t + 3 >= nt);
;         if (t + 2 < nt) { MU_B_WAIT(s0, 8); MU_G_LOAD(g0, t + 2); MU_B_WRITE(s0, 0, g0); __builtin_amdgcn_sched_barrier(0); MU_GLDS_A(0, t + 2); __builtin_amdgcn_sched_barrier(0); }
;         if (t + 4 < nt) { MU_B_ISSUE(s0, t + 4); }
;         MU_COMPUTE(1);
;         MU_END(t + 4 >= nt);
;     }
; #pragma unroll
;     for (int m = 0; m < NMU; ++m) if (m < mcnt) { const int r = 4 * (16 * m + fr) + wr;
	v_lshlrev_b32_e32 v5, 13, v5
	v_lshlrev_b32_e32 v6, 13, v6
	v_lshlrev_b32_e32 v4, 13, v4
	v_lshlrev_b32_e32 v8, 13, v8
	v_lshlrev_b32_e32 v7, 13, v7
	s_lshr_b32 s33, s58, 7
	s_bfe_u32 s70, s58, 0x10006
	v_add_u32_e32 v166, s33, v176
	v_add_u32_e32 v166, v166, v94
	v_ashrrev_i32_e32 v167, 31, v166
	v_lshl_add_u64 v[166:167], v[166:167], 2, v[96:97]
	v_lshl_add_u64 v[166:167], v[166:167], 0, s[10:11]
	global_load_dword v178, v[166:167], off
	global_load_dword v179, v[166:167], off offset:256
	global_load_dword v180, v[166:167], off offset:512
	global_load_dword v181, v[166:167], off offset:768
	global_load_dword v182, v[166:167], off offset:1024
	v_bfe_u32 v166, v131, 1, 3
	v_xor_b32_e32 v166, v171, v166
	v_lshlrev_b32_e32 v166, 4, v166
	v_lshl_add_u32 v166, v170, 7, v166
	s_mul_i32 s56, s33, 0x2800
	v_add_u32_e32 v135, s56, v166
	v_xor_b32_e32 v137, 64, v135
	s_lshl_b32 s56, s70, 13
	s_add_i32 s56, s56, 0x1e000
	v_add_u32_e32 v139, s56, v166
	v_xor_b32_e32 v141, 64, v139
	v_xor_b32_e32 v1, s62, v177
	v_lshl_add_u32 v1, v1, 4, v172
	v_add_u32_e32 v1, 0x1e000, v1
	s_lshl_b32 s56, s62, 2
	v_add_u32_e32 v166, s56, v171
	v_xor_b32_e32 v166, v166, v131
	v_and_b32_e32 v166, 7, v166
	v_lshlrev_b32_e32 v166, 4, v166
	v_or_b32_e32 v86, v5, v166
	v_or_b32_e32 v134, v6, v166
	v_or_b32_e32 v136, v4, v166
	v_or_b32_e32 v138, v8, v166
	v_or_b32_e32 v140, v7, v166
	s_lshl_b64 s[56:57], s[54:55], 23
	s_lshl_b32 s59, s60, 8
	s_add_u32 s56, s56, s59
	s_addc_u32 s57, s57, 0
	s_lshl_b32 s59, s62, 14
	s_add_u32 s56, s56, s59
	s_addc_u32 s57, s57, 0
	v_mov_b32_e32 v91, 0
	v_lshl_add_u64 v[132:133], v[82:83], 0, s[56:57]
	v_lshl_add_u64 v[132:133], v[132:133], 0, v[90:91]
	s_lshl_b32 s54, s60, 6
	s_ashr_i32 s55, s54, 31
	v_readlane_b32 s28, v254, 9
	v_readlane_b32 s29, v254, 10
	s_lshl_b32 s56, s62, 5
	s_mov_b64 s[30:31], s[4:5]
	s_mov_b64 s[34:35], 0x1000
	s_mov_b64 s[36:37], 0x2000
	s_mov_b64 s[38:39], 0x3000
	s_mov_b64 s[40:41], 0x20000
	s_add_u32 s28, s28, s56
	s_addc_u32 s29, s29, 0
	s_mov_b32 s42, 0
	s_mov_b32 s43, 0xa000
	s_mov_b32 s44, 0x14000
	s_lshl_b32 s6, s62, 10
	s_load_dwordx8 s[12:19], s[28:29], 0x0
	s_load_dwordx8 s[20:27], s[28:29], 0x100
	s_add_u32 s28, s28, 0x200
	s_addc_u32 s29, s29, 0
	s_add_i32 m0, s6, 0x0
	s_nop 0
	global_load_lds_dwordx4 v86, s[30:31]
	s_add_i32 m0, s6, 0x2000
	s_nop 0
	global_load_lds_dwordx4 v134, s[30:31]
	s_add_i32 m0, s6, 0x4000
	s_nop 0
	global_load_lds_dwordx4 v136, s[30:31]
	s_add_i32 m0, s6, 0x6000
	s_nop 0
	global_load_lds_dwordx4 v138, s[30:31]
	s_add_i32 m0, s6, 0x8000
	s_nop 0
	global_load_lds_dwordx4 v140, s[30:31]
	s_add_u32 s30, s30, 0x80
	s_addc_u32 s31, s31, 0
	s_add_i32 m0, s6, 0xa000
	s_nop 0
	global_load_lds_dwordx4 v86, s[30:31]
	s_add_i32 m0, s6, 0xc000
	s_nop 0
	global_load_lds_dwordx4 v134, s[30:31]
	s_add_i32 m0, s6, 0xe000
	s_nop 0
	global_load_lds_dwordx4 v136, s[30:31]
	s_add_i32 m0, s6, 0x10000
	s_nop 0
	global_load_lds_dwordx4 v138, s[30:31]
	s_add_i32 m0, s6, 0x12000
	s_nop 0
	global_load_lds_dwordx4 v140, s[30:31]
	global_load_dwordx2 v[98:99], v[132:133], off
	global_load_dwordx2 v[100:101], v[132:133], off offset:2048
	v_lshl_add_u64 v[166:167], v[132:133], 0, s[34:35]
	global_load_dwordx2 v[102:103], v[166:167], off
	global_load_dwordx2 v[104:105], v[166:167], off offset:2048
	v_lshl_add_u64 v[166:167], v[132:133], 0, s[36:37]
	global_load_dwordx2 v[106:107], v[166:167], off
	global_load_dwordx2 v[108:109], v[166:167], off offset:2048
	v_lshl_add_u64 v[166:167], v[132:133], 0, s[38:39]
	global_load_dwordx2 v[110:111], v[166:167], off
	global_load_dwordx2 v[112:113], v[166:167], off offset:2048
	v_lshl_add_u64 v[132:133], v[132:133], 0, s[40:41]
	global_load_dwordx2 v[114:115], v[132:133], off
	global_load_dwordx2 v[116:117], v[132:133], off offset:2048
	v_lshl_add_u64 v[166:167], v[132:133], 0, s[34:35]
	global_load_dwordx2 v[118:119], v[166:167], off
	global_load_dwordx2 v[120:121], v[166:167], off offset:2048
	v_lshl_add_u64 v[166:167], v[132:133], 0, s[36:37]
	global_load_dwordx2 v[122:123], v[166:167], off
	global_load_dwordx2 v[124:125], v[166:167], off offset:2048
	v_lshl_add_u64 v[166:167], v[132:133], 0, s[38:39]
	global_load_dwordx2 v[126:127], v[166:167], off
	global_load_dwordx2 v[128:129], v[166:167], off offset:2048
	v_lshl_add_u64 v[132:133], v[132:133], 0, s[40:41]
	global_load_dwordx2 v[186:187], v[132:133], off
	global_load_dwordx2 v[188:189], v[132:133], off offset:2048
	v_lshl_add_u64 v[166:167], v[132:133], 0, s[34:35]
	global_load_dwordx2 v[190:191], v[166:167], off
	global_load_dwordx2 v[192:193], v[166:167], off offset:2048
	v_lshl_add_u64 v[166:167], v[132:133], 0, s[36:37]
	global_load_dwordx2 v[194:195], v[166:167], off
	global_load_dwordx2 v[196:197], v[166:167], off offset:2048
	v_lshl_add_u64 v[166:167], v[132:133], 0, s[38:39]
	global_load_dwordx2 v[198:199], v[166:167], off
	global_load_dwordx2 v[200:201], v[166:167], off offset:2048
	v_lshl_add_u64 v[132:133], v[132:133], 0, s[40:41]
	global_load_dwordx2 v[202:203], v[132:133], off
	global_load_dwordx2 v[204:205], v[132:133], off offset:2048
	v_lshl_add_u64 v[166:167], v[132:133], 0, s[34:35]
	global_load_dwordx2 v[206:207], v[166:167], off
	global_load_dwordx2 v[208:209], v[166:167], off offset:2048
	v_lshl_add_u64 v[166:167], v[132:133], 0, s[36:37]
	global_load_dwordx2 v[210:211], v[166:167], off
	global_load_dwordx2 v[212:213], v[166:167], off offset:2048
	v_lshl_add_u64 v[166:167], v[132:133], 0, s[38:39]
	global_load_dwordx2 v[214:215], v[166:167], off
	global_load_dwordx2 v[216:217], v[166:167], off offset:2048
	v_mov_b32_e32 v78, 0
	v_mov_b32_e32 v79, 0
	v_mov_b32_e32 v80, 0
	v_mov_b32_e32 v81, 0
; #define MU_GLDS_A(buf, kt) do { _Pragma("unroll") for (int i = 0; i < NMU; ++i) \
;         __builtin_amdgcn_global_load_lds((const unsigned*)((const char*)A + aoff[i] + (size_t)(kt) * 128), (PG8_LAS unsigned*)(MU_SA(buf) + wid * 1024 + i * 8192), 16, 0, 0); } while (0)
; #define MU_B_ISSUE(sb, kt) do { const char* kb_ = Bb + (size_t)(kt) * (64 * (size_t)RB); _Pragma("unroll") for (int j = 0; j < 8; ++j) { const char* p_ = kb_ + (size_t)j * RB; \
;         asm volatile("global_load_dwordx2 %0, %1, off" : "=&v"(sb[j]) : "v"(p_) : "memory"); } } while (0)
; #define MU_B_WAIT(sb, N) asm volatile("s_waitcnt vmcnt(%8)" : "+v"(sb[0]), "+v"(sb[1]), "+v"(sb[2]), "+v"(sb[3]), "+v"(sb[4]), "+v"(sb[5]), "+v"(sb[6]), "+v"(sb[7]) : "n"(N) : "memory")
; #define MU_G_LOAD(ga, kt) do { const PG8_LAS f32x4* gk_ = (const PG8_LAS f32x4*)(lds + GAIN_OFF) + 16 * (kt) + 2 * wid; const f32x4 ga_ = gk_[0], gb_ = gk_[1]; \
;         ga[0] = ga_[0]; ga[1] = ga_[1]; ga[2] = ga_[2]; ga[3] = ga_[3]; ga[4] = gb_[0]; ga[5] = gb_[1]; ga[6] = gb_[2]; ga[7] = gb_[3]; } while (0)
; #define MU_COMPUTE(buf) MU_COMPUTE_N(buf, NMU)
; template <int MODE>
; __device__ __forceinline__ void moe_unit(PG8_LAS unsigned char* lds, int e, int cb, int slot0  , int nv  , const bf16_t* A, const int* slot_tok,
;                                          const float* W0, const float* W1, bf16_t* OUT, const float* slot_rs  , const int* slot_dst) {
;     ...
;     f32x4 acc[NMU][4];
; #pragma unroll
;     for (int m = 0; m < NMU; ++m)
; #pragma unroll
;         for (int n = 0; n < 4; ++n) acc[m][n] = (f32x4){0.f, 0.f, 0.f, 0.f};
;     f32x2 s0[8], s1[8];
;     float g0[8];
;     MU_GLDS_A(0, 0); MU_B_ISSUE(s0, 0); MU_G_LOAD(g0, 0); MU_B_ISSUE(s1, 1);
;     MU_B_WAIT(s0, 8); MU_B_WRITE(s0, 0, g0); __builtin_amdgcn_sched_barrier(0); MU_B_ISSUE(s0, 2);
;     asm volatile("s_waitcnt vmcnt(16)" ::: "memory");
;     asm volatile("s_waitcnt lgkmcnt(0)" ::: "memory"); __builtin_amdgcn_s_barrier(); asm volatile("" ::: "memory");
; #pragma unroll 1
;     for (int t = 0; t < nt; t += 2) {
;         if (t + 2 < nt) MU_B_WAIT(s1, 8); else MU_B_WAIT(s1, 0);
;         MU_G_LOAD(g0, t + 1); MU_B_WRITE(s1, 1, g0); __builtin_amdgcn_sched_barrier(0); MU_GLDS_A(1, t + 1); __builtin_amdgcn_sched_barrier(0);
;         if (t + 3 < nt) { MU_B_ISSUE(s1, t + 3); }
;         MU_COMPUTE(0);
	v_mov_b32_e32 v74, 0
	v_mov_b32_e32 v75, 0
	v_mov_b32_e32 v76, 0
	v_mov_b32_e32 v77, 0
	v_mov_b32_e32 v70, 0
	v_mov_b32_e32 v71, 0
	v_mov_b32_e32 v72, 0
	v_mov_b32_e32 v73, 0
	v_mov_b32_e32 v66, 0
	v_mov_b32_e32 v67, 0
	v_mov_b32_e32 v68, 0
	v_mov_b32_e32 v69, 0
	v_mov_b32_e32 v62, 0
	v_mov_b32_e32 v63, 0
	v_mov_b32_e32 v64, 0
	v_mov_b32_e32 v65, 0
	v_mov_b32_e32 v58, 0
	v_mov_b32_e32 v59, 0
	v_mov_b32_e32 v60, 0
	v_mov_b32_e32 v61, 0
	v_mov_b32_e32 v54, 0
	v_mov_b32_e32 v55, 0
	v_mov_b32_e32 v56, 0
	v_mov_b32_e32 v57, 0
	v_mov_b32_e32 v50, 0
	v_mov_b32_e32 v51, 0
	v_mov_b32_e32 v52, 0
	v_mov_b32_e32 v53, 0
	v_mov_b32_e32 v46, 0
	v_mov_b32_e32 v47, 0
	v_mov_b32_e32 v48, 0
	v_mov_b32_e32 v49, 0
	v_mov_b32_e32 v42, 0
	v_mov_b32_e32 v43, 0
	v_mov_b32_e32 v44, 0
	v_mov_b32_e32 v45, 0
	v_mov_b32_e32 v38, 0
	v_mov_b32_e32 v39, 0
	v_mov_b32_e32 v40, 0
	v_mov_b32_e32 v41, 0
	v_mov_b32_e32 v34, 0
	v_mov_b32_e32 v35, 0
	v_mov_b32_e32 v36, 0
	v_mov_b32_e32 v37, 0
	v_mov_b32_e32 v18, 0
	v_mov_b32_e32 v19, 0
	v_mov_b32_e32 v20, 0
	v_mov_b32_e32 v21, 0
	v_mov_b32_e32 v22, 0
	v_mov_b32_e32 v23, 0
	v_mov_b32_e32 v24, 0
	v_mov_b32_e32 v25, 0
	v_mov_b32_e32 v26, 0
	v_mov_b32_e32 v27, 0
	v_mov_b32_e32 v28, 0
	v_mov_b32_e32 v29, 0
	v_mov_b32_e32 v30, 0
	v_mov_b32_e32 v31, 0
	v_mov_b32_e32 v32, 0
	v_mov_b32_e32 v33, 0
	v_mov_b32_e32 v2, 0
	v_mov_b32_e32 v3, 0
	v_mov_b32_e32 v4, 0
	v_mov_b32_e32 v5, 0
	v_mov_b32_e32 v6, 0
	v_mov_b32_e32 v7, 0
	v_mov_b32_e32 v8, 0
	v_mov_b32_e32 v9, 0
	v_mov_b32_e32 v10, 0
	v_mov_b32_e32 v11, 0
	v_mov_b32_e32 v12, 0
	v_mov_b32_e32 v13, 0
	v_mov_b32_e32 v14, 0
	v_mov_b32_e32 v15, 0
	v_mov_b32_e32 v16, 0
	v_mov_b32_e32 v17, 0
	s_waitcnt vmcnt(24)
	s_waitcnt lgkmcnt(0)
	v_mul_f32_e32 v98, s12, v98
	v_mul_f32_e32 v99, s12, v99
	v_mul_f32_e32 v100, s13, v100
	v_mul_f32_e32 v101, s13, v101
	v_mul_f32_e32 v102, s14, v102
	v_mul_f32_e32 v103, s14, v103
	v_mul_f32_e32 v104, s15, v104
	v_mul_f32_e32 v105, s15, v105
	v_mul_f32_e32 v106, s16, v106
	v_mul_f32_e32 v107, s16, v107
	v_mul_f32_e32 v108, s17, v108
	v_mul_f32_e32 v109, s17, v109
	v_mul_f32_e32 v110, s18, v110
	v_mul_f32_e32 v111, s18, v111
	v_mul_f32_e32 v112, s19, v112
	v_mul_f32_e32 v113, s19, v113
	v_cvt_pk_bf16_f32 v158, v98, v100
	v_cvt_pk_bf16_f32 v159, v102, v104
	v_cvt_pk_bf16_f32 v160, v106, v108
	v_cvt_pk_bf16_f32 v161, v110, v112
	v_cvt_pk_bf16_f32 v162, v99, v101
	v_cvt_pk_bf16_f32 v163, v103, v105
	v_cvt_pk_bf16_f32 v164, v107, v109
	v_cvt_pk_bf16_f32 v165, v111, v113
	ds_write_b128 v1, v[158:161] offset:0
	ds_write_b128 v1, v[162:165] offset:128
	v_lshl_add_u64 v[132:133], v[132:133], 0, s[40:41]
	global_load_dwordx2 v[98:99], v[132:133], off
	global_load_dwordx2 v[100:101], v[132:133], off offset:2048
	v_lshl_add_u64 v[166:167], v[132:133], 0, s[34:35]
	global_load_dwordx2 v[102:103], v[166:167], off
	global_load_dwordx2 v[104:105], v[166:167], off offset:2048
	v_lshl_add_u64 v[166:167], v[132:133], 0, s[36:37]
	global_load_dwordx2 v[106:107], v[166:167], off
	global_load_dwordx2 v[108:109], v[166:167], off offset:2048
	v_lshl_add_u64 v[166:167], v[132:133], 0, s[38:39]
	global_load_dwordx2 v[110:111], v[166:167], off
	global_load_dwordx2 v[112:113], v[166:167], off offset:2048
	s_waitcnt lgkmcnt(0)
	s_barrier
	s_cmp_gt_u32 s62, 3
	s_cbranch_scc1 .Lmu_grpY
	s_waitcnt vmcnt(24)
	v_mul_f32_e32 v114, s20, v114
	v_mul_f32_e32 v115, s20, v115
	v_mul_f32_e32 v116, s21, v116
	v_mul_f32_e32 v117, s21, v117
	v_mul_f32_e32 v118, s22, v118
	v_mul_f32_e32 v119, s22, v119
	v_mul_f32_e32 v120, s23, v120
	v_mul_f32_e32 v121, s23, v121
	v_mul_f32_e32 v122, s24, v122
	v_mul_f32_e32 v123, s24, v123
	v_mul_f32_e32 v124, s25, v124
	v_mul_f32_e32 v125, s25, v125
	v_mul_f32_e32 v126, s26, v126
	v_mul_f32_e32 v127, s26, v127
	v_mul_f32_e32 v128, s27, v128
	v_mul_f32_e32 v129, s27, v129
	v_cvt_pk_bf16_f32 v158, v114, v116
	v_cvt_pk_bf16_f32 v159, v118, v120
	v_cvt_pk_bf16_f32 v160, v122, v124
	v_cvt_pk_bf16_f32 v161, v126, v128
	v_cvt_pk_bf16_f32 v162, v115, v117
	v_cvt_pk_bf16_f32 v163, v119, v121
	v_cvt_pk_bf16_f32 v164, v123, v125
	v_cvt_pk_bf16_f32 v165, v127, v129
	ds_write_b128 v1, v[158:161] offset:19456
	ds_write_b128 v1, v[162:165] offset:19584
	v_add_u32_e32 v91, s42, v135
	v_add_u32_e32 v93, s42, v137
	ds_read_b128 v[238:241], v139 offset:0
	ds_read_b128 v[242:245], v139 offset:2048
	ds_read_b128 v[246:249], v139 offset:4096
	ds_read_b128 v[250:253], v139 offset:6144
	ds_read_b128 v[218:221], v91 offset:0
	ds_read_b128 v[222:225], v91 offset:2048
	ds_read_b128 v[226:229], v91 offset:4096
	ds_read_b128 v[230:233], v91 offset:6144
	ds_read_b128 v[234:237], v91 offset:8192
	s_add_i32 s47, s44, s6
	s_add_u32 s30, s30, 0x80
	s_addc_u32 s31, s31, 0
	s_waitcnt lgkmcnt(0)
; #define MU_GLDS_A(buf, kt) do { _Pragma("unroll") for (int i = 0; i < NMU; ++i) \
;         __builtin_amdgcn_global_load_lds((const unsigned*)((const char*)A + aoff[i] + (size_t)(kt) * 128), (PG8_LAS unsigned*)(MU_SA(buf) + wid * 1024 + i * 8192), 16, 0, 0); } while (0)
; #define MU_B_ISSUE(sb, kt) do { const char* kb_ = Bb + (size_t)(kt) * (64 * (size_t)RB); _Pragma("unroll") for (int j = 0; j < 8; ++j) { const char* p_ = kb_ + (size_t)j * RB; \
;         asm volatile("global_load_dwordx2 %0, %1, off" : "=&v"(sb[j]) : "v"(p_) : "memory"); } } while (0)
; #define MU_B_WAIT(sb, N) asm volatile("s_waitcnt vmcnt(%8)" : "+v"(sb[0]), "+v"(sb[1]), "+v"(sb[2]), "+v"(sb[3]), "+v"(sb[4]), "+v"(sb[5]), "+v"(sb[6]), "+v"(sb[7]) : "n"(N) : "memory")
; #define MU_G_LOAD(ga, kt) do { const PG8_LAS f32x4* gk_ = (const PG8_LAS f32x4*)(lds + GAIN_OFF) + 16 * (kt) + 2 * wid; const f32x4 ga_ = gk_[0], gb_ = gk_[1]; \
;         ga[0] = ga_[0]; ga[1] = ga_[1]; ga[2] = ga_[2]; ga[3] = ga_[3]; ga[4] = gb_[0]; ga[5] = gb_[1]; ga[6] = gb_[2]; ga[7] = gb_[3]; } while (0)
; #define MU_COMPUTE(buf) MU_COMPUTE_N(buf, NMU)
; #define MU_END(last) do { if (last) asm volatile("s_waitcnt vmcnt(0)" ::: "memory"); else asm volatile("s_waitcnt vmcnt(8)" ::: "memory"); \
;         asm volatile("s_waitcnt lgkmcnt(0)" ::: "memory"); __builtin_amdgcn_s_barrier(); asm volatile("" ::: "memory"); } while (0)
; template <int MODE>
; __device__ __forceinline__ void moe_unit(PG8_LAS unsigned char* lds, int e, int cb, int slot0  , int nv  , const bf16_t* A, const int* slot_tok,
;                                          const float* W0, const float* W1, bf16_t* OUT, const float* slot_rs  , const int* slot_dst) {
;     ...
;     for (int t = 0; t < nt; t += 2) {
;         if (t + 2 < nt) MU_B_WAIT(s1, 8); else MU_B_WAIT(s1, 0);
;         MU_G_LOAD(g0, t + 1); MU_B_WRITE(s1, 1, g0); __builtin_amdgcn_sched_barrier(0); MU_GLDS_A(1, t + 1); __builtin_amdgcn_sched_barrier(0);
;         if (t + 3 < nt) { MU_B_ISSUE(s1, t + 3); }
;         MU_COMPUTE(0);
;         MU_END(t + 3 >= nt);
;         if (t + 2 < nt) { MU_B_WAIT(s0, 8); MU_G_LOAD(g0, t + 2); MU_B_WRITE(s0, 0, g0); __builtin_amdgcn_sched_barrier(0); MU_GLDS_A(0, t + 2); __builtin_amdgcn_sched_barrier(0); }
;         if (t + 4 < nt) { MU_B_ISSUE(s0, t + 4); }
;         MU_COMPUTE(1);
;         MU_END(t + 4 >= nt);
;     }
	v_mfma_f32_16x16x32_bf16 v[78:81], v[238:241], v[218:221], v[78:81]
	v_mfma_f32_16x16x32_bf16 v[74:77], v[242:245], v[218:221], v[74:77]
	v_mfma_f32_16x16x32_bf16 v[70:73], v[246:249], v[218:221], v[70:73]
	v_mfma_f32_16x16x32_bf16 v[66:69], v[250:253], v[218:221], v[66:69]
	ds_read_b128 v[218:221], v93 offset:0
	ds_read_b128 v[142:145], v141 offset:0
	s_mov_b32 m0, s47
	s_nop 0
	global_load_lds_dwordx4 v86, s[30:31]
	v_mfma_f32_16x16x32_bf16 v[62:65], v[238:241], v[222:225], v[62:65]
	v_mfma_f32_16x16x32_bf16 v[58:61], v[242:245], v[222:225], v[58:61]
	v_mfma_f32_16x16x32_bf16 v[54:57], v[246:249], v[222:225], v[54:57]
	v_mfma_f32_16x16x32_bf16 v[50:53], v[250:253], v[222:225], v[50:53]
	ds_read_b128 v[222:225], v93 offset:2048
	ds_read_b128 v[146:149], v141 offset:2048
	s_add_i32 m0, s47, 0x2000
	s_nop 0
	global_load_lds_dwordx4 v134, s[30:31]
	v_mfma_f32_16x16x32_bf16 v[46:49], v[238:241], v[226:229], v[46:49]
	v_mfma_f32_16x16x32_bf16 v[42:45], v[242:245], v[226:229], v[42:45]
	v_mfma_f32_16x16x32_bf16 v[38:41], v[246:249], v[226:229], v[38:41]
	v_mfma_f32_16x16x32_bf16 v[34:37], v[250:253], v[226:229], v[34:37]
	ds_read_b128 v[226:229], v93 offset:4096
	ds_read_b128 v[150:153], v141 offset:4096
	s_add_i32 m0, s47, 0x4000
	s_nop 0
	global_load_lds_dwordx4 v136, s[30:31]
	v_mfma_f32_16x16x32_bf16 v[18:21], v[238:241], v[230:233], v[18:21]
	v_mfma_f32_16x16x32_bf16 v[22:25], v[242:245], v[230:233], v[22:25]
	v_mfma_f32_16x16x32_bf16 v[26:29], v[246:249], v[230:233], v[26:29]
	v_mfma_f32_16x16x32_bf16 v[30:33], v[250:253], v[230:233], v[30:33]
	ds_read_b128 v[230:233], v93 offset:6144
	ds_read_b128 v[154:157], v141 offset:6144
	s_add_i32 m0, s47, 0x6000
	s_nop 0
	global_load_lds_dwordx4 v138, s[30:31]
	v_mfma_f32_16x16x32_bf16 v[2:5], v[238:241], v[234:237], v[2:5]
	v_mfma_f32_16x16x32_bf16 v[6:9], v[242:245], v[234:237], v[6:9]
	v_mfma_f32_16x16x32_bf16 v[10:13], v[246:249], v[234:237], v[10:13]
	v_mfma_f32_16x16x32_bf16 v[14:17], v[250:253], v[234:237], v[14:17]
	ds_read_b128 v[234:237], v93 offset:8192
	s_add_i32 m0, s47, 0x8000
	s_nop 0
	global_load_lds_dwordx4 v140, s[30:31]
	s_waitcnt lgkmcnt(0)
	s_load_dwordx8 s[12:19], s[28:29], 0x0
	s_add_u32 s28, s28, 0x100
	s_addc_u32 s29, s29, 0
	v_mfma_f32_16x16x32_bf16 v[78:81], v[142:145], v[218:221], v[78:81]
	v_mfma_f32_16x16x32_bf16 v[74:77], v[146:149], v[218:221], v[74:77]
	v_mfma_f32_16x16x32_bf16 v[70:73], v[150:153], v[218:221], v[70:73]
	v_mfma_f32_16x16x32_bf16 v[66:69], v[154:157], v[218:221], v[66:69]
	v_lshl_add_u64 v[132:133], v[132:133], 0, s[40:41]
	global_load_dwordx2 v[114:115], v[132:133], off
	global_load_dwordx2 v[116:117], v[132:133], off offset:2048
	v_mfma_f32_16x16x32_bf16 v[62:65], v[142:145], v[222:225], v[62:65]
	v_mfma_f32_16x16x32_bf16 v[58:61], v[146:149], v[222:225], v[58:61]
	v_mfma_f32_16x16x32_bf16 v[54:57], v[150:153], v[222:225], v[54:57]
	v_mfma_f32_16x16x32_bf16 v[50:53], v[154:157], v[222:225], v[50:53]
	v_lshl_add_u64 v[166:167], v[132:133], 0, s[34:35]
	global_load_dwordx2 v[118:119], v[166:167], off
	global_load_dwordx2 v[120:121], v[166:167], off offset:2048
	v_mfma_f32_16x16x32_bf16 v[46:49], v[142:145], v[226:229], v[46:49]
	v_mfma_f32_16x16x32_bf16 v[42:45], v[146:149], v[226:229], v[42:45]
	v_mfma_f32_16x16x32_bf16 v[38:41], v[150:153], v[226:229], v[38:41]
	v_mfma_f32_16x16x32_bf16 v[34:37], v[154:157], v[226:229], v[34:37]
	v_lshl_add_u64 v[166:167], v[132:133], 0, s[36:37]
	global_load_dwordx2 v[122:123], v[166:167], off
	global_load_dwordx2 v[124:125], v[166:167], off offset:2048
	v_mfma_f32_16x16x32_bf16 v[18:21], v[142:145], v[230:233], v[18:21]
	v_mfma_f32_16x16x32_bf16 v[22:25], v[146:149], v[230:233], v[22:25]
	v_mfma_f32_16x16x32_bf16 v[26:29], v[150:153], v[230:233], v[26:29]
	v_mfma_f32_16x16x32_bf16 v[30:33], v[154:157], v[230:233], v[30:33]
	v_lshl_add_u64 v[166:167], v[132:133], 0, s[38:39]
	global_load_dwordx2 v[126:127], v[166:167], off
	global_load_dwordx2 v[128:129], v[166:167], off offset:2048
	v_mfma_f32_16x16x32_bf16 v[2:5], v[142:145], v[234:237], v[2:5]
	v_mfma_f32_16x16x32_bf16 v[6:9], v[146:149], v[234:237], v[6:9]
	v_mfma_f32_16x16x32_bf16 v[10:13], v[150:153], v[234:237], v[10:13]
	v_mfma_f32_16x16x32_bf16 v[14:17], v[154:157], v[234:237], v[14:17]
	s_waitcnt lgkmcnt(0)
	s_barrier
; #define MU_GLDS_A(buf, kt) do { _Pragma("unroll") for (int i = 0; i < NMU; ++i) \
;         __builtin_amdgcn_global_load_lds((const unsigned*)((const char*)A + aoff[i] + (size_t)(kt) * 128), (PG8_LAS unsigned*)(MU_SA(buf) + wid * 1024 + i * 8192), 16, 0, 0); } while (0)
; #define MU_B_ISSUE(sb, kt) do { const char* kb_ = Bb + (size_t)(kt) * (64 * (size_t)RB); _Pragma("unroll") for (int j = 0; j < 8; ++j) { const char* p_ = kb_ + (size_t)j * RB; \
;         asm volatile("global_load_dwordx2 %0, %1, off" : "=&v"(sb[j]) : "v"(p_) : "memory"); } } while (0)
; #define MU_B_WAIT(sb, N) asm volatile("s_waitcnt vmcnt(%8)" : "+v"(sb[0]), "+v"(sb[1]), "+v"(sb[2]), "+v"(sb[3]), "+v"(sb[4]), "+v"(sb[5]), "+v"(sb[6]), "+v"(sb[7]) : "n"(N) : "memory")
; #define MU_G_LOAD(ga, kt) do { const PG8_LAS f32x4* gk_ = (const PG8_LAS f32x4*)(lds + GAIN_OFF) + 16 * (kt) + 2 * wid; const f32x4 ga_ = gk_[0], gb_ = gk_[1]; \
;         ga[0] = ga_[0]; ga[1] = ga_[1]; ga[2] = ga_[2]; ga[3] = ga_[3]; ga[4] = gb_[0]; ga[5] = gb_[1]; ga[6] = gb_[2]; ga[7] = gb_[3]; } while (0)
; #define MU_COMPUTE(buf) MU_COMPUTE_N(buf, NMU)
; #define MU_END(last) do { if (last) asm volatile("s_waitcnt vmcnt(0)" ::: "memory"); else asm volatile("s_waitcnt vmcnt(8)" ::: "memory"); \
;         asm volatile("s_waitcnt lgkmcnt(0)" ::: "memory"); __builtin_amdgcn_s_barrier(); asm volatile("" ::: "memory"); } while (0)
; template <int MODE>
; __device__ __forceinline__ void moe_unit(PG8_LAS unsigned char* lds, int e, int cb, int slot0  , int nv  , const bf16_t* A, const int* slot_tok,
;                                          const float* W0, const float* W1, bf16_t* OUT, const float* slot_rs  , const int* slot_dst) {
;     ...
;     for (int t = 0; t < nt; t += 2) {
;         if (t + 2 < nt) MU_B_WAIT(s1, 8); else MU_B_WAIT(s1, 0);
;         MU_G_LOAD(g0, t + 1); MU_B_WRITE(s1, 1, g0); __builtin_amdgcn_sched_barrier(0); MU_GLDS_A(1, t + 1); __builtin_amdgcn_sched_barrier(0);
;         if (t + 3 < nt) { MU_B_ISSUE(s1, t + 3); }
;         MU_COMPUTE(0);
;         MU_END(t + 3 >= nt);
;         if (t + 2 < nt) { MU_B_WAIT(s0, 8); MU_G_LOAD(g0, t + 2); MU_B_WRITE(s0, 0, g0); __builtin_amdgcn_sched_barrier(0); MU_GLDS_A(0, t + 2); __builtin_amdgcn_sched_barrier(0); }
;         if (t + 4 < nt) { MU_B_ISSUE(s0, t + 4); }
;         MU_COMPUTE(1);
;         MU_END(t + 4 >= nt);
;     }
	s_mov_b32 s47, s42
	s_mov_b32 s42, s43
	s_mov_b32 s43, s44
	s_mov_b32 s44, s47
	s_waitcnt vmcnt(29)
	v_mul_f32_e32 v186, s12, v186
	v_mul_f32_e32 v187, s12, v187
	v_mul_f32_e32 v188, s13, v188
	v_mul_f32_e32 v189, s13, v189
	v_mul_f32_e32 v190, s14, v190
	v_mul_f32_e32 v191, s14, v191
	v_mul_f32_e32 v192, s15, v192
	v_mul_f32_e32 v193, s15, v193
	v_mul_f32_e32 v194, s16, v194
	v_mul_f32_e32 v195, s16, v195
	v_mul_f32_e32 v196, s17, v196
	v_mul_f32_e32 v197, s17, v197
	v_mul_f32_e32 v198, s18, v198
	v_mul_f32_e32 v199, s18, v199
	v_mul_f32_e32 v200, s19, v200
	v_mul_f32_e32 v201, s19, v201
	v_cvt_pk_bf16_f32 v158, v186, v188
	v_cvt_pk_bf16_f32 v159, v190, v192
	v_cvt_pk_bf16_f32 v160, v194, v196
	v_cvt_pk_bf16_f32 v161, v198, v200
	v_cvt_pk_bf16_f32 v162, v187, v189
	v_cvt_pk_bf16_f32 v163, v191, v193
	v_cvt_pk_bf16_f32 v164, v195, v197
	v_cvt_pk_bf16_f32 v165, v199, v201
	ds_write_b128 v1, v[158:161] offset:0
	ds_write_b128 v1, v[162:165] offset:128
	v_add_u32_e32 v91, s42, v135
	v_add_u32_e32 v93, s42, v137
	ds_read_b128 v[238:241], v139 offset:19456
	ds_read_b128 v[242:245], v139 offset:21504
	ds_read_b128 v[246:249], v139 offset:23552
	ds_read_b128 v[250:253], v139 offset:25600
	ds_read_b128 v[218:221], v91 offset:0
	ds_read_b128 v[222:225], v91 offset:2048
	ds_read_b128 v[226:229], v91 offset:4096
	ds_read_b128 v[230:233], v91 offset:6144
	ds_read_b128 v[234:237], v91 offset:8192
	s_add_i32 s47, s44, s6
	s_add_u32 s30, s30, 0x80
	s_addc_u32 s31, s31, 0
	s_waitcnt lgkmcnt(0)
	v_mfma_f32_16x16x32_bf16 v[78:81], v[238:241], v[218:221], v[78:81]
	v_mfma_f32_16x16x32_bf16 v[74:77], v[242:245], v[218:221], v[74:77]
	v_mfma_f32_16x16x32_bf16 v[70:73], v[246:249], v[218:221], v[70:73]
	v_mfma_f32_16x16x32_bf16 v[66:69], v[250:253], v[218:221], v[66:69]
	ds_read_b128 v[218:221], v93 offset:0
	ds_read_b128 v[142:145], v141 offset:19456
	s_mov_b32 m0, s47
	s_nop 0
	global_load_lds_dwordx4 v86, s[30:31]
	v_mfma_f32_16x16x32_bf16 v[62:65], v[238:241], v[222:225], v[62:65]
	v_mfma_f32_16x16x32_bf16 v[58:61], v[242:245], v[222:225], v[58:61]
	v_mfma_f32_16x16x32_bf16 v[54:57], v[246:249], v[222:225], v[54:57]
	v_mfma_f32_16x16x32_bf16 v[50:53], v[250:253], v[222:225], v[50:53]
	ds_read_b128 v[222:225], v93 offset:2048
	ds_read_b128 v[146:149], v141 offset:21504
	s_add_i32 m0, s47, 0x2000
	s_nop 0
	global_load_lds_dwordx4 v134, s[30:31]
	v_mfma_f32_16x16x32_bf16 v[46:49], v[238:241], v[226:229], v[46:49]
	v_mfma_f32_16x16x32_bf16 v[42:45], v[242:245], v[226:229], v[42:45]
	v_mfma_f32_16x16x32_bf16 v[38:41], v[246:249], v[226:229], v[38:41]
	v_mfma_f32_16x16x32_bf16 v[34:37], v[250:253], v[226:229], v[34:37]
	ds_read_b128 v[226:229], v93 offset:4096
	ds_read_b128 v[150:153], v141 offset:23552
	s_add_i32 m0, s47, 0x4000
	s_nop 0
	global_load_lds_dwordx4 v136, s[30:31]
	v_mfma_f32_16x16x32_bf16 v[18:21], v[238:241], v[230:233], v[18:21]
	v_mfma_f32_16x16x32_bf16 v[22:25], v[242:245], v[230:233], v[22:25]
	v_mfma_f32_16x16x32_bf16 v[26:29], v[246:249], v[230:233], v[26:29]
	v_mfma_f32_16x16x32_bf16 v[30:33], v[250:253], v[230:233], v[30:33]
	ds_read_b128 v[230:233], v93 offset:6144
	ds_read_b128 v[154:157], v141 offset:25600
	s_add_i32 m0, s47, 0x6000
	s_nop 0
	global_load_lds_dwordx4 v138, s[30:31]
	v_mfma_f32_16x16x32_bf16 v[2:5], v[238:241], v[234:237], v[2:5]
	v_mfma_f32_16x16x32_bf16 v[6:9], v[242:245], v[234:237], v[6:9]
	v_mfma_f32_16x16x32_bf16 v[10:13], v[246:249], v[234:237], v[10:13]
	v_mfma_f32_16x16x32_bf16 v[14:17], v[250:253], v[234:237], v[14:17]
	ds_read_b128 v[234:237], v93 offset:8192
	s_add_i32 m0, s47, 0x8000
	s_nop 0
	global_load_lds_dwordx4 v140, s[30:31]
	s_waitcnt lgkmcnt(0)
	s_load_dwordx8 s[20:27], s[28:29], 0x0
	s_add_u32 s28, s28, 0x100
	s_addc_u32 s29, s29, 0
	v_mfma_f32_16x16x32_bf16 v[78:81], v[142:145], v[218:221], v[78:81]
	v_mfma_f32_16x16x32_bf16 v[74:77], v[146:149], v[218:221], v[74:77]
	v_mfma_f32_16x16x32_bf16 v[70:73], v[150:153], v[218:221], v[70:73]
	v_mfma_f32_16x16x32_bf16 v[66:69], v[154:157], v[218:221], v[66:69]
	v_lshl_add_u64 v[132:133], v[132:133], 0, s[40:41]
	global_load_dwordx2 v[186:187], v[132:133], off
	global_load_dwordx2 v[188:189], v[132:133], off offset:2048
	v_mfma_f32_16x16x32_bf16 v[62:65], v[142:145], v[222:225], v[62:65]
	v_mfma_f32_16x16x32_bf16 v[58:61], v[146:149], v[222:225], v[58:61]
	v_mfma_f32_16x16x32_bf16 v[54:57], v[150:153], v[222:225], v[54:57]
	v_mfma_f32_16x16x32_bf16 v[50:53], v[154:157], v[222:225], v[50:53]
	v_lshl_add_u64 v[166:167], v[132:133], 0, s[34:35]
	global_load_dwordx2 v[190:191], v[166:167], off
	global_load_dwordx2 v[192:193], v[166:167], off offset:2048
	v_mfma_f32_16x16x32_bf16 v[46:49], v[142:145], v[226:229], v[46:49]
	v_mfma_f32_16x16x32_bf16 v[42:45], v[146:149], v[226:229], v[42:45]
	v_mfma_f32_16x16x32_bf16 v[38:41], v[150:153], v[226:229], v[38:41]
	v_mfma_f32_16x16x32_bf16 v[34:37], v[154:157], v[226:229], v[34:37]
	v_lshl_add_u64 v[166:167], v[132:133], 0, s[36:37]
	global_load_dwordx2 v[194:195], v[166:167], off
	global_load_dwordx2 v[196:197], v[166:167], off offset:2048
	v_mfma_f32_16x16x32_bf16 v[18:21], v[142:145], v[230:233], v[18:21]
	v_mfma_f32_16x16x32_bf16 v[22:25], v[146:149], v[230:233], v[22:25]
	v_mfma_f32_16x16x32_bf16 v[26:29], v[150:153], v[230:233], v[26:29]
	v_mfma_f32_16x16x32_bf16 v[30:33], v[154:157], v[230:233], v[30:33]
	v_lshl_add_u64 v[166:167], v[132:133], 0, s[38:39]
	global_load_dwordx2 v[198:199], v[166:167], off
	global_load_dwordx2 v[200:201], v[166:167], off offset:2048
	v_mfma_f32_16x16x32_bf16 v[2:5], v[142:145], v[234:237], v[2:5]
	v_mfma_f32_16x16x32_bf16 v[6:9], v[146:149], v[234:237], v[6:9]
	v_mfma_f32_16x16x32_bf16 v[10:13], v[150:153], v[234:237], v[10:13]
	v_mfma_f32_16x16x32_bf16 v[14:17], v[154:157], v[234:237], v[14:17]
	s_waitcnt vmcnt(21)
	s_waitcnt lgkmcnt(0)
	s_barrier
; #define MU_GLDS_A(buf, kt) do { _Pragma("unroll") for (int i = 0; i < NMU; ++i) \
;         __builtin_amdgcn_global_load_lds((const unsigned*)((const char*)A + aoff[i] + (size_t)(kt) * 128), (PG8_LAS unsigned*)(MU_SA(buf) + wid * 1024 + i * 8192), 16, 0, 0); } while (0)
; #define MU_B_ISSUE(sb, kt) do { const char* kb_ = Bb + (size_t)(kt) * (64 * (size_t)RB); _Pragma("unroll") for (int j = 0; j < 8; ++j) { const char* p_ = kb_ + (size_t)j * RB; \
;         asm volatile("global_load_dwordx2 %0, %1, off" : "=&v"(sb[j]) : "v"(p_) : "memory"); } } while (0)
; #define MU_B_WAIT(sb, N) asm volatile("s_waitcnt vmcnt(%8)" : "+v"(sb[0]), "+v"(sb[1]), "+v"(sb[2]), "+v"(sb[3]), "+v"(sb[4]), "+v"(sb[5]), "+v"(sb[6]), "+v"(sb[7]) : "n"(N) : "memory")
; #define MU_G_LOAD(ga, kt) do { const PG8_LAS f32x4* gk_ = (const PG8_LAS f32x4*)(lds + GAIN_OFF) + 16 * (kt) + 2 * wid; const f32x4 ga_ = gk_[0], gb_ = gk_[1]; \
;         ga[0] = ga_[0]; ga[1] = ga_[1]; ga[2] = ga_[2]; ga[3] = ga_[3]; ga[4] = gb_[0]; ga[5] = gb_[1]; ga[6] = gb_[2]; ga[7] = gb_[3]; } while (0)
; #define MU_COMPUTE(buf) MU_COMPUTE_N(buf, NMU)
; #define MU_END(last) do { if (last) asm volatile("s_waitcnt vmcnt(0)" ::: "memory"); else asm volatile("s_waitcnt vmcnt(8)" ::: "memory"); \
;         asm volatile("s_waitcnt lgkmcnt(0)" ::: "memory"); __builtin_amdgcn_s_barrier(); asm volatile("" ::: "memory"); } while (0)
; template <int MODE>
; __device__ __forceinline__ void moe_unit(PG8_LAS unsigned char* lds, int e, int cb, int slot0  , int nv  , const bf16_t* A, const int* slot_tok,
;                                          const float* W0, const float* W1, bf16_t* OUT, const float* slot_rs  , const int* slot_dst) {
;     ...
;     for (int t = 0; t < nt; t += 2) {
;         if (t + 2 < nt) MU_B_WAIT(s1, 8); else MU_B_WAIT(s1, 0);
;         MU_G_LOAD(g0, t + 1); MU_B_WRITE(s1, 1, g0); __builtin_amdgcn_sched_barrier(0); MU_GLDS_A(1, t + 1); __builtin_amdgcn_sched_barrier(0);
;         if (t + 3 < nt) { MU_B_ISSUE(s1, t + 3); }
;         MU_COMPUTE(0);
;         MU_END(t + 3 >= nt);
;         if (t + 2 < nt) { MU_B_WAIT(s0, 8); MU_G_LOAD(g0, t + 2); MU_B_WRITE(s0, 0, g0); __builtin_amdgcn_sched_barrier(0); MU_GLDS_A(0, t + 2); __builtin_amdgcn_sched_barrier(0); }
;         if (t + 4 < nt) { MU_B_ISSUE(s0, t + 4); }
;         MU_COMPUTE(1);
;         MU_END(t + 4 >= nt);
;     }
	s_mov_b32 s47, s42
	s_mov_b32 s42, s43
	s_mov_b32 s43, s44
	s_mov_b32 s44, s47
	v_mul_f32_e32 v202, s20, v202
	v_mul_f32_e32 v203, s20, v203
	v_mul_f32_e32 v204, s21, v204
	v_mul_f32_e32 v205, s21, v205
	v_mul_f32_e32 v206, s22, v206
	v_mul_f32_e32 v207, s22, v207
	v_mul_f32_e32 v208, s23, v208
	v_mul_f32_e32 v209, s23, v209
	v_mul_f32_e32 v210, s24, v210
	v_mul_f32_e32 v211, s24, v211
	v_mul_f32_e32 v212, s25, v212
	v_mul_f32_e32 v213, s25, v213
	v_mul_f32_e32 v214, s26, v214
	v_mul_f32_e32 v215, s26, v215
	v_mul_f32_e32 v216, s27, v216
	v_mul_f32_e32 v217, s27, v217
	v_cvt_pk_bf16_f32 v158, v202, v204
	v_cvt_pk_bf16_f32 v159, v206, v208
	v_cvt_pk_bf16_f32 v160, v210, v212
	v_cvt_pk_bf16_f32 v161, v214, v216
	v_cvt_pk_bf16_f32 v162, v203, v205
	v_cvt_pk_bf16_f32 v163, v207, v209
	v_cvt_pk_bf16_f32 v164, v211, v213
	v_cvt_pk_bf16_f32 v165, v215, v217
	ds_write_b128 v1, v[158:161] offset:19456
	ds_write_b128 v1, v[162:165] offset:19584
	v_add_u32_e32 v91, s42, v135
	v_add_u32_e32 v93, s42, v137
	ds_read_b128 v[238:241], v139 offset:0
	ds_read_b128 v[242:245], v139 offset:2048
	ds_read_b128 v[246:249], v139 offset:4096
	ds_read_b128 v[250:253], v139 offset:6144
	ds_read_b128 v[218:221], v91 offset:0
	ds_read_b128 v[222:225], v91 offset:2048
	ds_read_b128 v[226:229], v91 offset:4096
	ds_read_b128 v[230:233], v91 offset:6144
	ds_read_b128 v[234:237], v91 offset:8192
	s_add_i32 s47, s44, s6
	s_add_u32 s30, s30, 0x80
	s_addc_u32 s31, s31, 0
	s_waitcnt lgkmcnt(0)
	v_mfma_f32_16x16x32_bf16 v[78:81], v[238:241], v[218:221], v[78:81]
	v_mfma_f32_16x16x32_bf16 v[74:77], v[242:245], v[218:221], v[74:77]
	v_mfma_f32_16x16x32_bf16 v[70:73], v[246:249], v[218:221], v[70:73]
	v_mfma_f32_16x16x32_bf16 v[66:69], v[250:253], v[218:221], v[66:69]
	ds_read_b128 v[218:221], v93 offset:0
	ds_read_b128 v[142:145], v141 offset:0
	s_mov_b32 m0, s47
	s_nop 0
	global_load_lds_dwordx4 v86, s[30:31]
	v_mfma_f32_16x16x32_bf16 v[62:65], v[238:241], v[222:225], v[62:65]
	v_mfma_f32_16x16x32_bf16 v[58:61], v[242:245], v[222:225], v[58:61]
	v_mfma_f32_16x16x32_bf16 v[54:57], v[246:249], v[222:225], v[54:57]
	v_mfma_f32_16x16x32_bf16 v[50:53], v[250:253], v[222:225], v[50:53]
	ds_read_b128 v[222:225], v93 offset:2048
	ds_read_b128 v[146:149], v141 offset:2048
	s_add_i32 m0, s47, 0x2000
	s_nop 0
	global_load_lds_dwordx4 v134, s[30:31]
	v_mfma_f32_16x16x32_bf16 v[46:49], v[238:241], v[226:229], v[46:49]
	v_mfma_f32_16x16x32_bf16 v[42:45], v[242:245], v[226:229], v[42:45]
	v_mfma_f32_16x16x32_bf16 v[38:41], v[246:249], v[226:229], v[38:41]
	v_mfma_f32_16x16x32_bf16 v[34:37], v[250:253], v[226:229], v[34:37]
	ds_read_b128 v[226:229], v93 offset:4096
	ds_read_b128 v[150:153], v141 offset:4096
	s_add_i32 m0, s47, 0x4000
	s_nop 0
	global_load_lds_dwordx4 v136, s[30:31]
	v_mfma_f32_16x16x32_bf16 v[18:21], v[238:241], v[230:233], v[18:21]
	v_mfma_f32_16x16x32_bf16 v[22:25], v[242:245], v[230:233], v[22:25]
	v_mfma_f32_16x16x32_bf16 v[26:29], v[246:249], v[230:233], v[26:29]
	v_mfma_f32_16x16x32_bf16 v[30:33], v[250:253], v[230:233], v[30:33]
	ds_read_b128 v[230:233], v93 offset:6144
	ds_read_b128 v[154:157], v141 offset:6144
	s_add_i32 m0, s47, 0x6000
	s_nop 0
	global_load_lds_dwordx4 v138, s[30:31]
	v_mfma_f32_16x16x32_bf16 v[2:5], v[238:241], v[234:237], v[2:5]
	v_mfma_f32_16x16x32_bf16 v[6:9], v[242:245], v[234:237], v[6:9]
	v_mfma_f32_16x16x32_bf16 v[10:13], v[246:249], v[234:237], v[10:13]
	v_mfma_f32_16x16x32_bf16 v[14:17], v[250:253], v[234:237], v[14:17]
	ds_read_b128 v[234:237], v93 offset:8192
	s_add_i32 m0, s47, 0x8000
	s_nop 0
	global_load_lds_dwordx4 v140, s[30:31]
	s_waitcnt lgkmcnt(0)
	s_load_dwordx8 s[12:19], s[28:29], 0x0
	s_add_u32 s28, s28, 0x100
	s_addc_u32 s29, s29, 0
	v_mfma_f32_16x16x32_bf16 v[78:81], v[142:145], v[218:221], v[78:81]
	v_mfma_f32_16x16x32_bf16 v[74:77], v[146:149], v[218:221], v[74:77]
	v_mfma_f32_16x16x32_bf16 v[70:73], v[150:153], v[218:221], v[70:73]
	v_mfma_f32_16x16x32_bf16 v[66:69], v[154:157], v[218:221], v[66:69]
	v_lshl_add_u64 v[132:133], v[132:133], 0, s[40:41]
	global_load_dwordx2 v[202:203], v[132:133], off
	global_load_dwordx2 v[204:205], v[132:133], off offset:2048
	v_mfma_f32_16x16x32_bf16 v[62:65], v[142:145], v[222:225], v[62:65]
	v_mfma_f32_16x16x32_bf16 v[58:61], v[146:149], v[222:225], v[58:61]
	v_mfma_f32_16x16x32_bf16 v[54:57], v[150:153], v[222:225], v[54:57]
	v_mfma_f32_16x16x32_bf16 v[50:53], v[154:157], v[222:225], v[50:53]
	v_lshl_add_u64 v[166:167], v[132:133], 0, s[34:35]
	global_load_dwordx2 v[206:207], v[166:167], off
	global_load_dwordx2 v[208:209], v[166:167], off offset:2048
	v_mfma_f32_16x16x32_bf16 v[46:49], v[142:145], v[226:229], v[46:49]
	v_mfma_f32_16x16x32_bf16 v[42:45], v[146:149], v[226:229], v[42:45]
	v_mfma_f32_16x16x32_bf16 v[38:41], v[150:153], v[226:229], v[38:41]
	v_mfma_f32_16x16x32_bf16 v[34:37], v[154:157], v[226:229], v[34:37]
	v_lshl_add_u64 v[166:167], v[132:133], 0, s[36:37]
	global_load_dwordx2 v[210:211], v[166:167], off
	global_load_dwordx2 v[212:213], v[166:167], off offset:2048
	v_mfma_f32_16x16x32_bf16 v[18:21], v[142:145], v[230:233], v[18:21]
	v_mfma_f32_16x16x32_bf16 v[22:25], v[146:149], v[230:233], v[22:25]
	v_mfma_f32_16x16x32_bf16 v[26:29], v[150:153], v[230:233], v[26:29]
	v_mfma_f32_16x16x32_bf16 v[30:33], v[154:157], v[230:233], v[30:33]
	v_lshl_add_u64 v[166:167], v[132:133], 0, s[38:39]
	global_load_dwordx2 v[214:215], v[166:167], off
	global_load_dwordx2 v[216:217], v[166:167], off offset:2048
	v_mfma_f32_16x16x32_bf16 v[2:5], v[142:145], v[234:237], v[2:5]
	v_mfma_f32_16x16x32_bf16 v[6:9], v[146:149], v[234:237], v[6:9]
	v_mfma_f32_16x16x32_bf16 v[10:13], v[150:153], v[234:237], v[10:13]
	v_mfma_f32_16x16x32_bf16 v[14:17], v[154:157], v[234:237], v[14:17]
	s_waitcnt vmcnt(21)
	s_waitcnt lgkmcnt(0)
	s_barrier
; #define MU_GLDS_A(buf, kt) do { _Pragma("unroll") for (int i = 0; i < NMU; ++i) \
;         __builtin_amdgcn_global_load_lds((const unsigned*)((const char*)A + aoff[i] + (size_t)(kt) * 128), (PG8_LAS unsigned*)(MU_SA(buf) + wid * 1024 + i * 8192), 16, 0, 0); } while (0)
; #define MU_B_ISSUE(sb, kt) do { const char* kb_ = Bb + (size_t)(kt) * (64 * (size_t)RB); _Pragma("unroll") for (int j = 0; j < 8; ++j) { const char* p_ = kb_ + (size_t)j * RB; \
;         asm volatile("global_load_dwordx2 %0, %1, off" : "=&v"(sb[j]) : "v"(p_) : "memory"); } } while (0)
; #define MU_B_WAIT(sb, N) asm volatile("s_waitcnt vmcnt(%8)" : "+v"(sb[0]), "+v"(sb[1]), "+v"(sb[2]), "+v"(sb[3]), "+v"(sb[4]), "+v"(sb[5]), "+v"(sb[6]), "+v"(sb[7]) : "n"(N) : "memory")
; #define MU_G_LOAD(ga, kt) do { const PG8_LAS f32x4* gk_ = (const PG8_LAS f32x4*)(lds + GAIN_OFF) + 16 * (kt) + 2 * wid; const f32x4 ga_ = gk_[0], gb_ = gk_[1]; \
;         ga[0] = ga_[0]; ga[1] = ga_[1]; ga[2] = ga_[2]; ga[3] = ga_[3]; ga[4] = gb_[0]; ga[5] = gb_[1]; ga[6] = gb_[2]; ga[7] = gb_[3]; } while (0)
; #define MU_COMPUTE(buf) MU_COMPUTE_N(buf, NMU)
; #define MU_END(last) do { if (last) asm volatile("s_waitcnt vmcnt(0)" ::: "memory"); else asm volatile("s_waitcnt vmcnt(8)" ::: "memory"); \
;         asm volatile("s_waitcnt lgkmcnt(0)" ::: "memory"); __builtin_amdgcn_s_barrier(); asm volatile("" ::: "memory"); } while (0)
; template <int MODE>
; __device__ __forceinline__ void moe_unit(PG8_LAS unsigned char* lds, int e, int cb, int slot0  , int nv  , const bf16_t* A, const int* slot_tok,
;                                          const float* W0, const float* W1, bf16_t* OUT, const float* slot_rs  , const int* slot_dst) {
;     ...
;     for (int t = 0; t < nt; t += 2) {
;         if (t + 2 < nt) MU_B_WAIT(s1, 8); else MU_B_WAIT(s1, 0);
;         MU_G_LOAD(g0, t + 1); MU_B_WRITE(s1, 1, g0); __builtin_amdgcn_sched_barrier(0); MU_GLDS_A(1, t + 1); __builtin_amdgcn_sched_barrier(0);
;         if (t + 3 < nt) { MU_B_ISSUE(s1, t + 3); }
;         MU_COMPUTE(0);
;         MU_END(t + 3 >= nt);
;         if (t + 2 < nt) { MU_B_WAIT(s0, 8); MU_G_LOAD(g0, t + 2); MU_B_WRITE(s0, 0, g0); __builtin_amdgcn_sched_barrier(0); MU_GLDS_A(0, t + 2); __builtin_amdgcn_sched_barrier(0); }
;         if (t + 4 < nt) { MU_B_ISSUE(s0, t + 4); }
;         MU_COMPUTE(1);
;         MU_END(t + 4 >= nt);
;     }
	s_mov_b32 s47, s42
	s_mov_b32 s42, s43
	s_mov_b32 s43, s44
	s_mov_b32 s44, s47
	v_mul_f32_e32 v98, s12, v98
	v_mul_f32_e32 v99, s12, v99
	v_mul_f32_e32 v100, s13, v100
	v_mul_f32_e32 v101, s13, v101
	v_mul_f32_e32 v102, s14, v102
	v_mul_f32_e32 v103, s14, v103
	v_mul_f32_e32 v104, s15, v104
	v_mul_f32_e32 v105, s15, v105
	v_mul_f32_e32 v106, s16, v106
	v_mul_f32_e32 v107, s16, v107
	v_mul_f32_e32 v108, s17, v108
	v_mul_f32_e32 v109, s17, v109
	v_mul_f32_e32 v110, s18, v110
	v_mul_f32_e32 v111, s18, v111
	v_mul_f32_e32 v112, s19, v112
	v_mul_f32_e32 v113, s19, v113
	v_cvt_pk_bf16_f32 v158, v98, v100
	v_cvt_pk_bf16_f32 v159, v102, v104
	v_cvt_pk_bf16_f32 v160, v106, v108
	v_cvt_pk_bf16_f32 v161, v110, v112
	v_cvt_pk_bf16_f32 v162, v99, v101
	v_cvt_pk_bf16_f32 v163, v103, v105
	v_cvt_pk_bf16_f32 v164, v107, v109
	v_cvt_pk_bf16_f32 v165, v111, v113
	ds_write_b128 v1, v[158:161] offset:0
	ds_write_b128 v1, v[162:165] offset:128
	v_add_u32_e32 v91, s42, v135
	v_add_u32_e32 v93, s42, v137
	ds_read_b128 v[238:241], v139 offset:19456
	ds_read_b128 v[242:245], v139 offset:21504
	ds_read_b128 v[246:249], v139 offset:23552
	ds_read_b128 v[250:253], v139 offset:25600
	ds_read_b128 v[218:221], v91 offset:0
	ds_read_b128 v[222:225], v91 offset:2048
	ds_read_b128 v[226:229], v91 offset:4096
	ds_read_b128 v[230:233], v91 offset:6144
	ds_read_b128 v[234:237], v91 offset:8192
	s_add_i32 s47, s44, s6
	s_add_u32 s30, s30, 0x80
	s_addc_u32 s31, s31, 0
	s_waitcnt lgkmcnt(0)
	v_mfma_f32_16x16x32_bf16 v[78:81], v[238:241], v[218:221], v[78:81]
	v_mfma_f32_16x16x32_bf16 v[74:77], v[242:245], v[218:221], v[74:77]
	v_mfma_f32_16x16x32_bf16 v[70:73], v[246:249], v[218:221], v[70:73]
	v_mfma_f32_16x16x32_bf16 v[66:69], v[250:253], v[218:221], v[66:69]
	ds_read_b128 v[218:221], v93 offset:0
	ds_read_b128 v[142:145], v141 offset:19456
	s_mov_b32 m0, s47
	s_nop 0
	global_load_lds_dwordx4 v86, s[30:31]
	v_mfma_f32_16x16x32_bf16 v[62:65], v[238:241], v[222:225], v[62:65]
	v_mfma_f32_16x16x32_bf16 v[58:61], v[242:245], v[222:225], v[58:61]
	v_mfma_f32_16x16x32_bf16 v[54:57], v[246:249], v[222:225], v[54:57]
	v_mfma_f32_16x16x32_bf16 v[50:53], v[250:253], v[222:225], v[50:53]
	ds_read_b128 v[222:225], v93 offset:2048
	ds_read_b128 v[146:149], v141 offset:21504
	s_add_i32 m0, s47, 0x2000
	s_nop 0
	global_load_lds_dwordx4 v134, s[30:31]
	v_mfma_f32_16x16x32_bf16 v[46:49], v[238:241], v[226:229], v[46:49]
	v_mfma_f32_16x16x32_bf16 v[42:45], v[242:245], v[226:229], v[42:45]
	v_mfma_f32_16x16x32_bf16 v[38:41], v[246:249], v[226:229], v[38:41]
	v_mfma_f32_16x16x32_bf16 v[34:37], v[250:253], v[226:229], v[34:37]
	ds_read_b128 v[226:229], v93 offset:4096
	ds_read_b128 v[150:153], v141 offset:23552
	s_add_i32 m0, s47, 0x4000
	s_nop 0
	global_load_lds_dwordx4 v136, s[30:31]
	v_mfma_f32_16x16x32_bf16 v[18:21], v[238:241], v[230:233], v[18:21]
	v_mfma_f32_16x16x32_bf16 v[22:25], v[242:245], v[230:233], v[22:25]
	v_mfma_f32_16x16x32_bf16 v[26:29], v[246:249], v[230:233], v[26:29]
	v_mfma_f32_16x16x32_bf16 v[30:33], v[250:253], v[230:233], v[30:33]
	ds_read_b128 v[230:233], v93 offset:6144
	ds_read_b128 v[154:157], v141 offset:25600
	s_add_i32 m0, s47, 0x6000
	s_nop 0
	global_load_lds_dwordx4 v138, s[30:31]
	v_mfma_f32_16x16x32_bf16 v[2:5], v[238:241], v[234:237], v[2:5]
	v_mfma_f32_16x16x32_bf16 v[6:9], v[242:245], v[234:237], v[6:9]
	v_mfma_f32_16x16x32_bf16 v[10:13], v[246:249], v[234:237], v[10:13]
	v_mfma_f32_16x16x32_bf16 v[14:17], v[250:253], v[234:237], v[14:17]
	ds_read_b128 v[234:237], v93 offset:8192
	s_add_i32 m0, s47, 0x8000
	s_nop 0
	global_load_lds_dwordx4 v140, s[30:31]
	s_waitcnt lgkmcnt(0)
	s_load_dwordx8 s[20:27], s[28:29], 0x0
	s_add_u32 s28, s28, 0x100
	s_addc_u32 s29, s29, 0
	v_mfma_f32_16x16x32_bf16 v[78:81], v[142:145], v[218:221], v[78:81]
	v_mfma_f32_16x16x32_bf16 v[74:77], v[146:149], v[218:221], v[74:77]
	v_mfma_f32_16x16x32_bf16 v[70:73], v[150:153], v[218:221], v[70:73]
	v_mfma_f32_16x16x32_bf16 v[66:69], v[154:157], v[218:221], v[66:69]
	v_lshl_add_u64 v[132:133], v[132:133], 0, s[40:41]
	global_load_dwordx2 v[98:99], v[132:133], off
	global_load_dwordx2 v[100:101], v[132:133], off offset:2048
	v_mfma_f32_16x16x32_bf16 v[62:65], v[142:145], v[222:225], v[62:65]
	v_mfma_f32_16x16x32_bf16 v[58:61], v[146:149], v[222:225], v[58:61]
	v_mfma_f32_16x16x32_bf16 v[54:57], v[150:153], v[222:225], v[54:57]
	v_mfma_f32_16x16x32_bf16 v[50:53], v[154:157], v[222:225], v[50:53]
	v_lshl_add_u64 v[166:167], v[132:133], 0, s[34:35]
	global_load_dwordx2 v[102:103], v[166:167], off
	global_load_dwordx2 v[104:105], v[166:167], off offset:2048
	v_mfma_f32_16x16x32_bf16 v[46:49], v[142:145], v[226:229], v[46:49]
	v_mfma_f32_16x16x32_bf16 v[42:45], v[146:149], v[226:229], v[42:45]
	v_mfma_f32_16x16x32_bf16 v[38:41], v[150:153], v[226:229], v[38:41]
	v_mfma_f32_16x16x32_bf16 v[34:37], v[154:157], v[226:229], v[34:37]
	v_lshl_add_u64 v[166:167], v[132:133], 0, s[36:37]
	global_load_dwordx2 v[106:107], v[166:167], off
	global_load_dwordx2 v[108:109], v[166:167], off offset:2048
	v_mfma_f32_16x16x32_bf16 v[18:21], v[142:145], v[230:233], v[18:21]
	v_mfma_f32_16x16x32_bf16 v[22:25], v[146:149], v[230:233], v[22:25]
	v_mfma_f32_16x16x32_bf16 v[26:29], v[150:153], v[230:233], v[26:29]
	v_mfma_f32_16x16x32_bf16 v[30:33], v[154:157], v[230:233], v[30:33]
	v_lshl_add_u64 v[166:167], v[132:133], 0, s[38:39]
	global_load_dwordx2 v[110:111], v[166:167], off
	global_load_dwordx2 v[112:113], v[166:167], off offset:2048
	v_mfma_f32_16x16x32_bf16 v[2:5], v[142:145], v[234:237], v[2:5]
	v_mfma_f32_16x16x32_bf16 v[6:9], v[146:149], v[234:237], v[6:9]
	v_mfma_f32_16x16x32_bf16 v[10:13], v[150:153], v[234:237], v[10:13]
	v_mfma_f32_16x16x32_bf16 v[14:17], v[154:157], v[234:237], v[14:17]
	s_waitcnt vmcnt(21)
	s_waitcnt lgkmcnt(0)
	s_barrier
	s_mov_b32 s47, s42
	s_mov_b32 s42, s43
	s_mov_b32 s43, s44
	s_mov_b32 s44, s47
	s_mov_b32 s46, 13
; #define MU_GLDS_A(buf, kt) do { _Pragma("unroll") for (int i = 0; i < NMU; ++i) \
;         __builtin_amdgcn_global_load_lds((const unsigned*)((const char*)A + aoff[i] + (size_t)(kt) * 128), (PG8_LAS unsigned*)(MU_SA(buf) + wid * 1024 + i * 8192), 16, 0, 0); } while (0)
; #define MU_B_ISSUE(sb, kt) do { const char* kb_ = Bb + (size_t)(kt) * (64 * (size_t)RB); _Pragma("unroll") for (int j = 0; j < 8; ++j) { const char* p_ = kb_ + (size_t)j * RB; \
;         asm volatile("global_load_dwordx2 %0, %1, off" : "=&v"(sb[j]) : "v"(p_) : "memory"); } } while (0)
; #define MU_B_WAIT(sb, N) asm volatile("s_waitcnt vmcnt(%8)" : "+v"(sb[0]), "+v"(sb[1]), "+v"(sb[2]), "+v"(sb[3]), "+v"(sb[4]), "+v"(sb[5]), "+v"(sb[6]), "+v"(sb[7]) : "n"(N) : "memory")
; #define MU_G_LOAD(ga, kt) do { const PG8_LAS f32x4* gk_ = (const PG8_LAS f32x4*)(lds + GAIN_OFF) + 16 * (kt) + 2 * wid; const f32x4 ga_ = gk_[0], gb_ = gk_[1]; \
;         ga[0] = ga_[0]; ga[1] = ga_[1]; ga[2] = ga_[2]; ga[3] = ga_[3]; ga[4] = gb_[0]; ga[5] = gb_[1]; ga[6] = gb_[2]; ga[7] = gb_[3]; } while (0)
; #define MU_COMPUTE(buf) MU_COMPUTE_N(buf, NMU)
; #define MU_END(last) do { if (last) asm volatile("s_waitcnt vmcnt(0)" ::: "memory"); else asm volatile("s_waitcnt vmcnt(8)" ::: "memory"); \
;         asm volatile("s_waitcnt lgkmcnt(0)" ::: "memory"); __builtin_amdgcn_s_barrier(); asm volatile("" ::: "memory"); } while (0)
; template <int MODE>
; __device__ __forceinline__ void moe_unit(PG8_LAS unsigned char* lds, int e, int cb, int slot0  , int nv  , const bf16_t* A, const int* slot_tok,
;                                          const float* W0, const float* W1, bf16_t* OUT, const float* slot_rs  , const int* slot_dst) {
;     ...
;     for (int t = 0; t < nt; t += 2) {
;         if (t + 2 < nt) MU_B_WAIT(s1, 8); else MU_B_WAIT(s1, 0);
;         MU_G_LOAD(g0, t + 1); MU_B_WRITE(s1, 1, g0); __builtin_amdgcn_sched_barrier(0); MU_GLDS_A(1, t + 1); __builtin_amdgcn_sched_barrier(0);
;         if (t + 3 < nt) { MU_B_ISSUE(s1, t + 3); }
;         MU_COMPUTE(0);
;         MU_END(t + 3 >= nt);
;         if (t + 2 < nt) { MU_B_WAIT(s0, 8); MU_G_LOAD(g0, t + 2); MU_B_WRITE(s0, 0, g0); __builtin_amdgcn_sched_barrier(0); MU_GLDS_A(0, t + 2); __builtin_amdgcn_sched_barrier(0); }
;         if (t + 4 < nt) { MU_B_ISSUE(s0, t + 4); }
;         MU_COMPUTE(1);
;         MU_END(t + 4 >= nt);
;     }
.Lmu_loop_X:
	v_mul_f32_e32 v114, s20, v114
	v_mul_f32_e32 v115, s20, v115
	v_mul_f32_e32 v116, s21, v116
	v_mul_f32_e32 v117, s21, v117
	v_mul_f32_e32 v118, s22, v118
	v_mul_f32_e32 v119, s22, v119
	v_mul_f32_e32 v120, s23, v120
	v_mul_f32_e32 v121, s23, v121
	v_mul_f32_e32 v122, s24, v122
	v_mul_f32_e32 v123, s24, v123
	v_mul_f32_e32 v124, s25, v124
	v_mul_f32_e32 v125, s25, v125
	v_mul_f32_e32 v126, s26, v126
	v_mul_f32_e32 v127, s26, v127
	v_mul_f32_e32 v128, s27, v128
	v_mul_f32_e32 v129, s27, v129
	v_cvt_pk_bf16_f32 v158, v114, v116
	v_cvt_pk_bf16_f32 v159, v118, v120
	v_cvt_pk_bf16_f32 v160, v122, v124
	v_cvt_pk_bf16_f32 v161, v126, v128
	v_cvt_pk_bf16_f32 v162, v115, v117
	v_cvt_pk_bf16_f32 v163, v119, v121
	v_cvt_pk_bf16_f32 v164, v123, v125
	v_cvt_pk_bf16_f32 v165, v127, v129
	ds_write_b128 v1, v[158:161] offset:19456
	ds_write_b128 v1, v[162:165] offset:19584
	v_add_u32_e32 v91, s42, v135
	v_add_u32_e32 v93, s42, v137
	ds_read_b128 v[238:241], v139 offset:0
	ds_read_b128 v[242:245], v139 offset:2048
	ds_read_b128 v[246:249], v139 offset:4096
	ds_read_b128 v[250:253], v139 offset:6144
	ds_read_b128 v[218:221], v91 offset:0
	ds_read_b128 v[222:225], v91 offset:2048
	ds_read_b128 v[226:229], v91 offset:4096
	ds_read_b128 v[230:233], v91 offset:6144
	ds_read_b128 v[234:237], v91 offset:8192
	s_add_i32 s47, s44, s6
	s_add_u32 s30, s30, 0x80
	s_addc_u32 s31, s31, 0
	s_waitcnt lgkmcnt(0)
	v_mfma_f32_16x16x32_bf16 v[78:81], v[238:241], v[218:221], v[78:81]
	v_mfma_f32_16x16x32_bf16 v[74:77], v[242:245], v[218:221], v[74:77]
	v_mfma_f32_16x16x32_bf16 v[70:73], v[246:249], v[218:221], v[70:73]
	v_mfma_f32_16x16x32_bf16 v[66:69], v[250:253], v[218:221], v[66:69]
	ds_read_b128 v[218:221], v93 offset:0
	ds_read_b128 v[142:145], v141 offset:0
	s_mov_b32 m0, s47
	s_nop 0
	global_load_lds_dwordx4 v86, s[30:31]
	v_mfma_f32_16x16x32_bf16 v[62:65], v[238:241], v[222:225], v[62:65]
	v_mfma_f32_16x16x32_bf16 v[58:61], v[242:245], v[222:225], v[58:61]
	v_mfma_f32_16x16x32_bf16 v[54:57], v[246:249], v[222:225], v[54:57]
	v_mfma_f32_16x16x32_bf16 v[50:53], v[250:253], v[222:225], v[50:53]
	ds_read_b128 v[222:225], v93 offset:2048
	ds_read_b128 v[146:149], v141 offset:2048
	s_add_i32 m0, s47, 0x2000
	s_nop 0
	global_load_lds_dwordx4 v134, s[30:31]
	v_mfma_f32_16x16x32_bf16 v[46:49], v[238:241], v[226:229], v[46:49]
	v_mfma_f32_16x16x32_bf16 v[42:45], v[242:245], v[226:229], v[42:45]
	v_mfma_f32_16x16x32_bf16 v[38:41], v[246:249], v[226:229], v[38:41]
	v_mfma_f32_16x16x32_bf16 v[34:37], v[250:253], v[226:229], v[34:37]
	ds_read_b128 v[226:229], v93 offset:4096
	ds_read_b128 v[150:153], v141 offset:4096
	s_add_i32 m0, s47, 0x4000
	s_nop 0
	global_load_lds_dwordx4 v136, s[30:31]
	v_mfma_f32_16x16x32_bf16 v[18:21], v[238:241], v[230:233], v[18:21]
	v_mfma_f32_16x16x32_bf16 v[22:25], v[242:245], v[230:233], v[22:25]
	v_mfma_f32_16x16x32_bf16 v[26:29], v[246:249], v[230:233], v[26:29]
	v_mfma_f32_16x16x32_bf16 v[30:33], v[250:253], v[230:233], v[30:33]
	ds_read_b128 v[230:233], v93 offset:6144
	ds_read_b128 v[154:157], v141 offset:6144
	s_add_i32 m0, s47, 0x6000
	s_nop 0
	global_load_lds_dwordx4 v138, s[30:31]
	v_mfma_f32_16x16x32_bf16 v[2:5], v[238:241], v[234:237], v[2:5]
	v_mfma_f32_16x16x32_bf16 v[6:9], v[242:245], v[234:237], v[6:9]
	v_mfma_f32_16x16x32_bf16 v[10:13], v[246:249], v[234:237], v[10:13]
	v_mfma_f32_16x16x32_bf16 v[14:17], v[250:253], v[234:237], v[14:17]
	ds_read_b128 v[234:237], v93 offset:8192
	s_add_i32 m0, s47, 0x8000
	s_nop 0
	global_load_lds_dwordx4 v140, s[30:31]
	s_waitcnt lgkmcnt(0)
	s_load_dwordx8 s[12:19], s[28:29], 0x0
	s_add_u32 s28, s28, 0x100
	s_addc_u32 s29, s29, 0
	v_mfma_f32_16x16x32_bf16 v[78:81], v[142:145], v[218:221], v[78:81]
	v_mfma_f32_16x16x32_bf16 v[74:77], v[146:149], v[218:221], v[74:77]
	v_mfma_f32_16x16x32_bf16 v[70:73], v[150:153], v[218:221], v[70:73]
	v_mfma_f32_16x16x32_bf16 v[66:69], v[154:157], v[218:221], v[66:69]
	v_lshl_add_u64 v[132:133], v[132:133], 0, s[40:41]
	global_load_dwordx2 v[114:115], v[132:133], off
	global_load_dwordx2 v[116:117], v[132:133], off offset:2048
	v_mfma_f32_16x16x32_bf16 v[62:65], v[142:145], v[222:225], v[62:65]
	v_mfma_f32_16x16x32_bf16 v[58:61], v[146:149], v[222:225], v[58:61]
	v_mfma_f32_16x16x32_bf16 v[54:57], v[150:153], v[222:225], v[54:57]
	v_mfma_f32_16x16x32_bf16 v[50:53], v[154:157], v[222:225], v[50:53]
	v_lshl_add_u64 v[166:167], v[132:133], 0, s[34:35]
	global_load_dwordx2 v[118:119], v[166:167], off
	global_load_dwordx2 v[120:121], v[166:167], off offset:2048
	v_mfma_f32_16x16x32_bf16 v[46:49], v[142:145], v[226:229], v[46:49]
	v_mfma_f32_16x16x32_bf16 v[42:45], v[146:149], v[226:229], v[42:45]
	v_mfma_f32_16x16x32_bf16 v[38:41], v[150:153], v[226:229], v[38:41]
	v_mfma_f32_16x16x32_bf16 v[34:37], v[154:157], v[226:229], v[34:37]
	v_lshl_add_u64 v[166:167], v[132:133], 0, s[36:37]
	global_load_dwordx2 v[122:123], v[166:167], off
	global_load_dwordx2 v[124:125], v[166:167], off offset:2048
	v_mfma_f32_16x16x32_bf16 v[18:21], v[142:145], v[230:233], v[18:21]
	v_mfma_f32_16x16x32_bf16 v[22:25], v[146:149], v[230:233], v[22:25]
	v_mfma_f32_16x16x32_bf16 v[26:29], v[150:153], v[230:233], v[26:29]
	v_mfma_f32_16x16x32_bf16 v[30:33], v[154:157], v[230:233], v[30:33]
	v_lshl_add_u64 v[166:167], v[132:133], 0, s[38:39]
	global_load_dwordx2 v[126:127], v[166:167], off
	global_load_dwordx2 v[128:129], v[166:167], off offset:2048
	v_mfma_f32_16x16x32_bf16 v[2:5], v[142:145], v[234:237], v[2:5]
	v_mfma_f32_16x16x32_bf16 v[6:9], v[146:149], v[234:237], v[6:9]
	v_mfma_f32_16x16x32_bf16 v[10:13], v[150:153], v[234:237], v[10:13]
	v_mfma_f32_16x16x32_bf16 v[14:17], v[154:157], v[234:237], v[14:17]
	s_waitcnt vmcnt(21)
	s_waitcnt lgkmcnt(0)
	s_barrier
; #define MU_GLDS_A(buf, kt) do { _Pragma("unroll") for (int i = 0; i < NMU; ++i) \
;         __builtin_amdgcn_global_load_lds((const unsigned*)((const char*)A + aoff[i] + (size_t)(kt) * 128), (PG8_LAS unsigned*)(MU_SA(buf) + wid * 1024 + i * 8192), 16, 0, 0); } while (0)
; #define MU_B_ISSUE(sb, kt) do { const char* kb_ = Bb + (size_t)(kt) * (64 * (size_t)RB); _Pragma("unroll") for (int j = 0; j < 8; ++j) { const char* p_ = kb_ + (size_t)j * RB; \
;         asm volatile("global_load_dwordx2 %0, %1, off" : "=&v"(sb[j]) : "v"(p_) : "memory"); } } while (0)
; #define MU_B_WAIT(sb, N) asm volatile("s_waitcnt vmcnt(%8)" : "+v"(sb[0]), "+v"(sb[1]), "+v"(sb[2]), "+v"(sb[3]), "+v"(sb[4]), "+v"(sb[5]), "+v"(sb[6]), "+v"(sb[7]) : "n"(N) : "memory")
; #define MU_G_LOAD(ga, kt) do { const PG8_LAS f32x4* gk_ = (const PG8_LAS f32x4*)(lds + GAIN_OFF) + 16 * (kt) + 2 * wid; const f32x4 ga_ = gk_[0], gb_ = gk_[1]; \
;         ga[0] = ga_[0]; ga[1] = ga_[1]; ga[2] = ga_[2]; ga[3] = ga_[3]; ga[4] = gb_[0]; ga[5] = gb_[1]; ga[6] = gb_[2]; ga[7] = gb_[3]; } while (0)
; #define MU_COMPUTE(buf) MU_COMPUTE_N(buf, NMU)
; #define MU_END(last) do { if (last) asm volatile("s_waitcnt vmcnt(0)" ::: "memory"); else asm volatile("s_waitcnt vmcnt(8)" ::: "memory"); \
;         asm volatile("s_waitcnt lgkmcnt(0)" ::: "memory"); __builtin_amdgcn_s_barrier(); asm volatile("" ::: "memory"); } while (0)
; template <int MODE>
; __device__ __forceinline__ void moe_unit(PG8_LAS unsigned char* lds, int e, int cb, int slot0  , int nv  , const bf16_t* A, const int* slot_tok,
;                                          const float* W0, const float* W1, bf16_t* OUT, const float* slot_rs  , const int* slot_dst) {
;     ...
;     for (int t = 0; t < nt; t += 2) {
;         if (t + 2 < nt) MU_B_WAIT(s1, 8); else MU_B_WAIT(s1, 0);
;         MU_G_LOAD(g0, t + 1); MU_B_WRITE(s1, 1, g0); __builtin_amdgcn_sched_barrier(0); MU_GLDS_A(1, t + 1); __builtin_amdgcn_sched_barrier(0);
;         if (t + 3 < nt) { MU_B_ISSUE(s1, t + 3); }
;         MU_COMPUTE(0);
;         MU_END(t + 3 >= nt);
;         if (t + 2 < nt) { MU_B_WAIT(s0, 8); MU_G_LOAD(g0, t + 2); MU_B_WRITE(s0, 0, g0); __builtin_amdgcn_sched_barrier(0); MU_GLDS_A(0, t + 2); __builtin_amdgcn_sched_barrier(0); }
;         if (t + 4 < nt) { MU_B_ISSUE(s0, t + 4); }
;         MU_COMPUTE(1);
;         MU_END(t + 4 >= nt);
;     }
	s_mov_b32 s47, s42
	s_mov_b32 s42, s43
	s_mov_b32 s43, s44
	s_mov_b32 s44, s47
	v_mul_f32_e32 v186, s12, v186
	v_mul_f32_e32 v187, s12, v187
	v_mul_f32_e32 v188, s13, v188
	v_mul_f32_e32 v189, s13, v189
	v_mul_f32_e32 v190, s14, v190
	v_mul_f32_e32 v191, s14, v191
	v_mul_f32_e32 v192, s15, v192
	v_mul_f32_e32 v193, s15, v193
	v_mul_f32_e32 v194, s16, v194
	v_mul_f32_e32 v195, s16, v195
	v_mul_f32_e32 v196, s17, v196
	v_mul_f32_e32 v197, s17, v197
	v_mul_f32_e32 v198, s18, v198
	v_mul_f32_e32 v199, s18, v199
	v_mul_f32_e32 v200, s19, v200
	v_mul_f32_e32 v201, s19, v201
	v_cvt_pk_bf16_f32 v158, v186, v188
	v_cvt_pk_bf16_f32 v159, v190, v192
	v_cvt_pk_bf16_f32 v160, v194, v196
	v_cvt_pk_bf16_f32 v161, v198, v200
	v_cvt_pk_bf16_f32 v162, v187, v189
	v_cvt_pk_bf16_f32 v163, v191, v193
	v_cvt_pk_bf16_f32 v164, v195, v197
	v_cvt_pk_bf16_f32 v165, v199, v201
	ds_write_b128 v1, v[158:161] offset:0
	ds_write_b128 v1, v[162:165] offset:128
	v_add_u32_e32 v91, s42, v135
	v_add_u32_e32 v93, s42, v137
	ds_read_b128 v[238:241], v139 offset:19456
	ds_read_b128 v[242:245], v139 offset:21504
	ds_read_b128 v[246:249], v139 offset:23552
	ds_read_b128 v[250:253], v139 offset:25600
	ds_read_b128 v[218:221], v91 offset:0
	ds_read_b128 v[222:225], v91 offset:2048
	ds_read_b128 v[226:229], v91 offset:4096
	ds_read_b128 v[230:233], v91 offset:6144
	ds_read_b128 v[234:237], v91 offset:8192
	s_add_i32 s47, s44, s6
	s_add_u32 s30, s30, 0x80
	s_addc_u32 s31, s31, 0
	s_waitcnt lgkmcnt(0)
	v_mfma_f32_16x16x32_bf16 v[78:81], v[238:241], v[218:221], v[78:81]
	v_mfma_f32_16x16x32_bf16 v[74:77], v[242:245], v[218:221], v[74:77]
	v_mfma_f32_16x16x32_bf16 v[70:73], v[246:249], v[218:221], v[70:73]
	v_mfma_f32_16x16x32_bf16 v[66:69], v[250:253], v[218:221], v[66:69]
	ds_read_b128 v[218:221], v93 offset:0
	ds_read_b128 v[142:145], v141 offset:19456
	s_mov_b32 m0, s47
	s_nop 0
	global_load_lds_dwordx4 v86, s[30:31]
	v_mfma_f32_16x16x32_bf16 v[62:65], v[238:241], v[222:225], v[62:65]
	v_mfma_f32_16x16x32_bf16 v[58:61], v[242:245], v[222:225], v[58:61]
	v_mfma_f32_16x16x32_bf16 v[54:57], v[246:249], v[222:225], v[54:57]
	v_mfma_f32_16x16x32_bf16 v[50:53], v[250:253], v[222:225], v[50:53]
	ds_read_b128 v[222:225], v93 offset:2048
	ds_read_b128 v[146:149], v141 offset:21504
	s_add_i32 m0, s47, 0x2000
	s_nop 0
	global_load_lds_dwordx4 v134, s[30:31]
	v_mfma_f32_16x16x32_bf16 v[46:49], v[238:241], v[226:229], v[46:49]
	v_mfma_f32_16x16x32_bf16 v[42:45], v[242:245], v[226:229], v[42:45]
	v_mfma_f32_16x16x32_bf16 v[38:41], v[246:249], v[226:229], v[38:41]
	v_mfma_f32_16x16x32_bf16 v[34:37], v[250:253], v[226:229], v[34:37]
	ds_read_b128 v[226:229], v93 offset:4096
	ds_read_b128 v[150:153], v141 offset:23552
	s_add_i32 m0, s47, 0x4000
	s_nop 0
	global_load_lds_dwordx4 v136, s[30:31]
	v_mfma_f32_16x16x32_bf16 v[18:21], v[238:241], v[230:233], v[18:21]
	v_mfma_f32_16x16x32_bf16 v[22:25], v[242:245], v[230:233], v[22:25]
	v_mfma_f32_16x16x32_bf16 v[26:29], v[246:249], v[230:233], v[26:29]
	v_mfma_f32_16x16x32_bf16 v[30:33], v[250:253], v[230:233], v[30:33]
	ds_read_b128 v[230:233], v93 offset:6144
	ds_read_b128 v[154:157], v141 offset:25600
	s_add_i32 m0, s47, 0x6000
	s_nop 0
	global_load_lds_dwordx4 v138, s[30:31]
	v_mfma_f32_16x16x32_bf16 v[2:5], v[238:241], v[234:237], v[2:5]
	v_mfma_f32_16x16x32_bf16 v[6:9], v[242:245], v[234:237], v[6:9]
	v_mfma_f32_16x16x32_bf16 v[10:13], v[246:249], v[234:237], v[10:13]
	v_mfma_f32_16x16x32_bf16 v[14:17], v[250:253], v[234:237], v[14:17]
	ds_read_b128 v[234:237], v93 offset:8192
	s_add_i32 m0, s47, 0x8000
	s_nop 0
	global_load_lds_dwordx4 v140, s[30:31]
	s_waitcnt lgkmcnt(0)
	s_load_dwordx8 s[20:27], s[28:29], 0x0
	s_add_u32 s28, s28, 0x100
	s_addc_u32 s29, s29, 0
	v_mfma_f32_16x16x32_bf16 v[78:81], v[142:145], v[218:221], v[78:81]
	v_mfma_f32_16x16x32_bf16 v[74:77], v[146:149], v[218:221], v[74:77]
	v_mfma_f32_16x16x32_bf16 v[70:73], v[150:153], v[218:221], v[70:73]
	v_mfma_f32_16x16x32_bf16 v[66:69], v[154:157], v[218:221], v[66:69]
	v_lshl_add_u64 v[132:133], v[132:133], 0, s[40:41]
	global_load_dwordx2 v[186:187], v[132:133], off
	global_load_dwordx2 v[188:189], v[132:133], off offset:2048
	v_mfma_f32_16x16x32_bf16 v[62:65], v[142:145], v[222:225], v[62:65]
	v_mfma_f32_16x16x32_bf16 v[58:61], v[146:149], v[222:225], v[58:61]
	v_mfma_f32_16x16x32_bf16 v[54:57], v[150:153], v[222:225], v[54:57]
	v_mfma_f32_16x16x32_bf16 v[50:53], v[154:157], v[222:225], v[50:53]
	v_lshl_add_u64 v[166:167], v[132:133], 0, s[34:35]
	global_load_dwordx2 v[190:191], v[166:167], off
	global_load_dwordx2 v[192:193], v[166:167], off offset:2048
	v_mfma_f32_16x16x32_bf16 v[46:49], v[142:145], v[226:229], v[46:49]
	v_mfma_f32_16x16x32_bf16 v[42:45], v[146:149], v[226:229], v[42:45]
	v_mfma_f32_16x16x32_bf16 v[38:41], v[150:153], v[226:229], v[38:41]
	v_mfma_f32_16x16x32_bf16 v[34:37], v[154:157], v[226:229], v[34:37]
	v_lshl_add_u64 v[166:167], v[132:133], 0, s[36:37]
	global_load_dwordx2 v[194:195], v[166:167], off
	global_load_dwordx2 v[196:197], v[166:167], off offset:2048
	v_mfma_f32_16x16x32_bf16 v[18:21], v[142:145], v[230:233], v[18:21]
	v_mfma_f32_16x16x32_bf16 v[22:25], v[146:149], v[230:233], v[22:25]
	v_mfma_f32_16x16x32_bf16 v[26:29], v[150:153], v[230:233], v[26:29]
	v_mfma_f32_16x16x32_bf16 v[30:33], v[154:157], v[230:233], v[30:33]
	v_lshl_add_u64 v[166:167], v[132:133], 0, s[38:39]
	global_load_dwordx2 v[198:199], v[166:167], off
	global_load_dwordx2 v[200:201], v[166:167], off offset:2048
	v_mfma_f32_16x16x32_bf16 v[2:5], v[142:145], v[234:237], v[2:5]
	v_mfma_f32_16x16x32_bf16 v[6:9], v[146:149], v[234:237], v[6:9]
	v_mfma_f32_16x16x32_bf16 v[10:13], v[150:153], v[234:237], v[10:13]
	v_mfma_f32_16x16x32_bf16 v[14:17], v[154:157], v[234:237], v[14:17]
	s_waitcnt vmcnt(21)
	s_waitcnt lgkmcnt(0)
	s_barrier
; #define MU_GLDS_A(buf, kt) do { _Pragma("unroll") for (int i = 0; i < NMU; ++i) \
;         __builtin_amdgcn_global_load_lds((const unsigned*)((const char*)A + aoff[i] + (size_t)(kt) * 128), (PG8_LAS unsigned*)(MU_SA(buf) + wid * 1024 + i * 8192), 16, 0, 0); } while (0)
; #define MU_B_ISSUE(sb, kt) do { const char* kb_ = Bb + (size_t)(kt) * (64 * (size_t)RB); _Pragma("unroll") for (int j = 0; j < 8; ++j) { const char* p_ = kb_ + (size_t)j * RB; \
;         asm volatile("global_load_dwordx2 %0, %1, off" : "=&v"(sb[j]) : "v"(p_) : "memory"); } } while (0)
; #define MU_B_WAIT(sb, N) asm volatile("s_waitcnt vmcnt(%8)" : "+v"(sb[0]), "+v"(sb[1]), "+v"(sb[2]), "+v"(sb[3]), "+v"(sb[4]), "+v"(sb[5]), "+v"(sb[6]), "+v"(sb[7]) : "n"(N) : "memory")
; #define MU_G_LOAD(ga, kt) do { const PG8_LAS f32x4* gk_ = (const PG8_LAS f32x4*)(lds + GAIN_OFF) + 16 * (kt) + 2 * wid; const f32x4 ga_ = gk_[0], gb_ = gk_[1]; \
;         ga[0] = ga_[0]; ga[1] = ga_[1]; ga[2] = ga_[2]; ga[3] = ga_[3]; ga[4] = gb_[0]; ga[5] = gb_[1]; ga[6] = gb_[2]; ga[7] = gb_[3]; } while (0)
; #define MU_COMPUTE(buf) MU_COMPUTE_N(buf, NMU)
; #define MU_END(last) do { if (last) asm volatile("s_waitcnt vmcnt(0)" ::: "memory"); else asm volatile("s_waitcnt vmcnt(8)" ::: "memory"); \
;         asm volatile("s_waitcnt lgkmcnt(0)" ::: "memory"); __builtin_amdgcn_s_barrier(); asm volatile("" ::: "memory"); } while (0)
; template <int MODE>
; __device__ __forceinline__ void moe_unit(PG8_LAS unsigned char* lds, int e, int cb, int slot0  , int nv  , const bf16_t* A, const int* slot_tok,
;                                          const float* W0, const float* W1, bf16_t* OUT, const float* slot_rs  , const int* slot_dst) {
;     ...
;     for (int t = 0; t < nt; t += 2) {
;         if (t + 2 < nt) MU_B_WAIT(s1, 8); else MU_B_WAIT(s1, 0);
;         MU_G_LOAD(g0, t + 1); MU_B_WRITE(s1, 1, g0); __builtin_amdgcn_sched_barrier(0); MU_GLDS_A(1, t + 1); __builtin_amdgcn_sched_barrier(0);
;         if (t + 3 < nt) { MU_B_ISSUE(s1, t + 3); }
;         MU_COMPUTE(0);
;         MU_END(t + 3 >= nt);
;         if (t + 2 < nt) { MU_B_WAIT(s0, 8); MU_G_LOAD(g0, t + 2); MU_B_WRITE(s0, 0, g0); __builtin_amdgcn_sched_barrier(0); MU_GLDS_A(0, t + 2); __builtin_amdgcn_sched_barrier(0); }
;         if (t + 4 < nt) { MU_B_ISSUE(s0, t + 4); }
;         MU_COMPUTE(1);
;         MU_END(t + 4 >= nt);
;     }
	s_mov_b32 s47, s42
	s_mov_b32 s42, s43
	s_mov_b32 s43, s44
	s_mov_b32 s44, s47
	v_mul_f32_e32 v202, s20, v202
	v_mul_f32_e32 v203, s20, v203
	v_mul_f32_e32 v204, s21, v204
	v_mul_f32_e32 v205, s21, v205
	v_mul_f32_e32 v206, s22, v206
	v_mul_f32_e32 v207, s22, v207
	v_mul_f32_e32 v208, s23, v208
	v_mul_f32_e32 v209, s23, v209
	v_mul_f32_e32 v210, s24, v210
	v_mul_f32_e32 v211, s24, v211
	v_mul_f32_e32 v212, s25, v212
	v_mul_f32_e32 v213, s25, v213
	v_mul_f32_e32 v214, s26, v214
	v_mul_f32_e32 v215, s26, v215
	v_mul_f32_e32 v216, s27, v216
	v_mul_f32_e32 v217, s27, v217
	v_cvt_pk_bf16_f32 v158, v202, v204
	v_cvt_pk_bf16_f32 v159, v206, v208
	v_cvt_pk_bf16_f32 v160, v210, v212
	v_cvt_pk_bf16_f32 v161, v214, v216
	v_cvt_pk_bf16_f32 v162, v203, v205
	v_cvt_pk_bf16_f32 v163, v207, v209
	v_cvt_pk_bf16_f32 v164, v211, v213
	v_cvt_pk_bf16_f32 v165, v215, v217
	ds_write_b128 v1, v[158:161] offset:19456
	ds_write_b128 v1, v[162:165] offset:19584
	v_add_u32_e32 v91, s42, v135
	v_add_u32_e32 v93, s42, v137
	ds_read_b128 v[238:241], v139 offset:0
	ds_read_b128 v[242:245], v139 offset:2048
	ds_read_b128 v[246:249], v139 offset:4096
	ds_read_b128 v[250:253], v139 offset:6144
	ds_read_b128 v[218:221], v91 offset:0
	ds_read_b128 v[222:225], v91 offset:2048
	ds_read_b128 v[226:229], v91 offset:4096
	ds_read_b128 v[230:233], v91 offset:6144
	ds_read_b128 v[234:237], v91 offset:8192
	s_add_i32 s47, s44, s6
	s_add_u32 s30, s30, 0x80
	s_addc_u32 s31, s31, 0
	s_waitcnt lgkmcnt(0)
	v_mfma_f32_16x16x32_bf16 v[78:81], v[238:241], v[218:221], v[78:81]
	v_mfma_f32_16x16x32_bf16 v[74:77], v[242:245], v[218:221], v[74:77]
	v_mfma_f32_16x16x32_bf16 v[70:73], v[246:249], v[218:221], v[70:73]
	v_mfma_f32_16x16x32_bf16 v[66:69], v[250:253], v[218:221], v[66:69]
	ds_read_b128 v[218:221], v93 offset:0
	ds_read_b128 v[142:145], v141 offset:0
	s_mov_b32 m0, s47
	s_nop 0
	global_load_lds_dwordx4 v86, s[30:31]
	v_mfma_f32_16x16x32_bf16 v[62:65], v[238:241], v[222:225], v[62:65]
	v_mfma_f32_16x16x32_bf16 v[58:61], v[242:245], v[222:225], v[58:61]
	v_mfma_f32_16x16x32_bf16 v[54:57], v[246:249], v[222:225], v[54:57]
	v_mfma_f32_16x16x32_bf16 v[50:53], v[250:253], v[222:225], v[50:53]
	ds_read_b128 v[222:225], v93 offset:2048
	ds_read_b128 v[146:149], v141 offset:2048
	s_add_i32 m0, s47, 0x2000
	s_nop 0
	global_load_lds_dwordx4 v134, s[30:31]
	v_mfma_f32_16x16x32_bf16 v[46:49], v[238:241], v[226:229], v[46:49]
	v_mfma_f32_16x16x32_bf16 v[42:45], v[242:245], v[226:229], v[42:45]
	v_mfma_f32_16x16x32_bf16 v[38:41], v[246:249], v[226:229], v[38:41]
	v_mfma_f32_16x16x32_bf16 v[34:37], v[250:253], v[226:229], v[34:37]
	ds_read_b128 v[226:229], v93 offset:4096
	ds_read_b128 v[150:153], v141 offset:4096
	s_add_i32 m0, s47, 0x4000
	s_nop 0
	global_load_lds_dwordx4 v136, s[30:31]
	v_mfma_f32_16x16x32_bf16 v[18:21], v[238:241], v[230:233], v[18:21]
	v_mfma_f32_16x16x32_bf16 v[22:25], v[242:245], v[230:233], v[22:25]
	v_mfma_f32_16x16x32_bf16 v[26:29], v[246:249], v[230:233], v[26:29]
	v_mfma_f32_16x16x32_bf16 v[30:33], v[250:253], v[230:233], v[30:33]
	ds_read_b128 v[230:233], v93 offset:6144
	ds_read_b128 v[154:157], v141 offset:6144
	s_add_i32 m0, s47, 0x6000
	s_nop 0
	global_load_lds_dwordx4 v138, s[30:31]
	v_mfma_f32_16x16x32_bf16 v[2:5], v[238:241], v[234:237], v[2:5]
	v_mfma_f32_16x16x32_bf16 v[6:9], v[242:245], v[234:237], v[6:9]
	v_mfma_f32_16x16x32_bf16 v[10:13], v[246:249], v[234:237], v[10:13]
	v_mfma_f32_16x16x32_bf16 v[14:17], v[250:253], v[234:237], v[14:17]
	ds_read_b128 v[234:237], v93 offset:8192
	s_add_i32 m0, s47, 0x8000
	s_nop 0
	global_load_lds_dwordx4 v140, s[30:31]
	s_waitcnt lgkmcnt(0)
	s_load_dwordx8 s[12:19], s[28:29], 0x0
	s_add_u32 s28, s28, 0x100
	s_addc_u32 s29, s29, 0
	v_mfma_f32_16x16x32_bf16 v[78:81], v[142:145], v[218:221], v[78:81]
	v_mfma_f32_16x16x32_bf16 v[74:77], v[146:149], v[218:221], v[74:77]
	v_mfma_f32_16x16x32_bf16 v[70:73], v[150:153], v[218:221], v[70:73]
	v_mfma_f32_16x16x32_bf16 v[66:69], v[154:157], v[218:221], v[66:69]
	v_lshl_add_u64 v[132:133], v[132:133], 0, s[40:41]
	global_load_dwordx2 v[202:203], v[132:133], off
	global_load_dwordx2 v[204:205], v[132:133], off offset:2048
	v_mfma_f32_16x16x32_bf16 v[62:65], v[142:145], v[222:225], v[62:65]
	v_mfma_f32_16x16x32_bf16 v[58:61], v[146:149], v[222:225], v[58:61]
	v_mfma_f32_16x16x32_bf16 v[54:57], v[150:153], v[222:225], v[54:57]
	v_mfma_f32_16x16x32_bf16 v[50:53], v[154:157], v[222:225], v[50:53]
	v_lshl_add_u64 v[166:167], v[132:133], 0, s[34:35]
	global_load_dwordx2 v[206:207], v[166:167], off
	global_load_dwordx2 v[208:209], v[166:167], off offset:2048
	v_mfma_f32_16x16x32_bf16 v[46:49], v[142:145], v[226:229], v[46:49]
	v_mfma_f32_16x16x32_bf16 v[42:45], v[146:149], v[226:229], v[42:45]
	v_mfma_f32_16x16x32_bf16 v[38:41], v[150:153], v[226:229], v[38:41]
	v_mfma_f32_16x16x32_bf16 v[34:37], v[154:157], v[226:229], v[34:37]
	v_lshl_add_u64 v[166:167], v[132:133], 0, s[36:37]
	global_load_dwordx2 v[210:211], v[166:167], off
	global_load_dwordx2 v[212:213], v[166:167], off offset:2048
	v_mfma_f32_16x16x32_bf16 v[18:21], v[142:145], v[230:233], v[18:21]
	v_mfma_f32_16x16x32_bf16 v[22:25], v[146:149], v[230:233], v[22:25]
	v_mfma_f32_16x16x32_bf16 v[26:29], v[150:153], v[230:233], v[26:29]
	v_mfma_f32_16x16x32_bf16 v[30:33], v[154:157], v[230:233], v[30:33]
	v_lshl_add_u64 v[166:167], v[132:133], 0, s[38:39]
	global_load_dwordx2 v[214:215], v[166:167], off
	global_load_dwordx2 v[216:217], v[166:167], off offset:2048
	v_mfma_f32_16x16x32_bf16 v[2:5], v[142:145], v[234:237], v[2:5]
	v_mfma_f32_16x16x32_bf16 v[6:9], v[146:149], v[234:237], v[6:9]
	v_mfma_f32_16x16x32_bf16 v[10:13], v[150:153], v[234:237], v[10:13]
	v_mfma_f32_16x16x32_bf16 v[14:17], v[154:157], v[234:237], v[14:17]
	s_waitcnt vmcnt(21)
	s_waitcnt lgkmcnt(0)
	s_barrier
; #define MU_GLDS_A(buf, kt) do { _Pragma("unroll") for (int i = 0; i < NMU; ++i) \
;         __builtin_amdgcn_global_load_lds((const unsigned*)((const char*)A + aoff[i] + (size_t)(kt) * 128), (PG8_LAS unsigned*)(MU_SA(buf) + wid * 1024 + i * 8192), 16, 0, 0); } while (0)
; #define MU_B_ISSUE(sb, kt) do { const char* kb_ = Bb + (size_t)(kt) * (64 * (size_t)RB); _Pragma("unroll") for (int j = 0; j < 8; ++j) { const char* p_ = kb_ + (size_t)j * RB; \
;         asm volatile("global_load_dwordx2 %0, %1, off" : "=&v"(sb[j]) : "v"(p_) : "memory"); } } while (0)
; #define MU_B_WAIT(sb, N) asm volatile("s_waitcnt vmcnt(%8)" : "+v"(sb[0]), "+v"(sb[1]), "+v"(sb[2]), "+v"(sb[3]), "+v"(sb[4]), "+v"(sb[5]), "+v"(sb[6]), "+v"(sb[7]) : "n"(N) : "memory")
; #define MU_G_LOAD(ga, kt) do { const PG8_LAS f32x4* gk_ = (const PG8_LAS f32x4*)(lds + GAIN_OFF) + 16 * (kt) + 2 * wid; const f32x4 ga_ = gk_[0], gb_ = gk_[1]; \
;         ga[0] = ga_[0]; ga[1] = ga_[1]; ga[2] = ga_[2]; ga[3] = ga_[3]; ga[4] = gb_[0]; ga[5] = gb_[1]; ga[6] = gb_[2]; ga[7] = gb_[3]; } while (0)
; #define MU_COMPUTE(buf) MU_COMPUTE_N(buf, NMU)
; #define MU_END(last) do { if (last) asm volatile("s_waitcnt vmcnt(0)" ::: "memory"); else asm volatile("s_waitcnt vmcnt(8)" ::: "memory"); \
;         asm volatile("s_waitcnt lgkmcnt(0)" ::: "memory"); __builtin_amdgcn_s_barrier(); asm volatile("" ::: "memory"); } while (0)
; template <int MODE>
; __device__ __forceinline__ void moe_unit(PG8_LAS unsigned char* lds, int e, int cb, int slot0  , int nv  , const bf16_t* A, const int* slot_tok,
;                                          const float* W0, const float* W1, bf16_t* OUT, const float* slot_rs  , const int* slot_dst) {
;     ...
;     for (int t = 0; t < nt; t += 2) {
;         if (t + 2 < nt) MU_B_WAIT(s1, 8); else MU_B_WAIT(s1, 0);
;         MU_G_LOAD(g0, t + 1); MU_B_WRITE(s1, 1, g0); __builtin_amdgcn_sched_barrier(0); MU_GLDS_A(1, t + 1); __builtin_amdgcn_sched_barrier(0);
;         if (t + 3 < nt) { MU_B_ISSUE(s1, t + 3); }
;         MU_COMPUTE(0);
;         MU_END(t + 3 >= nt);
;         if (t + 2 < nt) { MU_B_WAIT(s0, 8); MU_G_LOAD(g0, t + 2); MU_B_WRITE(s0, 0, g0); __builtin_amdgcn_sched_barrier(0); MU_GLDS_A(0, t + 2); __builtin_amdgcn_sched_barrier(0); }
;         if (t + 4 < nt) { MU_B_ISSUE(s0, t + 4); }
;         MU_COMPUTE(1);
;         MU_END(t + 4 >= nt);
;     }
	s_mov_b32 s47, s42
	s_mov_b32 s42, s43
	s_mov_b32 s43, s44
	s_mov_b32 s44, s47
	v_mul_f32_e32 v98, s12, v98
	v_mul_f32_e32 v99, s12, v99
	v_mul_f32_e32 v100, s13, v100
	v_mul_f32_e32 v101, s13, v101
	v_mul_f32_e32 v102, s14, v102
	v_mul_f32_e32 v103, s14, v103
	v_mul_f32_e32 v104, s15, v104
	v_mul_f32_e32 v105, s15, v105
	v_mul_f32_e32 v106, s16, v106
	v_mul_f32_e32 v107, s16, v107
	v_mul_f32_e32 v108, s17, v108
	v_mul_f32_e32 v109, s17, v109
	v_mul_f32_e32 v110, s18, v110
	v_mul_f32_e32 v111, s18, v111
	v_mul_f32_e32 v112, s19, v112
	v_mul_f32_e32 v113, s19, v113
	v_cvt_pk_bf16_f32 v158, v98, v100
	v_cvt_pk_bf16_f32 v159, v102, v104
	v_cvt_pk_bf16_f32 v160, v106, v108
	v_cvt_pk_bf16_f32 v161, v110, v112
	v_cvt_pk_bf16_f32 v162, v99, v101
	v_cvt_pk_bf16_f32 v163, v103, v105
	v_cvt_pk_bf16_f32 v164, v107, v109
	v_cvt_pk_bf16_f32 v165, v111, v113
	ds_write_b128 v1, v[158:161] offset:0
	ds_write_b128 v1, v[162:165] offset:128
	v_add_u32_e32 v91, s42, v135
	v_add_u32_e32 v93, s42, v137
	ds_read_b128 v[238:241], v139 offset:19456
	ds_read_b128 v[242:245], v139 offset:21504
	ds_read_b128 v[246:249], v139 offset:23552
	ds_read_b128 v[250:253], v139 offset:25600
	ds_read_b128 v[218:221], v91 offset:0
	ds_read_b128 v[222:225], v91 offset:2048
	ds_read_b128 v[226:229], v91 offset:4096
	ds_read_b128 v[230:233], v91 offset:6144
	ds_read_b128 v[234:237], v91 offset:8192
	s_add_i32 s47, s44, s6
	s_add_u32 s30, s30, 0x80
	s_addc_u32 s31, s31, 0
	s_waitcnt lgkmcnt(0)
	v_mfma_f32_16x16x32_bf16 v[78:81], v[238:241], v[218:221], v[78:81]
	v_mfma_f32_16x16x32_bf16 v[74:77], v[242:245], v[218:221], v[74:77]
	v_mfma_f32_16x16x32_bf16 v[70:73], v[246:249], v[218:221], v[70:73]
	v_mfma_f32_16x16x32_bf16 v[66:69], v[250:253], v[218:221], v[66:69]
	ds_read_b128 v[218:221], v93 offset:0
	ds_read_b128 v[142:145], v141 offset:19456
	s_mov_b32 m0, s47
	s_nop 0
	global_load_lds_dwordx4 v86, s[30:31]
	v_mfma_f32_16x16x32_bf16 v[62:65], v[238:241], v[222:225], v[62:65]
	v_mfma_f32_16x16x32_bf16 v[58:61], v[242:245], v[222:225], v[58:61]
	v_mfma_f32_16x16x32_bf16 v[54:57], v[246:249], v[222:225], v[54:57]
	v_mfma_f32_16x16x32_bf16 v[50:53], v[250:253], v[222:225], v[50:53]
	ds_read_b128 v[222:225], v93 offset:2048
	ds_read_b128 v[146:149], v141 offset:21504
	s_add_i32 m0, s47, 0x2000
	s_nop 0
	global_load_lds_dwordx4 v134, s[30:31]
	v_mfma_f32_16x16x32_bf16 v[46:49], v[238:241], v[226:229], v[46:49]
	v_mfma_f32_16x16x32_bf16 v[42:45], v[242:245], v[226:229], v[42:45]
	v_mfma_f32_16x16x32_bf16 v[38:41], v[246:249], v[226:229], v[38:41]
	v_mfma_f32_16x16x32_bf16 v[34:37], v[250:253], v[226:229], v[34:37]
	ds_read_b128 v[226:229], v93 offset:4096
	ds_read_b128 v[150:153], v141 offset:23552
	s_add_i32 m0, s47, 0x4000
	s_nop 0
	global_load_lds_dwordx4 v136, s[30:31]
	v_mfma_f32_16x16x32_bf16 v[18:21], v[238:241], v[230:233], v[18:21]
	v_mfma_f32_16x16x32_bf16 v[22:25], v[242:245], v[230:233], v[22:25]
	v_mfma_f32_16x16x32_bf16 v[26:29], v[246:249], v[230:233], v[26:29]
	v_mfma_f32_16x16x32_bf16 v[30:33], v[250:253], v[230:233], v[30:33]
	ds_read_b128 v[230:233], v93 offset:6144
	ds_read_b128 v[154:157], v141 offset:25600
	s_add_i32 m0, s47, 0x6000
	s_nop 0
	global_load_lds_dwordx4 v138, s[30:31]
	v_mfma_f32_16x16x32_bf16 v[2:5], v[238:241], v[234:237], v[2:5]
	v_mfma_f32_16x16x32_bf16 v[6:9], v[242:245], v[234:237], v[6:9]
	v_mfma_f32_16x16x32_bf16 v[10:13], v[246:249], v[234:237], v[10:13]
	v_mfma_f32_16x16x32_bf16 v[14:17], v[250:253], v[234:237], v[14:17]
	ds_read_b128 v[234:237], v93 offset:8192
	s_add_i32 m0, s47, 0x8000
	s_nop 0
	global_load_lds_dwordx4 v140, s[30:31]
	s_waitcnt lgkmcnt(0)
	s_load_dwordx8 s[20:27], s[28:29], 0x0
	s_add_u32 s28, s28, 0x100
	s_addc_u32 s29, s29, 0
	v_mfma_f32_16x16x32_bf16 v[78:81], v[142:145], v[218:221], v[78:81]
	v_mfma_f32_16x16x32_bf16 v[74:77], v[146:149], v[218:221], v[74:77]
	v_mfma_f32_16x16x32_bf16 v[70:73], v[150:153], v[218:221], v[70:73]
	v_mfma_f32_16x16x32_bf16 v[66:69], v[154:157], v[218:221], v[66:69]
	v_lshl_add_u64 v[132:133], v[132:133], 0, s[40:41]
	global_load_dwordx2 v[98:99], v[132:133], off
	global_load_dwordx2 v[100:101], v[132:133], off offset:2048
	v_mfma_f32_16x16x32_bf16 v[62:65], v[142:145], v[222:225], v[62:65]
	v_mfma_f32_16x16x32_bf16 v[58:61], v[146:149], v[222:225], v[58:61]
	v_mfma_f32_16x16x32_bf16 v[54:57], v[150:153], v[222:225], v[54:57]
	v_mfma_f32_16x16x32_bf16 v[50:53], v[154:157], v[222:225], v[50:53]
	v_lshl_add_u64 v[166:167], v[132:133], 0, s[34:35]
	global_load_dwordx2 v[102:103], v[166:167], off
	global_load_dwordx2 v[104:105], v[166:167], off offset:2048
	v_mfma_f32_16x16x32_bf16 v[46:49], v[142:145], v[226:229], v[46:49]
	v_mfma_f32_16x16x32_bf16 v[42:45], v[146:149], v[226:229], v[42:45]
	v_mfma_f32_16x16x32_bf16 v[38:41], v[150:153], v[226:229], v[38:41]
	v_mfma_f32_16x16x32_bf16 v[34:37], v[154:157], v[226:229], v[34:37]
	v_lshl_add_u64 v[166:167], v[132:133], 0, s[36:37]
	global_load_dwordx2 v[106:107], v[166:167], off
	global_load_dwordx2 v[108:109], v[166:167], off offset:2048
	v_mfma_f32_16x16x32_bf16 v[18:21], v[142:145], v[230:233], v[18:21]
	v_mfma_f32_16x16x32_bf16 v[22:25], v[146:149], v[230:233], v[22:25]
	v_mfma_f32_16x16x32_bf16 v[26:29], v[150:153], v[230:233], v[26:29]
	v_mfma_f32_16x16x32_bf16 v[30:33], v[154:157], v[230:233], v[30:33]
	v_lshl_add_u64 v[166:167], v[132:133], 0, s[38:39]
	global_load_dwordx2 v[110:111], v[166:167], off
	global_load_dwordx2 v[112:113], v[166:167], off offset:2048
	v_mfma_f32_16x16x32_bf16 v[2:5], v[142:145], v[234:237], v[2:5]
	v_mfma_f32_16x16x32_bf16 v[6:9], v[146:149], v[234:237], v[6:9]
	v_mfma_f32_16x16x32_bf16 v[10:13], v[150:153], v[234:237], v[10:13]
	v_mfma_f32_16x16x32_bf16 v[14:17], v[154:157], v[234:237], v[14:17]
	s_waitcnt vmcnt(21)
	s_waitcnt lgkmcnt(0)
	s_barrier
; #define MU_GLDS_A(buf, kt) do { _Pragma("unroll") for (int i = 0; i < NMU; ++i) \
;         __builtin_amdgcn_global_load_lds((const unsigned*)((const char*)A + aoff[i] + (size_t)(kt) * 128), (PG8_LAS unsigned*)(MU_SA(buf) + wid * 1024 + i * 8192), 16, 0, 0); } while (0)
; #define MU_B_ISSUE(sb, kt) do { const char* kb_ = Bb + (size_t)(kt) * (64 * (size_t)RB); _Pragma("unroll") for (int j = 0; j < 8; ++j) { const char* p_ = kb_ + (size_t)j * RB; \
;         asm volatile("global_load_dwordx2 %0, %1, off" : "=&v"(sb[j]) : "v"(p_) : "memory"); } } while (0)
; #define MU_B_WAIT(sb, N) asm volatile("s_waitcnt vmcnt(%8)" : "+v"(sb[0]), "+v"(sb[1]), "+v"(sb[2]), "+v"(sb[3]), "+v"(sb[4]), "+v"(sb[5]), "+v"(sb[6]), "+v"(sb[7]) : "n"(N) : "memory")
; #define MU_G_LOAD(ga, kt) do { const PG8_LAS f32x4* gk_ = (const PG8_LAS f32x4*)(lds + GAIN_OFF) + 16 * (kt) + 2 * wid; const f32x4 ga_ = gk_[0], gb_ = gk_[1]; \
;         ga[0] = ga_[0]; ga[1] = ga_[1]; ga[2] = ga_[2]; ga[3] = ga_[3]; ga[4] = gb_[0]; ga[5] = gb_[1]; ga[6] = gb_[2]; ga[7] = gb_[3]; } while (0)
; #define MU_COMPUTE(buf) MU_COMPUTE_N(buf, NMU)
; #define MU_END(last) do { if (last) asm volatile("s_waitcnt vmcnt(0)" ::: "memory"); else asm volatile("s_waitcnt vmcnt(8)" ::: "memory"); \
;         asm volatile("s_waitcnt lgkmcnt(0)" ::: "memory"); __builtin_amdgcn_s_barrier(); asm volatile("" ::: "memory"); } while (0)
; template <int MODE>
; __device__ __forceinline__ void moe_unit(PG8_LAS unsigned char* lds, int e, int cb, int slot0  , int nv  , const bf16_t* A, const int* slot_tok,
;                                          const float* W0, const float* W1, bf16_t* OUT, const float* slot_rs  , const int* slot_dst) {
;     ...
;     for (int t = 0; t < nt; t += 2) {
;         if (t + 2 < nt) MU_B_WAIT(s1, 8); else MU_B_WAIT(s1, 0);
;         MU_G_LOAD(g0, t + 1); MU_B_WRITE(s1, 1, g0); __builtin_amdgcn_sched_barrier(0); MU_GLDS_A(1, t + 1); __builtin_amdgcn_sched_barrier(0);
;         if (t + 3 < nt) { MU_B_ISSUE(s1, t + 3); }
;         MU_COMPUTE(0);
;         MU_END(t + 3 >= nt);
;         if (t + 2 < nt) { MU_B_WAIT(s0, 8); MU_G_LOAD(g0, t + 2); MU_B_WRITE(s0, 0, g0); __builtin_amdgcn_sched_barrier(0); MU_GLDS_A(0, t + 2); __builtin_amdgcn_sched_barrier(0); }
;         if (t + 4 < nt) { MU_B_ISSUE(s0, t + 4); }
;         MU_COMPUTE(1);
;         MU_END(t + 4 >= nt);
;     }
	s_mov_b32 s47, s42
	s_mov_b32 s42, s43
	s_mov_b32 s43, s44
	s_mov_b32 s44, s47
	s_sub_u32 s46, s46, 1
	s_cmp_lg_u32 s46, 0
	s_cbranch_scc1 .Lmu_loop_X
	v_mul_f32_e32 v114, s20, v114
	v_mul_f32_e32 v115, s20, v115
	v_mul_f32_e32 v116, s21, v116
	v_mul_f32_e32 v117, s21, v117
	v_mul_f32_e32 v118, s22, v118
	v_mul_f32_e32 v119, s22, v119
	v_mul_f32_e32 v120, s23, v120
	v_mul_f32_e32 v121, s23, v121
	v_mul_f32_e32 v122, s24, v122
	v_mul_f32_e32 v123, s24, v123
	v_mul_f32_e32 v124, s25, v124
	v_mul_f32_e32 v125, s25, v125
	v_mul_f32_e32 v126, s26, v126
	v_mul_f32_e32 v127, s26, v127
	v_mul_f32_e32 v128, s27, v128
	v_mul_f32_e32 v129, s27, v129
	v_cvt_pk_bf16_f32 v158, v114, v116
	v_cvt_pk_bf16_f32 v159, v118, v120
	v_cvt_pk_bf16_f32 v160, v122, v124
	v_cvt_pk_bf16_f32 v161, v126, v128
	v_cvt_pk_bf16_f32 v162, v115, v117
	v_cvt_pk_bf16_f32 v163, v119, v121
	v_cvt_pk_bf16_f32 v164, v123, v125
	v_cvt_pk_bf16_f32 v165, v127, v129
	ds_write_b128 v1, v[158:161] offset:19456
	ds_write_b128 v1, v[162:165] offset:19584
	v_add_u32_e32 v91, s42, v135
	v_add_u32_e32 v93, s42, v137
	ds_read_b128 v[238:241], v139 offset:0
	ds_read_b128 v[242:245], v139 offset:2048
	ds_read_b128 v[246:249], v139 offset:4096
	ds_read_b128 v[250:253], v139 offset:6144
	ds_read_b128 v[218:221], v91 offset:0
	ds_read_b128 v[222:225], v91 offset:2048
	ds_read_b128 v[226:229], v91 offset:4096
	ds_read_b128 v[230:233], v91 offset:6144
	ds_read_b128 v[234:237], v91 offset:8192
	s_add_i32 s47, s44, s6
	s_add_u32 s30, s30, 0x80
	s_addc_u32 s31, s31, 0
	s_waitcnt lgkmcnt(0)
	v_mfma_f32_16x16x32_bf16 v[78:81], v[238:241], v[218:221], v[78:81]
	v_mfma_f32_16x16x32_bf16 v[74:77], v[242:245], v[218:221], v[74:77]
	v_mfma_f32_16x16x32_bf16 v[70:73], v[246:249], v[218:221], v[70:73]
	v_mfma_f32_16x16x32_bf16 v[66:69], v[250:253], v[218:221], v[66:69]
	ds_read_b128 v[218:221], v93 offset:0
	ds_read_b128 v[142:145], v141 offset:0
	s_mov_b32 m0, s47
	s_nop 0
	global_load_lds_dwordx4 v86, s[30:31]
	v_mfma_f32_16x16x32_bf16 v[62:65], v[238:241], v[222:225], v[62:65]
	v_mfma_f32_16x16x32_bf16 v[58:61], v[242:245], v[222:225], v[58:61]
	v_mfma_f32_16x16x32_bf16 v[54:57], v[246:249], v[222:225], v[54:57]
	v_mfma_f32_16x16x32_bf16 v[50:53], v[250:253], v[222:225], v[50:53]
	ds_read_b128 v[222:225], v93 offset:2048
	ds_read_b128 v[146:149], v141 offset:2048
	s_add_i32 m0, s47, 0x2000
	s_nop 0
	global_load_lds_dwordx4 v134, s[30:31]
	v_mfma_f32_16x16x32_bf16 v[46:49], v[238:241], v[226:229], v[46:49]
	v_mfma_f32_16x16x32_bf16 v[42:45], v[242:245], v[226:229], v[42:45]
	v_mfma_f32_16x16x32_bf16 v[38:41], v[246:249], v[226:229], v[38:41]
	v_mfma_f32_16x16x32_bf16 v[34:37], v[250:253], v[226:229], v[34:37]
	ds_read_b128 v[226:229], v93 offset:4096
	ds_read_b128 v[150:153], v141 offset:4096
	s_add_i32 m0, s47, 0x4000
	s_nop 0
	global_load_lds_dwordx4 v136, s[30:31]
	v_mfma_f32_16x16x32_bf16 v[18:21], v[238:241], v[230:233], v[18:21]
	v_mfma_f32_16x16x32_bf16 v[22:25], v[242:245], v[230:233], v[22:25]
	v_mfma_f32_16x16x32_bf16 v[26:29], v[246:249], v[230:233], v[26:29]
	v_mfma_f32_16x16x32_bf16 v[30:33], v[250:253], v[230:233], v[30:33]
	ds_read_b128 v[230:233], v93 offset:6144
	ds_read_b128 v[154:157], v141 offset:6144
	s_add_i32 m0, s47, 0x6000
	s_nop 0
	global_load_lds_dwordx4 v138, s[30:31]
	v_mfma_f32_16x16x32_bf16 v[2:5], v[238:241], v[234:237], v[2:5]
	v_mfma_f32_16x16x32_bf16 v[6:9], v[242:245], v[234:237], v[6:9]
	v_mfma_f32_16x16x32_bf16 v[10:13], v[246:249], v[234:237], v[10:13]
	v_mfma_f32_16x16x32_bf16 v[14:17], v[250:253], v[234:237], v[14:17]
	ds_read_b128 v[234:237], v93 offset:8192
	s_add_i32 m0, s47, 0x8000
	s_nop 0
	global_load_lds_dwordx4 v140, s[30:31]
	s_waitcnt lgkmcnt(0)
	s_load_dwordx8 s[12:19], s[28:29], 0x0
	s_add_u32 s28, s28, 0x100
	s_addc_u32 s29, s29, 0
	v_mfma_f32_16x16x32_bf16 v[78:81], v[142:145], v[218:221], v[78:81]
	v_mfma_f32_16x16x32_bf16 v[74:77], v[146:149], v[218:221], v[74:77]
	v_mfma_f32_16x16x32_bf16 v[70:73], v[150:153], v[218:221], v[70:73]
	v_mfma_f32_16x16x32_bf16 v[66:69], v[154:157], v[218:221], v[66:69]
	v_lshl_add_u64 v[132:133], v[132:133], 0, s[40:41]
	global_load_dwordx2 v[114:115], v[132:133], off
	global_load_dwordx2 v[116:117], v[132:133], off offset:2048
	v_mfma_f32_16x16x32_bf16 v[62:65], v[142:145], v[222:225], v[62:65]
	v_mfma_f32_16x16x32_bf16 v[58:61], v[146:149], v[222:225], v[58:61]
	v_mfma_f32_16x16x32_bf16 v[54:57], v[150:153], v[222:225], v[54:57]
	v_mfma_f32_16x16x32_bf16 v[50:53], v[154:157], v[222:225], v[50:53]
	v_lshl_add_u64 v[166:167], v[132:133], 0, s[34:35]
	global_load_dwordx2 v[118:119], v[166:167], off
	global_load_dwordx2 v[120:121], v[166:167], off offset:2048
	v_mfma_f32_16x16x32_bf16 v[46:49], v[142:145], v[226:229], v[46:49]
	v_mfma_f32_16x16x32_bf16 v[42:45], v[146:149], v[226:229], v[42:45]
	v_mfma_f32_16x16x32_bf16 v[38:41], v[150:153], v[226:229], v[38:41]
	v_mfma_f32_16x16x32_bf16 v[34:37], v[154:157], v[226:229], v[34:37]
	v_lshl_add_u64 v[166:167], v[132:133], 0, s[36:37]
	global_load_dwordx2 v[122:123], v[166:167], off
	global_load_dwordx2 v[124:125], v[166:167], off offset:2048
	v_mfma_f32_16x16x32_bf16 v[18:21], v[142:145], v[230:233], v[18:21]
	v_mfma_f32_16x16x32_bf16 v[22:25], v[146:149], v[230:233], v[22:25]
	v_mfma_f32_16x16x32_bf16 v[26:29], v[150:153], v[230:233], v[26:29]
	v_mfma_f32_16x16x32_bf16 v[30:33], v[154:157], v[230:233], v[30:33]
	v_lshl_add_u64 v[166:167], v[132:133], 0, s[38:39]
	global_load_dwordx2 v[126:127], v[166:167], off
	global_load_dwordx2 v[128:129], v[166:167], off offset:2048
	v_mfma_f32_16x16x32_bf16 v[2:5], v[142:145], v[234:237], v[2:5]
	v_mfma_f32_16x16x32_bf16 v[6:9], v[146:149], v[234:237], v[6:9]
	v_mfma_f32_16x16x32_bf16 v[10:13], v[150:153], v[234:237], v[10:13]
	v_mfma_f32_16x16x32_bf16 v[14:17], v[154:157], v[234:237], v[14:17]
	s_waitcnt vmcnt(21)
	s_waitcnt lgkmcnt(0)
	s_barrier
; #define MU_GLDS_A(buf, kt) do { _Pragma("unroll") for (int i = 0; i < NMU; ++i) \
;         __builtin_amdgcn_global_load_lds((const unsigned*)((const char*)A + aoff[i] + (size_t)(kt) * 128), (PG8_LAS unsigned*)(MU_SA(buf) + wid * 1024 + i * 8192), 16, 0, 0); } while (0)
; #define MU_B_ISSUE(sb, kt) do { const char* kb_ = Bb + (size_t)(kt) * (64 * (size_t)RB); _Pragma("unroll") for (int j = 0; j < 8; ++j) { const char* p_ = kb_ + (size_t)j * RB; \
;         asm volatile("global_load_dwordx2 %0, %1, off" : "=&v"(sb[j]) : "v"(p_) : "memory"); } } while (0)
; #define MU_B_WAIT(sb, N) asm volatile("s_waitcnt vmcnt(%8)" : "+v"(sb[0]), "+v"(sb[1]), "+v"(sb[2]), "+v"(sb[3]), "+v"(sb[4]), "+v"(sb[5]), "+v"(sb[6]), "+v"(sb[7]) : "n"(N) : "memory")
; #define MU_G_LOAD(ga, kt) do { const PG8_LAS f32x4* gk_ = (const PG8_LAS f32x4*)(lds + GAIN_OFF) + 16 * (kt) + 2 * wid; const f32x4 ga_ = gk_[0], gb_ = gk_[1]; \
;         ga[0] = ga_[0]; ga[1] = ga_[1]; ga[2] = ga_[2]; ga[3] = ga_[3]; ga[4] = gb_[0]; ga[5] = gb_[1]; ga[6] = gb_[2]; ga[7] = gb_[3]; } while (0)
; #define MU_COMPUTE(buf) MU_COMPUTE_N(buf, NMU)
; #define MU_END(last) do { if (last) asm volatile("s_waitcnt vmcnt(0)" ::: "memory"); else asm volatile("s_waitcnt vmcnt(8)" ::: "memory"); \
;         asm volatile("s_waitcnt lgkmcnt(0)" ::: "memory"); __builtin_amdgcn_s_barrier(); asm volatile("" ::: "memory"); } while (0)
; template <int MODE>
; __device__ __forceinline__ void moe_unit(PG8_LAS unsigned char* lds, int e, int cb, int slot0  , int nv  , const bf16_t* A, const int* slot_tok,
;                                          const float* W0, const float* W1, bf16_t* OUT, const float* slot_rs  , const int* slot_dst) {
;     ...
;     for (int t = 0; t < nt; t += 2) {
;         if (t + 2 < nt) MU_B_WAIT(s1, 8); else MU_B_WAIT(s1, 0);
;         MU_G_LOAD(g0, t + 1); MU_B_WRITE(s1, 1, g0); __builtin_amdgcn_sched_barrier(0); MU_GLDS_A(1, t + 1); __builtin_amdgcn_sched_barrier(0);
;         if (t + 3 < nt) { MU_B_ISSUE(s1, t + 3); }
;         MU_COMPUTE(0);
;         MU_END(t + 3 >= nt);
;         if (t + 2 < nt) { MU_B_WAIT(s0, 8); MU_G_LOAD(g0, t + 2); MU_B_WRITE(s0, 0, g0); __builtin_amdgcn_sched_barrier(0); MU_GLDS_A(0, t + 2); __builtin_amdgcn_sched_barrier(0); }
;         if (t + 4 < nt) { MU_B_ISSUE(s0, t + 4); }
;         MU_COMPUTE(1);
;         MU_END(t + 4 >= nt);
;     }
	s_mov_b32 s47, s42
	s_mov_b32 s42, s43
	s_mov_b32 s43, s44
	s_mov_b32 s44, s47
	v_mul_f32_e32 v186, s12, v186
	v_mul_f32_e32 v187, s12, v187
	v_mul_f32_e32 v188, s13, v188
	v_mul_f32_e32 v189, s13, v189
	v_mul_f32_e32 v190, s14, v190
	v_mul_f32_e32 v191, s14, v191
	v_mul_f32_e32 v192, s15, v192
	v_mul_f32_e32 v193, s15, v193
	v_mul_f32_e32 v194, s16, v194
	v_mul_f32_e32 v195, s16, v195
	v_mul_f32_e32 v196, s17, v196
	v_mul_f32_e32 v197, s17, v197
	v_mul_f32_e32 v198, s18, v198
	v_mul_f32_e32 v199, s18, v199
	v_mul_f32_e32 v200, s19, v200
	v_mul_f32_e32 v201, s19, v201
	v_cvt_pk_bf16_f32 v158, v186, v188
	v_cvt_pk_bf16_f32 v159, v190, v192
	v_cvt_pk_bf16_f32 v160, v194, v196
	v_cvt_pk_bf16_f32 v161, v198, v200
	v_cvt_pk_bf16_f32 v162, v187, v189
	v_cvt_pk_bf16_f32 v163, v191, v193
	v_cvt_pk_bf16_f32 v164, v195, v197
	v_cvt_pk_bf16_f32 v165, v199, v201
	ds_write_b128 v1, v[158:161] offset:0
	ds_write_b128 v1, v[162:165] offset:128
	v_add_u32_e32 v91, s42, v135
	v_add_u32_e32 v93, s42, v137
	ds_read_b128 v[238:241], v139 offset:19456
	ds_read_b128 v[242:245], v139 offset:21504
	ds_read_b128 v[246:249], v139 offset:23552
	ds_read_b128 v[250:253], v139 offset:25600
	ds_read_b128 v[218:221], v91 offset:0
	ds_read_b128 v[222:225], v91 offset:2048
	ds_read_b128 v[226:229], v91 offset:4096
	ds_read_b128 v[230:233], v91 offset:6144
	ds_read_b128 v[234:237], v91 offset:8192
	s_add_i32 s47, s44, s6
	s_add_u32 s30, s30, 0x80
	s_addc_u32 s31, s31, 0
	s_waitcnt lgkmcnt(0)
	v_mfma_f32_16x16x32_bf16 v[78:81], v[238:241], v[218:221], v[78:81]
	v_mfma_f32_16x16x32_bf16 v[74:77], v[242:245], v[218:221], v[74:77]
	v_mfma_f32_16x16x32_bf16 v[70:73], v[246:249], v[218:221], v[70:73]
	v_mfma_f32_16x16x32_bf16 v[66:69], v[250:253], v[218:221], v[66:69]
	ds_read_b128 v[218:221], v93 offset:0
	ds_read_b128 v[142:145], v141 offset:19456
	s_mov_b32 m0, s47
	s_nop 0
	global_load_lds_dwordx4 v86, s[30:31]
	v_mfma_f32_16x16x32_bf16 v[62:65], v[238:241], v[222:225], v[62:65]
	v_mfma_f32_16x16x32_bf16 v[58:61], v[242:245], v[222:225], v[58:61]
	v_mfma_f32_16x16x32_bf16 v[54:57], v[246:249], v[222:225], v[54:57]
	v_mfma_f32_16x16x32_bf16 v[50:53], v[250:253], v[222:225], v[50:53]
	ds_read_b128 v[222:225], v93 offset:2048
	ds_read_b128 v[146:149], v141 offset:21504
	s_add_i32 m0, s47, 0x2000
	s_nop 0
	global_load_lds_dwordx4 v134, s[30:31]
	v_mfma_f32_16x16x32_bf16 v[46:49], v[238:241], v[226:229], v[46:49]
	v_mfma_f32_16x16x32_bf16 v[42:45], v[242:245], v[226:229], v[42:45]
	v_mfma_f32_16x16x32_bf16 v[38:41], v[246:249], v[226:229], v[38:41]
	v_mfma_f32_16x16x32_bf16 v[34:37], v[250:253], v[226:229], v[34:37]
	ds_read_b128 v[226:229], v93 offset:4096
	ds_read_b128 v[150:153], v141 offset:23552
	s_add_i32 m0, s47, 0x4000
	s_nop 0
	global_load_lds_dwordx4 v136, s[30:31]
	v_mfma_f32_16x16x32_bf16 v[18:21], v[238:241], v[230:233], v[18:21]
	v_mfma_f32_16x16x32_bf16 v[22:25], v[242:245], v[230:233], v[22:25]
	v_mfma_f32_16x16x32_bf16 v[26:29], v[246:249], v[230:233], v[26:29]
	v_mfma_f32_16x16x32_bf16 v[30:33], v[250:253], v[230:233], v[30:33]
	ds_read_b128 v[230:233], v93 offset:6144
	ds_read_b128 v[154:157], v141 offset:25600
	s_add_i32 m0, s47, 0x6000
	s_nop 0
	global_load_lds_dwordx4 v138, s[30:31]
	v_mfma_f32_16x16x32_bf16 v[2:5], v[238:241], v[234:237], v[2:5]
	v_mfma_f32_16x16x32_bf16 v[6:9], v[242:245], v[234:237], v[6:9]
	v_mfma_f32_16x16x32_bf16 v[10:13], v[246:249], v[234:237], v[10:13]
	v_mfma_f32_16x16x32_bf16 v[14:17], v[250:253], v[234:237], v[14:17]
	ds_read_b128 v[234:237], v93 offset:8192
	s_add_i32 m0, s47, 0x8000
	s_nop 0
	global_load_lds_dwordx4 v140, s[30:31]
	s_waitcnt lgkmcnt(0)
	s_load_dwordx8 s[20:27], s[28:29], 0x0
	s_add_u32 s28, s28, 0x100
	s_addc_u32 s29, s29, 0
	v_mfma_f32_16x16x32_bf16 v[78:81], v[142:145], v[218:221], v[78:81]
	v_mfma_f32_16x16x32_bf16 v[74:77], v[146:149], v[218:221], v[74:77]
	v_mfma_f32_16x16x32_bf16 v[70:73], v[150:153], v[218:221], v[70:73]
	v_mfma_f32_16x16x32_bf16 v[66:69], v[154:157], v[218:221], v[66:69]
	v_lshl_add_u64 v[132:133], v[132:133], 0, s[40:41]
	global_load_dwordx2 v[186:187], v[132:133], off
	global_load_dwordx2 v[188:189], v[132:133], off offset:2048
	v_mfma_f32_16x16x32_bf16 v[62:65], v[142:145], v[222:225], v[62:65]
	v_mfma_f32_16x16x32_bf16 v[58:61], v[146:149], v[222:225], v[58:61]
	v_mfma_f32_16x16x32_bf16 v[54:57], v[150:153], v[222:225], v[54:57]
	v_mfma_f32_16x16x32_bf16 v[50:53], v[154:157], v[222:225], v[50:53]
	v_lshl_add_u64 v[166:167], v[132:133], 0, s[34:35]
	global_load_dwordx2 v[190:191], v[166:167], off
	global_load_dwordx2 v[192:193], v[166:167], off offset:2048
	v_mfma_f32_16x16x32_bf16 v[46:49], v[142:145], v[226:229], v[46:49]
	v_mfma_f32_16x16x32_bf16 v[42:45], v[146:149], v[226:229], v[42:45]
	v_mfma_f32_16x16x32_bf16 v[38:41], v[150:153], v[226:229], v[38:41]
	v_mfma_f32_16x16x32_bf16 v[34:37], v[154:157], v[226:229], v[34:37]
	v_lshl_add_u64 v[166:167], v[132:133], 0, s[36:37]
	global_load_dwordx2 v[194:195], v[166:167], off
	global_load_dwordx2 v[196:197], v[166:167], off offset:2048
	v_mfma_f32_16x16x32_bf16 v[18:21], v[142:145], v[230:233], v[18:21]
	v_mfma_f32_16x16x32_bf16 v[22:25], v[146:149], v[230:233], v[22:25]
	v_mfma_f32_16x16x32_bf16 v[26:29], v[150:153], v[230:233], v[26:29]
	v_mfma_f32_16x16x32_bf16 v[30:33], v[154:157], v[230:233], v[30:33]
	v_lshl_add_u64 v[166:167], v[132:133], 0, s[38:39]
	global_load_dwordx2 v[198:199], v[166:167], off
	global_load_dwordx2 v[200:201], v[166:167], off offset:2048
	v_mfma_f32_16x16x32_bf16 v[2:5], v[142:145], v[234:237], v[2:5]
	v_mfma_f32_16x16x32_bf16 v[6:9], v[146:149], v[234:237], v[6:9]
	v_mfma_f32_16x16x32_bf16 v[10:13], v[150:153], v[234:237], v[10:13]
	v_mfma_f32_16x16x32_bf16 v[14:17], v[154:157], v[234:237], v[14:17]
	s_waitcnt vmcnt(21)
	s_waitcnt lgkmcnt(0)
	s_barrier
; #define MU_GLDS_A(buf, kt) do { _Pragma("unroll") for (int i = 0; i < NMU; ++i) \
;         __builtin_amdgcn_global_load_lds((const unsigned*)((const char*)A + aoff[i] + (size_t)(kt) * 128), (PG8_LAS unsigned*)(MU_SA(buf) + wid * 1024 + i * 8192), 16, 0, 0); } while (0)
; #define MU_B_ISSUE(sb, kt) do { const char* kb_ = Bb + (size_t)(kt) * (64 * (size_t)RB); _Pragma("unroll") for (int j = 0; j < 8; ++j) { const char* p_ = kb_ + (size_t)j * RB; \
;         asm volatile("global_load_dwordx2 %0, %1, off" : "=&v"(sb[j]) : "v"(p_) : "memory"); } } while (0)
; #define MU_B_WAIT(sb, N) asm volatile("s_waitcnt vmcnt(%8)" : "+v"(sb[0]), "+v"(sb[1]), "+v"(sb[2]), "+v"(sb[3]), "+v"(sb[4]), "+v"(sb[5]), "+v"(sb[6]), "+v"(sb[7]) : "n"(N) : "memory")
; #define MU_G_LOAD(ga, kt) do { const PG8_LAS f32x4* gk_ = (const PG8_LAS f32x4*)(lds + GAIN_OFF) + 16 * (kt) + 2 * wid; const f32x4 ga_ = gk_[0], gb_ = gk_[1]; \
;         ga[0] = ga_[0]; ga[1] = ga_[1]; ga[2] = ga_[2]; ga[3] = ga_[3]; ga[4] = gb_[0]; ga[5] = gb_[1]; ga[6] = gb_[2]; ga[7] = gb_[3]; } while (0)
; #define MU_COMPUTE(buf) MU_COMPUTE_N(buf, NMU)
; #define MU_END(last) do { if (last) asm volatile("s_waitcnt vmcnt(0)" ::: "memory"); else asm volatile("s_waitcnt vmcnt(8)" ::: "memory"); \
;         asm volatile("s_waitcnt lgkmcnt(0)" ::: "memory"); __builtin_amdgcn_s_barrier(); asm volatile("" ::: "memory"); } while (0)
; template <int MODE>
; __device__ __forceinline__ void moe_unit(PG8_LAS unsigned char* lds, int e, int cb, int slot0  , int nv  , const bf16_t* A, const int* slot_tok,
;                                          const float* W0, const float* W1, bf16_t* OUT, const float* slot_rs  , const int* slot_dst) {
;     ...
;     for (int t = 0; t < nt; t += 2) {
;         if (t + 2 < nt) MU_B_WAIT(s1, 8); else MU_B_WAIT(s1, 0);
;         MU_G_LOAD(g0, t + 1); MU_B_WRITE(s1, 1, g0); __builtin_amdgcn_sched_barrier(0); MU_GLDS_A(1, t + 1); __builtin_amdgcn_sched_barrier(0);
;         if (t + 3 < nt) { MU_B_ISSUE(s1, t + 3); }
;         MU_COMPUTE(0);
;         MU_END(t + 3 >= nt);
;         if (t + 2 < nt) { MU_B_WAIT(s0, 8); MU_G_LOAD(g0, t + 2); MU_B_WRITE(s0, 0, g0); __builtin_amdgcn_sched_barrier(0); MU_GLDS_A(0, t + 2); __builtin_amdgcn_sched_barrier(0); }
;         if (t + 4 < nt) { MU_B_ISSUE(s0, t + 4); }
;         MU_COMPUTE(1);
;         MU_END(t + 4 >= nt);
;     }
	s_mov_b32 s47, s42
	s_mov_b32 s42, s43
	s_mov_b32 s43, s44
	s_mov_b32 s44, s47
	v_mul_f32_e32 v202, s20, v202
	v_mul_f32_e32 v203, s20, v203
	v_mul_f32_e32 v204, s21, v204
	v_mul_f32_e32 v205, s21, v205
	v_mul_f32_e32 v206, s22, v206
	v_mul_f32_e32 v207, s22, v207
	v_mul_f32_e32 v208, s23, v208
	v_mul_f32_e32 v209, s23, v209
	v_mul_f32_e32 v210, s24, v210
	v_mul_f32_e32 v211, s24, v211
	v_mul_f32_e32 v212, s25, v212
	v_mul_f32_e32 v213, s25, v213
	v_mul_f32_e32 v214, s26, v214
	v_mul_f32_e32 v215, s26, v215
	v_mul_f32_e32 v216, s27, v216
	v_mul_f32_e32 v217, s27, v217
	v_cvt_pk_bf16_f32 v158, v202, v204
	v_cvt_pk_bf16_f32 v159, v206, v208
	v_cvt_pk_bf16_f32 v160, v210, v212
	v_cvt_pk_bf16_f32 v161, v214, v216
	v_cvt_pk_bf16_f32 v162, v203, v205
	v_cvt_pk_bf16_f32 v163, v207, v209
	v_cvt_pk_bf16_f32 v164, v211, v213
	v_cvt_pk_bf16_f32 v165, v215, v217
	ds_write_b128 v1, v[158:161] offset:19456
	ds_write_b128 v1, v[162:165] offset:19584
	v_add_u32_e32 v91, s42, v135
	v_add_u32_e32 v93, s42, v137
	ds_read_b128 v[238:241], v139 offset:0
	ds_read_b128 v[242:245], v139 offset:2048
	ds_read_b128 v[246:249], v139 offset:4096
	ds_read_b128 v[250:253], v139 offset:6144
	ds_read_b128 v[218:221], v91 offset:0
	ds_read_b128 v[222:225], v91 offset:2048
	ds_read_b128 v[226:229], v91 offset:4096
	ds_read_b128 v[230:233], v91 offset:6144
	ds_read_b128 v[234:237], v91 offset:8192
	s_add_i32 s47, s44, s6
	s_add_u32 s30, s30, 0x80
	s_addc_u32 s31, s31, 0
	s_waitcnt lgkmcnt(0)
	v_mfma_f32_16x16x32_bf16 v[78:81], v[238:241], v[218:221], v[78:81]
	v_mfma_f32_16x16x32_bf16 v[74:77], v[242:245], v[218:221], v[74:77]
	v_mfma_f32_16x16x32_bf16 v[70:73], v[246:249], v[218:221], v[70:73]
	v_mfma_f32_16x16x32_bf16 v[66:69], v[250:253], v[218:221], v[66:69]
	ds_read_b128 v[218:221], v93 offset:0
	ds_read_b128 v[142:145], v141 offset:0
	s_mov_b32 m0, s47
	s_nop 0
	global_load_lds_dwordx4 v86, s[30:31]
	v_mfma_f32_16x16x32_bf16 v[62:65], v[238:241], v[222:225], v[62:65]
	v_mfma_f32_16x16x32_bf16 v[58:61], v[242:245], v[222:225], v[58:61]
	v_mfma_f32_16x16x32_bf16 v[54:57], v[246:249], v[222:225], v[54:57]
	v_mfma_f32_16x16x32_bf16 v[50:53], v[250:253], v[222:225], v[50:53]
	ds_read_b128 v[222:225], v93 offset:2048
	ds_read_b128 v[146:149], v141 offset:2048
	s_add_i32 m0, s47, 0x2000
	s_nop 0
	global_load_lds_dwordx4 v134, s[30:31]
	v_mfma_f32_16x16x32_bf16 v[46:49], v[238:241], v[226:229], v[46:49]
	v_mfma_f32_16x16x32_bf16 v[42:45], v[242:245], v[226:229], v[42:45]
	v_mfma_f32_16x16x32_bf16 v[38:41], v[246:249], v[226:229], v[38:41]
	v_mfma_f32_16x16x32_bf16 v[34:37], v[250:253], v[226:229], v[34:37]
	ds_read_b128 v[226:229], v93 offset:4096
	ds_read_b128 v[150:153], v141 offset:4096
	s_add_i32 m0, s47, 0x4000
	s_nop 0
	global_load_lds_dwordx4 v136, s[30:31]
	v_mfma_f32_16x16x32_bf16 v[18:21], v[238:241], v[230:233], v[18:21]
	v_mfma_f32_16x16x32_bf16 v[22:25], v[242:245], v[230:233], v[22:25]
	v_mfma_f32_16x16x32_bf16 v[26:29], v[246:249], v[230:233], v[26:29]
	v_mfma_f32_16x16x32_bf16 v[30:33], v[250:253], v[230:233], v[30:33]
	ds_read_b128 v[230:233], v93 offset:6144
	ds_read_b128 v[154:157], v141 offset:6144
	s_add_i32 m0, s47, 0x6000
	s_nop 0
	global_load_lds_dwordx4 v138, s[30:31]
	v_mfma_f32_16x16x32_bf16 v[2:5], v[238:241], v[234:237], v[2:5]
	v_mfma_f32_16x16x32_bf16 v[6:9], v[242:245], v[234:237], v[6:9]
	v_mfma_f32_16x16x32_bf16 v[10:13], v[246:249], v[234:237], v[10:13]
	v_mfma_f32_16x16x32_bf16 v[14:17], v[250:253], v[234:237], v[14:17]
	ds_read_b128 v[234:237], v93 offset:8192
	s_add_i32 m0, s47, 0x8000
	s_nop 0
	global_load_lds_dwordx4 v140, s[30:31]
	s_waitcnt lgkmcnt(0)
	s_load_dwordx8 s[12:19], s[28:29], 0x0
	s_add_u32 s28, s28, 0x100
	s_addc_u32 s29, s29, 0
	v_mfma_f32_16x16x32_bf16 v[78:81], v[142:145], v[218:221], v[78:81]
	v_mfma_f32_16x16x32_bf16 v[74:77], v[146:149], v[218:221], v[74:77]
	v_mfma_f32_16x16x32_bf16 v[70:73], v[150:153], v[218:221], v[70:73]
	v_mfma_f32_16x16x32_bf16 v[66:69], v[154:157], v[218:221], v[66:69]
	v_lshl_add_u64 v[132:133], v[132:133], 0, s[40:41]
	global_load_dwordx2 v[202:203], v[132:133], off
	global_load_dwordx2 v[204:205], v[132:133], off offset:2048
	v_mfma_f32_16x16x32_bf16 v[62:65], v[142:145], v[222:225], v[62:65]
	v_mfma_f32_16x16x32_bf16 v[58:61], v[146:149], v[222:225], v[58:61]
	v_mfma_f32_16x16x32_bf16 v[54:57], v[150:153], v[222:225], v[54:57]
	v_mfma_f32_16x16x32_bf16 v[50:53], v[154:157], v[222:225], v[50:53]
	v_lshl_add_u64 v[166:167], v[132:133], 0, s[34:35]
	global_load_dwordx2 v[206:207], v[166:167], off
	global_load_dwordx2 v[208:209], v[166:167], off offset:2048
	v_mfma_f32_16x16x32_bf16 v[46:49], v[142:145], v[226:229], v[46:49]
	v_mfma_f32_16x16x32_bf16 v[42:45], v[146:149], v[226:229], v[42:45]
	v_mfma_f32_16x16x32_bf16 v[38:41], v[150:153], v[226:229], v[38:41]
	v_mfma_f32_16x16x32_bf16 v[34:37], v[154:157], v[226:229], v[34:37]
	v_lshl_add_u64 v[166:167], v[132:133], 0, s[36:37]
	global_load_dwordx2 v[210:211], v[166:167], off
	global_load_dwordx2 v[212:213], v[166:167], off offset:2048
	v_mfma_f32_16x16x32_bf16 v[18:21], v[142:145], v[230:233], v[18:21]
	v_mfma_f32_16x16x32_bf16 v[22:25], v[146:149], v[230:233], v[22:25]
	v_mfma_f32_16x16x32_bf16 v[26:29], v[150:153], v[230:233], v[26:29]
	v_mfma_f32_16x16x32_bf16 v[30:33], v[154:157], v[230:233], v[30:33]
	v_lshl_add_u64 v[166:167], v[132:133], 0, s[38:39]
	global_load_dwordx2 v[214:215], v[166:167], off
	global_load_dwordx2 v[216:217], v[166:167], off offset:2048
	v_mfma_f32_16x16x32_bf16 v[2:5], v[142:145], v[234:237], v[2:5]
	v_mfma_f32_16x16x32_bf16 v[6:9], v[146:149], v[234:237], v[6:9]
	v_mfma_f32_16x16x32_bf16 v[10:13], v[150:153], v[234:237], v[10:13]
	v_mfma_f32_16x16x32_bf16 v[14:17], v[154:157], v[234:237], v[14:17]
	s_waitcnt vmcnt(21)
	s_waitcnt lgkmcnt(0)
	s_barrier
; #define MU_GLDS_A(buf, kt) do { _Pragma("unroll") for (int i = 0; i < NMU; ++i) \
;         __builtin_amdgcn_global_load_lds((const unsigned*)((const char*)A + aoff[i] + (size_t)(kt) * 128), (PG8_LAS unsigned*)(MU_SA(buf) + wid * 1024 + i * 8192), 16, 0, 0); } while (0)
; #define MU_B_ISSUE(sb, kt) do { const char* kb_ = Bb + (size_t)(kt) * (64 * (size_t)RB); _Pragma("unroll") for (int j = 0; j < 8; ++j) { const char* p_ = kb_ + (size_t)j * RB; \
;         asm volatile("global_load_dwordx2 %0, %1, off" : "=&v"(sb[j]) : "v"(p_) : "memory"); } } while (0)
; #define MU_B_WAIT(sb, N) asm volatile("s_waitcnt vmcnt(%8)" : "+v"(sb[0]), "+v"(sb[1]), "+v"(sb[2]), "+v"(sb[3]), "+v"(sb[4]), "+v"(sb[5]), "+v"(sb[6]), "+v"(sb[7]) : "n"(N) : "memory")
; #define MU_G_LOAD(ga, kt) do { const PG8_LAS f32x4* gk_ = (const PG8_LAS f32x4*)(lds + GAIN_OFF) + 16 * (kt) + 2 * wid; const f32x4 ga_ = gk_[0], gb_ = gk_[1]; \
;         ga[0] = ga_[0]; ga[1] = ga_[1]; ga[2] = ga_[2]; ga[3] = ga_[3]; ga[4] = gb_[0]; ga[5] = gb_[1]; ga[6] = gb_[2]; ga[7] = gb_[3]; } while (0)
; #define MU_COMPUTE(buf) MU_COMPUTE_N(buf, NMU)
; #define MU_END(last) do { if (last) asm volatile("s_waitcnt vmcnt(0)" ::: "memory"); else asm volatile("s_waitcnt vmcnt(8)" ::: "memory"); \
;         asm volatile("s_waitcnt lgkmcnt(0)" ::: "memory"); __builtin_amdgcn_s_barrier(); asm volatile("" ::: "memory"); } while (0)
; template <int MODE>
; __device__ __forceinline__ void moe_unit(PG8_LAS unsigned char* lds, int e, int cb, int slot0  , int nv  , const bf16_t* A, const int* slot_tok,
;                                          const float* W0, const float* W1, bf16_t* OUT, const float* slot_rs  , const int* slot_dst) {
;     ...
;     for (int t = 0; t < nt; t += 2) {
;         if (t + 2 < nt) MU_B_WAIT(s1, 8); else MU_B_WAIT(s1, 0);
;         MU_G_LOAD(g0, t + 1); MU_B_WRITE(s1, 1, g0); __builtin_amdgcn_sched_barrier(0); MU_GLDS_A(1, t + 1); __builtin_amdgcn_sched_barrier(0);
;         if (t + 3 < nt) { MU_B_ISSUE(s1, t + 3); }
;         MU_COMPUTE(0);
;         MU_END(t + 3 >= nt);
;         if (t + 2 < nt) { MU_B_WAIT(s0, 8); MU_G_LOAD(g0, t + 2); MU_B_WRITE(s0, 0, g0); __builtin_amdgcn_sched_barrier(0); MU_GLDS_A(0, t + 2); __builtin_amdgcn_sched_barrier(0); }
;         if (t + 4 < nt) { MU_B_ISSUE(s0, t + 4); }
;         MU_COMPUTE(1);
;         MU_END(t + 4 >= nt);
;     }
	s_mov_b32 s47, s42
	s_mov_b32 s42, s43
	s_mov_b32 s43, s44
	s_mov_b32 s44, s47
	v_mul_f32_e32 v98, s12, v98
	v_mul_f32_e32 v99, s12, v99
	v_mul_f32_e32 v100, s13, v100
	v_mul_f32_e32 v101, s13, v101
	v_mul_f32_e32 v102, s14, v102
	v_mul_f32_e32 v103, s14, v103
	v_mul_f32_e32 v104, s15, v104
	v_mul_f32_e32 v105, s15, v105
	v_mul_f32_e32 v106, s16, v106
	v_mul_f32_e32 v107, s16, v107
	v_mul_f32_e32 v108, s17, v108
	v_mul_f32_e32 v109, s17, v109
	v_mul_f32_e32 v110, s18, v110
	v_mul_f32_e32 v111, s18, v111
	v_mul_f32_e32 v112, s19, v112
	v_mul_f32_e32 v113, s19, v113
	v_cvt_pk_bf16_f32 v158, v98, v100
	v_cvt_pk_bf16_f32 v159, v102, v104
	v_cvt_pk_bf16_f32 v160, v106, v108
	v_cvt_pk_bf16_f32 v161, v110, v112
	v_cvt_pk_bf16_f32 v162, v99, v101
	v_cvt_pk_bf16_f32 v163, v103, v105
	v_cvt_pk_bf16_f32 v164, v107, v109
	v_cvt_pk_bf16_f32 v165, v111, v113
	ds_write_b128 v1, v[158:161] offset:0
	ds_write_b128 v1, v[162:165] offset:128
	v_add_u32_e32 v91, s42, v135
	v_add_u32_e32 v93, s42, v137
	ds_read_b128 v[238:241], v139 offset:19456
	ds_read_b128 v[242:245], v139 offset:21504
	ds_read_b128 v[246:249], v139 offset:23552
	ds_read_b128 v[250:253], v139 offset:25600
	ds_read_b128 v[218:221], v91 offset:0
	ds_read_b128 v[222:225], v91 offset:2048
	ds_read_b128 v[226:229], v91 offset:4096
	ds_read_b128 v[230:233], v91 offset:6144
	ds_read_b128 v[234:237], v91 offset:8192
	s_add_i32 s47, s44, s6
	s_add_u32 s30, s30, 0x80
	s_addc_u32 s31, s31, 0
	s_waitcnt lgkmcnt(0)
	v_mfma_f32_16x16x32_bf16 v[78:81], v[238:241], v[218:221], v[78:81]
	v_mfma_f32_16x16x32_bf16 v[74:77], v[242:245], v[218:221], v[74:77]
	v_mfma_f32_16x16x32_bf16 v[70:73], v[246:249], v[218:221], v[70:73]
	v_mfma_f32_16x16x32_bf16 v[66:69], v[250:253], v[218:221], v[66:69]
	ds_read_b128 v[218:221], v93 offset:0
	ds_read_b128 v[142:145], v141 offset:19456
	s_mov_b32 m0, s47
	s_nop 0
	global_load_lds_dwordx4 v86, s[30:31]
	v_mfma_f32_16x16x32_bf16 v[62:65], v[238:241], v[222:225], v[62:65]
	v_mfma_f32_16x16x32_bf16 v[58:61], v[242:245], v[222:225], v[58:61]
	v_mfma_f32_16x16x32_bf16 v[54:57], v[246:249], v[222:225], v[54:57]
	v_mfma_f32_16x16x32_bf16 v[50:53], v[250:253], v[222:225], v[50:53]
	ds_read_b128 v[222:225], v93 offset:2048
	ds_read_b128 v[146:149], v141 offset:21504
	s_add_i32 m0, s47, 0x2000
	s_nop 0
	global_load_lds_dwordx4 v134, s[30:31]
	v_mfma_f32_16x16x32_bf16 v[46:49], v[238:241], v[226:229], v[46:49]
	v_mfma_f32_16x16x32_bf16 v[42:45], v[242:245], v[226:229], v[42:45]
	v_mfma_f32_16x16x32_bf16 v[38:41], v[246:249], v[226:229], v[38:41]
	v_mfma_f32_16x16x32_bf16 v[34:37], v[250:253], v[226:229], v[34:37]
	ds_read_b128 v[226:229], v93 offset:4096
	ds_read_b128 v[150:153], v141 offset:23552
	s_add_i32 m0, s47, 0x4000
	s_nop 0
	global_load_lds_dwordx4 v136, s[30:31]
	v_mfma_f32_16x16x32_bf16 v[18:21], v[238:241], v[230:233], v[18:21]
	v_mfma_f32_16x16x32_bf16 v[22:25], v[242:245], v[230:233], v[22:25]
	v_mfma_f32_16x16x32_bf16 v[26:29], v[246:249], v[230:233], v[26:29]
	v_mfma_f32_16x16x32_bf16 v[30:33], v[250:253], v[230:233], v[30:33]
	ds_read_b128 v[230:233], v93 offset:6144
	ds_read_b128 v[154:157], v141 offset:25600
	s_add_i32 m0, s47, 0x6000
	s_nop 0
	global_load_lds_dwordx4 v138, s[30:31]
	v_mfma_f32_16x16x32_bf16 v[2:5], v[238:241], v[234:237], v[2:5]
	v_mfma_f32_16x16x32_bf16 v[6:9], v[242:245], v[234:237], v[6:9]
	v_mfma_f32_16x16x32_bf16 v[10:13], v[246:249], v[234:237], v[10:13]
	v_mfma_f32_16x16x32_bf16 v[14:17], v[250:253], v[234:237], v[14:17]
	ds_read_b128 v[234:237], v93 offset:8192
	s_add_i32 m0, s47, 0x8000
	s_nop 0
	global_load_lds_dwordx4 v140, s[30:31]
	s_waitcnt lgkmcnt(0)
	s_load_dwordx8 s[20:27], s[28:29], 0x0
	s_add_u32 s28, s28, 0x100
	s_addc_u32 s29, s29, 0
	v_mfma_f32_16x16x32_bf16 v[78:81], v[142:145], v[218:221], v[78:81]
	v_mfma_f32_16x16x32_bf16 v[74:77], v[146:149], v[218:221], v[74:77]
	v_mfma_f32_16x16x32_bf16 v[70:73], v[150:153], v[218:221], v[70:73]
	v_mfma_f32_16x16x32_bf16 v[66:69], v[154:157], v[218:221], v[66:69]
	v_mfma_f32_16x16x32_bf16 v[62:65], v[142:145], v[222:225], v[62:65]
	v_mfma_f32_16x16x32_bf16 v[58:61], v[146:149], v[222:225], v[58:61]
	v_mfma_f32_16x16x32_bf16 v[54:57], v[150:153], v[222:225], v[54:57]
	v_mfma_f32_16x16x32_bf16 v[50:53], v[154:157], v[222:225], v[50:53]
	v_mfma_f32_16x16x32_bf16 v[46:49], v[142:145], v[226:229], v[46:49]
	v_mfma_f32_16x16x32_bf16 v[42:45], v[146:149], v[226:229], v[42:45]
	v_mfma_f32_16x16x32_bf16 v[38:41], v[150:153], v[226:229], v[38:41]
	v_mfma_f32_16x16x32_bf16 v[34:37], v[154:157], v[226:229], v[34:37]
	v_mfma_f32_16x16x32_bf16 v[18:21], v[142:145], v[230:233], v[18:21]
	v_mfma_f32_16x16x32_bf16 v[22:25], v[146:149], v[230:233], v[22:25]
	v_mfma_f32_16x16x32_bf16 v[26:29], v[150:153], v[230:233], v[26:29]
	v_mfma_f32_16x16x32_bf16 v[30:33], v[154:157], v[230:233], v[30:33]
	v_mfma_f32_16x16x32_bf16 v[2:5], v[142:145], v[234:237], v[2:5]
	v_mfma_f32_16x16x32_bf16 v[6:9], v[146:149], v[234:237], v[6:9]
	v_mfma_f32_16x16x32_bf16 v[10:13], v[150:153], v[234:237], v[10:13]
	v_mfma_f32_16x16x32_bf16 v[14:17], v[154:157], v[234:237], v[14:17]
	s_waitcnt vmcnt(13)
	s_waitcnt lgkmcnt(0)
	s_barrier
; #define MU_GLDS_A(buf, kt) do { _Pragma("unroll") for (int i = 0; i < NMU; ++i) \
;         __builtin_amdgcn_global_load_lds((const unsigned*)((const char*)A + aoff[i] + (size_t)(kt) * 128), (PG8_LAS unsigned*)(MU_SA(buf) + wid * 1024 + i * 8192), 16, 0, 0); } while (0)
; #define MU_B_ISSUE(sb, kt) do { const char* kb_ = Bb + (size_t)(kt) * (64 * (size_t)RB); _Pragma("unroll") for (int j = 0; j < 8; ++j) { const char* p_ = kb_ + (size_t)j * RB; \
;         asm volatile("global_load_dwordx2 %0, %1, off" : "=&v"(sb[j]) : "v"(p_) : "memory"); } } while (0)
; #define MU_B_WAIT(sb, N) asm volatile("s_waitcnt vmcnt(%8)" : "+v"(sb[0]), "+v"(sb[1]), "+v"(sb[2]), "+v"(sb[3]), "+v"(sb[4]), "+v"(sb[5]), "+v"(sb[6]), "+v"(sb[7]) : "n"(N) : "memory")
; #define MU_G_LOAD(ga, kt) do { const PG8_LAS f32x4* gk_ = (const PG8_LAS f32x4*)(lds + GAIN_OFF) + 16 * (kt) + 2 * wid; const f32x4 ga_ = gk_[0], gb_ = gk_[1]; \
;         ga[0] = ga_[0]; ga[1] = ga_[1]; ga[2] = ga_[2]; ga[3] = ga_[3]; ga[4] = gb_[0]; ga[5] = gb_[1]; ga[6] = gb_[2]; ga[7] = gb_[3]; } while (0)
; #define MU_COMPUTE(buf) MU_COMPUTE_N(buf, NMU)
; #define MU_END(last) do { if (last) asm volatile("s_waitcnt vmcnt(0)" ::: "memory"); else asm volatile("s_waitcnt vmcnt(8)" ::: "memory"); \
;         asm volatile("s_waitcnt lgkmcnt(0)" ::: "memory"); __builtin_amdgcn_s_barrier(); asm volatile("" ::: "memory"); } while (0)
; template <int MODE>
; __device__ __forceinline__ void moe_unit(PG8_LAS unsigned char* lds, int e, int cb, int slot0  , int nv  , const bf16_t* A, const int* slot_tok,
;                                          const float* W0, const float* W1, bf16_t* OUT, const float* slot_rs  , const int* slot_dst) {
;     ...
;     for (int t = 0; t < nt; t += 2) {
;         if (t + 2 < nt) MU_B_WAIT(s1, 8); else MU_B_WAIT(s1, 0);
;         MU_G_LOAD(g0, t + 1); MU_B_WRITE(s1, 1, g0); __builtin_amdgcn_sched_barrier(0); MU_GLDS_A(1, t + 1); __builtin_amdgcn_sched_barrier(0);
;         if (t + 3 < nt) { MU_B_ISSUE(s1, t + 3); }
;         MU_COMPUTE(0);
;         MU_END(t + 3 >= nt);
;         if (t + 2 < nt) { MU_B_WAIT(s0, 8); MU_G_LOAD(g0, t + 2); MU_B_WRITE(s0, 0, g0); __builtin_amdgcn_sched_barrier(0); MU_GLDS_A(0, t + 2); __builtin_amdgcn_sched_barrier(0); }
;         if (t + 4 < nt) { MU_B_ISSUE(s0, t + 4); }
;         MU_COMPUTE(1);
;         MU_END(t + 4 >= nt);
;     }
	s_mov_b32 s47, s42
	s_mov_b32 s42, s43
	s_mov_b32 s43, s44
	s_mov_b32 s44, s47
	v_mul_f32_e32 v114, s20, v114
	v_mul_f32_e32 v115, s20, v115
	v_mul_f32_e32 v116, s21, v116
	v_mul_f32_e32 v117, s21, v117
	v_mul_f32_e32 v118, s22, v118
	v_mul_f32_e32 v119, s22, v119
	v_mul_f32_e32 v120, s23, v120
	v_mul_f32_e32 v121, s23, v121
	v_mul_f32_e32 v122, s24, v122
	v_mul_f32_e32 v123, s24, v123
	v_mul_f32_e32 v124, s25, v124
	v_mul_f32_e32 v125, s25, v125
	v_mul_f32_e32 v126, s26, v126
	v_mul_f32_e32 v127, s26, v127
	v_mul_f32_e32 v128, s27, v128
	v_mul_f32_e32 v129, s27, v129
	v_cvt_pk_bf16_f32 v158, v114, v116
	v_cvt_pk_bf16_f32 v159, v118, v120
	v_cvt_pk_bf16_f32 v160, v122, v124
	v_cvt_pk_bf16_f32 v161, v126, v128
	v_cvt_pk_bf16_f32 v162, v115, v117
	v_cvt_pk_bf16_f32 v163, v119, v121
	v_cvt_pk_bf16_f32 v164, v123, v125
	v_cvt_pk_bf16_f32 v165, v127, v129
	ds_write_b128 v1, v[158:161] offset:19456
	ds_write_b128 v1, v[162:165] offset:19584
	v_add_u32_e32 v91, s42, v135
	v_add_u32_e32 v93, s42, v137
	ds_read_b128 v[238:241], v139 offset:0
	ds_read_b128 v[242:245], v139 offset:2048
	ds_read_b128 v[246:249], v139 offset:4096
	ds_read_b128 v[250:253], v139 offset:6144
	ds_read_b128 v[218:221], v91 offset:0
	ds_read_b128 v[222:225], v91 offset:2048
	ds_read_b128 v[226:229], v91 offset:4096
	ds_read_b128 v[230:233], v91 offset:6144
	ds_read_b128 v[234:237], v91 offset:8192
	s_add_i32 s47, s44, s6
	s_add_u32 s30, s30, 0x80
	s_addc_u32 s31, s31, 0
	s_waitcnt lgkmcnt(0)
	v_mfma_f32_16x16x32_bf16 v[78:81], v[238:241], v[218:221], v[78:81]
	v_mfma_f32_16x16x32_bf16 v[74:77], v[242:245], v[218:221], v[74:77]
	v_mfma_f32_16x16x32_bf16 v[70:73], v[246:249], v[218:221], v[70:73]
	v_mfma_f32_16x16x32_bf16 v[66:69], v[250:253], v[218:221], v[66:69]
	ds_read_b128 v[218:221], v93 offset:0
	ds_read_b128 v[142:145], v141 offset:0
	s_mov_b32 m0, s47
	s_nop 0
	global_load_lds_dwordx4 v86, s[30:31]
	v_mfma_f32_16x16x32_bf16 v[62:65], v[238:241], v[222:225], v[62:65]
	v_mfma_f32_16x16x32_bf16 v[58:61], v[242:245], v[222:225], v[58:61]
	v_mfma_f32_16x16x32_bf16 v[54:57], v[246:249], v[222:225], v[54:57]
	v_mfma_f32_16x16x32_bf16 v[50:53], v[250:253], v[222:225], v[50:53]
	ds_read_b128 v[222:225], v93 offset:2048
	ds_read_b128 v[146:149], v141 offset:2048
	s_add_i32 m0, s47, 0x2000
	s_nop 0
	global_load_lds_dwordx4 v134, s[30:31]
	v_mfma_f32_16x16x32_bf16 v[46:49], v[238:241], v[226:229], v[46:49]
	v_mfma_f32_16x16x32_bf16 v[42:45], v[242:245], v[226:229], v[42:45]
	v_mfma_f32_16x16x32_bf16 v[38:41], v[246:249], v[226:229], v[38:41]
	v_mfma_f32_16x16x32_bf16 v[34:37], v[250:253], v[226:229], v[34:37]
	ds_read_b128 v[226:229], v93 offset:4096
	ds_read_b128 v[150:153], v141 offset:4096
	s_add_i32 m0, s47, 0x4000
	s_nop 0
	global_load_lds_dwordx4 v136, s[30:31]
	v_mfma_f32_16x16x32_bf16 v[18:21], v[238:241], v[230:233], v[18:21]
	v_mfma_f32_16x16x32_bf16 v[22:25], v[242:245], v[230:233], v[22:25]
	v_mfma_f32_16x16x32_bf16 v[26:29], v[246:249], v[230:233], v[26:29]
	v_mfma_f32_16x16x32_bf16 v[30:33], v[250:253], v[230:233], v[30:33]
	ds_read_b128 v[230:233], v93 offset:6144
	ds_read_b128 v[154:157], v141 offset:6144
	s_add_i32 m0, s47, 0x6000
	s_nop 0
	global_load_lds_dwordx4 v138, s[30:31]
	v_mfma_f32_16x16x32_bf16 v[2:5], v[238:241], v[234:237], v[2:5]
	v_mfma_f32_16x16x32_bf16 v[6:9], v[242:245], v[234:237], v[6:9]
	v_mfma_f32_16x16x32_bf16 v[10:13], v[246:249], v[234:237], v[10:13]
	v_mfma_f32_16x16x32_bf16 v[14:17], v[250:253], v[234:237], v[14:17]
	ds_read_b128 v[234:237], v93 offset:8192
	s_add_i32 m0, s47, 0x8000
	s_nop 0
	global_load_lds_dwordx4 v140, s[30:31]
	s_waitcnt lgkmcnt(0)
	s_load_dwordx8 s[12:19], s[28:29], 0x0
	s_add_u32 s28, s28, 0x100
	s_addc_u32 s29, s29, 0
	v_mfma_f32_16x16x32_bf16 v[78:81], v[142:145], v[218:221], v[78:81]
	v_mfma_f32_16x16x32_bf16 v[74:77], v[146:149], v[218:221], v[74:77]
	v_mfma_f32_16x16x32_bf16 v[70:73], v[150:153], v[218:221], v[70:73]
	v_mfma_f32_16x16x32_bf16 v[66:69], v[154:157], v[218:221], v[66:69]
	v_mfma_f32_16x16x32_bf16 v[62:65], v[142:145], v[222:225], v[62:65]
	v_mfma_f32_16x16x32_bf16 v[58:61], v[146:149], v[222:225], v[58:61]
	v_mfma_f32_16x16x32_bf16 v[54:57], v[150:153], v[222:225], v[54:57]
	v_mfma_f32_16x16x32_bf16 v[50:53], v[154:157], v[222:225], v[50:53]
	v_mfma_f32_16x16x32_bf16 v[46:49], v[142:145], v[226:229], v[46:49]
	v_mfma_f32_16x16x32_bf16 v[42:45], v[146:149], v[226:229], v[42:45]
	v_mfma_f32_16x16x32_bf16 v[38:41], v[150:153], v[226:229], v[38:41]
	v_mfma_f32_16x16x32_bf16 v[34:37], v[154:157], v[226:229], v[34:37]
	v_mfma_f32_16x16x32_bf16 v[18:21], v[142:145], v[230:233], v[18:21]
	v_mfma_f32_16x16x32_bf16 v[22:25], v[146:149], v[230:233], v[22:25]
	v_mfma_f32_16x16x32_bf16 v[26:29], v[150:153], v[230:233], v[26:29]
	v_mfma_f32_16x16x32_bf16 v[30:33], v[154:157], v[230:233], v[30:33]
	v_mfma_f32_16x16x32_bf16 v[2:5], v[142:145], v[234:237], v[2:5]
	v_mfma_f32_16x16x32_bf16 v[6:9], v[146:149], v[234:237], v[6:9]
	v_mfma_f32_16x16x32_bf16 v[10:13], v[150:153], v[234:237], v[10:13]
	v_mfma_f32_16x16x32_bf16 v[14:17], v[154:157], v[234:237], v[14:17]
	s_waitcnt vmcnt(5)
	s_waitcnt lgkmcnt(0)
	s_barrier
; #define MU_GLDS_A(buf, kt) do { _Pragma("unroll") for (int i = 0; i < NMU; ++i) \
;         __builtin_amdgcn_global_load_lds((const unsigned*)((const char*)A + aoff[i] + (size_t)(kt) * 128), (PG8_LAS unsigned*)(MU_SA(buf) + wid * 1024 + i * 8192), 16, 0, 0); } while (0)
; #define MU_B_ISSUE(sb, kt) do { const char* kb_ = Bb + (size_t)(kt) * (64 * (size_t)RB); _Pragma("unroll") for (int j = 0; j < 8; ++j) { const char* p_ = kb_ + (size_t)j * RB; \
;         asm volatile("global_load_dwordx2 %0, %1, off" : "=&v"(sb[j]) : "v"(p_) : "memory"); } } while (0)
; #define MU_B_WAIT(sb, N) asm volatile("s_waitcnt vmcnt(%8)" : "+v"(sb[0]), "+v"(sb[1]), "+v"(sb[2]), "+v"(sb[3]), "+v"(sb[4]), "+v"(sb[5]), "+v"(sb[6]), "+v"(sb[7]) : "n"(N) : "memory")
; #define MU_G_LOAD(ga, kt) do { const PG8_LAS f32x4* gk_ = (const PG8_LAS f32x4*)(lds + GAIN_OFF) + 16 * (kt) + 2 * wid; const f32x4 ga_ = gk_[0], gb_ = gk_[1]; \
;         ga[0] = ga_[0]; ga[1] = ga_[1]; ga[2] = ga_[2]; ga[3] = ga_[3]; ga[4] = gb_[0]; ga[5] = gb_[1]; ga[6] = gb_[2]; ga[7] = gb_[3]; } while (0)
; #define MU_COMPUTE(buf) MU_COMPUTE_N(buf, NMU)
; #define MU_END(last) do { if (last) asm volatile("s_waitcnt vmcnt(0)" ::: "memory"); else asm volatile("s_waitcnt vmcnt(8)" ::: "memory"); \
;         asm volatile("s_waitcnt lgkmcnt(0)" ::: "memory"); __builtin_amdgcn_s_barrier(); asm volatile("" ::: "memory"); } while (0)
; template <int MODE>
; __device__ __forceinline__ void moe_unit(PG8_LAS unsigned char* lds, int e, int cb, int slot0  , int nv  , const bf16_t* A, const int* slot_tok,
;                                          const float* W0, const float* W1, bf16_t* OUT, const float* slot_rs  , const int* slot_dst) {
;     ...
;     for (int t = 0; t < nt; t += 2) {
;         if (t + 2 < nt) MU_B_WAIT(s1, 8); else MU_B_WAIT(s1, 0);
;         MU_G_LOAD(g0, t + 1); MU_B_WRITE(s1, 1, g0); __builtin_amdgcn_sched_barrier(0); MU_GLDS_A(1, t + 1); __builtin_amdgcn_sched_barrier(0);
;         if (t + 3 < nt) { MU_B_ISSUE(s1, t + 3); }
;         MU_COMPUTE(0);
;         MU_END(t + 3 >= nt);
;         if (t + 2 < nt) { MU_B_WAIT(s0, 8); MU_G_LOAD(g0, t + 2); MU_B_WRITE(s0, 0, g0); __builtin_amdgcn_sched_barrier(0); MU_GLDS_A(0, t + 2); __builtin_amdgcn_sched_barrier(0); }
;         if (t + 4 < nt) { MU_B_ISSUE(s0, t + 4); }
;         MU_COMPUTE(1);
;         MU_END(t + 4 >= nt);
;     }
	s_mov_b32 s47, s42
	s_mov_b32 s42, s43
	s_mov_b32 s43, s44
	s_mov_b32 s44, s47
	v_mul_f32_e32 v186, s12, v186
	v_mul_f32_e32 v187, s12, v187
	v_mul_f32_e32 v188, s13, v188
	v_mul_f32_e32 v189, s13, v189
	v_mul_f32_e32 v190, s14, v190
	v_mul_f32_e32 v191, s14, v191
	v_mul_f32_e32 v192, s15, v192
	v_mul_f32_e32 v193, s15, v193
	v_mul_f32_e32 v194, s16, v194
	v_mul_f32_e32 v195, s16, v195
	v_mul_f32_e32 v196, s17, v196
	v_mul_f32_e32 v197, s17, v197
	v_mul_f32_e32 v198, s18, v198
	v_mul_f32_e32 v199, s18, v199
	v_mul_f32_e32 v200, s19, v200
	v_mul_f32_e32 v201, s19, v201
	v_cvt_pk_bf16_f32 v158, v186, v188
	v_cvt_pk_bf16_f32 v159, v190, v192
	v_cvt_pk_bf16_f32 v160, v194, v196
	v_cvt_pk_bf16_f32 v161, v198, v200
	v_cvt_pk_bf16_f32 v162, v187, v189
	v_cvt_pk_bf16_f32 v163, v191, v193
	v_cvt_pk_bf16_f32 v164, v195, v197
	v_cvt_pk_bf16_f32 v165, v199, v201
	ds_write_b128 v1, v[158:161] offset:0
	ds_write_b128 v1, v[162:165] offset:128
	v_add_u32_e32 v91, s42, v135
	v_add_u32_e32 v93, s42, v137
	ds_read_b128 v[238:241], v139 offset:19456
	ds_read_b128 v[242:245], v139 offset:21504
	ds_read_b128 v[246:249], v139 offset:23552
	ds_read_b128 v[250:253], v139 offset:25600
	ds_read_b128 v[218:221], v91 offset:0
	ds_read_b128 v[222:225], v91 offset:2048
	ds_read_b128 v[226:229], v91 offset:4096
	ds_read_b128 v[230:233], v91 offset:6144
	ds_read_b128 v[234:237], v91 offset:8192
	s_add_i32 s47, s44, s6
	s_add_u32 s30, s30, 0x80
	s_addc_u32 s31, s31, 0
	s_waitcnt lgkmcnt(0)
	v_mfma_f32_16x16x32_bf16 v[78:81], v[238:241], v[218:221], v[78:81]
	v_mfma_f32_16x16x32_bf16 v[74:77], v[242:245], v[218:221], v[74:77]
	v_mfma_f32_16x16x32_bf16 v[70:73], v[246:249], v[218:221], v[70:73]
	v_mfma_f32_16x16x32_bf16 v[66:69], v[250:253], v[218:221], v[66:69]
	ds_read_b128 v[218:221], v93 offset:0
	ds_read_b128 v[142:145], v141 offset:19456
	s_mov_b32 m0, s47
	s_nop 0
	global_load_lds_dwordx4 v86, s[30:31]
	v_mfma_f32_16x16x32_bf16 v[62:65], v[238:241], v[222:225], v[62:65]
	v_mfma_f32_16x16x32_bf16 v[58:61], v[242:245], v[222:225], v[58:61]
	v_mfma_f32_16x16x32_bf16 v[54:57], v[246:249], v[222:225], v[54:57]
	v_mfma_f32_16x16x32_bf16 v[50:53], v[250:253], v[222:225], v[50:53]
	ds_read_b128 v[222:225], v93 offset:2048
	ds_read_b128 v[146:149], v141 offset:21504
	s_add_i32 m0, s47, 0x2000
	s_nop 0
	global_load_lds_dwordx4 v134, s[30:31]
	v_mfma_f32_16x16x32_bf16 v[46:49], v[238:241], v[226:229], v[46:49]
	v_mfma_f32_16x16x32_bf16 v[42:45], v[242:245], v[226:229], v[42:45]
	v_mfma_f32_16x16x32_bf16 v[38:41], v[246:249], v[226:229], v[38:41]
	v_mfma_f32_16x16x32_bf16 v[34:37], v[250:253], v[226:229], v[34:37]
	ds_read_b128 v[226:229], v93 offset:4096
	ds_read_b128 v[150:153], v141 offset:23552
	s_add_i32 m0, s47, 0x4000
	s_nop 0
	global_load_lds_dwordx4 v136, s[30:31]
	v_mfma_f32_16x16x32_bf16 v[18:21], v[238:241], v[230:233], v[18:21]
	v_mfma_f32_16x16x32_bf16 v[22:25], v[242:245], v[230:233], v[22:25]
	v_mfma_f32_16x16x32_bf16 v[26:29], v[246:249], v[230:233], v[26:29]
	v_mfma_f32_16x16x32_bf16 v[30:33], v[250:253], v[230:233], v[30:33]
	ds_read_b128 v[230:233], v93 offset:6144
	ds_read_b128 v[154:157], v141 offset:25600
	s_add_i32 m0, s47, 0x6000
	s_nop 0
	global_load_lds_dwordx4 v138, s[30:31]
	v_mfma_f32_16x16x32_bf16 v[2:5], v[238:241], v[234:237], v[2:5]
	v_mfma_f32_16x16x32_bf16 v[6:9], v[242:245], v[234:237], v[6:9]
	v_mfma_f32_16x16x32_bf16 v[10:13], v[246:249], v[234:237], v[10:13]
	v_mfma_f32_16x16x32_bf16 v[14:17], v[250:253], v[234:237], v[14:17]
	ds_read_b128 v[234:237], v93 offset:8192
	s_add_i32 m0, s47, 0x8000
	s_nop 0
	global_load_lds_dwordx4 v140, s[30:31]
	s_waitcnt lgkmcnt(0)
	s_load_dwordx8 s[20:27], s[28:29], 0x0
	s_add_u32 s28, s28, 0x100
	s_addc_u32 s29, s29, 0
	v_mfma_f32_16x16x32_bf16 v[78:81], v[142:145], v[218:221], v[78:81]
	v_mfma_f32_16x16x32_bf16 v[74:77], v[146:149], v[218:221], v[74:77]
	v_mfma_f32_16x16x32_bf16 v[70:73], v[150:153], v[218:221], v[70:73]
	v_mfma_f32_16x16x32_bf16 v[66:69], v[154:157], v[218:221], v[66:69]
	v_mfma_f32_16x16x32_bf16 v[62:65], v[142:145], v[222:225], v[62:65]
	v_mfma_f32_16x16x32_bf16 v[58:61], v[146:149], v[222:225], v[58:61]
	v_mfma_f32_16x16x32_bf16 v[54:57], v[150:153], v[222:225], v[54:57]
	v_mfma_f32_16x16x32_bf16 v[50:53], v[154:157], v[222:225], v[50:53]
	v_mfma_f32_16x16x32_bf16 v[46:49], v[142:145], v[226:229], v[46:49]
	v_mfma_f32_16x16x32_bf16 v[42:45], v[146:149], v[226:229], v[42:45]
	v_mfma_f32_16x16x32_bf16 v[38:41], v[150:153], v[226:229], v[38:41]
	v_mfma_f32_16x16x32_bf16 v[34:37], v[154:157], v[226:229], v[34:37]
	v_mfma_f32_16x16x32_bf16 v[18:21], v[142:145], v[230:233], v[18:21]
	v_mfma_f32_16x16x32_bf16 v[22:25], v[146:149], v[230:233], v[22:25]
	v_mfma_f32_16x16x32_bf16 v[26:29], v[150:153], v[230:233], v[26:29]
	v_mfma_f32_16x16x32_bf16 v[30:33], v[154:157], v[230:233], v[30:33]
	v_mfma_f32_16x16x32_bf16 v[2:5], v[142:145], v[234:237], v[2:5]
	v_mfma_f32_16x16x32_bf16 v[6:9], v[146:149], v[234:237], v[6:9]
	v_mfma_f32_16x16x32_bf16 v[10:13], v[150:153], v[234:237], v[10:13]
	v_mfma_f32_16x16x32_bf16 v[14:17], v[154:157], v[234:237], v[14:17]
	s_waitcnt vmcnt(5)
	s_waitcnt lgkmcnt(0)
	s_barrier
; #define MU_GLDS_A(buf, kt) do { _Pragma("unroll") for (int i = 0; i < NMU; ++i) \
;         __builtin_amdgcn_global_load_lds((const unsigned*)((const char*)A + aoff[i] + (size_t)(kt) * 128), (PG8_LAS unsigned*)(MU_SA(buf) + wid * 1024 + i * 8192), 16, 0, 0); } while (0)
; #define MU_B_ISSUE(sb, kt) do { const char* kb_ = Bb + (size_t)(kt) * (64 * (size_t)RB); _Pragma("unroll") for (int j = 0; j < 8; ++j) { const char* p_ = kb_ + (size_t)j * RB; \
;         asm volatile("global_load_dwordx2 %0, %1, off" : "=&v"(sb[j]) : "v"(p_) : "memory"); } } while (0)
; #define MU_B_WAIT(sb, N) asm volatile("s_waitcnt vmcnt(%8)" : "+v"(sb[0]), "+v"(sb[1]), "+v"(sb[2]), "+v"(sb[3]), "+v"(sb[4]), "+v"(sb[5]), "+v"(sb[6]), "+v"(sb[7]) : "n"(N) : "memory")
; #define MU_G_LOAD(ga, kt) do { const PG8_LAS f32x4* gk_ = (const PG8_LAS f32x4*)(lds + GAIN_OFF) + 16 * (kt) + 2 * wid; const f32x4 ga_ = gk_[0], gb_ = gk_[1]; \
;         ga[0] = ga_[0]; ga[1] = ga_[1]; ga[2] = ga_[2]; ga[3] = ga_[3]; ga[4] = gb_[0]; ga[5] = gb_[1]; ga[6] = gb_[2]; ga[7] = gb_[3]; } while (0)
; #define MU_COMPUTE(buf) MU_COMPUTE_N(buf, NMU)
; #define MU_END(last) do { if (last) asm volatile("s_waitcnt vmcnt(0)" ::: "memory"); else asm volatile("s_waitcnt vmcnt(8)" ::: "memory"); \
;         asm volatile("s_waitcnt lgkmcnt(0)" ::: "memory"); __builtin_amdgcn_s_barrier(); asm volatile("" ::: "memory"); } while (0)
; template <int MODE>
; __device__ __forceinline__ void moe_unit(PG8_LAS unsigned char* lds, int e, int cb, int slot0  , int nv  , const bf16_t* A, const int* slot_tok,
;                                          const float* W0, const float* W1, bf16_t* OUT, const float* slot_rs  , const int* slot_dst) {
;     ...
;     for (int t = 0; t < nt; t += 2) {
;         if (t + 2 < nt) MU_B_WAIT(s1, 8); else MU_B_WAIT(s1, 0);
;         MU_G_LOAD(g0, t + 1); MU_B_WRITE(s1, 1, g0); __builtin_amdgcn_sched_barrier(0); MU_GLDS_A(1, t + 1); __builtin_amdgcn_sched_barrier(0);
;         if (t + 3 < nt) { MU_B_ISSUE(s1, t + 3); }
;         MU_COMPUTE(0);
;         MU_END(t + 3 >= nt);
;         if (t + 2 < nt) { MU_B_WAIT(s0, 8); MU_G_LOAD(g0, t + 2); MU_B_WRITE(s0, 0, g0); __builtin_amdgcn_sched_barrier(0); MU_GLDS_A(0, t + 2); __builtin_amdgcn_sched_barrier(0); }
;         if (t + 4 < nt) { MU_B_ISSUE(s0, t + 4); }
;         MU_COMPUTE(1);
;         MU_END(t + 4 >= nt);
;     }
	s_mov_b32 s47, s42
	s_mov_b32 s42, s43
	s_mov_b32 s43, s44
	s_mov_b32 s44, s47
	v_mul_f32_e32 v202, s20, v202
	v_mul_f32_e32 v203, s20, v203
	v_mul_f32_e32 v204, s21, v204
	v_mul_f32_e32 v205, s21, v205
	v_mul_f32_e32 v206, s22, v206
	v_mul_f32_e32 v207, s22, v207
	v_mul_f32_e32 v208, s23, v208
	v_mul_f32_e32 v209, s23, v209
	v_mul_f32_e32 v210, s24, v210
	v_mul_f32_e32 v211, s24, v211
	v_mul_f32_e32 v212, s25, v212
	v_mul_f32_e32 v213, s25, v213
	v_mul_f32_e32 v214, s26, v214
	v_mul_f32_e32 v215, s26, v215
	v_mul_f32_e32 v216, s27, v216
	v_mul_f32_e32 v217, s27, v217
	v_cvt_pk_bf16_f32 v158, v202, v204
	v_cvt_pk_bf16_f32 v159, v206, v208
	v_cvt_pk_bf16_f32 v160, v210, v212
	v_cvt_pk_bf16_f32 v161, v214, v216
	v_cvt_pk_bf16_f32 v162, v203, v205
	v_cvt_pk_bf16_f32 v163, v207, v209
	v_cvt_pk_bf16_f32 v164, v211, v213
	v_cvt_pk_bf16_f32 v165, v215, v217
	ds_write_b128 v1, v[158:161] offset:19456
	ds_write_b128 v1, v[162:165] offset:19584
	v_add_u32_e32 v91, s42, v135
	v_add_u32_e32 v93, s42, v137
	ds_read_b128 v[238:241], v139 offset:0
	ds_read_b128 v[242:245], v139 offset:2048
	ds_read_b128 v[246:249], v139 offset:4096
	ds_read_b128 v[250:253], v139 offset:6144
	ds_read_b128 v[218:221], v91 offset:0
	ds_read_b128 v[222:225], v91 offset:2048
	ds_read_b128 v[226:229], v91 offset:4096
	ds_read_b128 v[230:233], v91 offset:6144
	ds_read_b128 v[234:237], v91 offset:8192
	s_waitcnt lgkmcnt(0)
	v_mfma_f32_16x16x32_bf16 v[78:81], v[238:241], v[218:221], v[78:81]
	v_mfma_f32_16x16x32_bf16 v[74:77], v[242:245], v[218:221], v[74:77]
	v_mfma_f32_16x16x32_bf16 v[70:73], v[246:249], v[218:221], v[70:73]
	v_mfma_f32_16x16x32_bf16 v[66:69], v[250:253], v[218:221], v[66:69]
	ds_read_b128 v[218:221], v93 offset:0
	ds_read_b128 v[142:145], v141 offset:0
	v_mfma_f32_16x16x32_bf16 v[62:65], v[238:241], v[222:225], v[62:65]
	v_mfma_f32_16x16x32_bf16 v[58:61], v[242:245], v[222:225], v[58:61]
	v_mfma_f32_16x16x32_bf16 v[54:57], v[246:249], v[222:225], v[54:57]
	v_mfma_f32_16x16x32_bf16 v[50:53], v[250:253], v[222:225], v[50:53]
	ds_read_b128 v[222:225], v93 offset:2048
	ds_read_b128 v[146:149], v141 offset:2048
	v_mfma_f32_16x16x32_bf16 v[46:49], v[238:241], v[226:229], v[46:49]
	v_mfma_f32_16x16x32_bf16 v[42:45], v[242:245], v[226:229], v[42:45]
	v_mfma_f32_16x16x32_bf16 v[38:41], v[246:249], v[226:229], v[38:41]
	v_mfma_f32_16x16x32_bf16 v[34:37], v[250:253], v[226:229], v[34:37]
	ds_read_b128 v[226:229], v93 offset:4096
	ds_read_b128 v[150:153], v141 offset:4096
	v_mfma_f32_16x16x32_bf16 v[18:21], v[238:241], v[230:233], v[18:21]
	v_mfma_f32_16x16x32_bf16 v[22:25], v[242:245], v[230:233], v[22:25]
	v_mfma_f32_16x16x32_bf16 v[26:29], v[246:249], v[230:233], v[26:29]
	v_mfma_f32_16x16x32_bf16 v[30:33], v[250:253], v[230:233], v[30:33]
	ds_read_b128 v[230:233], v93 offset:6144
	ds_read_b128 v[154:157], v141 offset:6144
	v_mfma_f32_16x16x32_bf16 v[2:5], v[238:241], v[234:237], v[2:5]
	v_mfma_f32_16x16x32_bf16 v[6:9], v[242:245], v[234:237], v[6:9]
	v_mfma_f32_16x16x32_bf16 v[10:13], v[246:249], v[234:237], v[10:13]
	v_mfma_f32_16x16x32_bf16 v[14:17], v[250:253], v[234:237], v[14:17]
	ds_read_b128 v[234:237], v93 offset:8192
	s_waitcnt lgkmcnt(0)
	v_mfma_f32_16x16x32_bf16 v[78:81], v[142:145], v[218:221], v[78:81]
	v_mfma_f32_16x16x32_bf16 v[74:77], v[146:149], v[218:221], v[74:77]
	v_mfma_f32_16x16x32_bf16 v[70:73], v[150:153], v[218:221], v[70:73]
	v_mfma_f32_16x16x32_bf16 v[66:69], v[154:157], v[218:221], v[66:69]
	v_mfma_f32_16x16x32_bf16 v[62:65], v[142:145], v[222:225], v[62:65]
	v_mfma_f32_16x16x32_bf16 v[58:61], v[146:149], v[222:225], v[58:61]
	v_mfma_f32_16x16x32_bf16 v[54:57], v[150:153], v[222:225], v[54:57]
	v_mfma_f32_16x16x32_bf16 v[50:53], v[154:157], v[222:225], v[50:53]
	v_mfma_f32_16x16x32_bf16 v[46:49], v[142:145], v[226:229], v[46:49]
	v_mfma_f32_16x16x32_bf16 v[42:45], v[146:149], v[226:229], v[42:45]
	v_mfma_f32_16x16x32_bf16 v[38:41], v[150:153], v[226:229], v[38:41]
	v_mfma_f32_16x16x32_bf16 v[34:37], v[154:157], v[226:229], v[34:37]
	v_mfma_f32_16x16x32_bf16 v[18:21], v[142:145], v[230:233], v[18:21]
	v_mfma_f32_16x16x32_bf16 v[22:25], v[146:149], v[230:233], v[22:25]
	v_mfma_f32_16x16x32_bf16 v[26:29], v[150:153], v[230:233], v[26:29]
	v_mfma_f32_16x16x32_bf16 v[30:33], v[154:157], v[230:233], v[30:33]
	v_mfma_f32_16x16x32_bf16 v[2:5], v[142:145], v[234:237], v[2:5]
	v_mfma_f32_16x16x32_bf16 v[6:9], v[146:149], v[234:237], v[6:9]
	v_mfma_f32_16x16x32_bf16 v[10:13], v[150:153], v[234:237], v[10:13]
	v_mfma_f32_16x16x32_bf16 v[14:17], v[154:157], v[234:237], v[14:17]
	s_waitcnt vmcnt(0)
	s_waitcnt lgkmcnt(0)
	s_barrier
; #define MU_GLDS_A(buf, kt) do { _Pragma("unroll") for (int i = 0; i < NMU; ++i) \
;         __builtin_amdgcn_global_load_lds((const unsigned*)((const char*)A + aoff[i] + (size_t)(kt) * 128), (PG8_LAS unsigned*)(MU_SA(buf) + wid * 1024 + i * 8192), 16, 0, 0); } while (0)
; #define MU_B_ISSUE(sb, kt) do { const char* kb_ = Bb + (size_t)(kt) * (64 * (size_t)RB); _Pragma("unroll") for (int j = 0; j < 8; ++j) { const char* p_ = kb_ + (size_t)j * RB; \
;         asm volatile("global_load_dwordx2 %0, %1, off" : "=&v"(sb[j]) : "v"(p_) : "memory"); } } while (0)
; #define MU_B_WAIT(sb, N) asm volatile("s_waitcnt vmcnt(%8)" : "+v"(sb[0]), "+v"(sb[1]), "+v"(sb[2]), "+v"(sb[3]), "+v"(sb[4]), "+v"(sb[5]), "+v"(sb[6]), "+v"(sb[7]) : "n"(N) : "memory")
; #define MU_G_LOAD(ga, kt) do { const PG8_LAS f32x4* gk_ = (const PG8_LAS f32x4*)(lds + GAIN_OFF) + 16 * (kt) + 2 * wid; const f32x4 ga_ = gk_[0], gb_ = gk_[1]; \
;         ga[0] = ga_[0]; ga[1] = ga_[1]; ga[2] = ga_[2]; ga[3] = ga_[3]; ga[4] = gb_[0]; ga[5] = gb_[1]; ga[6] = gb_[2]; ga[7] = gb_[3]; } while (0)
; #define MU_COMPUTE(buf) MU_COMPUTE_N(buf, NMU)
; #define MU_END(last) do { if (last) asm volatile("s_waitcnt vmcnt(0)" ::: "memory"); else asm volatile("s_waitcnt vmcnt(8)" ::: "memory"); \
;         asm volatile("s_waitcnt lgkmcnt(0)" ::: "memory"); __builtin_amdgcn_s_barrier(); asm volatile("" ::: "memory"); } while (0)
; template <int MODE>
; __device__ __forceinline__ void moe_unit(PG8_LAS unsigned char* lds, int e, int cb, int slot0  , int nv  , const bf16_t* A, const int* slot_tok,
;                                          const float* W0, const float* W1, bf16_t* OUT, const float* slot_rs  , const int* slot_dst) {
;     ...
;     for (int t = 0; t < nt; t += 2) {
;         if (t + 2 < nt) MU_B_WAIT(s1, 8); else MU_B_WAIT(s1, 0);
;         MU_G_LOAD(g0, t + 1); MU_B_WRITE(s1, 1, g0); __builtin_amdgcn_sched_barrier(0); MU_GLDS_A(1, t + 1); __builtin_amdgcn_sched_barrier(0);
;         if (t + 3 < nt) { MU_B_ISSUE(s1, t + 3); }
;         MU_COMPUTE(0);
;         MU_END(t + 3 >= nt);
;         if (t + 2 < nt) { MU_B_WAIT(s0, 8); MU_G_LOAD(g0, t + 2); MU_B_WRITE(s0, 0, g0); __builtin_amdgcn_sched_barrier(0); MU_GLDS_A(0, t + 2); __builtin_amdgcn_sched_barrier(0); }
;         if (t + 4 < nt) { MU_B_ISSUE(s0, t + 4); }
;         MU_COMPUTE(1);
;         MU_END(t + 4 >= nt);
;     }
	s_mov_b32 s47, s42
	s_mov_b32 s42, s43
	s_mov_b32 s43, s44
	s_mov_b32 s44, s47
	v_add_u32_e32 v91, s42, v135
	v_add_u32_e32 v93, s42, v137
	ds_read_b128 v[238:241], v139 offset:19456
	ds_read_b128 v[242:245], v139 offset:21504
	ds_read_b128 v[246:249], v139 offset:23552
	ds_read_b128 v[250:253], v139 offset:25600
	ds_read_b128 v[218:221], v91 offset:0
	ds_read_b128 v[222:225], v91 offset:2048
	ds_read_b128 v[226:229], v91 offset:4096
	ds_read_b128 v[230:233], v91 offset:6144
	ds_read_b128 v[234:237], v91 offset:8192
	s_waitcnt lgkmcnt(0)
	v_mfma_f32_16x16x32_bf16 v[78:81], v[238:241], v[218:221], v[78:81]
	v_mfma_f32_16x16x32_bf16 v[74:77], v[242:245], v[218:221], v[74:77]
	v_mfma_f32_16x16x32_bf16 v[70:73], v[246:249], v[218:221], v[70:73]
	v_mfma_f32_16x16x32_bf16 v[66:69], v[250:253], v[218:221], v[66:69]
	ds_read_b128 v[218:221], v93 offset:0
	ds_read_b128 v[142:145], v141 offset:19456
	v_mfma_f32_16x16x32_bf16 v[62:65], v[238:241], v[222:225], v[62:65]
	v_mfma_f32_16x16x32_bf16 v[58:61], v[242:245], v[222:225], v[58:61]
	v_mfma_f32_16x16x32_bf16 v[54:57], v[246:249], v[222:225], v[54:57]
	v_mfma_f32_16x16x32_bf16 v[50:53], v[250:253], v[222:225], v[50:53]
	ds_read_b128 v[222:225], v93 offset:2048
	ds_read_b128 v[146:149], v141 offset:21504
	v_mfma_f32_16x16x32_bf16 v[46:49], v[238:241], v[226:229], v[46:49]
	v_mfma_f32_16x16x32_bf16 v[42:45], v[242:245], v[226:229], v[42:45]
	v_mfma_f32_16x16x32_bf16 v[38:41], v[246:249], v[226:229], v[38:41]
	v_mfma_f32_16x16x32_bf16 v[34:37], v[250:253], v[226:229], v[34:37]
	ds_read_b128 v[226:229], v93 offset:4096
	ds_read_b128 v[150:153], v141 offset:23552
	v_mfma_f32_16x16x32_bf16 v[18:21], v[238:241], v[230:233], v[18:21]
	v_mfma_f32_16x16x32_bf16 v[22:25], v[242:245], v[230:233], v[22:25]
	v_mfma_f32_16x16x32_bf16 v[26:29], v[246:249], v[230:233], v[26:29]
	v_mfma_f32_16x16x32_bf16 v[30:33], v[250:253], v[230:233], v[30:33]
	ds_read_b128 v[230:233], v93 offset:6144
	ds_read_b128 v[154:157], v141 offset:25600
	v_mfma_f32_16x16x32_bf16 v[2:5], v[238:241], v[234:237], v[2:5]
	v_mfma_f32_16x16x32_bf16 v[6:9], v[242:245], v[234:237], v[6:9]
	v_mfma_f32_16x16x32_bf16 v[10:13], v[246:249], v[234:237], v[10:13]
	v_mfma_f32_16x16x32_bf16 v[14:17], v[250:253], v[234:237], v[14:17]
	ds_read_b128 v[234:237], v93 offset:8192
	s_waitcnt lgkmcnt(0)
	v_mfma_f32_16x16x32_bf16 v[78:81], v[142:145], v[218:221], v[78:81]
	v_mfma_f32_16x16x32_bf16 v[74:77], v[146:149], v[218:221], v[74:77]
	v_mfma_f32_16x16x32_bf16 v[70:73], v[150:153], v[218:221], v[70:73]
	v_mfma_f32_16x16x32_bf16 v[66:69], v[154:157], v[218:221], v[66:69]
	v_mfma_f32_16x16x32_bf16 v[62:65], v[142:145], v[222:225], v[62:65]
	v_mfma_f32_16x16x32_bf16 v[58:61], v[146:149], v[222:225], v[58:61]
	v_mfma_f32_16x16x32_bf16 v[54:57], v[150:153], v[222:225], v[54:57]
	v_mfma_f32_16x16x32_bf16 v[50:53], v[154:157], v[222:225], v[50:53]
	v_mfma_f32_16x16x32_bf16 v[46:49], v[142:145], v[226:229], v[46:49]
	v_mfma_f32_16x16x32_bf16 v[42:45], v[146:149], v[226:229], v[42:45]
	v_mfma_f32_16x16x32_bf16 v[38:41], v[150:153], v[226:229], v[38:41]
	v_mfma_f32_16x16x32_bf16 v[34:37], v[154:157], v[226:229], v[34:37]
	v_mfma_f32_16x16x32_bf16 v[18:21], v[142:145], v[230:233], v[18:21]
	v_mfma_f32_16x16x32_bf16 v[22:25], v[146:149], v[230:233], v[22:25]
	v_mfma_f32_16x16x32_bf16 v[26:29], v[150:153], v[230:233], v[26:29]
	v_mfma_f32_16x16x32_bf16 v[30:33], v[154:157], v[230:233], v[30:33]
	v_mfma_f32_16x16x32_bf16 v[2:5], v[142:145], v[234:237], v[2:5]
	v_mfma_f32_16x16x32_bf16 v[6:9], v[146:149], v[234:237], v[6:9]
	v_mfma_f32_16x16x32_bf16 v[10:13], v[150:153], v[234:237], v[10:13]
	v_mfma_f32_16x16x32_bf16 v[14:17], v[154:157], v[234:237], v[14:17]
	s_waitcnt lgkmcnt(0)
	s_barrier
	s_mov_b32 s47, s42
	s_mov_b32 s42, s43
	s_mov_b32 s43, s44
	s_mov_b32 s44, s47
	s_branch .Lmu_done
.Lmu_grpY:
	s_add_i32 s47, s44, s6
	s_add_u32 s30, s30, 0x80
	s_addc_u32 s31, s31, 0
	s_mov_b32 m0, s47
	s_nop 0
	global_load_lds_dwordx4 v86, s[30:31]
	s_add_i32 m0, s47, 0x2000
	s_nop 0
	global_load_lds_dwordx4 v134, s[30:31]
	s_add_i32 m0, s47, 0x4000
	s_nop 0
	global_load_lds_dwordx4 v136, s[30:31]
	s_add_i32 m0, s47, 0x6000
	s_nop 0
	global_load_lds_dwordx4 v138, s[30:31]
	s_add_i32 m0, s47, 0x8000
	s_nop 0
	global_load_lds_dwordx4 v140, s[30:31]
	s_waitcnt vmcnt(29)
	v_mul_f32_e32 v114, s20, v114
	v_mul_f32_e32 v115, s20, v115
	v_mul_f32_e32 v116, s21, v116
	v_mul_f32_e32 v117, s21, v117
	v_mul_f32_e32 v118, s22, v118
	v_mul_f32_e32 v119, s22, v119
	v_mul_f32_e32 v120, s23, v120
	v_mul_f32_e32 v121, s23, v121
	v_mul_f32_e32 v122, s24, v122
	v_mul_f32_e32 v123, s24, v123
	v_mul_f32_e32 v124, s25, v124
	v_mul_f32_e32 v125, s25, v125
	v_mul_f32_e32 v126, s26, v126
	v_mul_f32_e32 v127, s26, v127
	v_mul_f32_e32 v128, s27, v128
	v_mul_f32_e32 v129, s27, v129
	v_cvt_pk_bf16_f32 v158, v114, v116
	v_cvt_pk_bf16_f32 v159, v118, v120
	v_cvt_pk_bf16_f32 v160, v122, v124
	v_cvt_pk_bf16_f32 v161, v126, v128
	v_cvt_pk_bf16_f32 v162, v115, v117
	v_cvt_pk_bf16_f32 v163, v119, v121
	v_cvt_pk_bf16_f32 v164, v123, v125
	v_cvt_pk_bf16_f32 v165, v127, v129
	ds_write_b128 v1, v[158:161] offset:19456
	ds_write_b128 v1, v[162:165] offset:19584
	v_add_u32_e32 v91, s42, v135
	v_add_u32_e32 v93, s42, v137
	ds_read_b128 v[238:241], v139 offset:0
	ds_read_b128 v[242:245], v139 offset:2048
	ds_read_b128 v[246:249], v139 offset:4096
	ds_read_b128 v[250:253], v139 offset:6144
	ds_read_b128 v[218:221], v91 offset:0
	ds_read_b128 v[222:225], v91 offset:2048
	ds_read_b128 v[226:229], v91 offset:4096
	ds_read_b128 v[230:233], v91 offset:6144
	ds_read_b128 v[234:237], v91 offset:8192
	s_waitcnt lgkmcnt(0)
; #define MU_GLDS_A(buf, kt) do { _Pragma("unroll") for (int i = 0; i < NMU; ++i) \
;         __builtin_amdgcn_global_load_lds((const unsigned*)((const char*)A + aoff[i] + (size_t)(kt) * 128), (PG8_LAS unsigned*)(MU_SA(buf) + wid * 1024 + i * 8192), 16, 0, 0); } while (0)
; #define MU_B_ISSUE(sb, kt) do { const char* kb_ = Bb + (size_t)(kt) * (64 * (size_t)RB); _Pragma("unroll") for (int j = 0; j < 8; ++j) { const char* p_ = kb_ + (size_t)j * RB; \
;         asm volatile("global_load_dwordx2 %0, %1, off" : "=&v"(sb[j]) : "v"(p_) : "memory"); } } while (0)
; #define MU_B_WAIT(sb, N) asm volatile("s_waitcnt vmcnt(%8)" : "+v"(sb[0]), "+v"(sb[1]), "+v"(sb[2]), "+v"(sb[3]), "+v"(sb[4]), "+v"(sb[5]), "+v"(sb[6]), "+v"(sb[7]) : "n"(N) : "memory")
; #define MU_G_LOAD(ga, kt) do { const PG8_LAS f32x4* gk_ = (const PG8_LAS f32x4*)(lds + GAIN_OFF) + 16 * (kt) + 2 * wid; const f32x4 ga_ = gk_[0], gb_ = gk_[1]; \
;         ga[0] = ga_[0]; ga[1] = ga_[1]; ga[2] = ga_[2]; ga[3] = ga_[3]; ga[4] = gb_[0]; ga[5] = gb_[1]; ga[6] = gb_[2]; ga[7] = gb_[3]; } while (0)
; #define MU_COMPUTE(buf) MU_COMPUTE_N(buf, NMU)
; #define MU_END(last) do { if (last) asm volatile("s_waitcnt vmcnt(0)" ::: "memory"); else asm volatile("s_waitcnt vmcnt(8)" ::: "memory"); \
;         asm volatile("s_waitcnt lgkmcnt(0)" ::: "memory"); __builtin_amdgcn_s_barrier(); asm volatile("" ::: "memory"); } while (0)
; template <int MODE>
; __device__ __forceinline__ void moe_unit(PG8_LAS unsigned char* lds, int e, int cb, int slot0  , int nv  , const bf16_t* A, const int* slot_tok,
;                                          const float* W0, const float* W1, bf16_t* OUT, const float* slot_rs  , const int* slot_dst) {
;     ...
;     for (int t = 0; t < nt; t += 2) {
;         if (t + 2 < nt) MU_B_WAIT(s1, 8); else MU_B_WAIT(s1, 0);
;         MU_G_LOAD(g0, t + 1); MU_B_WRITE(s1, 1, g0); __builtin_amdgcn_sched_barrier(0); MU_GLDS_A(1, t + 1); __builtin_amdgcn_sched_barrier(0);
;         if (t + 3 < nt) { MU_B_ISSUE(s1, t + 3); }
;         MU_COMPUTE(0);
;         MU_END(t + 3 >= nt);
;         if (t + 2 < nt) { MU_B_WAIT(s0, 8); MU_G_LOAD(g0, t + 2); MU_B_WRITE(s0, 0, g0); __builtin_amdgcn_sched_barrier(0); MU_GLDS_A(0, t + 2); __builtin_amdgcn_sched_barrier(0); }
;         if (t + 4 < nt) { MU_B_ISSUE(s0, t + 4); }
;         MU_COMPUTE(1);
;         MU_END(t + 4 >= nt);
;     }
	s_load_dwordx8 s[12:19], s[28:29], 0x0
	s_add_u32 s28, s28, 0x100
	s_addc_u32 s29, s29, 0
	v_mfma_f32_16x16x32_bf16 v[78:81], v[238:241], v[218:221], v[78:81]
	v_mfma_f32_16x16x32_bf16 v[74:77], v[242:245], v[218:221], v[74:77]
	v_mfma_f32_16x16x32_bf16 v[70:73], v[246:249], v[218:221], v[70:73]
	v_mfma_f32_16x16x32_bf16 v[66:69], v[250:253], v[218:221], v[66:69]
	ds_read_b128 v[218:221], v93 offset:0
	ds_read_b128 v[142:145], v141 offset:0
	v_lshl_add_u64 v[132:133], v[132:133], 0, s[40:41]
	global_load_dwordx2 v[114:115], v[132:133], off
	global_load_dwordx2 v[116:117], v[132:133], off offset:2048
	v_mfma_f32_16x16x32_bf16 v[62:65], v[238:241], v[222:225], v[62:65]
	v_mfma_f32_16x16x32_bf16 v[58:61], v[242:245], v[222:225], v[58:61]
	v_mfma_f32_16x16x32_bf16 v[54:57], v[246:249], v[222:225], v[54:57]
	v_mfma_f32_16x16x32_bf16 v[50:53], v[250:253], v[222:225], v[50:53]
	ds_read_b128 v[222:225], v93 offset:2048
	ds_read_b128 v[146:149], v141 offset:2048
	v_lshl_add_u64 v[166:167], v[132:133], 0, s[34:35]
	global_load_dwordx2 v[118:119], v[166:167], off
	global_load_dwordx2 v[120:121], v[166:167], off offset:2048
	v_mfma_f32_16x16x32_bf16 v[46:49], v[238:241], v[226:229], v[46:49]
	v_mfma_f32_16x16x32_bf16 v[42:45], v[242:245], v[226:229], v[42:45]
	v_mfma_f32_16x16x32_bf16 v[38:41], v[246:249], v[226:229], v[38:41]
	v_mfma_f32_16x16x32_bf16 v[34:37], v[250:253], v[226:229], v[34:37]
	ds_read_b128 v[226:229], v93 offset:4096
	ds_read_b128 v[150:153], v141 offset:4096
	v_lshl_add_u64 v[166:167], v[132:133], 0, s[36:37]
	global_load_dwordx2 v[122:123], v[166:167], off
	global_load_dwordx2 v[124:125], v[166:167], off offset:2048
	v_mfma_f32_16x16x32_bf16 v[18:21], v[238:241], v[230:233], v[18:21]
	v_mfma_f32_16x16x32_bf16 v[22:25], v[242:245], v[230:233], v[22:25]
	v_mfma_f32_16x16x32_bf16 v[26:29], v[246:249], v[230:233], v[26:29]
	v_mfma_f32_16x16x32_bf16 v[30:33], v[250:253], v[230:233], v[30:33]
	ds_read_b128 v[230:233], v93 offset:6144
	ds_read_b128 v[154:157], v141 offset:6144
	v_lshl_add_u64 v[166:167], v[132:133], 0, s[38:39]
	global_load_dwordx2 v[126:127], v[166:167], off
	global_load_dwordx2 v[128:129], v[166:167], off offset:2048
	v_mfma_f32_16x16x32_bf16 v[2:5], v[238:241], v[234:237], v[2:5]
	v_mfma_f32_16x16x32_bf16 v[6:9], v[242:245], v[234:237], v[6:9]
	v_mfma_f32_16x16x32_bf16 v[10:13], v[246:249], v[234:237], v[10:13]
	v_mfma_f32_16x16x32_bf16 v[14:17], v[250:253], v[234:237], v[14:17]
	ds_read_b128 v[234:237], v93 offset:8192
	s_waitcnt lgkmcnt(0)
	s_barrier
	s_mov_b32 s47, s42
	s_mov_b32 s42, s43
	s_mov_b32 s43, s44
	s_mov_b32 s44, s47
	s_add_i32 s47, s44, s6
	s_add_u32 s30, s30, 0x80
	s_addc_u32 s31, s31, 0
	v_mfma_f32_16x16x32_bf16 v[78:81], v[142:145], v[218:221], v[78:81]
	v_mfma_f32_16x16x32_bf16 v[74:77], v[146:149], v[218:221], v[74:77]
	v_mfma_f32_16x16x32_bf16 v[70:73], v[150:153], v[218:221], v[70:73]
	v_mfma_f32_16x16x32_bf16 v[66:69], v[154:157], v[218:221], v[66:69]
	s_mov_b32 m0, s47
	s_nop 0
	global_load_lds_dwordx4 v86, s[30:31]
	v_mfma_f32_16x16x32_bf16 v[62:65], v[142:145], v[222:225], v[62:65]
	v_mfma_f32_16x16x32_bf16 v[58:61], v[146:149], v[222:225], v[58:61]
	v_mfma_f32_16x16x32_bf16 v[54:57], v[150:153], v[222:225], v[54:57]
	v_mfma_f32_16x16x32_bf16 v[50:53], v[154:157], v[222:225], v[50:53]
	s_add_i32 m0, s47, 0x2000
	s_nop 0
	global_load_lds_dwordx4 v134, s[30:31]
	v_mfma_f32_16x16x32_bf16 v[46:49], v[142:145], v[226:229], v[46:49]
	v_mfma_f32_16x16x32_bf16 v[42:45], v[146:149], v[226:229], v[42:45]
	v_mfma_f32_16x16x32_bf16 v[38:41], v[150:153], v[226:229], v[38:41]
	v_mfma_f32_16x16x32_bf16 v[34:37], v[154:157], v[226:229], v[34:37]
	s_add_i32 m0, s47, 0x4000
	s_nop 0
	global_load_lds_dwordx4 v136, s[30:31]
	v_mfma_f32_16x16x32_bf16 v[18:21], v[142:145], v[230:233], v[18:21]
	v_mfma_f32_16x16x32_bf16 v[22:25], v[146:149], v[230:233], v[22:25]
	v_mfma_f32_16x16x32_bf16 v[26:29], v[150:153], v[230:233], v[26:29]
	v_mfma_f32_16x16x32_bf16 v[30:33], v[154:157], v[230:233], v[30:33]
	s_add_i32 m0, s47, 0x6000
	s_nop 0
	global_load_lds_dwordx4 v138, s[30:31]
	v_mfma_f32_16x16x32_bf16 v[2:5], v[142:145], v[234:237], v[2:5]
	v_mfma_f32_16x16x32_bf16 v[6:9], v[146:149], v[234:237], v[6:9]
	v_mfma_f32_16x16x32_bf16 v[10:13], v[150:153], v[234:237], v[10:13]
	v_mfma_f32_16x16x32_bf16 v[14:17], v[154:157], v[234:237], v[14:17]
	s_add_i32 m0, s47, 0x8000
	s_nop 0
	global_load_lds_dwordx4 v140, s[30:31]
	s_waitcnt vmcnt(34)
	v_mul_f32_e32 v186, s12, v186
	v_mul_f32_e32 v187, s12, v187
	v_mul_f32_e32 v188, s13, v188
	v_mul_f32_e32 v189, s13, v189
	v_mul_f32_e32 v190, s14, v190
	v_mul_f32_e32 v191, s14, v191
	v_mul_f32_e32 v192, s15, v192
	v_mul_f32_e32 v193, s15, v193
	v_mul_f32_e32 v194, s16, v194
	v_mul_f32_e32 v195, s16, v195
	v_mul_f32_e32 v196, s17, v196
	v_mul_f32_e32 v197, s17, v197
	v_mul_f32_e32 v198, s18, v198
	v_mul_f32_e32 v199, s18, v199
	v_mul_f32_e32 v200, s19, v200
	v_mul_f32_e32 v201, s19, v201
	v_cvt_pk_bf16_f32 v158, v186, v188
	v_cvt_pk_bf16_f32 v159, v190, v192
	v_cvt_pk_bf16_f32 v160, v194, v196
	v_cvt_pk_bf16_f32 v161, v198, v200
	v_cvt_pk_bf16_f32 v162, v187, v189
	v_cvt_pk_bf16_f32 v163, v191, v193
	v_cvt_pk_bf16_f32 v164, v195, v197
	v_cvt_pk_bf16_f32 v165, v199, v201
	ds_write_b128 v1, v[158:161] offset:0
	ds_write_b128 v1, v[162:165] offset:128
	v_add_u32_e32 v91, s42, v135
	v_add_u32_e32 v93, s42, v137
	ds_read_b128 v[238:241], v139 offset:19456
	ds_read_b128 v[242:245], v139 offset:21504
	ds_read_b128 v[246:249], v139 offset:23552
	ds_read_b128 v[250:253], v139 offset:25600
	ds_read_b128 v[218:221], v91 offset:0
	ds_read_b128 v[222:225], v91 offset:2048
	ds_read_b128 v[226:229], v91 offset:4096
	ds_read_b128 v[230:233], v91 offset:6144
	ds_read_b128 v[234:237], v91 offset:8192
	s_waitcnt lgkmcnt(0)
; #define MU_GLDS_A(buf, kt) do { _Pragma("unroll") for (int i = 0; i < NMU; ++i) \
;         __builtin_amdgcn_global_load_lds((const unsigned*)((const char*)A + aoff[i] + (size_t)(kt) * 128), (PG8_LAS unsigned*)(MU_SA(buf) + wid * 1024 + i * 8192), 16, 0, 0); } while (0)
; #define MU_B_ISSUE(sb, kt) do { const char* kb_ = Bb + (size_t)(kt) * (64 * (size_t)RB); _Pragma("unroll") for (int j = 0; j < 8; ++j) { const char* p_ = kb_ + (size_t)j * RB; \
;         asm volatile("global_load_dwordx2 %0, %1, off" : "=&v"(sb[j]) : "v"(p_) : "memory"); } } while (0)
; #define MU_B_WAIT(sb, N) asm volatile("s_waitcnt vmcnt(%8)" : "+v"(sb[0]), "+v"(sb[1]), "+v"(sb[2]), "+v"(sb[3]), "+v"(sb[4]), "+v"(sb[5]), "+v"(sb[6]), "+v"(sb[7]) : "n"(N) : "memory")
; #define MU_G_LOAD(ga, kt) do { const PG8_LAS f32x4* gk_ = (const PG8_LAS f32x4*)(lds + GAIN_OFF) + 16 * (kt) + 2 * wid; const f32x4 ga_ = gk_[0], gb_ = gk_[1]; \
;         ga[0] = ga_[0]; ga[1] = ga_[1]; ga[2] = ga_[2]; ga[3] = ga_[3]; ga[4] = gb_[0]; ga[5] = gb_[1]; ga[6] = gb_[2]; ga[7] = gb_[3]; } while (0)
; #define MU_COMPUTE(buf) MU_COMPUTE_N(buf, NMU)
; #define MU_END(last) do { if (last) asm volatile("s_waitcnt vmcnt(0)" ::: "memory"); else asm volatile("s_waitcnt vmcnt(8)" ::: "memory"); \
;         asm volatile("s_waitcnt lgkmcnt(0)" ::: "memory"); __builtin_amdgcn_s_barrier(); asm volatile("" ::: "memory"); } while (0)
; template <int MODE>
; __device__ __forceinline__ void moe_unit(PG8_LAS unsigned char* lds, int e, int cb, int slot0  , int nv  , const bf16_t* A, const int* slot_tok,
;                                          const float* W0, const float* W1, bf16_t* OUT, const float* slot_rs  , const int* slot_dst) {
;     ...
;     for (int t = 0; t < nt; t += 2) {
;         if (t + 2 < nt) MU_B_WAIT(s1, 8); else MU_B_WAIT(s1, 0);
;         MU_G_LOAD(g0, t + 1); MU_B_WRITE(s1, 1, g0); __builtin_amdgcn_sched_barrier(0); MU_GLDS_A(1, t + 1); __builtin_amdgcn_sched_barrier(0);
;         if (t + 3 < nt) { MU_B_ISSUE(s1, t + 3); }
;         MU_COMPUTE(0);
;         MU_END(t + 3 >= nt);
;         if (t + 2 < nt) { MU_B_WAIT(s0, 8); MU_G_LOAD(g0, t + 2); MU_B_WRITE(s0, 0, g0); __builtin_amdgcn_sched_barrier(0); MU_GLDS_A(0, t + 2); __builtin_amdgcn_sched_barrier(0); }
;         if (t + 4 < nt) { MU_B_ISSUE(s0, t + 4); }
;         MU_COMPUTE(1);
;         MU_END(t + 4 >= nt);
;     }
	s_load_dwordx8 s[20:27], s[28:29], 0x0
	s_add_u32 s28, s28, 0x100
	s_addc_u32 s29, s29, 0
	v_mfma_f32_16x16x32_bf16 v[78:81], v[238:241], v[218:221], v[78:81]
	v_mfma_f32_16x16x32_bf16 v[74:77], v[242:245], v[218:221], v[74:77]
	v_mfma_f32_16x16x32_bf16 v[70:73], v[246:249], v[218:221], v[70:73]
	v_mfma_f32_16x16x32_bf16 v[66:69], v[250:253], v[218:221], v[66:69]
	ds_read_b128 v[218:221], v93 offset:0
	ds_read_b128 v[142:145], v141 offset:19456
	v_lshl_add_u64 v[132:133], v[132:133], 0, s[40:41]
	global_load_dwordx2 v[186:187], v[132:133], off
	global_load_dwordx2 v[188:189], v[132:133], off offset:2048
	v_mfma_f32_16x16x32_bf16 v[62:65], v[238:241], v[222:225], v[62:65]
	v_mfma_f32_16x16x32_bf16 v[58:61], v[242:245], v[222:225], v[58:61]
	v_mfma_f32_16x16x32_bf16 v[54:57], v[246:249], v[222:225], v[54:57]
	v_mfma_f32_16x16x32_bf16 v[50:53], v[250:253], v[222:225], v[50:53]
	ds_read_b128 v[222:225], v93 offset:2048
	ds_read_b128 v[146:149], v141 offset:21504
	v_lshl_add_u64 v[166:167], v[132:133], 0, s[34:35]
	global_load_dwordx2 v[190:191], v[166:167], off
	global_load_dwordx2 v[192:193], v[166:167], off offset:2048
	v_mfma_f32_16x16x32_bf16 v[46:49], v[238:241], v[226:229], v[46:49]
	v_mfma_f32_16x16x32_bf16 v[42:45], v[242:245], v[226:229], v[42:45]
	v_mfma_f32_16x16x32_bf16 v[38:41], v[246:249], v[226:229], v[38:41]
	v_mfma_f32_16x16x32_bf16 v[34:37], v[250:253], v[226:229], v[34:37]
	ds_read_b128 v[226:229], v93 offset:4096
	ds_read_b128 v[150:153], v141 offset:23552
	v_lshl_add_u64 v[166:167], v[132:133], 0, s[36:37]
	global_load_dwordx2 v[194:195], v[166:167], off
	global_load_dwordx2 v[196:197], v[166:167], off offset:2048
	v_mfma_f32_16x16x32_bf16 v[18:21], v[238:241], v[230:233], v[18:21]
	v_mfma_f32_16x16x32_bf16 v[22:25], v[242:245], v[230:233], v[22:25]
	v_mfma_f32_16x16x32_bf16 v[26:29], v[246:249], v[230:233], v[26:29]
	v_mfma_f32_16x16x32_bf16 v[30:33], v[250:253], v[230:233], v[30:33]
	ds_read_b128 v[230:233], v93 offset:6144
	ds_read_b128 v[154:157], v141 offset:25600
	v_lshl_add_u64 v[166:167], v[132:133], 0, s[38:39]
	global_load_dwordx2 v[198:199], v[166:167], off
	global_load_dwordx2 v[200:201], v[166:167], off offset:2048
	v_mfma_f32_16x16x32_bf16 v[2:5], v[238:241], v[234:237], v[2:5]
	v_mfma_f32_16x16x32_bf16 v[6:9], v[242:245], v[234:237], v[6:9]
	v_mfma_f32_16x16x32_bf16 v[10:13], v[246:249], v[234:237], v[10:13]
	v_mfma_f32_16x16x32_bf16 v[14:17], v[250:253], v[234:237], v[14:17]
	ds_read_b128 v[234:237], v93 offset:8192
	s_waitcnt vmcnt(21)
	s_waitcnt lgkmcnt(0)
	s_barrier
	s_mov_b32 s47, s42
	s_mov_b32 s42, s43
	s_mov_b32 s43, s44
	s_mov_b32 s44, s47
	s_add_i32 s47, s44, s6
	s_add_u32 s30, s30, 0x80
	s_addc_u32 s31, s31, 0
	v_mfma_f32_16x16x32_bf16 v[78:81], v[142:145], v[218:221], v[78:81]
	v_mfma_f32_16x16x32_bf16 v[74:77], v[146:149], v[218:221], v[74:77]
	v_mfma_f32_16x16x32_bf16 v[70:73], v[150:153], v[218:221], v[70:73]
	v_mfma_f32_16x16x32_bf16 v[66:69], v[154:157], v[218:221], v[66:69]
	s_mov_b32 m0, s47
	s_nop 0
	global_load_lds_dwordx4 v86, s[30:31]
	v_mfma_f32_16x16x32_bf16 v[62:65], v[142:145], v[222:225], v[62:65]
	v_mfma_f32_16x16x32_bf16 v[58:61], v[146:149], v[222:225], v[58:61]
	v_mfma_f32_16x16x32_bf16 v[54:57], v[150:153], v[222:225], v[54:57]
	v_mfma_f32_16x16x32_bf16 v[50:53], v[154:157], v[222:225], v[50:53]
	s_add_i32 m0, s47, 0x2000
	s_nop 0
	global_load_lds_dwordx4 v134, s[30:31]
	v_mfma_f32_16x16x32_bf16 v[46:49], v[142:145], v[226:229], v[46:49]
	v_mfma_f32_16x16x32_bf16 v[42:45], v[146:149], v[226:229], v[42:45]
	v_mfma_f32_16x16x32_bf16 v[38:41], v[150:153], v[226:229], v[38:41]
	v_mfma_f32_16x16x32_bf16 v[34:37], v[154:157], v[226:229], v[34:37]
	s_add_i32 m0, s47, 0x4000
	s_nop 0
	global_load_lds_dwordx4 v136, s[30:31]
	v_mfma_f32_16x16x32_bf16 v[18:21], v[142:145], v[230:233], v[18:21]
	v_mfma_f32_16x16x32_bf16 v[22:25], v[146:149], v[230:233], v[22:25]
	v_mfma_f32_16x16x32_bf16 v[26:29], v[150:153], v[230:233], v[26:29]
	v_mfma_f32_16x16x32_bf16 v[30:33], v[154:157], v[230:233], v[30:33]
	s_add_i32 m0, s47, 0x6000
	s_nop 0
	global_load_lds_dwordx4 v138, s[30:31]
	v_mfma_f32_16x16x32_bf16 v[2:5], v[142:145], v[234:237], v[2:5]
	v_mfma_f32_16x16x32_bf16 v[6:9], v[146:149], v[234:237], v[6:9]
	v_mfma_f32_16x16x32_bf16 v[10:13], v[150:153], v[234:237], v[10:13]
	v_mfma_f32_16x16x32_bf16 v[14:17], v[154:157], v[234:237], v[14:17]
	s_add_i32 m0, s47, 0x8000
	s_nop 0
	global_load_lds_dwordx4 v140, s[30:31]
	v_mul_f32_e32 v202, s20, v202
	v_mul_f32_e32 v203, s20, v203
	v_mul_f32_e32 v204, s21, v204
	v_mul_f32_e32 v205, s21, v205
	v_mul_f32_e32 v206, s22, v206
	v_mul_f32_e32 v207, s22, v207
	v_mul_f32_e32 v208, s23, v208
	v_mul_f32_e32 v209, s23, v209
	v_mul_f32_e32 v210, s24, v210
	v_mul_f32_e32 v211, s24, v211
	v_mul_f32_e32 v212, s25, v212
	v_mul_f32_e32 v213, s25, v213
	v_mul_f32_e32 v214, s26, v214
	v_mul_f32_e32 v215, s26, v215
	v_mul_f32_e32 v216, s27, v216
	v_mul_f32_e32 v217, s27, v217
	v_cvt_pk_bf16_f32 v158, v202, v204
	v_cvt_pk_bf16_f32 v159, v206, v208
	v_cvt_pk_bf16_f32 v160, v210, v212
	v_cvt_pk_bf16_f32 v161, v214, v216
	v_cvt_pk_bf16_f32 v162, v203, v205
	v_cvt_pk_bf16_f32 v163, v207, v209
	v_cvt_pk_bf16_f32 v164, v211, v213
	v_cvt_pk_bf16_f32 v165, v215, v217
	ds_write_b128 v1, v[158:161] offset:19456
	ds_write_b128 v1, v[162:165] offset:19584
	v_add_u32_e32 v91, s42, v135
	v_add_u32_e32 v93, s42, v137
	ds_read_b128 v[238:241], v139 offset:0
	ds_read_b128 v[242:245], v139 offset:2048
	ds_read_b128 v[246:249], v139 offset:4096
	ds_read_b128 v[250:253], v139 offset:6144
	ds_read_b128 v[218:221], v91 offset:0
	ds_read_b128 v[222:225], v91 offset:2048
	ds_read_b128 v[226:229], v91 offset:4096
	ds_read_b128 v[230:233], v91 offset:6144
	ds_read_b128 v[234:237], v91 offset:8192
	s_waitcnt lgkmcnt(0)
; #define MU_GLDS_A(buf, kt) do { _Pragma("unroll") for (int i = 0; i < NMU; ++i) \
;         __builtin_amdgcn_global_load_lds((const unsigned*)((const char*)A + aoff[i] + (size_t)(kt) * 128), (PG8_LAS unsigned*)(MU_SA(buf) + wid * 1024 + i * 8192), 16, 0, 0); } while (0)
; #define MU_B_ISSUE(sb, kt) do { const char* kb_ = Bb + (size_t)(kt) * (64 * (size_t)RB); _Pragma("unroll") for (int j = 0; j < 8; ++j) { const char* p_ = kb_ + (size_t)j * RB; \
;         asm volatile("global_load_dwordx2 %0, %1, off" : "=&v"(sb[j]) : "v"(p_) : "memory"); } } while (0)
; #define MU_B_WAIT(sb, N) asm volatile("s_waitcnt vmcnt(%8)" : "+v"(sb[0]), "+v"(sb[1]), "+v"(sb[2]), "+v"(sb[3]), "+v"(sb[4]), "+v"(sb[5]), "+v"(sb[6]), "+v"(sb[7]) : "n"(N) : "memory")
; #define MU_G_LOAD(ga, kt) do { const PG8_LAS f32x4* gk_ = (const PG8_LAS f32x4*)(lds + GAIN_OFF) + 16 * (kt) + 2 * wid; const f32x4 ga_ = gk_[0], gb_ = gk_[1]; \
;         ga[0] = ga_[0]; ga[1] = ga_[1]; ga[2] = ga_[2]; ga[3] = ga_[3]; ga[4] = gb_[0]; ga[5] = gb_[1]; ga[6] = gb_[2]; ga[7] = gb_[3]; } while (0)
; #define MU_COMPUTE(buf) MU_COMPUTE_N(buf, NMU)
; #define MU_END(last) do { if (last) asm volatile("s_waitcnt vmcnt(0)" ::: "memory"); else asm volatile("s_waitcnt vmcnt(8)" ::: "memory"); \
;         asm volatile("s_waitcnt lgkmcnt(0)" ::: "memory"); __builtin_amdgcn_s_barrier(); asm volatile("" ::: "memory"); } while (0)
; template <int MODE>
; __device__ __forceinline__ void moe_unit(PG8_LAS unsigned char* lds, int e, int cb, int slot0  , int nv  , const bf16_t* A, const int* slot_tok,
;                                          const float* W0, const float* W1, bf16_t* OUT, const float* slot_rs  , const int* slot_dst) {
;     ...
;     for (int t = 0; t < nt; t += 2) {
;         if (t + 2 < nt) MU_B_WAIT(s1, 8); else MU_B_WAIT(s1, 0);
;         MU_G_LOAD(g0, t + 1); MU_B_WRITE(s1, 1, g0); __builtin_amdgcn_sched_barrier(0); MU_GLDS_A(1, t + 1); __builtin_amdgcn_sched_barrier(0);
;         if (t + 3 < nt) { MU_B_ISSUE(s1, t + 3); }
;         MU_COMPUTE(0);
;         MU_END(t + 3 >= nt);
;         if (t + 2 < nt) { MU_B_WAIT(s0, 8); MU_G_LOAD(g0, t + 2); MU_B_WRITE(s0, 0, g0); __builtin_amdgcn_sched_barrier(0); MU_GLDS_A(0, t + 2); __builtin_amdgcn_sched_barrier(0); }
;         if (t + 4 < nt) { MU_B_ISSUE(s0, t + 4); }
;         MU_COMPUTE(1);
;         MU_END(t + 4 >= nt);
;     }
	s_load_dwordx8 s[12:19], s[28:29], 0x0
	s_add_u32 s28, s28, 0x100
	s_addc_u32 s29, s29, 0
	v_mfma_f32_16x16x32_bf16 v[78:81], v[238:241], v[218:221], v[78:81]
	v_mfma_f32_16x16x32_bf16 v[74:77], v[242:245], v[218:221], v[74:77]
	v_mfma_f32_16x16x32_bf16 v[70:73], v[246:249], v[218:221], v[70:73]
	v_mfma_f32_16x16x32_bf16 v[66:69], v[250:253], v[218:221], v[66:69]
	ds_read_b128 v[218:221], v93 offset:0
	ds_read_b128 v[142:145], v141 offset:0
	v_lshl_add_u64 v[132:133], v[132:133], 0, s[40:41]
	global_load_dwordx2 v[202:203], v[132:133], off
	global_load_dwordx2 v[204:205], v[132:133], off offset:2048
	v_mfma_f32_16x16x32_bf16 v[62:65], v[238:241], v[222:225], v[62:65]
	v_mfma_f32_16x16x32_bf16 v[58:61], v[242:245], v[222:225], v[58:61]
	v_mfma_f32_16x16x32_bf16 v[54:57], v[246:249], v[222:225], v[54:57]
	v_mfma_f32_16x16x32_bf16 v[50:53], v[250:253], v[222:225], v[50:53]
	ds_read_b128 v[222:225], v93 offset:2048
	ds_read_b128 v[146:149], v141 offset:2048
	v_lshl_add_u64 v[166:167], v[132:133], 0, s[34:35]
	global_load_dwordx2 v[206:207], v[166:167], off
	global_load_dwordx2 v[208:209], v[166:167], off offset:2048
	v_mfma_f32_16x16x32_bf16 v[46:49], v[238:241], v[226:229], v[46:49]
	v_mfma_f32_16x16x32_bf16 v[42:45], v[242:245], v[226:229], v[42:45]
	v_mfma_f32_16x16x32_bf16 v[38:41], v[246:249], v[226:229], v[38:41]
	v_mfma_f32_16x16x32_bf16 v[34:37], v[250:253], v[226:229], v[34:37]
	ds_read_b128 v[226:229], v93 offset:4096
	ds_read_b128 v[150:153], v141 offset:4096
	v_lshl_add_u64 v[166:167], v[132:133], 0, s[36:37]
	global_load_dwordx2 v[210:211], v[166:167], off
	global_load_dwordx2 v[212:213], v[166:167], off offset:2048
	v_mfma_f32_16x16x32_bf16 v[18:21], v[238:241], v[230:233], v[18:21]
	v_mfma_f32_16x16x32_bf16 v[22:25], v[242:245], v[230:233], v[22:25]
	v_mfma_f32_16x16x32_bf16 v[26:29], v[246:249], v[230:233], v[26:29]
	v_mfma_f32_16x16x32_bf16 v[30:33], v[250:253], v[230:233], v[30:33]
	ds_read_b128 v[230:233], v93 offset:6144
	ds_read_b128 v[154:157], v141 offset:6144
	v_lshl_add_u64 v[166:167], v[132:133], 0, s[38:39]
	global_load_dwordx2 v[214:215], v[166:167], off
	global_load_dwordx2 v[216:217], v[166:167], off offset:2048
	v_mfma_f32_16x16x32_bf16 v[2:5], v[238:241], v[234:237], v[2:5]
	v_mfma_f32_16x16x32_bf16 v[6:9], v[242:245], v[234:237], v[6:9]
	v_mfma_f32_16x16x32_bf16 v[10:13], v[246:249], v[234:237], v[10:13]
	v_mfma_f32_16x16x32_bf16 v[14:17], v[250:253], v[234:237], v[14:17]
	ds_read_b128 v[234:237], v93 offset:8192
	s_waitcnt vmcnt(21)
	s_waitcnt lgkmcnt(0)
	s_barrier
	s_mov_b32 s47, s42
	s_mov_b32 s42, s43
	s_mov_b32 s43, s44
	s_mov_b32 s44, s47
	s_add_i32 s47, s44, s6
	s_add_u32 s30, s30, 0x80
	s_addc_u32 s31, s31, 0
	v_mfma_f32_16x16x32_bf16 v[78:81], v[142:145], v[218:221], v[78:81]
	v_mfma_f32_16x16x32_bf16 v[74:77], v[146:149], v[218:221], v[74:77]
	v_mfma_f32_16x16x32_bf16 v[70:73], v[150:153], v[218:221], v[70:73]
	v_mfma_f32_16x16x32_bf16 v[66:69], v[154:157], v[218:221], v[66:69]
	s_mov_b32 m0, s47
	s_nop 0
	global_load_lds_dwordx4 v86, s[30:31]
	v_mfma_f32_16x16x32_bf16 v[62:65], v[142:145], v[222:225], v[62:65]
	v_mfma_f32_16x16x32_bf16 v[58:61], v[146:149], v[222:225], v[58:61]
	v_mfma_f32_16x16x32_bf16 v[54:57], v[150:153], v[222:225], v[54:57]
	v_mfma_f32_16x16x32_bf16 v[50:53], v[154:157], v[222:225], v[50:53]
	s_add_i32 m0, s47, 0x2000
	s_nop 0
	global_load_lds_dwordx4 v134, s[30:31]
	v_mfma_f32_16x16x32_bf16 v[46:49], v[142:145], v[226:229], v[46:49]
	v_mfma_f32_16x16x32_bf16 v[42:45], v[146:149], v[226:229], v[42:45]
	v_mfma_f32_16x16x32_bf16 v[38:41], v[150:153], v[226:229], v[38:41]
	v_mfma_f32_16x16x32_bf16 v[34:37], v[154:157], v[226:229], v[34:37]
	s_add_i32 m0, s47, 0x4000
	s_nop 0
	global_load_lds_dwordx4 v136, s[30:31]
	v_mfma_f32_16x16x32_bf16 v[18:21], v[142:145], v[230:233], v[18:21]
	v_mfma_f32_16x16x32_bf16 v[22:25], v[146:149], v[230:233], v[22:25]
	v_mfma_f32_16x16x32_bf16 v[26:29], v[150:153], v[230:233], v[26:29]
	v_mfma_f32_16x16x32_bf16 v[30:33], v[154:157], v[230:233], v[30:33]
	s_add_i32 m0, s47, 0x6000
	s_nop 0
	global_load_lds_dwordx4 v138, s[30:31]
	v_mfma_f32_16x16x32_bf16 v[2:5], v[142:145], v[234:237], v[2:5]
	v_mfma_f32_16x16x32_bf16 v[6:9], v[146:149], v[234:237], v[6:9]
	v_mfma_f32_16x16x32_bf16 v[10:13], v[150:153], v[234:237], v[10:13]
	v_mfma_f32_16x16x32_bf16 v[14:17], v[154:157], v[234:237], v[14:17]
	s_add_i32 m0, s47, 0x8000
	s_nop 0
	global_load_lds_dwordx4 v140, s[30:31]
	v_mul_f32_e32 v98, s12, v98
	v_mul_f32_e32 v99, s12, v99
	v_mul_f32_e32 v100, s13, v100
	v_mul_f32_e32 v101, s13, v101
	v_mul_f32_e32 v102, s14, v102
	v_mul_f32_e32 v103, s14, v103
	v_mul_f32_e32 v104, s15, v104
	v_mul_f32_e32 v105, s15, v105
	v_mul_f32_e32 v106, s16, v106
	v_mul_f32_e32 v107, s16, v107
	v_mul_f32_e32 v108, s17, v108
	v_mul_f32_e32 v109, s17, v109
	v_mul_f32_e32 v110, s18, v110
	v_mul_f32_e32 v111, s18, v111
	v_mul_f32_e32 v112, s19, v112
	v_mul_f32_e32 v113, s19, v113
	v_cvt_pk_bf16_f32 v158, v98, v100
	v_cvt_pk_bf16_f32 v159, v102, v104
	v_cvt_pk_bf16_f32 v160, v106, v108
	v_cvt_pk_bf16_f32 v161, v110, v112
	v_cvt_pk_bf16_f32 v162, v99, v101
	v_cvt_pk_bf16_f32 v163, v103, v105
	v_cvt_pk_bf16_f32 v164, v107, v109
	v_cvt_pk_bf16_f32 v165, v111, v113
	ds_write_b128 v1, v[158:161] offset:0
	ds_write_b128 v1, v[162:165] offset:128
	v_add_u32_e32 v91, s42, v135
	v_add_u32_e32 v93, s42, v137
	ds_read_b128 v[238:241], v139 offset:19456
	ds_read_b128 v[242:245], v139 offset:21504
	ds_read_b128 v[246:249], v139 offset:23552
	ds_read_b128 v[250:253], v139 offset:25600
	ds_read_b128 v[218:221], v91 offset:0
	ds_read_b128 v[222:225], v91 offset:2048
	ds_read_b128 v[226:229], v91 offset:4096
	ds_read_b128 v[230:233], v91 offset:6144
	ds_read_b128 v[234:237], v91 offset:8192
	s_waitcnt lgkmcnt(0)
; #define MU_GLDS_A(buf, kt) do { _Pragma("unroll") for (int i = 0; i < NMU; ++i) \
;         __builtin_amdgcn_global_load_lds((const unsigned*)((const char*)A + aoff[i] + (size_t)(kt) * 128), (PG8_LAS unsigned*)(MU_SA(buf) + wid * 1024 + i * 8192), 16, 0, 0); } while (0)
; #define MU_B_ISSUE(sb, kt) do { const char* kb_ = Bb + (size_t)(kt) * (64 * (size_t)RB); _Pragma("unroll") for (int j = 0; j < 8; ++j) { const char* p_ = kb_ + (size_t)j * RB; \
;         asm volatile("global_load_dwordx2 %0, %1, off" : "=&v"(sb[j]) : "v"(p_) : "memory"); } } while (0)
; #define MU_B_WAIT(sb, N) asm volatile("s_waitcnt vmcnt(%8)" : "+v"(sb[0]), "+v"(sb[1]), "+v"(sb[2]), "+v"(sb[3]), "+v"(sb[4]), "+v"(sb[5]), "+v"(sb[6]), "+v"(sb[7]) : "n"(N) : "memory")
; #define MU_COMPUTE(buf) MU_COMPUTE_N(buf, NMU)
; template <int MODE>
; __device__ __forceinline__ void moe_unit(PG8_LAS unsigned char* lds, int e, int cb, int slot0  , int nv  , const bf16_t* A, const int* slot_tok,
;                                          const float* W0, const float* W1, bf16_t* OUT, const float* slot_rs  , const int* slot_dst) {
;     ...
;     f32x4 acc[NMU][4];
; #pragma unroll
;     for (int m = 0; m < NMU; ++m)
; #pragma unroll
;         for (int n = 0; n < 4; ++n) acc[m][n] = (f32x4){0.f, 0.f, 0.f, 0.f};
;     f32x2 s0[8], s1[8];
;     float g0[8];
;     MU_GLDS_A(0, 0); MU_B_ISSUE(s0, 0); MU_G_LOAD(g0, 0); MU_B_ISSUE(s1, 1);
;     MU_B_WAIT(s0, 8); MU_B_WRITE(s0, 0, g0); __builtin_amdgcn_sched_barrier(0); MU_B_ISSUE(s0, 2);
;     asm volatile("s_waitcnt vmcnt(16)" ::: "memory");
;     asm volatile("s_waitcnt lgkmcnt(0)" ::: "memory"); __builtin_amdgcn_s_barrier(); asm volatile("" ::: "memory");
; #pragma unroll 1
;     for (int t = 0; t < nt; t += 2) {
;         if (t + 2 < nt) MU_B_WAIT(s1, 8); else MU_B_WAIT(s1, 0);
;         MU_G_LOAD(g0, t + 1); MU_B_WRITE(s1, 1, g0); __builtin_amdgcn_sched_barrier(0); MU_GLDS_A(1, t + 1); __builtin_amdgcn_sched_barrier(0);
;         if (t + 3 < nt) { MU_B_ISSUE(s1, t + 3); }
;         MU_COMPUTE(0);
;         MU_END(t + 3 >= nt);
;         if (t + 2 < nt) { MU_B_WAIT(s0, 8); MU_G_LOAD(g0, t + 2); MU_B_WRITE(s0, 0, g0); __builtin_amdgcn_sched_barrier(0); MU_GLDS_A(0, t + 2); __builtin_amdgcn_sched_barrier(0); }
;         if (t + 4 < nt) { MU_B_ISSUE(s0, t + 4); }
;         MU_COMPUTE(1);
;         MU_END(t + 4 >= nt);
	s_load_dwordx8 s[20:27], s[28:29], 0x0
	s_add_u32 s28, s28, 0x100
	s_addc_u32 s29, s29, 0
	v_mfma_f32_16x16x32_bf16 v[78:81], v[238:241], v[218:221], v[78:81]
	v_mfma_f32_16x16x32_bf16 v[74:77], v[242:245], v[218:221], v[74:77]
	v_mfma_f32_16x16x32_bf16 v[70:73], v[246:249], v[218:221], v[70:73]
	v_mfma_f32_16x16x32_bf16 v[66:69], v[250:253], v[218:221], v[66:69]
	ds_read_b128 v[218:221], v93 offset:0
	ds_read_b128 v[142:145], v141 offset:19456
	v_lshl_add_u64 v[132:133], v[132:133], 0, s[40:41]
	global_load_dwordx2 v[98:99], v[132:133], off
	global_load_dwordx2 v[100:101], v[132:133], off offset:2048
	v_mfma_f32_16x16x32_bf16 v[62:65], v[238:241], v[222:225], v[62:65]
	v_mfma_f32_16x16x32_bf16 v[58:61], v[242:245], v[222:225], v[58:61]
	v_mfma_f32_16x16x32_bf16 v[54:57], v[246:249], v[222:225], v[54:57]
	v_mfma_f32_16x16x32_bf16 v[50:53], v[250:253], v[222:225], v[50:53]
	ds_read_b128 v[222:225], v93 offset:2048
	ds_read_b128 v[146:149], v141 offset:21504
	v_lshl_add_u64 v[166:167], v[132:133], 0, s[34:35]
	global_load_dwordx2 v[102:103], v[166:167], off
	global_load_dwordx2 v[104:105], v[166:167], off offset:2048
	v_mfma_f32_16x16x32_bf16 v[46:49], v[238:241], v[226:229], v[46:49]
	v_mfma_f32_16x16x32_bf16 v[42:45], v[242:245], v[226:229], v[42:45]
	v_mfma_f32_16x16x32_bf16 v[38:41], v[246:249], v[226:229], v[38:41]
	v_mfma_f32_16x16x32_bf16 v[34:37], v[250:253], v[226:229], v[34:37]
	ds_read_b128 v[226:229], v93 offset:4096
	ds_read_b128 v[150:153], v141 offset:23552
	v_lshl_add_u64 v[166:167], v[132:133], 0, s[36:37]
	global_load_dwordx2 v[106:107], v[166:167], off
	global_load_dwordx2 v[108:109], v[166:167], off offset:2048
	v_mfma_f32_16x16x32_bf16 v[18:21], v[238:241], v[230:233], v[18:21]
	v_mfma_f32_16x16x32_bf16 v[22:25], v[242:245], v[230:233], v[22:25]
	v_mfma_f32_16x16x32_bf16 v[26:29], v[246:249], v[230:233], v[26:29]
	v_mfma_f32_16x16x32_bf16 v[30:33], v[250:253], v[230:233], v[30:33]
	ds_read_b128 v[230:233], v93 offset:6144
	ds_read_b128 v[154:157], v141 offset:25600
	v_lshl_add_u64 v[166:167], v[132:133], 0, s[38:39]
	global_load_dwordx2 v[110:111], v[166:167], off
	global_load_dwordx2 v[112:113], v[166:167], off offset:2048
	v_mfma_f32_16x16x32_bf16 v[2:5], v[238:241], v[234:237], v[2:5]
	v_mfma_f32_16x16x32_bf16 v[6:9], v[242:245], v[234:237], v[6:9]
	v_mfma_f32_16x16x32_bf16 v[10:13], v[246:249], v[234:237], v[10:13]
	v_mfma_f32_16x16x32_bf16 v[14:17], v[250:253], v[234:237], v[14:17]
	ds_read_b128 v[234:237], v93 offset:8192
	s_waitcnt vmcnt(21)
	s_waitcnt lgkmcnt(0)
	s_barrier
	s_mov_b32 s47, s42
	s_mov_b32 s42, s43
	s_mov_b32 s43, s44
	s_mov_b32 s44, s47
	s_mov_b32 s46, 13
.Lmu_loop_Y:
	s_add_i32 s47, s44, s6
	s_add_u32 s30, s30, 0x80
	s_addc_u32 s31, s31, 0
	v_mfma_f32_16x16x32_bf16 v[78:81], v[142:145], v[218:221], v[78:81]
	v_mfma_f32_16x16x32_bf16 v[74:77], v[146:149], v[218:221], v[74:77]
	v_mfma_f32_16x16x32_bf16 v[70:73], v[150:153], v[218:221], v[70:73]
	v_mfma_f32_16x16x32_bf16 v[66:69], v[154:157], v[218:221], v[66:69]
	s_mov_b32 m0, s47
	s_nop 0
	global_load_lds_dwordx4 v86, s[30:31]
	v_mfma_f32_16x16x32_bf16 v[62:65], v[142:145], v[222:225], v[62:65]
	v_mfma_f32_16x16x32_bf16 v[58:61], v[146:149], v[222:225], v[58:61]
	v_mfma_f32_16x16x32_bf16 v[54:57], v[150:153], v[222:225], v[54:57]
	v_mfma_f32_16x16x32_bf16 v[50:53], v[154:157], v[222:225], v[50:53]
	s_add_i32 m0, s47, 0x2000
	s_nop 0
	global_load_lds_dwordx4 v134, s[30:31]
	v_mfma_f32_16x16x32_bf16 v[46:49], v[142:145], v[226:229], v[46:49]
	v_mfma_f32_16x16x32_bf16 v[42:45], v[146:149], v[226:229], v[42:45]
	v_mfma_f32_16x16x32_bf16 v[38:41], v[150:153], v[226:229], v[38:41]
	v_mfma_f32_16x16x32_bf16 v[34:37], v[154:157], v[226:229], v[34:37]
	s_add_i32 m0, s47, 0x4000
	s_nop 0
	global_load_lds_dwordx4 v136, s[30:31]
	v_mfma_f32_16x16x32_bf16 v[18:21], v[142:145], v[230:233], v[18:21]
	v_mfma_f32_16x16x32_bf16 v[22:25], v[146:149], v[230:233], v[22:25]
	v_mfma_f32_16x16x32_bf16 v[26:29], v[150:153], v[230:233], v[26:29]
	v_mfma_f32_16x16x32_bf16 v[30:33], v[154:157], v[230:233], v[30:33]
	s_add_i32 m0, s47, 0x6000
	s_nop 0
	global_load_lds_dwordx4 v138, s[30:31]
	v_mfma_f32_16x16x32_bf16 v[2:5], v[142:145], v[234:237], v[2:5]
	v_mfma_f32_16x16x32_bf16 v[6:9], v[146:149], v[234:237], v[6:9]
	v_mfma_f32_16x16x32_bf16 v[10:13], v[150:153], v[234:237], v[10:13]
	v_mfma_f32_16x16x32_bf16 v[14:17], v[154:157], v[234:237], v[14:17]
	s_add_i32 m0, s47, 0x8000
	s_nop 0
	global_load_lds_dwordx4 v140, s[30:31]
	v_mul_f32_e32 v114, s20, v114
	v_mul_f32_e32 v115, s20, v115
	v_mul_f32_e32 v116, s21, v116
	v_mul_f32_e32 v117, s21, v117
	v_mul_f32_e32 v118, s22, v118
	v_mul_f32_e32 v119, s22, v119
	v_mul_f32_e32 v120, s23, v120
	v_mul_f32_e32 v121, s23, v121
	v_mul_f32_e32 v122, s24, v122
	v_mul_f32_e32 v123, s24, v123
	v_mul_f32_e32 v124, s25, v124
	v_mul_f32_e32 v125, s25, v125
	v_mul_f32_e32 v126, s26, v126
	v_mul_f32_e32 v127, s26, v127
	v_mul_f32_e32 v128, s27, v128
	v_mul_f32_e32 v129, s27, v129
	v_cvt_pk_bf16_f32 v158, v114, v116
	v_cvt_pk_bf16_f32 v159, v118, v120
	v_cvt_pk_bf16_f32 v160, v122, v124
	v_cvt_pk_bf16_f32 v161, v126, v128
	v_cvt_pk_bf16_f32 v162, v115, v117
	v_cvt_pk_bf16_f32 v163, v119, v121
	v_cvt_pk_bf16_f32 v164, v123, v125
	v_cvt_pk_bf16_f32 v165, v127, v129
	ds_write_b128 v1, v[158:161] offset:19456
	ds_write_b128 v1, v[162:165] offset:19584
	v_add_u32_e32 v91, s42, v135
	v_add_u32_e32 v93, s42, v137
	ds_read_b128 v[238:241], v139 offset:0
	ds_read_b128 v[242:245], v139 offset:2048
	ds_read_b128 v[246:249], v139 offset:4096
	ds_read_b128 v[250:253], v139 offset:6144
	ds_read_b128 v[218:221], v91 offset:0
	ds_read_b128 v[222:225], v91 offset:2048
	ds_read_b128 v[226:229], v91 offset:4096
	ds_read_b128 v[230:233], v91 offset:6144
	ds_read_b128 v[234:237], v91 offset:8192
	s_waitcnt lgkmcnt(0)
; #define MU_GLDS_A(buf, kt) do { _Pragma("unroll") for (int i = 0; i < NMU; ++i) \
;         __builtin_amdgcn_global_load_lds((const unsigned*)((const char*)A + aoff[i] + (size_t)(kt) * 128), (PG8_LAS unsigned*)(MU_SA(buf) + wid * 1024 + i * 8192), 16, 0, 0); } while (0)
; #define MU_B_ISSUE(sb, kt) do { const char* kb_ = Bb + (size_t)(kt) * (64 * (size_t)RB); _Pragma("unroll") for (int j = 0; j < 8; ++j) { const char* p_ = kb_ + (size_t)j * RB; \
;         asm volatile("global_load_dwordx2 %0, %1, off" : "=&v"(sb[j]) : "v"(p_) : "memory"); } } while (0)
; #define MU_B_WAIT(sb, N) asm volatile("s_waitcnt vmcnt(%8)" : "+v"(sb[0]), "+v"(sb[1]), "+v"(sb[2]), "+v"(sb[3]), "+v"(sb[4]), "+v"(sb[5]), "+v"(sb[6]), "+v"(sb[7]) : "n"(N) : "memory")
; #define MU_COMPUTE(buf) MU_COMPUTE_N(buf, NMU)
; template <int MODE>
; __device__ __forceinline__ void moe_unit(PG8_LAS unsigned char* lds, int e, int cb, int slot0  , int nv  , const bf16_t* A, const int* slot_tok,
;                                          const float* W0, const float* W1, bf16_t* OUT, const float* slot_rs  , const int* slot_dst) {
;     ...
;     f32x4 acc[NMU][4];
; #pragma unroll
;     for (int m = 0; m < NMU; ++m)
; #pragma unroll
;         for (int n = 0; n < 4; ++n) acc[m][n] = (f32x4){0.f, 0.f, 0.f, 0.f};
;     f32x2 s0[8], s1[8];
;     float g0[8];
;     MU_GLDS_A(0, 0); MU_B_ISSUE(s0, 0); MU_G_LOAD(g0, 0); MU_B_ISSUE(s1, 1);
;     MU_B_WAIT(s0, 8); MU_B_WRITE(s0, 0, g0); __builtin_amdgcn_sched_barrier(0); MU_B_ISSUE(s0, 2);
;     asm volatile("s_waitcnt vmcnt(16)" ::: "memory");
;     asm volatile("s_waitcnt lgkmcnt(0)" ::: "memory"); __builtin_amdgcn_s_barrier(); asm volatile("" ::: "memory");
; #pragma unroll 1
;     for (int t = 0; t < nt; t += 2) {
;         if (t + 2 < nt) MU_B_WAIT(s1, 8); else MU_B_WAIT(s1, 0);
;         MU_G_LOAD(g0, t + 1); MU_B_WRITE(s1, 1, g0); __builtin_amdgcn_sched_barrier(0); MU_GLDS_A(1, t + 1); __builtin_amdgcn_sched_barrier(0);
;         if (t + 3 < nt) { MU_B_ISSUE(s1, t + 3); }
;         MU_COMPUTE(0);
;         MU_END(t + 3 >= nt);
;         if (t + 2 < nt) { MU_B_WAIT(s0, 8); MU_G_LOAD(g0, t + 2); MU_B_WRITE(s0, 0, g0); __builtin_amdgcn_sched_barrier(0); MU_GLDS_A(0, t + 2); __builtin_amdgcn_sched_barrier(0); }
;         if (t + 4 < nt) { MU_B_ISSUE(s0, t + 4); }
;         MU_COMPUTE(1);
;         MU_END(t + 4 >= nt);
	s_load_dwordx8 s[12:19], s[28:29], 0x0
	s_add_u32 s28, s28, 0x100
	s_addc_u32 s29, s29, 0
	v_mfma_f32_16x16x32_bf16 v[78:81], v[238:241], v[218:221], v[78:81]
	v_mfma_f32_16x16x32_bf16 v[74:77], v[242:245], v[218:221], v[74:77]
	v_mfma_f32_16x16x32_bf16 v[70:73], v[246:249], v[218:221], v[70:73]
	v_mfma_f32_16x16x32_bf16 v[66:69], v[250:253], v[218:221], v[66:69]
	ds_read_b128 v[218:221], v93 offset:0
	ds_read_b128 v[142:145], v141 offset:0
	v_lshl_add_u64 v[132:133], v[132:133], 0, s[40:41]
	global_load_dwordx2 v[114:115], v[132:133], off
	global_load_dwordx2 v[116:117], v[132:133], off offset:2048
	v_mfma_f32_16x16x32_bf16 v[62:65], v[238:241], v[222:225], v[62:65]
	v_mfma_f32_16x16x32_bf16 v[58:61], v[242:245], v[222:225], v[58:61]
	v_mfma_f32_16x16x32_bf16 v[54:57], v[246:249], v[222:225], v[54:57]
	v_mfma_f32_16x16x32_bf16 v[50:53], v[250:253], v[222:225], v[50:53]
	ds_read_b128 v[222:225], v93 offset:2048
	ds_read_b128 v[146:149], v141 offset:2048
	v_lshl_add_u64 v[166:167], v[132:133], 0, s[34:35]
	global_load_dwordx2 v[118:119], v[166:167], off
	global_load_dwordx2 v[120:121], v[166:167], off offset:2048
	v_mfma_f32_16x16x32_bf16 v[46:49], v[238:241], v[226:229], v[46:49]
	v_mfma_f32_16x16x32_bf16 v[42:45], v[242:245], v[226:229], v[42:45]
	v_mfma_f32_16x16x32_bf16 v[38:41], v[246:249], v[226:229], v[38:41]
	v_mfma_f32_16x16x32_bf16 v[34:37], v[250:253], v[226:229], v[34:37]
	ds_read_b128 v[226:229], v93 offset:4096
	ds_read_b128 v[150:153], v141 offset:4096
	v_lshl_add_u64 v[166:167], v[132:133], 0, s[36:37]
	global_load_dwordx2 v[122:123], v[166:167], off
	global_load_dwordx2 v[124:125], v[166:167], off offset:2048
	v_mfma_f32_16x16x32_bf16 v[18:21], v[238:241], v[230:233], v[18:21]
	v_mfma_f32_16x16x32_bf16 v[22:25], v[242:245], v[230:233], v[22:25]
	v_mfma_f32_16x16x32_bf16 v[26:29], v[246:249], v[230:233], v[26:29]
	v_mfma_f32_16x16x32_bf16 v[30:33], v[250:253], v[230:233], v[30:33]
	ds_read_b128 v[230:233], v93 offset:6144
	ds_read_b128 v[154:157], v141 offset:6144
	v_lshl_add_u64 v[166:167], v[132:133], 0, s[38:39]
	global_load_dwordx2 v[126:127], v[166:167], off
	global_load_dwordx2 v[128:129], v[166:167], off offset:2048
	v_mfma_f32_16x16x32_bf16 v[2:5], v[238:241], v[234:237], v[2:5]
	v_mfma_f32_16x16x32_bf16 v[6:9], v[242:245], v[234:237], v[6:9]
	v_mfma_f32_16x16x32_bf16 v[10:13], v[246:249], v[234:237], v[10:13]
	v_mfma_f32_16x16x32_bf16 v[14:17], v[250:253], v[234:237], v[14:17]
	ds_read_b128 v[234:237], v93 offset:8192
	s_waitcnt vmcnt(21)
	s_waitcnt lgkmcnt(0)
	s_barrier
	s_mov_b32 s47, s42
	s_mov_b32 s42, s43
	s_mov_b32 s43, s44
	s_mov_b32 s44, s47
	s_add_i32 s47, s44, s6
	s_add_u32 s30, s30, 0x80
	s_addc_u32 s31, s31, 0
	v_mfma_f32_16x16x32_bf16 v[78:81], v[142:145], v[218:221], v[78:81]
	v_mfma_f32_16x16x32_bf16 v[74:77], v[146:149], v[218:221], v[74:77]
	v_mfma_f32_16x16x32_bf16 v[70:73], v[150:153], v[218:221], v[70:73]
	v_mfma_f32_16x16x32_bf16 v[66:69], v[154:157], v[218:221], v[66:69]
	s_mov_b32 m0, s47
	s_nop 0
	global_load_lds_dwordx4 v86, s[30:31]
	v_mfma_f32_16x16x32_bf16 v[62:65], v[142:145], v[222:225], v[62:65]
	v_mfma_f32_16x16x32_bf16 v[58:61], v[146:149], v[222:225], v[58:61]
	v_mfma_f32_16x16x32_bf16 v[54:57], v[150:153], v[222:225], v[54:57]
	v_mfma_f32_16x16x32_bf16 v[50:53], v[154:157], v[222:225], v[50:53]
	s_add_i32 m0, s47, 0x2000
	s_nop 0
	global_load_lds_dwordx4 v134, s[30:31]
	v_mfma_f32_16x16x32_bf16 v[46:49], v[142:145], v[226:229], v[46:49]
	v_mfma_f32_16x16x32_bf16 v[42:45], v[146:149], v[226:229], v[42:45]
	v_mfma_f32_16x16x32_bf16 v[38:41], v[150:153], v[226:229], v[38:41]
	v_mfma_f32_16x16x32_bf16 v[34:37], v[154:157], v[226:229], v[34:37]
	s_add_i32 m0, s47, 0x4000
	s_nop 0
	global_load_lds_dwordx4 v136, s[30:31]
	v_mfma_f32_16x16x32_bf16 v[18:21], v[142:145], v[230:233], v[18:21]
	v_mfma_f32_16x16x32_bf16 v[22:25], v[146:149], v[230:233], v[22:25]
	v_mfma_f32_16x16x32_bf16 v[26:29], v[150:153], v[230:233], v[26:29]
	v_mfma_f32_16x16x32_bf16 v[30:33], v[154:157], v[230:233], v[30:33]
	s_add_i32 m0, s47, 0x6000
	s_nop 0
	global_load_lds_dwordx4 v138, s[30:31]
	v_mfma_f32_16x16x32_bf16 v[2:5], v[142:145], v[234:237], v[2:5]
	v_mfma_f32_16x16x32_bf16 v[6:9], v[146:149], v[234:237], v[6:9]
	v_mfma_f32_16x16x32_bf16 v[10:13], v[150:153], v[234:237], v[10:13]
	v_mfma_f32_16x16x32_bf16 v[14:17], v[154:157], v[234:237], v[14:17]
	s_add_i32 m0, s47, 0x8000
	s_nop 0
	global_load_lds_dwordx4 v140, s[30:31]
	v_mul_f32_e32 v186, s12, v186
	v_mul_f32_e32 v187, s12, v187
	v_mul_f32_e32 v188, s13, v188
	v_mul_f32_e32 v189, s13, v189
	v_mul_f32_e32 v190, s14, v190
	v_mul_f32_e32 v191, s14, v191
	v_mul_f32_e32 v192, s15, v192
	v_mul_f32_e32 v193, s15, v193
	v_mul_f32_e32 v194, s16, v194
	v_mul_f32_e32 v195, s16, v195
	v_mul_f32_e32 v196, s17, v196
	v_mul_f32_e32 v197, s17, v197
	v_mul_f32_e32 v198, s18, v198
	v_mul_f32_e32 v199, s18, v199
	v_mul_f32_e32 v200, s19, v200
	v_mul_f32_e32 v201, s19, v201
	v_cvt_pk_bf16_f32 v158, v186, v188
	v_cvt_pk_bf16_f32 v159, v190, v192
	v_cvt_pk_bf16_f32 v160, v194, v196
	v_cvt_pk_bf16_f32 v161, v198, v200
	v_cvt_pk_bf16_f32 v162, v187, v189
	v_cvt_pk_bf16_f32 v163, v191, v193
	v_cvt_pk_bf16_f32 v164, v195, v197
	v_cvt_pk_bf16_f32 v165, v199, v201
	ds_write_b128 v1, v[158:161] offset:0
	ds_write_b128 v1, v[162:165] offset:128
	v_add_u32_e32 v91, s42, v135
	v_add_u32_e32 v93, s42, v137
	ds_read_b128 v[238:241], v139 offset:19456
	ds_read_b128 v[242:245], v139 offset:21504
	ds_read_b128 v[246:249], v139 offset:23552
	ds_read_b128 v[250:253], v139 offset:25600
	ds_read_b128 v[218:221], v91 offset:0
	ds_read_b128 v[222:225], v91 offset:2048
	ds_read_b128 v[226:229], v91 offset:4096
	ds_read_b128 v[230:233], v91 offset:6144
	ds_read_b128 v[234:237], v91 offset:8192
	s_waitcnt lgkmcnt(0)
; #define MU_GLDS_A(buf, kt) do { _Pragma("unroll") for (int i = 0; i < NMU; ++i) \
;         __builtin_amdgcn_global_load_lds((const unsigned*)((const char*)A + aoff[i] + (size_t)(kt) * 128), (PG8_LAS unsigned*)(MU_SA(buf) + wid * 1024 + i * 8192), 16, 0, 0); } while (0)
; #define MU_B_ISSUE(sb, kt) do { const char* kb_ = Bb + (size_t)(kt) * (64 * (size_t)RB); _Pragma("unroll") for (int j = 0; j < 8; ++j) { const char* p_ = kb_ + (size_t)j * RB; \
;         asm volatile("global_load_dwordx2 %0, %1, off" : "=&v"(sb[j]) : "v"(p_) : "memory"); } } while (0)
; #define MU_B_WAIT(sb, N) asm volatile("s_waitcnt vmcnt(%8)" : "+v"(sb[0]), "+v"(sb[1]), "+v"(sb[2]), "+v"(sb[3]), "+v"(sb[4]), "+v"(sb[5]), "+v"(sb[6]), "+v"(sb[7]) : "n"(N) : "memory")
; #define MU_COMPUTE(buf) MU_COMPUTE_N(buf, NMU)
; template <int MODE>
; __device__ __forceinline__ void moe_unit(PG8_LAS unsigned char* lds, int e, int cb, int slot0  , int nv  , const bf16_t* A, const int* slot_tok,
;                                          const float* W0, const float* W1, bf16_t* OUT, const float* slot_rs  , const int* slot_dst) {
;     ...
;     f32x4 acc[NMU][4];
; #pragma unroll
;     for (int m = 0; m < NMU; ++m)
; #pragma unroll
;         for (int n = 0; n < 4; ++n) acc[m][n] = (f32x4){0.f, 0.f, 0.f, 0.f};
;     f32x2 s0[8], s1[8];
;     float g0[8];
;     MU_GLDS_A(0, 0); MU_B_ISSUE(s0, 0); MU_G_LOAD(g0, 0); MU_B_ISSUE(s1, 1);
;     MU_B_WAIT(s0, 8); MU_B_WRITE(s0, 0, g0); __builtin_amdgcn_sched_barrier(0); MU_B_ISSUE(s0, 2);
;     asm volatile("s_waitcnt vmcnt(16)" ::: "memory");
;     asm volatile("s_waitcnt lgkmcnt(0)" ::: "memory"); __builtin_amdgcn_s_barrier(); asm volatile("" ::: "memory");
; #pragma unroll 1
;     for (int t = 0; t < nt; t += 2) {
;         if (t + 2 < nt) MU_B_WAIT(s1, 8); else MU_B_WAIT(s1, 0);
;         MU_G_LOAD(g0, t + 1); MU_B_WRITE(s1, 1, g0); __builtin_amdgcn_sched_barrier(0); MU_GLDS_A(1, t + 1); __builtin_amdgcn_sched_barrier(0);
;         if (t + 3 < nt) { MU_B_ISSUE(s1, t + 3); }
;         MU_COMPUTE(0);
;         MU_END(t + 3 >= nt);
;         if (t + 2 < nt) { MU_B_WAIT(s0, 8); MU_G_LOAD(g0, t + 2); MU_B_WRITE(s0, 0, g0); __builtin_amdgcn_sched_barrier(0); MU_GLDS_A(0, t + 2); __builtin_amdgcn_sched_barrier(0); }
;         if (t + 4 < nt) { MU_B_ISSUE(s0, t + 4); }
;         MU_COMPUTE(1);
;         MU_END(t + 4 >= nt);
	s_load_dwordx8 s[20:27], s[28:29], 0x0
	s_add_u32 s28, s28, 0x100
	s_addc_u32 s29, s29, 0
	v_mfma_f32_16x16x32_bf16 v[78:81], v[238:241], v[218:221], v[78:81]
	v_mfma_f32_16x16x32_bf16 v[74:77], v[242:245], v[218:221], v[74:77]
	v_mfma_f32_16x16x32_bf16 v[70:73], v[246:249], v[218:221], v[70:73]
	v_mfma_f32_16x16x32_bf16 v[66:69], v[250:253], v[218:221], v[66:69]
	ds_read_b128 v[218:221], v93 offset:0
	ds_read_b128 v[142:145], v141 offset:19456
	v_lshl_add_u64 v[132:133], v[132:133], 0, s[40:41]
	global_load_dwordx2 v[186:187], v[132:133], off
	global_load_dwordx2 v[188:189], v[132:133], off offset:2048
	v_mfma_f32_16x16x32_bf16 v[62:65], v[238:241], v[222:225], v[62:65]
	v_mfma_f32_16x16x32_bf16 v[58:61], v[242:245], v[222:225], v[58:61]
	v_mfma_f32_16x16x32_bf16 v[54:57], v[246:249], v[222:225], v[54:57]
	v_mfma_f32_16x16x32_bf16 v[50:53], v[250:253], v[222:225], v[50:53]
	ds_read_b128 v[222:225], v93 offset:2048
	ds_read_b128 v[146:149], v141 offset:21504
	v_lshl_add_u64 v[166:167], v[132:133], 0, s[34:35]
	global_load_dwordx2 v[190:191], v[166:167], off
	global_load_dwordx2 v[192:193], v[166:167], off offset:2048
	v_mfma_f32_16x16x32_bf16 v[46:49], v[238:241], v[226:229], v[46:49]
	v_mfma_f32_16x16x32_bf16 v[42:45], v[242:245], v[226:229], v[42:45]
	v_mfma_f32_16x16x32_bf16 v[38:41], v[246:249], v[226:229], v[38:41]
	v_mfma_f32_16x16x32_bf16 v[34:37], v[250:253], v[226:229], v[34:37]
	ds_read_b128 v[226:229], v93 offset:4096
	ds_read_b128 v[150:153], v141 offset:23552
	v_lshl_add_u64 v[166:167], v[132:133], 0, s[36:37]
	global_load_dwordx2 v[194:195], v[166:167], off
	global_load_dwordx2 v[196:197], v[166:167], off offset:2048
	v_mfma_f32_16x16x32_bf16 v[18:21], v[238:241], v[230:233], v[18:21]
	v_mfma_f32_16x16x32_bf16 v[22:25], v[242:245], v[230:233], v[22:25]
	v_mfma_f32_16x16x32_bf16 v[26:29], v[246:249], v[230:233], v[26:29]
	v_mfma_f32_16x16x32_bf16 v[30:33], v[250:253], v[230:233], v[30:33]
	ds_read_b128 v[230:233], v93 offset:6144
	ds_read_b128 v[154:157], v141 offset:25600
	v_lshl_add_u64 v[166:167], v[132:133], 0, s[38:39]
	global_load_dwordx2 v[198:199], v[166:167], off
	global_load_dwordx2 v[200:201], v[166:167], off offset:2048
	v_mfma_f32_16x16x32_bf16 v[2:5], v[238:241], v[234:237], v[2:5]
	v_mfma_f32_16x16x32_bf16 v[6:9], v[242:245], v[234:237], v[6:9]
	v_mfma_f32_16x16x32_bf16 v[10:13], v[246:249], v[234:237], v[10:13]
	v_mfma_f32_16x16x32_bf16 v[14:17], v[250:253], v[234:237], v[14:17]
	ds_read_b128 v[234:237], v93 offset:8192
	s_waitcnt vmcnt(21)
	s_waitcnt lgkmcnt(0)
	s_barrier
	s_mov_b32 s47, s42
	s_mov_b32 s42, s43
	s_mov_b32 s43, s44
	s_mov_b32 s44, s47
	s_add_i32 s47, s44, s6
	s_add_u32 s30, s30, 0x80
	s_addc_u32 s31, s31, 0
	v_mfma_f32_16x16x32_bf16 v[78:81], v[142:145], v[218:221], v[78:81]
	v_mfma_f32_16x16x32_bf16 v[74:77], v[146:149], v[218:221], v[74:77]
	v_mfma_f32_16x16x32_bf16 v[70:73], v[150:153], v[218:221], v[70:73]
	v_mfma_f32_16x16x32_bf16 v[66:69], v[154:157], v[218:221], v[66:69]
	s_mov_b32 m0, s47
	s_nop 0
	global_load_lds_dwordx4 v86, s[30:31]
	v_mfma_f32_16x16x32_bf16 v[62:65], v[142:145], v[222:225], v[62:65]
	v_mfma_f32_16x16x32_bf16 v[58:61], v[146:149], v[222:225], v[58:61]
	v_mfma_f32_16x16x32_bf16 v[54:57], v[150:153], v[222:225], v[54:57]
	v_mfma_f32_16x16x32_bf16 v[50:53], v[154:157], v[222:225], v[50:53]
	s_add_i32 m0, s47, 0x2000
	s_nop 0
	global_load_lds_dwordx4 v134, s[30:31]
	v_mfma_f32_16x16x32_bf16 v[46:49], v[142:145], v[226:229], v[46:49]
	v_mfma_f32_16x16x32_bf16 v[42:45], v[146:149], v[226:229], v[42:45]
	v_mfma_f32_16x16x32_bf16 v[38:41], v[150:153], v[226:229], v[38:41]
	v_mfma_f32_16x16x32_bf16 v[34:37], v[154:157], v[226:229], v[34:37]
	s_add_i32 m0, s47, 0x4000
	s_nop 0
	global_load_lds_dwordx4 v136, s[30:31]
	v_mfma_f32_16x16x32_bf16 v[18:21], v[142:145], v[230:233], v[18:21]
	v_mfma_f32_16x16x32_bf16 v[22:25], v[146:149], v[230:233], v[22:25]
	v_mfma_f32_16x16x32_bf16 v[26:29], v[150:153], v[230:233], v[26:29]
	v_mfma_f32_16x16x32_bf16 v[30:33], v[154:157], v[230:233], v[30:33]
	s_add_i32 m0, s47, 0x6000
	s_nop 0
	global_load_lds_dwordx4 v138, s[30:31]
	v_mfma_f32_16x16x32_bf16 v[2:5], v[142:145], v[234:237], v[2:5]
	v_mfma_f32_16x16x32_bf16 v[6:9], v[146:149], v[234:237], v[6:9]
	v_mfma_f32_16x16x32_bf16 v[10:13], v[150:153], v[234:237], v[10:13]
	v_mfma_f32_16x16x32_bf16 v[14:17], v[154:157], v[234:237], v[14:17]
	s_add_i32 m0, s47, 0x8000
	s_nop 0
	global_load_lds_dwordx4 v140, s[30:31]
	v_mul_f32_e32 v202, s20, v202
	v_mul_f32_e32 v203, s20, v203
	v_mul_f32_e32 v204, s21, v204
	v_mul_f32_e32 v205, s21, v205
	v_mul_f32_e32 v206, s22, v206
	v_mul_f32_e32 v207, s22, v207
	v_mul_f32_e32 v208, s23, v208
	v_mul_f32_e32 v209, s23, v209
	v_mul_f32_e32 v210, s24, v210
	v_mul_f32_e32 v211, s24, v211
	v_mul_f32_e32 v212, s25, v212
	v_mul_f32_e32 v213, s25, v213
	v_mul_f32_e32 v214, s26, v214
	v_mul_f32_e32 v215, s26, v215
	v_mul_f32_e32 v216, s27, v216
	v_mul_f32_e32 v217, s27, v217
	v_cvt_pk_bf16_f32 v158, v202, v204
	v_cvt_pk_bf16_f32 v159, v206, v208
	v_cvt_pk_bf16_f32 v160, v210, v212
	v_cvt_pk_bf16_f32 v161, v214, v216
	v_cvt_pk_bf16_f32 v162, v203, v205
	v_cvt_pk_bf16_f32 v163, v207, v209
	v_cvt_pk_bf16_f32 v164, v211, v213
	v_cvt_pk_bf16_f32 v165, v215, v217
	ds_write_b128 v1, v[158:161] offset:19456
	ds_write_b128 v1, v[162:165] offset:19584
	v_add_u32_e32 v91, s42, v135
	v_add_u32_e32 v93, s42, v137
	ds_read_b128 v[238:241], v139 offset:0
	ds_read_b128 v[242:245], v139 offset:2048
	ds_read_b128 v[246:249], v139 offset:4096
	ds_read_b128 v[250:253], v139 offset:6144
	ds_read_b128 v[218:221], v91 offset:0
	ds_read_b128 v[222:225], v91 offset:2048
	ds_read_b128 v[226:229], v91 offset:4096
	ds_read_b128 v[230:233], v91 offset:6144
	ds_read_b128 v[234:237], v91 offset:8192
	s_waitcnt lgkmcnt(0)
; #define MU_GLDS_A(buf, kt) do { _Pragma("unroll") for (int i = 0; i < NMU; ++i) \
;         __builtin_amdgcn_global_load_lds((const unsigned*)((const char*)A + aoff[i] + (size_t)(kt) * 128), (PG8_LAS unsigned*)(MU_SA(buf) + wid * 1024 + i * 8192), 16, 0, 0); } while (0)
; #define MU_B_ISSUE(sb, kt) do { const char* kb_ = Bb + (size_t)(kt) * (64 * (size_t)RB); _Pragma("unroll") for (int j = 0; j < 8; ++j) { const char* p_ = kb_ + (size_t)j * RB; \
;         asm volatile("global_load_dwordx2 %0, %1, off" : "=&v"(sb[j]) : "v"(p_) : "memory"); } } while (0)
; #define MU_B_WAIT(sb, N) asm volatile("s_waitcnt vmcnt(%8)" : "+v"(sb[0]), "+v"(sb[1]), "+v"(sb[2]), "+v"(sb[3]), "+v"(sb[4]), "+v"(sb[5]), "+v"(sb[6]), "+v"(sb[7]) : "n"(N) : "memory")
; #define MU_COMPUTE(buf) MU_COMPUTE_N(buf, NMU)
; template <int MODE>
; __device__ __forceinline__ void moe_unit(PG8_LAS unsigned char* lds, int e, int cb, int slot0  , int nv  , const bf16_t* A, const int* slot_tok,
;                                          const float* W0, const float* W1, bf16_t* OUT, const float* slot_rs  , const int* slot_dst) {
;     ...
;     f32x4 acc[NMU][4];
; #pragma unroll
;     for (int m = 0; m < NMU; ++m)
; #pragma unroll
;         for (int n = 0; n < 4; ++n) acc[m][n] = (f32x4){0.f, 0.f, 0.f, 0.f};
;     f32x2 s0[8], s1[8];
;     float g0[8];
;     MU_GLDS_A(0, 0); MU_B_ISSUE(s0, 0); MU_G_LOAD(g0, 0); MU_B_ISSUE(s1, 1);
;     MU_B_WAIT(s0, 8); MU_B_WRITE(s0, 0, g0); __builtin_amdgcn_sched_barrier(0); MU_B_ISSUE(s0, 2);
;     asm volatile("s_waitcnt vmcnt(16)" ::: "memory");
;     asm volatile("s_waitcnt lgkmcnt(0)" ::: "memory"); __builtin_amdgcn_s_barrier(); asm volatile("" ::: "memory");
; #pragma unroll 1
;     for (int t = 0; t < nt; t += 2) {
;         if (t + 2 < nt) MU_B_WAIT(s1, 8); else MU_B_WAIT(s1, 0);
;         MU_G_LOAD(g0, t + 1); MU_B_WRITE(s1, 1, g0); __builtin_amdgcn_sched_barrier(0); MU_GLDS_A(1, t + 1); __builtin_amdgcn_sched_barrier(0);
;         if (t + 3 < nt) { MU_B_ISSUE(s1, t + 3); }
;         MU_COMPUTE(0);
;         MU_END(t + 3 >= nt);
;         if (t + 2 < nt) { MU_B_WAIT(s0, 8); MU_G_LOAD(g0, t + 2); MU_B_WRITE(s0, 0, g0); __builtin_amdgcn_sched_barrier(0); MU_GLDS_A(0, t + 2); __builtin_amdgcn_sched_barrier(0); }
;         if (t + 4 < nt) { MU_B_ISSUE(s0, t + 4); }
;         MU_COMPUTE(1);
;         MU_END(t + 4 >= nt);
	s_load_dwordx8 s[12:19], s[28:29], 0x0
	s_add_u32 s28, s28, 0x100
	s_addc_u32 s29, s29, 0
	v_mfma_f32_16x16x32_bf16 v[78:81], v[238:241], v[218:221], v[78:81]
	v_mfma_f32_16x16x32_bf16 v[74:77], v[242:245], v[218:221], v[74:77]
	v_mfma_f32_16x16x32_bf16 v[70:73], v[246:249], v[218:221], v[70:73]
	v_mfma_f32_16x16x32_bf16 v[66:69], v[250:253], v[218:221], v[66:69]
	ds_read_b128 v[218:221], v93 offset:0
	ds_read_b128 v[142:145], v141 offset:0
	v_lshl_add_u64 v[132:133], v[132:133], 0, s[40:41]
	global_load_dwordx2 v[202:203], v[132:133], off
	global_load_dwordx2 v[204:205], v[132:133], off offset:2048
	v_mfma_f32_16x16x32_bf16 v[62:65], v[238:241], v[222:225], v[62:65]
	v_mfma_f32_16x16x32_bf16 v[58:61], v[242:245], v[222:225], v[58:61]
	v_mfma_f32_16x16x32_bf16 v[54:57], v[246:249], v[222:225], v[54:57]
	v_mfma_f32_16x16x32_bf16 v[50:53], v[250:253], v[222:225], v[50:53]
	ds_read_b128 v[222:225], v93 offset:2048
	ds_read_b128 v[146:149], v141 offset:2048
	v_lshl_add_u64 v[166:167], v[132:133], 0, s[34:35]
	global_load_dwordx2 v[206:207], v[166:167], off
	global_load_dwordx2 v[208:209], v[166:167], off offset:2048
	v_mfma_f32_16x16x32_bf16 v[46:49], v[238:241], v[226:229], v[46:49]
	v_mfma_f32_16x16x32_bf16 v[42:45], v[242:245], v[226:229], v[42:45]
	v_mfma_f32_16x16x32_bf16 v[38:41], v[246:249], v[226:229], v[38:41]
	v_mfma_f32_16x16x32_bf16 v[34:37], v[250:253], v[226:229], v[34:37]
	ds_read_b128 v[226:229], v93 offset:4096
	ds_read_b128 v[150:153], v141 offset:4096
	v_lshl_add_u64 v[166:167], v[132:133], 0, s[36:37]
	global_load_dwordx2 v[210:211], v[166:167], off
	global_load_dwordx2 v[212:213], v[166:167], off offset:2048
	v_mfma_f32_16x16x32_bf16 v[18:21], v[238:241], v[230:233], v[18:21]
	v_mfma_f32_16x16x32_bf16 v[22:25], v[242:245], v[230:233], v[22:25]
	v_mfma_f32_16x16x32_bf16 v[26:29], v[246:249], v[230:233], v[26:29]
	v_mfma_f32_16x16x32_bf16 v[30:33], v[250:253], v[230:233], v[30:33]
	ds_read_b128 v[230:233], v93 offset:6144
	ds_read_b128 v[154:157], v141 offset:6144
	v_lshl_add_u64 v[166:167], v[132:133], 0, s[38:39]
	global_load_dwordx2 v[214:215], v[166:167], off
	global_load_dwordx2 v[216:217], v[166:167], off offset:2048
	v_mfma_f32_16x16x32_bf16 v[2:5], v[238:241], v[234:237], v[2:5]
	v_mfma_f32_16x16x32_bf16 v[6:9], v[242:245], v[234:237], v[6:9]
	v_mfma_f32_16x16x32_bf16 v[10:13], v[246:249], v[234:237], v[10:13]
	v_mfma_f32_16x16x32_bf16 v[14:17], v[250:253], v[234:237], v[14:17]
	ds_read_b128 v[234:237], v93 offset:8192
	s_waitcnt vmcnt(21)
	s_waitcnt lgkmcnt(0)
	s_barrier
	s_mov_b32 s47, s42
	s_mov_b32 s42, s43
	s_mov_b32 s43, s44
	s_mov_b32 s44, s47
	s_add_i32 s47, s44, s6
	s_add_u32 s30, s30, 0x80
	s_addc_u32 s31, s31, 0
	v_mfma_f32_16x16x32_bf16 v[78:81], v[142:145], v[218:221], v[78:81]
	v_mfma_f32_16x16x32_bf16 v[74:77], v[146:149], v[218:221], v[74:77]
	v_mfma_f32_16x16x32_bf16 v[70:73], v[150:153], v[218:221], v[70:73]
	v_mfma_f32_16x16x32_bf16 v[66:69], v[154:157], v[218:221], v[66:69]
	s_mov_b32 m0, s47
	s_nop 0
	global_load_lds_dwordx4 v86, s[30:31]
	v_mfma_f32_16x16x32_bf16 v[62:65], v[142:145], v[222:225], v[62:65]
	v_mfma_f32_16x16x32_bf16 v[58:61], v[146:149], v[222:225], v[58:61]
	v_mfma_f32_16x16x32_bf16 v[54:57], v[150:153], v[222:225], v[54:57]
	v_mfma_f32_16x16x32_bf16 v[50:53], v[154:157], v[222:225], v[50:53]
	s_add_i32 m0, s47, 0x2000
	s_nop 0
	global_load_lds_dwordx4 v134, s[30:31]
	v_mfma_f32_16x16x32_bf16 v[46:49], v[142:145], v[226:229], v[46:49]
	v_mfma_f32_16x16x32_bf16 v[42:45], v[146:149], v[226:229], v[42:45]
	v_mfma_f32_16x16x32_bf16 v[38:41], v[150:153], v[226:229], v[38:41]
	v_mfma_f32_16x16x32_bf16 v[34:37], v[154:157], v[226:229], v[34:37]
	s_add_i32 m0, s47, 0x4000
	s_nop 0
	global_load_lds_dwordx4 v136, s[30:31]
	v_mfma_f32_16x16x32_bf16 v[18:21], v[142:145], v[230:233], v[18:21]
	v_mfma_f32_16x16x32_bf16 v[22:25], v[146:149], v[230:233], v[22:25]
	v_mfma_f32_16x16x32_bf16 v[26:29], v[150:153], v[230:233], v[26:29]
	v_mfma_f32_16x16x32_bf16 v[30:33], v[154:157], v[230:233], v[30:33]
	s_add_i32 m0, s47, 0x6000
	s_nop 0
	global_load_lds_dwordx4 v138, s[30:31]
	v_mfma_f32_16x16x32_bf16 v[2:5], v[142:145], v[234:237], v[2:5]
	v_mfma_f32_16x16x32_bf16 v[6:9], v[146:149], v[234:237], v[6:9]
	v_mfma_f32_16x16x32_bf16 v[10:13], v[150:153], v[234:237], v[10:13]
	v_mfma_f32_16x16x32_bf16 v[14:17], v[154:157], v[234:237], v[14:17]
	s_add_i32 m0, s47, 0x8000
	s_nop 0
	global_load_lds_dwordx4 v140, s[30:31]
	v_mul_f32_e32 v98, s12, v98
	v_mul_f32_e32 v99, s12, v99
	v_mul_f32_e32 v100, s13, v100
	v_mul_f32_e32 v101, s13, v101
	v_mul_f32_e32 v102, s14, v102
	v_mul_f32_e32 v103, s14, v103
	v_mul_f32_e32 v104, s15, v104
	v_mul_f32_e32 v105, s15, v105
	v_mul_f32_e32 v106, s16, v106
	v_mul_f32_e32 v107, s16, v107
	v_mul_f32_e32 v108, s17, v108
	v_mul_f32_e32 v109, s17, v109
	v_mul_f32_e32 v110, s18, v110
	v_mul_f32_e32 v111, s18, v111
	v_mul_f32_e32 v112, s19, v112
	v_mul_f32_e32 v113, s19, v113
	v_cvt_pk_bf16_f32 v158, v98, v100
	v_cvt_pk_bf16_f32 v159, v102, v104
	v_cvt_pk_bf16_f32 v160, v106, v108
	v_cvt_pk_bf16_f32 v161, v110, v112
	v_cvt_pk_bf16_f32 v162, v99, v101
	v_cvt_pk_bf16_f32 v163, v103, v105
	v_cvt_pk_bf16_f32 v164, v107, v109
	v_cvt_pk_bf16_f32 v165, v111, v113
	ds_write_b128 v1, v[158:161] offset:0
	ds_write_b128 v1, v[162:165] offset:128
	v_add_u32_e32 v91, s42, v135
	v_add_u32_e32 v93, s42, v137
	ds_read_b128 v[238:241], v139 offset:19456
	ds_read_b128 v[242:245], v139 offset:21504
	ds_read_b128 v[246:249], v139 offset:23552
	ds_read_b128 v[250:253], v139 offset:25600
	ds_read_b128 v[218:221], v91 offset:0
	ds_read_b128 v[222:225], v91 offset:2048
	ds_read_b128 v[226:229], v91 offset:4096
	ds_read_b128 v[230:233], v91 offset:6144
	ds_read_b128 v[234:237], v91 offset:8192
	s_waitcnt lgkmcnt(0)
; #define MU_GLDS_A(buf, kt) do { _Pragma("unroll") for (int i = 0; i < NMU; ++i) \
;         __builtin_amdgcn_global_load_lds((const unsigned*)((const char*)A + aoff[i] + (size_t)(kt) * 128), (PG8_LAS unsigned*)(MU_SA(buf) + wid * 1024 + i * 8192), 16, 0, 0); } while (0)
; #define MU_B_ISSUE(sb, kt) do { const char* kb_ = Bb + (size_t)(kt) * (64 * (size_t)RB); _Pragma("unroll") for (int j = 0; j < 8; ++j) { const char* p_ = kb_ + (size_t)j * RB; \
;         asm volatile("global_load_dwordx2 %0, %1, off" : "=&v"(sb[j]) : "v"(p_) : "memory"); } } while (0)
; #define MU_B_WAIT(sb, N) asm volatile("s_waitcnt vmcnt(%8)" : "+v"(sb[0]), "+v"(sb[1]), "+v"(sb[2]), "+v"(sb[3]), "+v"(sb[4]), "+v"(sb[5]), "+v"(sb[6]), "+v"(sb[7]) : "n"(N) : "memory")
; #define MU_COMPUTE(buf) MU_COMPUTE_N(buf, NMU)
; template <int MODE>
; __device__ __forceinline__ void moe_unit(PG8_LAS unsigned char* lds, int e, int cb, int slot0  , int nv  , const bf16_t* A, const int* slot_tok,
;                                          const float* W0, const float* W1, bf16_t* OUT, const float* slot_rs  , const int* slot_dst) {
;     ...
;     f32x4 acc[NMU][4];
; #pragma unroll
;     for (int m = 0; m < NMU; ++m)
; #pragma unroll
;         for (int n = 0; n < 4; ++n) acc[m][n] = (f32x4){0.f, 0.f, 0.f, 0.f};
;     f32x2 s0[8], s1[8];
;     float g0[8];
;     MU_GLDS_A(0, 0); MU_B_ISSUE(s0, 0); MU_G_LOAD(g0, 0); MU_B_ISSUE(s1, 1);
;     MU_B_WAIT(s0, 8); MU_B_WRITE(s0, 0, g0); __builtin_amdgcn_sched_barrier(0); MU_B_ISSUE(s0, 2);
;     asm volatile("s_waitcnt vmcnt(16)" ::: "memory");
;     asm volatile("s_waitcnt lgkmcnt(0)" ::: "memory"); __builtin_amdgcn_s_barrier(); asm volatile("" ::: "memory");
; #pragma unroll 1
;     for (int t = 0; t < nt; t += 2) {
;         if (t + 2 < nt) MU_B_WAIT(s1, 8); else MU_B_WAIT(s1, 0);
;         MU_G_LOAD(g0, t + 1); MU_B_WRITE(s1, 1, g0); __builtin_amdgcn_sched_barrier(0); MU_GLDS_A(1, t + 1); __builtin_amdgcn_sched_barrier(0);
;         if (t + 3 < nt) { MU_B_ISSUE(s1, t + 3); }
;         MU_COMPUTE(0);
;         MU_END(t + 3 >= nt);
;         if (t + 2 < nt) { MU_B_WAIT(s0, 8); MU_G_LOAD(g0, t + 2); MU_B_WRITE(s0, 0, g0); __builtin_amdgcn_sched_barrier(0); MU_GLDS_A(0, t + 2); __builtin_amdgcn_sched_barrier(0); }
;         if (t + 4 < nt) { MU_B_ISSUE(s0, t + 4); }
;         MU_COMPUTE(1);
;         MU_END(t + 4 >= nt);
	s_load_dwordx8 s[20:27], s[28:29], 0x0
	s_add_u32 s28, s28, 0x100
	s_addc_u32 s29, s29, 0
	v_mfma_f32_16x16x32_bf16 v[78:81], v[238:241], v[218:221], v[78:81]
	v_mfma_f32_16x16x32_bf16 v[74:77], v[242:245], v[218:221], v[74:77]
	v_mfma_f32_16x16x32_bf16 v[70:73], v[246:249], v[218:221], v[70:73]
	v_mfma_f32_16x16x32_bf16 v[66:69], v[250:253], v[218:221], v[66:69]
	ds_read_b128 v[218:221], v93 offset:0
	ds_read_b128 v[142:145], v141 offset:19456
	v_lshl_add_u64 v[132:133], v[132:133], 0, s[40:41]
	global_load_dwordx2 v[98:99], v[132:133], off
	global_load_dwordx2 v[100:101], v[132:133], off offset:2048
	v_mfma_f32_16x16x32_bf16 v[62:65], v[238:241], v[222:225], v[62:65]
	v_mfma_f32_16x16x32_bf16 v[58:61], v[242:245], v[222:225], v[58:61]
	v_mfma_f32_16x16x32_bf16 v[54:57], v[246:249], v[222:225], v[54:57]
	v_mfma_f32_16x16x32_bf16 v[50:53], v[250:253], v[222:225], v[50:53]
	ds_read_b128 v[222:225], v93 offset:2048
	ds_read_b128 v[146:149], v141 offset:21504
	v_lshl_add_u64 v[166:167], v[132:133], 0, s[34:35]
	global_load_dwordx2 v[102:103], v[166:167], off
	global_load_dwordx2 v[104:105], v[166:167], off offset:2048
	v_mfma_f32_16x16x32_bf16 v[46:49], v[238:241], v[226:229], v[46:49]
	v_mfma_f32_16x16x32_bf16 v[42:45], v[242:245], v[226:229], v[42:45]
	v_mfma_f32_16x16x32_bf16 v[38:41], v[246:249], v[226:229], v[38:41]
	v_mfma_f32_16x16x32_bf16 v[34:37], v[250:253], v[226:229], v[34:37]
	ds_read_b128 v[226:229], v93 offset:4096
	ds_read_b128 v[150:153], v141 offset:23552
	v_lshl_add_u64 v[166:167], v[132:133], 0, s[36:37]
	global_load_dwordx2 v[106:107], v[166:167], off
	global_load_dwordx2 v[108:109], v[166:167], off offset:2048
	v_mfma_f32_16x16x32_bf16 v[18:21], v[238:241], v[230:233], v[18:21]
	v_mfma_f32_16x16x32_bf16 v[22:25], v[242:245], v[230:233], v[22:25]
	v_mfma_f32_16x16x32_bf16 v[26:29], v[246:249], v[230:233], v[26:29]
	v_mfma_f32_16x16x32_bf16 v[30:33], v[250:253], v[230:233], v[30:33]
	ds_read_b128 v[230:233], v93 offset:6144
	ds_read_b128 v[154:157], v141 offset:25600
	v_lshl_add_u64 v[166:167], v[132:133], 0, s[38:39]
	global_load_dwordx2 v[110:111], v[166:167], off
	global_load_dwordx2 v[112:113], v[166:167], off offset:2048
	v_mfma_f32_16x16x32_bf16 v[2:5], v[238:241], v[234:237], v[2:5]
	v_mfma_f32_16x16x32_bf16 v[6:9], v[242:245], v[234:237], v[6:9]
	v_mfma_f32_16x16x32_bf16 v[10:13], v[246:249], v[234:237], v[10:13]
	v_mfma_f32_16x16x32_bf16 v[14:17], v[250:253], v[234:237], v[14:17]
	ds_read_b128 v[234:237], v93 offset:8192
	s_waitcnt vmcnt(21)
	s_waitcnt lgkmcnt(0)
	s_barrier
	s_mov_b32 s47, s42
	s_mov_b32 s42, s43
	s_mov_b32 s43, s44
	s_mov_b32 s44, s47
	s_sub_u32 s46, s46, 1
	s_cmp_lg_u32 s46, 0
	s_cbranch_scc1 .Lmu_loop_Y
	s_add_i32 s47, s44, s6
	s_add_u32 s30, s30, 0x80
	s_addc_u32 s31, s31, 0
	v_mfma_f32_16x16x32_bf16 v[78:81], v[142:145], v[218:221], v[78:81]
	v_mfma_f32_16x16x32_bf16 v[74:77], v[146:149], v[218:221], v[74:77]
	v_mfma_f32_16x16x32_bf16 v[70:73], v[150:153], v[218:221], v[70:73]
	v_mfma_f32_16x16x32_bf16 v[66:69], v[154:157], v[218:221], v[66:69]
	s_mov_b32 m0, s47
	s_nop 0
	global_load_lds_dwordx4 v86, s[30:31]
	v_mfma_f32_16x16x32_bf16 v[62:65], v[142:145], v[222:225], v[62:65]
	v_mfma_f32_16x16x32_bf16 v[58:61], v[146:149], v[222:225], v[58:61]
	v_mfma_f32_16x16x32_bf16 v[54:57], v[150:153], v[222:225], v[54:57]
	v_mfma_f32_16x16x32_bf16 v[50:53], v[154:157], v[222:225], v[50:53]
	s_add_i32 m0, s47, 0x2000
	s_nop 0
	global_load_lds_dwordx4 v134, s[30:31]
	v_mfma_f32_16x16x32_bf16 v[46:49], v[142:145], v[226:229], v[46:49]
	v_mfma_f32_16x16x32_bf16 v[42:45], v[146:149], v[226:229], v[42:45]
	v_mfma_f32_16x16x32_bf16 v[38:41], v[150:153], v[226:229], v[38:41]
	v_mfma_f32_16x16x32_bf16 v[34:37], v[154:157], v[226:229], v[34:37]
	s_add_i32 m0, s47, 0x4000
	s_nop 0
	global_load_lds_dwordx4 v136, s[30:31]
	v_mfma_f32_16x16x32_bf16 v[18:21], v[142:145], v[230:233], v[18:21]
	v_mfma_f32_16x16x32_bf16 v[22:25], v[146:149], v[230:233], v[22:25]
	v_mfma_f32_16x16x32_bf16 v[26:29], v[150:153], v[230:233], v[26:29]
	v_mfma_f32_16x16x32_bf16 v[30:33], v[154:157], v[230:233], v[30:33]
	s_add_i32 m0, s47, 0x6000
	s_nop 0
	global_load_lds_dwordx4 v138, s[30:31]
	v_mfma_f32_16x16x32_bf16 v[2:5], v[142:145], v[234:237], v[2:5]
	v_mfma_f32_16x16x32_bf16 v[6:9], v[146:149], v[234:237], v[6:9]
	v_mfma_f32_16x16x32_bf16 v[10:13], v[150:153], v[234:237], v[10:13]
	v_mfma_f32_16x16x32_bf16 v[14:17], v[154:157], v[234:237], v[14:17]
	s_add_i32 m0, s47, 0x8000
	s_nop 0
	global_load_lds_dwordx4 v140, s[30:31]
	v_mul_f32_e32 v114, s20, v114
	v_mul_f32_e32 v115, s20, v115
	v_mul_f32_e32 v116, s21, v116
	v_mul_f32_e32 v117, s21, v117
	v_mul_f32_e32 v118, s22, v118
	v_mul_f32_e32 v119, s22, v119
	v_mul_f32_e32 v120, s23, v120
	v_mul_f32_e32 v121, s23, v121
	v_mul_f32_e32 v122, s24, v122
	v_mul_f32_e32 v123, s24, v123
	v_mul_f32_e32 v124, s25, v124
	v_mul_f32_e32 v125, s25, v125
	v_mul_f32_e32 v126, s26, v126
	v_mul_f32_e32 v127, s26, v127
	v_mul_f32_e32 v128, s27, v128
	v_mul_f32_e32 v129, s27, v129
	v_cvt_pk_bf16_f32 v158, v114, v116
	v_cvt_pk_bf16_f32 v159, v118, v120
	v_cvt_pk_bf16_f32 v160, v122, v124
	v_cvt_pk_bf16_f32 v161, v126, v128
	v_cvt_pk_bf16_f32 v162, v115, v117
	v_cvt_pk_bf16_f32 v163, v119, v121
	v_cvt_pk_bf16_f32 v164, v123, v125
	v_cvt_pk_bf16_f32 v165, v127, v129
	ds_write_b128 v1, v[158:161] offset:19456
	ds_write_b128 v1, v[162:165] offset:19584
	v_add_u32_e32 v91, s42, v135
	v_add_u32_e32 v93, s42, v137
	ds_read_b128 v[238:241], v139 offset:0
	ds_read_b128 v[242:245], v139 offset:2048
	ds_read_b128 v[246:249], v139 offset:4096
	ds_read_b128 v[250:253], v139 offset:6144
	ds_read_b128 v[218:221], v91 offset:0
	ds_read_b128 v[222:225], v91 offset:2048
	ds_read_b128 v[226:229], v91 offset:4096
	ds_read_b128 v[230:233], v91 offset:6144
	ds_read_b128 v[234:237], v91 offset:8192
	s_waitcnt lgkmcnt(0)
; #define MU_GLDS_A(buf, kt) do { _Pragma("unroll") for (int i = 0; i < NMU; ++i) \
;         __builtin_amdgcn_global_load_lds((const unsigned*)((const char*)A + aoff[i] + (size_t)(kt) * 128), (PG8_LAS unsigned*)(MU_SA(buf) + wid * 1024 + i * 8192), 16, 0, 0); } while (0)
; #define MU_B_ISSUE(sb, kt) do { const char* kb_ = Bb + (size_t)(kt) * (64 * (size_t)RB); _Pragma("unroll") for (int j = 0; j < 8; ++j) { const char* p_ = kb_ + (size_t)j * RB; \
;         asm volatile("global_load_dwordx2 %0, %1, off" : "=&v"(sb[j]) : "v"(p_) : "memory"); } } while (0)
; #define MU_B_WAIT(sb, N) asm volatile("s_waitcnt vmcnt(%8)" : "+v"(sb[0]), "+v"(sb[1]), "+v"(sb[2]), "+v"(sb[3]), "+v"(sb[4]), "+v"(sb[5]), "+v"(sb[6]), "+v"(sb[7]) : "n"(N) : "memory")
; #define MU_COMPUTE(buf) MU_COMPUTE_N(buf, NMU)
; template <int MODE>
; __device__ __forceinline__ void moe_unit(PG8_LAS unsigned char* lds, int e, int cb, int slot0  , int nv  , const bf16_t* A, const int* slot_tok,
;                                          const float* W0, const float* W1, bf16_t* OUT, const float* slot_rs  , const int* slot_dst) {
;     ...
;     f32x4 acc[NMU][4];
; #pragma unroll
;     for (int m = 0; m < NMU; ++m)
; #pragma unroll
;         for (int n = 0; n < 4; ++n) acc[m][n] = (f32x4){0.f, 0.f, 0.f, 0.f};
;     f32x2 s0[8], s1[8];
;     float g0[8];
;     MU_GLDS_A(0, 0); MU_B_ISSUE(s0, 0); MU_G_LOAD(g0, 0); MU_B_ISSUE(s1, 1);
;     MU_B_WAIT(s0, 8); MU_B_WRITE(s0, 0, g0); __builtin_amdgcn_sched_barrier(0); MU_B_ISSUE(s0, 2);
;     asm volatile("s_waitcnt vmcnt(16)" ::: "memory");
;     asm volatile("s_waitcnt lgkmcnt(0)" ::: "memory"); __builtin_amdgcn_s_barrier(); asm volatile("" ::: "memory");
; #pragma unroll 1
;     for (int t = 0; t < nt; t += 2) {
;         if (t + 2 < nt) MU_B_WAIT(s1, 8); else MU_B_WAIT(s1, 0);
;         MU_G_LOAD(g0, t + 1); MU_B_WRITE(s1, 1, g0); __builtin_amdgcn_sched_barrier(0); MU_GLDS_A(1, t + 1); __builtin_amdgcn_sched_barrier(0);
;         if (t + 3 < nt) { MU_B_ISSUE(s1, t + 3); }
;         MU_COMPUTE(0);
;         MU_END(t + 3 >= nt);
;         if (t + 2 < nt) { MU_B_WAIT(s0, 8); MU_G_LOAD(g0, t + 2); MU_B_WRITE(s0, 0, g0); __builtin_amdgcn_sched_barrier(0); MU_GLDS_A(0, t + 2); __builtin_amdgcn_sched_barrier(0); }
;         if (t + 4 < nt) { MU_B_ISSUE(s0, t + 4); }
;         MU_COMPUTE(1);
;         MU_END(t + 4 >= nt);
	s_load_dwordx8 s[12:19], s[28:29], 0x0
	s_add_u32 s28, s28, 0x100
	s_addc_u32 s29, s29, 0
	v_mfma_f32_16x16x32_bf16 v[78:81], v[238:241], v[218:221], v[78:81]
	v_mfma_f32_16x16x32_bf16 v[74:77], v[242:245], v[218:221], v[74:77]
	v_mfma_f32_16x16x32_bf16 v[70:73], v[246:249], v[218:221], v[70:73]
	v_mfma_f32_16x16x32_bf16 v[66:69], v[250:253], v[218:221], v[66:69]
	ds_read_b128 v[218:221], v93 offset:0
	ds_read_b128 v[142:145], v141 offset:0
	v_lshl_add_u64 v[132:133], v[132:133], 0, s[40:41]
	global_load_dwordx2 v[114:115], v[132:133], off
	global_load_dwordx2 v[116:117], v[132:133], off offset:2048
	v_mfma_f32_16x16x32_bf16 v[62:65], v[238:241], v[222:225], v[62:65]
	v_mfma_f32_16x16x32_bf16 v[58:61], v[242:245], v[222:225], v[58:61]
	v_mfma_f32_16x16x32_bf16 v[54:57], v[246:249], v[222:225], v[54:57]
	v_mfma_f32_16x16x32_bf16 v[50:53], v[250:253], v[222:225], v[50:53]
	ds_read_b128 v[222:225], v93 offset:2048
	ds_read_b128 v[146:149], v141 offset:2048
	v_lshl_add_u64 v[166:167], v[132:133], 0, s[34:35]
	global_load_dwordx2 v[118:119], v[166:167], off
	global_load_dwordx2 v[120:121], v[166:167], off offset:2048
	v_mfma_f32_16x16x32_bf16 v[46:49], v[238:241], v[226:229], v[46:49]
	v_mfma_f32_16x16x32_bf16 v[42:45], v[242:245], v[226:229], v[42:45]
	v_mfma_f32_16x16x32_bf16 v[38:41], v[246:249], v[226:229], v[38:41]
	v_mfma_f32_16x16x32_bf16 v[34:37], v[250:253], v[226:229], v[34:37]
	ds_read_b128 v[226:229], v93 offset:4096
	ds_read_b128 v[150:153], v141 offset:4096
	v_lshl_add_u64 v[166:167], v[132:133], 0, s[36:37]
	global_load_dwordx2 v[122:123], v[166:167], off
	global_load_dwordx2 v[124:125], v[166:167], off offset:2048
	v_mfma_f32_16x16x32_bf16 v[18:21], v[238:241], v[230:233], v[18:21]
	v_mfma_f32_16x16x32_bf16 v[22:25], v[242:245], v[230:233], v[22:25]
	v_mfma_f32_16x16x32_bf16 v[26:29], v[246:249], v[230:233], v[26:29]
	v_mfma_f32_16x16x32_bf16 v[30:33], v[250:253], v[230:233], v[30:33]
	ds_read_b128 v[230:233], v93 offset:6144
	ds_read_b128 v[154:157], v141 offset:6144
	v_lshl_add_u64 v[166:167], v[132:133], 0, s[38:39]
	global_load_dwordx2 v[126:127], v[166:167], off
	global_load_dwordx2 v[128:129], v[166:167], off offset:2048
	v_mfma_f32_16x16x32_bf16 v[2:5], v[238:241], v[234:237], v[2:5]
	v_mfma_f32_16x16x32_bf16 v[6:9], v[242:245], v[234:237], v[6:9]
	v_mfma_f32_16x16x32_bf16 v[10:13], v[246:249], v[234:237], v[10:13]
	v_mfma_f32_16x16x32_bf16 v[14:17], v[250:253], v[234:237], v[14:17]
	ds_read_b128 v[234:237], v93 offset:8192
	s_waitcnt vmcnt(21)
	s_waitcnt lgkmcnt(0)
	s_barrier
	s_mov_b32 s47, s42
	s_mov_b32 s42, s43
	s_mov_b32 s43, s44
	s_mov_b32 s44, s47
	s_add_i32 s47, s44, s6
	s_add_u32 s30, s30, 0x80
	s_addc_u32 s31, s31, 0
	v_mfma_f32_16x16x32_bf16 v[78:81], v[142:145], v[218:221], v[78:81]
	v_mfma_f32_16x16x32_bf16 v[74:77], v[146:149], v[218:221], v[74:77]
	v_mfma_f32_16x16x32_bf16 v[70:73], v[150:153], v[218:221], v[70:73]
	v_mfma_f32_16x16x32_bf16 v[66:69], v[154:157], v[218:221], v[66:69]
	s_mov_b32 m0, s47
	s_nop 0
	global_load_lds_dwordx4 v86, s[30:31]
	v_mfma_f32_16x16x32_bf16 v[62:65], v[142:145], v[222:225], v[62:65]
	v_mfma_f32_16x16x32_bf16 v[58:61], v[146:149], v[222:225], v[58:61]
	v_mfma_f32_16x16x32_bf16 v[54:57], v[150:153], v[222:225], v[54:57]
	v_mfma_f32_16x16x32_bf16 v[50:53], v[154:157], v[222:225], v[50:53]
	s_add_i32 m0, s47, 0x2000
	s_nop 0
	global_load_lds_dwordx4 v134, s[30:31]
	v_mfma_f32_16x16x32_bf16 v[46:49], v[142:145], v[226:229], v[46:49]
	v_mfma_f32_16x16x32_bf16 v[42:45], v[146:149], v[226:229], v[42:45]
	v_mfma_f32_16x16x32_bf16 v[38:41], v[150:153], v[226:229], v[38:41]
	v_mfma_f32_16x16x32_bf16 v[34:37], v[154:157], v[226:229], v[34:37]
	s_add_i32 m0, s47, 0x4000
	s_nop 0
	global_load_lds_dwordx4 v136, s[30:31]
	v_mfma_f32_16x16x32_bf16 v[18:21], v[142:145], v[230:233], v[18:21]
	v_mfma_f32_16x16x32_bf16 v[22:25], v[146:149], v[230:233], v[22:25]
	v_mfma_f32_16x16x32_bf16 v[26:29], v[150:153], v[230:233], v[26:29]
	v_mfma_f32_16x16x32_bf16 v[30:33], v[154:157], v[230:233], v[30:33]
	s_add_i32 m0, s47, 0x6000
	s_nop 0
	global_load_lds_dwordx4 v138, s[30:31]
	v_mfma_f32_16x16x32_bf16 v[2:5], v[142:145], v[234:237], v[2:5]
	v_mfma_f32_16x16x32_bf16 v[6:9], v[146:149], v[234:237], v[6:9]
	v_mfma_f32_16x16x32_bf16 v[10:13], v[150:153], v[234:237], v[10:13]
	v_mfma_f32_16x16x32_bf16 v[14:17], v[154:157], v[234:237], v[14:17]
	s_add_i32 m0, s47, 0x8000
	s_nop 0
	global_load_lds_dwordx4 v140, s[30:31]
	v_mul_f32_e32 v186, s12, v186
	v_mul_f32_e32 v187, s12, v187
	v_mul_f32_e32 v188, s13, v188
	v_mul_f32_e32 v189, s13, v189
	v_mul_f32_e32 v190, s14, v190
	v_mul_f32_e32 v191, s14, v191
	v_mul_f32_e32 v192, s15, v192
	v_mul_f32_e32 v193, s15, v193
	v_mul_f32_e32 v194, s16, v194
	v_mul_f32_e32 v195, s16, v195
	v_mul_f32_e32 v196, s17, v196
	v_mul_f32_e32 v197, s17, v197
	v_mul_f32_e32 v198, s18, v198
	v_mul_f32_e32 v199, s18, v199
	v_mul_f32_e32 v200, s19, v200
	v_mul_f32_e32 v201, s19, v201
	v_cvt_pk_bf16_f32 v158, v186, v188
	v_cvt_pk_bf16_f32 v159, v190, v192
	v_cvt_pk_bf16_f32 v160, v194, v196
	v_cvt_pk_bf16_f32 v161, v198, v200
	v_cvt_pk_bf16_f32 v162, v187, v189
	v_cvt_pk_bf16_f32 v163, v191, v193
	v_cvt_pk_bf16_f32 v164, v195, v197
	v_cvt_pk_bf16_f32 v165, v199, v201
	ds_write_b128 v1, v[158:161] offset:0
	ds_write_b128 v1, v[162:165] offset:128
	v_add_u32_e32 v91, s42, v135
	v_add_u32_e32 v93, s42, v137
	ds_read_b128 v[238:241], v139 offset:19456
	ds_read_b128 v[242:245], v139 offset:21504
	ds_read_b128 v[246:249], v139 offset:23552
	ds_read_b128 v[250:253], v139 offset:25600
	ds_read_b128 v[218:221], v91 offset:0
	ds_read_b128 v[222:225], v91 offset:2048
	ds_read_b128 v[226:229], v91 offset:4096
	ds_read_b128 v[230:233], v91 offset:6144
	ds_read_b128 v[234:237], v91 offset:8192
	s_waitcnt lgkmcnt(0)
; #define MU_GLDS_A(buf, kt) do { _Pragma("unroll") for (int i = 0; i < NMU; ++i) \
;         __builtin_amdgcn_global_load_lds((const unsigned*)((const char*)A + aoff[i] + (size_t)(kt) * 128), (PG8_LAS unsigned*)(MU_SA(buf) + wid * 1024 + i * 8192), 16, 0, 0); } while (0)
; #define MU_B_ISSUE(sb, kt) do { const char* kb_ = Bb + (size_t)(kt) * (64 * (size_t)RB); _Pragma("unroll") for (int j = 0; j < 8; ++j) { const char* p_ = kb_ + (size_t)j * RB; \
;         asm volatile("global_load_dwordx2 %0, %1, off" : "=&v"(sb[j]) : "v"(p_) : "memory"); } } while (0)
; #define MU_B_WAIT(sb, N) asm volatile("s_waitcnt vmcnt(%8)" : "+v"(sb[0]), "+v"(sb[1]), "+v"(sb[2]), "+v"(sb[3]), "+v"(sb[4]), "+v"(sb[5]), "+v"(sb[6]), "+v"(sb[7]) : "n"(N) : "memory")
; #define MU_COMPUTE(buf) MU_COMPUTE_N(buf, NMU)
; template <int MODE>
; __device__ __forceinline__ void moe_unit(PG8_LAS unsigned char* lds, int e, int cb, int slot0  , int nv  , const bf16_t* A, const int* slot_tok,
;                                          const float* W0, const float* W1, bf16_t* OUT, const float* slot_rs  , const int* slot_dst) {
;     ...
;     f32x4 acc[NMU][4];
; #pragma unroll
;     for (int m = 0; m < NMU; ++m)
; #pragma unroll
;         for (int n = 0; n < 4; ++n) acc[m][n] = (f32x4){0.f, 0.f, 0.f, 0.f};
;     f32x2 s0[8], s1[8];
;     float g0[8];
;     MU_GLDS_A(0, 0); MU_B_ISSUE(s0, 0); MU_G_LOAD(g0, 0); MU_B_ISSUE(s1, 1);
;     MU_B_WAIT(s0, 8); MU_B_WRITE(s0, 0, g0); __builtin_amdgcn_sched_barrier(0); MU_B_ISSUE(s0, 2);
;     asm volatile("s_waitcnt vmcnt(16)" ::: "memory");
;     asm volatile("s_waitcnt lgkmcnt(0)" ::: "memory"); __builtin_amdgcn_s_barrier(); asm volatile("" ::: "memory");
; #pragma unroll 1
;     for (int t = 0; t < nt; t += 2) {
;         if (t + 2 < nt) MU_B_WAIT(s1, 8); else MU_B_WAIT(s1, 0);
;         MU_G_LOAD(g0, t + 1); MU_B_WRITE(s1, 1, g0); __builtin_amdgcn_sched_barrier(0); MU_GLDS_A(1, t + 1); __builtin_amdgcn_sched_barrier(0);
;         if (t + 3 < nt) { MU_B_ISSUE(s1, t + 3); }
;         MU_COMPUTE(0);
;         MU_END(t + 3 >= nt);
;         if (t + 2 < nt) { MU_B_WAIT(s0, 8); MU_G_LOAD(g0, t + 2); MU_B_WRITE(s0, 0, g0); __builtin_amdgcn_sched_barrier(0); MU_GLDS_A(0, t + 2); __builtin_amdgcn_sched_barrier(0); }
;         if (t + 4 < nt) { MU_B_ISSUE(s0, t + 4); }
;         MU_COMPUTE(1);
;         MU_END(t + 4 >= nt);
	s_load_dwordx8 s[20:27], s[28:29], 0x0
	s_add_u32 s28, s28, 0x100
	s_addc_u32 s29, s29, 0
	v_mfma_f32_16x16x32_bf16 v[78:81], v[238:241], v[218:221], v[78:81]
	v_mfma_f32_16x16x32_bf16 v[74:77], v[242:245], v[218:221], v[74:77]
	v_mfma_f32_16x16x32_bf16 v[70:73], v[246:249], v[218:221], v[70:73]
	v_mfma_f32_16x16x32_bf16 v[66:69], v[250:253], v[218:221], v[66:69]
	ds_read_b128 v[218:221], v93 offset:0
	ds_read_b128 v[142:145], v141 offset:19456
	v_lshl_add_u64 v[132:133], v[132:133], 0, s[40:41]
	global_load_dwordx2 v[186:187], v[132:133], off
	global_load_dwordx2 v[188:189], v[132:133], off offset:2048
	v_mfma_f32_16x16x32_bf16 v[62:65], v[238:241], v[222:225], v[62:65]
	v_mfma_f32_16x16x32_bf16 v[58:61], v[242:245], v[222:225], v[58:61]
	v_mfma_f32_16x16x32_bf16 v[54:57], v[246:249], v[222:225], v[54:57]
	v_mfma_f32_16x16x32_bf16 v[50:53], v[250:253], v[222:225], v[50:53]
	ds_read_b128 v[222:225], v93 offset:2048
	ds_read_b128 v[146:149], v141 offset:21504
	v_lshl_add_u64 v[166:167], v[132:133], 0, s[34:35]
	global_load_dwordx2 v[190:191], v[166:167], off
	global_load_dwordx2 v[192:193], v[166:167], off offset:2048
	v_mfma_f32_16x16x32_bf16 v[46:49], v[238:241], v[226:229], v[46:49]
	v_mfma_f32_16x16x32_bf16 v[42:45], v[242:245], v[226:229], v[42:45]
	v_mfma_f32_16x16x32_bf16 v[38:41], v[246:249], v[226:229], v[38:41]
	v_mfma_f32_16x16x32_bf16 v[34:37], v[250:253], v[226:229], v[34:37]
	ds_read_b128 v[226:229], v93 offset:4096
	ds_read_b128 v[150:153], v141 offset:23552
	v_lshl_add_u64 v[166:167], v[132:133], 0, s[36:37]
	global_load_dwordx2 v[194:195], v[166:167], off
	global_load_dwordx2 v[196:197], v[166:167], off offset:2048
	v_mfma_f32_16x16x32_bf16 v[18:21], v[238:241], v[230:233], v[18:21]
	v_mfma_f32_16x16x32_bf16 v[22:25], v[242:245], v[230:233], v[22:25]
	v_mfma_f32_16x16x32_bf16 v[26:29], v[246:249], v[230:233], v[26:29]
	v_mfma_f32_16x16x32_bf16 v[30:33], v[250:253], v[230:233], v[30:33]
	ds_read_b128 v[230:233], v93 offset:6144
	ds_read_b128 v[154:157], v141 offset:25600
	v_lshl_add_u64 v[166:167], v[132:133], 0, s[38:39]
	global_load_dwordx2 v[198:199], v[166:167], off
	global_load_dwordx2 v[200:201], v[166:167], off offset:2048
	v_mfma_f32_16x16x32_bf16 v[2:5], v[238:241], v[234:237], v[2:5]
	v_mfma_f32_16x16x32_bf16 v[6:9], v[242:245], v[234:237], v[6:9]
	v_mfma_f32_16x16x32_bf16 v[10:13], v[246:249], v[234:237], v[10:13]
	v_mfma_f32_16x16x32_bf16 v[14:17], v[250:253], v[234:237], v[14:17]
	ds_read_b128 v[234:237], v93 offset:8192
	s_waitcnt vmcnt(21)
	s_waitcnt lgkmcnt(0)
	s_barrier
	s_mov_b32 s47, s42
	s_mov_b32 s42, s43
	s_mov_b32 s43, s44
	s_mov_b32 s44, s47
	s_add_i32 s47, s44, s6
	s_add_u32 s30, s30, 0x80
	s_addc_u32 s31, s31, 0
	v_mfma_f32_16x16x32_bf16 v[78:81], v[142:145], v[218:221], v[78:81]
	v_mfma_f32_16x16x32_bf16 v[74:77], v[146:149], v[218:221], v[74:77]
	v_mfma_f32_16x16x32_bf16 v[70:73], v[150:153], v[218:221], v[70:73]
	v_mfma_f32_16x16x32_bf16 v[66:69], v[154:157], v[218:221], v[66:69]
	s_mov_b32 m0, s47
	s_nop 0
	global_load_lds_dwordx4 v86, s[30:31]
	v_mfma_f32_16x16x32_bf16 v[62:65], v[142:145], v[222:225], v[62:65]
	v_mfma_f32_16x16x32_bf16 v[58:61], v[146:149], v[222:225], v[58:61]
	v_mfma_f32_16x16x32_bf16 v[54:57], v[150:153], v[222:225], v[54:57]
	v_mfma_f32_16x16x32_bf16 v[50:53], v[154:157], v[222:225], v[50:53]
	s_add_i32 m0, s47, 0x2000
	s_nop 0
	global_load_lds_dwordx4 v134, s[30:31]
	v_mfma_f32_16x16x32_bf16 v[46:49], v[142:145], v[226:229], v[46:49]
	v_mfma_f32_16x16x32_bf16 v[42:45], v[146:149], v[226:229], v[42:45]
	v_mfma_f32_16x16x32_bf16 v[38:41], v[150:153], v[226:229], v[38:41]
	v_mfma_f32_16x16x32_bf16 v[34:37], v[154:157], v[226:229], v[34:37]
	s_add_i32 m0, s47, 0x4000
	s_nop 0
	global_load_lds_dwordx4 v136, s[30:31]
	v_mfma_f32_16x16x32_bf16 v[18:21], v[142:145], v[230:233], v[18:21]
	v_mfma_f32_16x16x32_bf16 v[22:25], v[146:149], v[230:233], v[22:25]
	v_mfma_f32_16x16x32_bf16 v[26:29], v[150:153], v[230:233], v[26:29]
	v_mfma_f32_16x16x32_bf16 v[30:33], v[154:157], v[230:233], v[30:33]
	s_add_i32 m0, s47, 0x6000
	s_nop 0
	global_load_lds_dwordx4 v138, s[30:31]
	v_mfma_f32_16x16x32_bf16 v[2:5], v[142:145], v[234:237], v[2:5]
	v_mfma_f32_16x16x32_bf16 v[6:9], v[146:149], v[234:237], v[6:9]
	v_mfma_f32_16x16x32_bf16 v[10:13], v[150:153], v[234:237], v[10:13]
	v_mfma_f32_16x16x32_bf16 v[14:17], v[154:157], v[234:237], v[14:17]
	s_add_i32 m0, s47, 0x8000
	s_nop 0
	global_load_lds_dwordx4 v140, s[30:31]
	v_mul_f32_e32 v202, s20, v202
	v_mul_f32_e32 v203, s20, v203
	v_mul_f32_e32 v204, s21, v204
	v_mul_f32_e32 v205, s21, v205
	v_mul_f32_e32 v206, s22, v206
	v_mul_f32_e32 v207, s22, v207
	v_mul_f32_e32 v208, s23, v208
	v_mul_f32_e32 v209, s23, v209
	v_mul_f32_e32 v210, s24, v210
	v_mul_f32_e32 v211, s24, v211
	v_mul_f32_e32 v212, s25, v212
	v_mul_f32_e32 v213, s25, v213
	v_mul_f32_e32 v214, s26, v214
	v_mul_f32_e32 v215, s26, v215
	v_mul_f32_e32 v216, s27, v216
	v_mul_f32_e32 v217, s27, v217
	v_cvt_pk_bf16_f32 v158, v202, v204
	v_cvt_pk_bf16_f32 v159, v206, v208
	v_cvt_pk_bf16_f32 v160, v210, v212
	v_cvt_pk_bf16_f32 v161, v214, v216
	v_cvt_pk_bf16_f32 v162, v203, v205
	v_cvt_pk_bf16_f32 v163, v207, v209
	v_cvt_pk_bf16_f32 v164, v211, v213
	v_cvt_pk_bf16_f32 v165, v215, v217
	ds_write_b128 v1, v[158:161] offset:19456
	ds_write_b128 v1, v[162:165] offset:19584
	v_add_u32_e32 v91, s42, v135
	v_add_u32_e32 v93, s42, v137
	ds_read_b128 v[238:241], v139 offset:0
	ds_read_b128 v[242:245], v139 offset:2048
	ds_read_b128 v[246:249], v139 offset:4096
	ds_read_b128 v[250:253], v139 offset:6144
	ds_read_b128 v[218:221], v91 offset:0
	ds_read_b128 v[222:225], v91 offset:2048
	ds_read_b128 v[226:229], v91 offset:4096
	ds_read_b128 v[230:233], v91 offset:6144
	ds_read_b128 v[234:237], v91 offset:8192
	s_waitcnt lgkmcnt(0)
; #define MU_GLDS_A(buf, kt) do { _Pragma("unroll") for (int i = 0; i < NMU; ++i) \
;         __builtin_amdgcn_global_load_lds((const unsigned*)((const char*)A + aoff[i] + (size_t)(kt) * 128), (PG8_LAS unsigned*)(MU_SA(buf) + wid * 1024 + i * 8192), 16, 0, 0); } while (0)
; #define MU_B_ISSUE(sb, kt) do { const char* kb_ = Bb + (size_t)(kt) * (64 * (size_t)RB); _Pragma("unroll") for (int j = 0; j < 8; ++j) { const char* p_ = kb_ + (size_t)j * RB; \
;         asm volatile("global_load_dwordx2 %0, %1, off" : "=&v"(sb[j]) : "v"(p_) : "memory"); } } while (0)
; #define MU_B_WAIT(sb, N) asm volatile("s_waitcnt vmcnt(%8)" : "+v"(sb[0]), "+v"(sb[1]), "+v"(sb[2]), "+v"(sb[3]), "+v"(sb[4]), "+v"(sb[5]), "+v"(sb[6]), "+v"(sb[7]) : "n"(N) : "memory")
; #define MU_COMPUTE(buf) MU_COMPUTE_N(buf, NMU)
; template <int MODE>
; __device__ __forceinline__ void moe_unit(PG8_LAS unsigned char* lds, int e, int cb, int slot0  , int nv  , const bf16_t* A, const int* slot_tok,
;                                          const float* W0, const float* W1, bf16_t* OUT, const float* slot_rs  , const int* slot_dst) {
;     ...
;     f32x4 acc[NMU][4];
; #pragma unroll
;     for (int m = 0; m < NMU; ++m)
; #pragma unroll
;         for (int n = 0; n < 4; ++n) acc[m][n] = (f32x4){0.f, 0.f, 0.f, 0.f};
;     f32x2 s0[8], s1[8];
;     float g0[8];
;     MU_GLDS_A(0, 0); MU_B_ISSUE(s0, 0); MU_G_LOAD(g0, 0); MU_B_ISSUE(s1, 1);
;     MU_B_WAIT(s0, 8); MU_B_WRITE(s0, 0, g0); __builtin_amdgcn_sched_barrier(0); MU_B_ISSUE(s0, 2);
;     asm volatile("s_waitcnt vmcnt(16)" ::: "memory");
;     asm volatile("s_waitcnt lgkmcnt(0)" ::: "memory"); __builtin_amdgcn_s_barrier(); asm volatile("" ::: "memory");
; #pragma unroll 1
;     for (int t = 0; t < nt; t += 2) {
;         if (t + 2 < nt) MU_B_WAIT(s1, 8); else MU_B_WAIT(s1, 0);
;         MU_G_LOAD(g0, t + 1); MU_B_WRITE(s1, 1, g0); __builtin_amdgcn_sched_barrier(0); MU_GLDS_A(1, t + 1); __builtin_amdgcn_sched_barrier(0);
;         if (t + 3 < nt) { MU_B_ISSUE(s1, t + 3); }
;         MU_COMPUTE(0);
;         MU_END(t + 3 >= nt);
;         if (t + 2 < nt) { MU_B_WAIT(s0, 8); MU_G_LOAD(g0, t + 2); MU_B_WRITE(s0, 0, g0); __builtin_amdgcn_sched_barrier(0); MU_GLDS_A(0, t + 2); __builtin_amdgcn_sched_barrier(0); }
;         if (t + 4 < nt) { MU_B_ISSUE(s0, t + 4); }
;         MU_COMPUTE(1);
;         MU_END(t + 4 >= nt);
	s_load_dwordx8 s[12:19], s[28:29], 0x0
	s_add_u32 s28, s28, 0x100
	s_addc_u32 s29, s29, 0
	v_mfma_f32_16x16x32_bf16 v[78:81], v[238:241], v[218:221], v[78:81]
	v_mfma_f32_16x16x32_bf16 v[74:77], v[242:245], v[218:221], v[74:77]
	v_mfma_f32_16x16x32_bf16 v[70:73], v[246:249], v[218:221], v[70:73]
	v_mfma_f32_16x16x32_bf16 v[66:69], v[250:253], v[218:221], v[66:69]
	ds_read_b128 v[218:221], v93 offset:0
	ds_read_b128 v[142:145], v141 offset:0
	v_lshl_add_u64 v[132:133], v[132:133], 0, s[40:41]
	global_load_dwordx2 v[202:203], v[132:133], off
	global_load_dwordx2 v[204:205], v[132:133], off offset:2048
	v_mfma_f32_16x16x32_bf16 v[62:65], v[238:241], v[222:225], v[62:65]
	v_mfma_f32_16x16x32_bf16 v[58:61], v[242:245], v[222:225], v[58:61]
	v_mfma_f32_16x16x32_bf16 v[54:57], v[246:249], v[222:225], v[54:57]
	v_mfma_f32_16x16x32_bf16 v[50:53], v[250:253], v[222:225], v[50:53]
	ds_read_b128 v[222:225], v93 offset:2048
	ds_read_b128 v[146:149], v141 offset:2048
	v_lshl_add_u64 v[166:167], v[132:133], 0, s[34:35]
	global_load_dwordx2 v[206:207], v[166:167], off
	global_load_dwordx2 v[208:209], v[166:167], off offset:2048
	v_mfma_f32_16x16x32_bf16 v[46:49], v[238:241], v[226:229], v[46:49]
	v_mfma_f32_16x16x32_bf16 v[42:45], v[242:245], v[226:229], v[42:45]
	v_mfma_f32_16x16x32_bf16 v[38:41], v[246:249], v[226:229], v[38:41]
	v_mfma_f32_16x16x32_bf16 v[34:37], v[250:253], v[226:229], v[34:37]
	ds_read_b128 v[226:229], v93 offset:4096
	ds_read_b128 v[150:153], v141 offset:4096
	v_lshl_add_u64 v[166:167], v[132:133], 0, s[36:37]
	global_load_dwordx2 v[210:211], v[166:167], off
	global_load_dwordx2 v[212:213], v[166:167], off offset:2048
	v_mfma_f32_16x16x32_bf16 v[18:21], v[238:241], v[230:233], v[18:21]
	v_mfma_f32_16x16x32_bf16 v[22:25], v[242:245], v[230:233], v[22:25]
	v_mfma_f32_16x16x32_bf16 v[26:29], v[246:249], v[230:233], v[26:29]
	v_mfma_f32_16x16x32_bf16 v[30:33], v[250:253], v[230:233], v[30:33]
	ds_read_b128 v[230:233], v93 offset:6144
	ds_read_b128 v[154:157], v141 offset:6144
	v_lshl_add_u64 v[166:167], v[132:133], 0, s[38:39]
	global_load_dwordx2 v[214:215], v[166:167], off
	global_load_dwordx2 v[216:217], v[166:167], off offset:2048
	v_mfma_f32_16x16x32_bf16 v[2:5], v[238:241], v[234:237], v[2:5]
	v_mfma_f32_16x16x32_bf16 v[6:9], v[242:245], v[234:237], v[6:9]
	v_mfma_f32_16x16x32_bf16 v[10:13], v[246:249], v[234:237], v[10:13]
	v_mfma_f32_16x16x32_bf16 v[14:17], v[250:253], v[234:237], v[14:17]
	ds_read_b128 v[234:237], v93 offset:8192
	s_waitcnt vmcnt(21)
	s_waitcnt lgkmcnt(0)
	s_barrier
	s_mov_b32 s47, s42
	s_mov_b32 s42, s43
	s_mov_b32 s43, s44
	s_mov_b32 s44, s47
	s_add_i32 s47, s44, s6
	s_add_u32 s30, s30, 0x80
	s_addc_u32 s31, s31, 0
	v_mfma_f32_16x16x32_bf16 v[78:81], v[142:145], v[218:221], v[78:81]
	v_mfma_f32_16x16x32_bf16 v[74:77], v[146:149], v[218:221], v[74:77]
	v_mfma_f32_16x16x32_bf16 v[70:73], v[150:153], v[218:221], v[70:73]
	v_mfma_f32_16x16x32_bf16 v[66:69], v[154:157], v[218:221], v[66:69]
	s_mov_b32 m0, s47
	s_nop 0
	global_load_lds_dwordx4 v86, s[30:31]
	v_mfma_f32_16x16x32_bf16 v[62:65], v[142:145], v[222:225], v[62:65]
	v_mfma_f32_16x16x32_bf16 v[58:61], v[146:149], v[222:225], v[58:61]
	v_mfma_f32_16x16x32_bf16 v[54:57], v[150:153], v[222:225], v[54:57]
	v_mfma_f32_16x16x32_bf16 v[50:53], v[154:157], v[222:225], v[50:53]
	s_add_i32 m0, s47, 0x2000
	s_nop 0
	global_load_lds_dwordx4 v134, s[30:31]
	v_mfma_f32_16x16x32_bf16 v[46:49], v[142:145], v[226:229], v[46:49]
	v_mfma_f32_16x16x32_bf16 v[42:45], v[146:149], v[226:229], v[42:45]
	v_mfma_f32_16x16x32_bf16 v[38:41], v[150:153], v[226:229], v[38:41]
	v_mfma_f32_16x16x32_bf16 v[34:37], v[154:157], v[226:229], v[34:37]
	s_add_i32 m0, s47, 0x4000
	s_nop 0
	global_load_lds_dwordx4 v136, s[30:31]
	v_mfma_f32_16x16x32_bf16 v[18:21], v[142:145], v[230:233], v[18:21]
	v_mfma_f32_16x16x32_bf16 v[22:25], v[146:149], v[230:233], v[22:25]
	v_mfma_f32_16x16x32_bf16 v[26:29], v[150:153], v[230:233], v[26:29]
	v_mfma_f32_16x16x32_bf16 v[30:33], v[154:157], v[230:233], v[30:33]
	s_add_i32 m0, s47, 0x6000
	s_nop 0
	global_load_lds_dwordx4 v138, s[30:31]
	v_mfma_f32_16x16x32_bf16 v[2:5], v[142:145], v[234:237], v[2:5]
	v_mfma_f32_16x16x32_bf16 v[6:9], v[146:149], v[234:237], v[6:9]
	v_mfma_f32_16x16x32_bf16 v[10:13], v[150:153], v[234:237], v[10:13]
	v_mfma_f32_16x16x32_bf16 v[14:17], v[154:157], v[234:237], v[14:17]
	s_add_i32 m0, s47, 0x8000
	s_nop 0
	global_load_lds_dwordx4 v140, s[30:31]
	v_mul_f32_e32 v98, s12, v98
	v_mul_f32_e32 v99, s12, v99
	v_mul_f32_e32 v100, s13, v100
	v_mul_f32_e32 v101, s13, v101
	v_mul_f32_e32 v102, s14, v102
	v_mul_f32_e32 v103, s14, v103
	v_mul_f32_e32 v104, s15, v104
	v_mul_f32_e32 v105, s15, v105
	v_mul_f32_e32 v106, s16, v106
	v_mul_f32_e32 v107, s16, v107
	v_mul_f32_e32 v108, s17, v108
	v_mul_f32_e32 v109, s17, v109
	v_mul_f32_e32 v110, s18, v110
	v_mul_f32_e32 v111, s18, v111
	v_mul_f32_e32 v112, s19, v112
	v_mul_f32_e32 v113, s19, v113
	v_cvt_pk_bf16_f32 v158, v98, v100
	v_cvt_pk_bf16_f32 v159, v102, v104
	v_cvt_pk_bf16_f32 v160, v106, v108
	v_cvt_pk_bf16_f32 v161, v110, v112
	v_cvt_pk_bf16_f32 v162, v99, v101
	v_cvt_pk_bf16_f32 v163, v103, v105
	v_cvt_pk_bf16_f32 v164, v107, v109
	v_cvt_pk_bf16_f32 v165, v111, v113
	ds_write_b128 v1, v[158:161] offset:0
	ds_write_b128 v1, v[162:165] offset:128
	v_add_u32_e32 v91, s42, v135
	v_add_u32_e32 v93, s42, v137
	ds_read_b128 v[238:241], v139 offset:19456
	ds_read_b128 v[242:245], v139 offset:21504
	ds_read_b128 v[246:249], v139 offset:23552
	ds_read_b128 v[250:253], v139 offset:25600
	ds_read_b128 v[218:221], v91 offset:0
	ds_read_b128 v[222:225], v91 offset:2048
	ds_read_b128 v[226:229], v91 offset:4096
	ds_read_b128 v[230:233], v91 offset:6144
	ds_read_b128 v[234:237], v91 offset:8192
	s_waitcnt lgkmcnt(0)
; #define MU_GLDS_A(buf, kt) do { _Pragma("unroll") for (int i = 0; i < NMU; ++i) \
;         __builtin_amdgcn_global_load_lds((const unsigned*)((const char*)A + aoff[i] + (size_t)(kt) * 128), (PG8_LAS unsigned*)(MU_SA(buf) + wid * 1024 + i * 8192), 16, 0, 0); } while (0)
; #define MU_B_ISSUE(sb, kt) do { const char* kb_ = Bb + (size_t)(kt) * (64 * (size_t)RB); _Pragma("unroll") for (int j = 0; j < 8; ++j) { const char* p_ = kb_ + (size_t)j * RB; \
;         asm volatile("global_load_dwordx2 %0, %1, off" : "=&v"(sb[j]) : "v"(p_) : "memory"); } } while (0)
; #define MU_B_WAIT(sb, N) asm volatile("s_waitcnt vmcnt(%8)" : "+v"(sb[0]), "+v"(sb[1]), "+v"(sb[2]), "+v"(sb[3]), "+v"(sb[4]), "+v"(sb[5]), "+v"(sb[6]), "+v"(sb[7]) : "n"(N) : "memory")
; #define MU_COMPUTE(buf) MU_COMPUTE_N(buf, NMU)
; template <int MODE>
; __device__ __forceinline__ void moe_unit(PG8_LAS unsigned char* lds, int e, int cb, int slot0  , int nv  , const bf16_t* A, const int* slot_tok,
;                                          const float* W0, const float* W1, bf16_t* OUT, const float* slot_rs  , const int* slot_dst) {
;     ...
;     f32x4 acc[NMU][4];
; #pragma unroll
;     for (int m = 0; m < NMU; ++m)
; #pragma unroll
;         for (int n = 0; n < 4; ++n) acc[m][n] = (f32x4){0.f, 0.f, 0.f, 0.f};
;     f32x2 s0[8], s1[8];
;     float g0[8];
;     MU_GLDS_A(0, 0); MU_B_ISSUE(s0, 0); MU_G_LOAD(g0, 0); MU_B_ISSUE(s1, 1);
;     MU_B_WAIT(s0, 8); MU_B_WRITE(s0, 0, g0); __builtin_amdgcn_sched_barrier(0); MU_B_ISSUE(s0, 2);
;     asm volatile("s_waitcnt vmcnt(16)" ::: "memory");
;     asm volatile("s_waitcnt lgkmcnt(0)" ::: "memory"); __builtin_amdgcn_s_barrier(); asm volatile("" ::: "memory");
; #pragma unroll 1
;     for (int t = 0; t < nt; t += 2) {
;         if (t + 2 < nt) MU_B_WAIT(s1, 8); else MU_B_WAIT(s1, 0);
;         MU_G_LOAD(g0, t + 1); MU_B_WRITE(s1, 1, g0); __builtin_amdgcn_sched_barrier(0); MU_GLDS_A(1, t + 1); __builtin_amdgcn_sched_barrier(0);
;         if (t + 3 < nt) { MU_B_ISSUE(s1, t + 3); }
;         MU_COMPUTE(0);
;         MU_END(t + 3 >= nt);
;         if (t + 2 < nt) { MU_B_WAIT(s0, 8); MU_G_LOAD(g0, t + 2); MU_B_WRITE(s0, 0, g0); __builtin_amdgcn_sched_barrier(0); MU_GLDS_A(0, t + 2); __builtin_amdgcn_sched_barrier(0); }
;         if (t + 4 < nt) { MU_B_ISSUE(s0, t + 4); }
;         MU_COMPUTE(1);
;         MU_END(t + 4 >= nt);
	s_load_dwordx8 s[20:27], s[28:29], 0x0
	s_add_u32 s28, s28, 0x100
	s_addc_u32 s29, s29, 0
	v_mfma_f32_16x16x32_bf16 v[78:81], v[238:241], v[218:221], v[78:81]
	v_mfma_f32_16x16x32_bf16 v[74:77], v[242:245], v[218:221], v[74:77]
	v_mfma_f32_16x16x32_bf16 v[70:73], v[246:249], v[218:221], v[70:73]
	v_mfma_f32_16x16x32_bf16 v[66:69], v[250:253], v[218:221], v[66:69]
	ds_read_b128 v[218:221], v93 offset:0
	ds_read_b128 v[142:145], v141 offset:19456
	v_mfma_f32_16x16x32_bf16 v[62:65], v[238:241], v[222:225], v[62:65]
	v_mfma_f32_16x16x32_bf16 v[58:61], v[242:245], v[222:225], v[58:61]
	v_mfma_f32_16x16x32_bf16 v[54:57], v[246:249], v[222:225], v[54:57]
	v_mfma_f32_16x16x32_bf16 v[50:53], v[250:253], v[222:225], v[50:53]
	ds_read_b128 v[222:225], v93 offset:2048
	ds_read_b128 v[146:149], v141 offset:21504
	v_mfma_f32_16x16x32_bf16 v[46:49], v[238:241], v[226:229], v[46:49]
	v_mfma_f32_16x16x32_bf16 v[42:45], v[242:245], v[226:229], v[42:45]
	v_mfma_f32_16x16x32_bf16 v[38:41], v[246:249], v[226:229], v[38:41]
	v_mfma_f32_16x16x32_bf16 v[34:37], v[250:253], v[226:229], v[34:37]
	ds_read_b128 v[226:229], v93 offset:4096
	ds_read_b128 v[150:153], v141 offset:23552
	v_mfma_f32_16x16x32_bf16 v[18:21], v[238:241], v[230:233], v[18:21]
	v_mfma_f32_16x16x32_bf16 v[22:25], v[242:245], v[230:233], v[22:25]
	v_mfma_f32_16x16x32_bf16 v[26:29], v[246:249], v[230:233], v[26:29]
	v_mfma_f32_16x16x32_bf16 v[30:33], v[250:253], v[230:233], v[30:33]
	ds_read_b128 v[230:233], v93 offset:6144
	ds_read_b128 v[154:157], v141 offset:25600
	v_mfma_f32_16x16x32_bf16 v[2:5], v[238:241], v[234:237], v[2:5]
	v_mfma_f32_16x16x32_bf16 v[6:9], v[242:245], v[234:237], v[6:9]
	v_mfma_f32_16x16x32_bf16 v[10:13], v[246:249], v[234:237], v[10:13]
	v_mfma_f32_16x16x32_bf16 v[14:17], v[250:253], v[234:237], v[14:17]
	ds_read_b128 v[234:237], v93 offset:8192
	s_waitcnt vmcnt(13)
	s_waitcnt lgkmcnt(0)
	s_barrier
	s_mov_b32 s47, s42
	s_mov_b32 s42, s43
	s_mov_b32 s43, s44
	s_mov_b32 s44, s47
	s_add_i32 s47, s44, s6
	s_add_u32 s30, s30, 0x80
	s_addc_u32 s31, s31, 0
	v_mfma_f32_16x16x32_bf16 v[78:81], v[142:145], v[218:221], v[78:81]
	v_mfma_f32_16x16x32_bf16 v[74:77], v[146:149], v[218:221], v[74:77]
	v_mfma_f32_16x16x32_bf16 v[70:73], v[150:153], v[218:221], v[70:73]
	v_mfma_f32_16x16x32_bf16 v[66:69], v[154:157], v[218:221], v[66:69]
	s_mov_b32 m0, s47
	s_nop 0
	global_load_lds_dwordx4 v86, s[30:31]
	v_mfma_f32_16x16x32_bf16 v[62:65], v[142:145], v[222:225], v[62:65]
	v_mfma_f32_16x16x32_bf16 v[58:61], v[146:149], v[222:225], v[58:61]
	v_mfma_f32_16x16x32_bf16 v[54:57], v[150:153], v[222:225], v[54:57]
	v_mfma_f32_16x16x32_bf16 v[50:53], v[154:157], v[222:225], v[50:53]
	s_add_i32 m0, s47, 0x2000
	s_nop 0
	global_load_lds_dwordx4 v134, s[30:31]
	v_mfma_f32_16x16x32_bf16 v[46:49], v[142:145], v[226:229], v[46:49]
	v_mfma_f32_16x16x32_bf16 v[42:45], v[146:149], v[226:229], v[42:45]
	v_mfma_f32_16x16x32_bf16 v[38:41], v[150:153], v[226:229], v[38:41]
	v_mfma_f32_16x16x32_bf16 v[34:37], v[154:157], v[226:229], v[34:37]
	s_add_i32 m0, s47, 0x4000
	s_nop 0
	global_load_lds_dwordx4 v136, s[30:31]
	v_mfma_f32_16x16x32_bf16 v[18:21], v[142:145], v[230:233], v[18:21]
	v_mfma_f32_16x16x32_bf16 v[22:25], v[146:149], v[230:233], v[22:25]
	v_mfma_f32_16x16x32_bf16 v[26:29], v[150:153], v[230:233], v[26:29]
	v_mfma_f32_16x16x32_bf16 v[30:33], v[154:157], v[230:233], v[30:33]
	s_add_i32 m0, s47, 0x6000
	s_nop 0
	global_load_lds_dwordx4 v138, s[30:31]
	v_mfma_f32_16x16x32_bf16 v[2:5], v[142:145], v[234:237], v[2:5]
	v_mfma_f32_16x16x32_bf16 v[6:9], v[146:149], v[234:237], v[6:9]
	v_mfma_f32_16x16x32_bf16 v[10:13], v[150:153], v[234:237], v[10:13]
	v_mfma_f32_16x16x32_bf16 v[14:17], v[154:157], v[234:237], v[14:17]
	s_add_i32 m0, s47, 0x8000
	s_nop 0
	global_load_lds_dwordx4 v140, s[30:31]
	v_mul_f32_e32 v114, s20, v114
	v_mul_f32_e32 v115, s20, v115
	v_mul_f32_e32 v116, s21, v116
	v_mul_f32_e32 v117, s21, v117
	v_mul_f32_e32 v118, s22, v118
	v_mul_f32_e32 v119, s22, v119
	v_mul_f32_e32 v120, s23, v120
	v_mul_f32_e32 v121, s23, v121
	v_mul_f32_e32 v122, s24, v122
	v_mul_f32_e32 v123, s24, v123
	v_mul_f32_e32 v124, s25, v124
	v_mul_f32_e32 v125, s25, v125
	v_mul_f32_e32 v126, s26, v126
	v_mul_f32_e32 v127, s26, v127
	v_mul_f32_e32 v128, s27, v128
	v_mul_f32_e32 v129, s27, v129
	v_cvt_pk_bf16_f32 v158, v114, v116
	v_cvt_pk_bf16_f32 v159, v118, v120
	v_cvt_pk_bf16_f32 v160, v122, v124
	v_cvt_pk_bf16_f32 v161, v126, v128
	v_cvt_pk_bf16_f32 v162, v115, v117
	v_cvt_pk_bf16_f32 v163, v119, v121
	v_cvt_pk_bf16_f32 v164, v123, v125
	v_cvt_pk_bf16_f32 v165, v127, v129
	ds_write_b128 v1, v[158:161] offset:19456
	ds_write_b128 v1, v[162:165] offset:19584
	v_add_u32_e32 v91, s42, v135
	v_add_u32_e32 v93, s42, v137
	ds_read_b128 v[238:241], v139 offset:0
	ds_read_b128 v[242:245], v139 offset:2048
	ds_read_b128 v[246:249], v139 offset:4096
	ds_read_b128 v[250:253], v139 offset:6144
	ds_read_b128 v[218:221], v91 offset:0
	ds_read_b128 v[222:225], v91 offset:2048
	ds_read_b128 v[226:229], v91 offset:4096
	ds_read_b128 v[230:233], v91 offset:6144
	ds_read_b128 v[234:237], v91 offset:8192
	s_waitcnt lgkmcnt(0)
	s_load_dwordx8 s[12:19], s[28:29], 0x0
	s_add_u32 s28, s28, 0x100
	s_addc_u32 s29, s29, 0
	v_mfma_f32_16x16x32_bf16 v[78:81], v[238:241], v[218:221], v[78:81]
	v_mfma_f32_16x16x32_bf16 v[74:77], v[242:245], v[218:221], v[74:77]
	v_mfma_f32_16x16x32_bf16 v[70:73], v[246:249], v[218:221], v[70:73]
	v_mfma_f32_16x16x32_bf16 v[66:69], v[250:253], v[218:221], v[66:69]
	ds_read_b128 v[218:221], v93 offset:0
	ds_read_b128 v[142:145], v141 offset:0
	v_mfma_f32_16x16x32_bf16 v[62:65], v[238:241], v[222:225], v[62:65]
	v_mfma_f32_16x16x32_bf16 v[58:61], v[242:245], v[222:225], v[58:61]
	v_mfma_f32_16x16x32_bf16 v[54:57], v[246:249], v[222:225], v[54:57]
	v_mfma_f32_16x16x32_bf16 v[50:53], v[250:253], v[222:225], v[50:53]
	ds_read_b128 v[222:225], v93 offset:2048
	ds_read_b128 v[146:149], v141 offset:2048
	v_mfma_f32_16x16x32_bf16 v[46:49], v[238:241], v[226:229], v[46:49]
	v_mfma_f32_16x16x32_bf16 v[42:45], v[242:245], v[226:229], v[42:45]
	v_mfma_f32_16x16x32_bf16 v[38:41], v[246:249], v[226:229], v[38:41]
	v_mfma_f32_16x16x32_bf16 v[34:37], v[250:253], v[226:229], v[34:37]
	ds_read_b128 v[226:229], v93 offset:4096
	ds_read_b128 v[150:153], v141 offset:4096
	v_mfma_f32_16x16x32_bf16 v[18:21], v[238:241], v[230:233], v[18:21]
	v_mfma_f32_16x16x32_bf16 v[22:25], v[242:245], v[230:233], v[22:25]
	v_mfma_f32_16x16x32_bf16 v[26:29], v[246:249], v[230:233], v[26:29]
	v_mfma_f32_16x16x32_bf16 v[30:33], v[250:253], v[230:233], v[30:33]
	ds_read_b128 v[230:233], v93 offset:6144
	ds_read_b128 v[154:157], v141 offset:6144
	v_mfma_f32_16x16x32_bf16 v[2:5], v[238:241], v[234:237], v[2:5]
	v_mfma_f32_16x16x32_bf16 v[6:9], v[242:245], v[234:237], v[6:9]
	v_mfma_f32_16x16x32_bf16 v[10:13], v[246:249], v[234:237], v[10:13]
	v_mfma_f32_16x16x32_bf16 v[14:17], v[250:253], v[234:237], v[14:17]
	ds_read_b128 v[234:237], v93 offset:8192
	s_waitcnt vmcnt(5)
	s_waitcnt lgkmcnt(0)
	s_barrier
; #define MU_GLDS_A(buf, kt) do { _Pragma("unroll") for (int i = 0; i < NMU; ++i) \
;         __builtin_amdgcn_global_load_lds((const unsigned*)((const char*)A + aoff[i] + (size_t)(kt) * 128), (PG8_LAS unsigned*)(MU_SA(buf) + wid * 1024 + i * 8192), 16, 0, 0); } while (0)
; #define MU_B_ISSUE(sb, kt) do { const char* kb_ = Bb + (size_t)(kt) * (64 * (size_t)RB); _Pragma("unroll") for (int j = 0; j < 8; ++j) { const char* p_ = kb_ + (size_t)j * RB; \
;         asm volatile("global_load_dwordx2 %0, %1, off" : "=&v"(sb[j]) : "v"(p_) : "memory"); } } while (0)
; #define MU_B_WAIT(sb, N) asm volatile("s_waitcnt vmcnt(%8)" : "+v"(sb[0]), "+v"(sb[1]), "+v"(sb[2]), "+v"(sb[3]), "+v"(sb[4]), "+v"(sb[5]), "+v"(sb[6]), "+v"(sb[7]) : "n"(N) : "memory")
; #define MU_COMPUTE(buf) MU_COMPUTE_N(buf, NMU)
; template <int MODE>
; __device__ __forceinline__ void moe_unit(PG8_LAS unsigned char* lds, int e, int cb, int slot0  , int nv  , const bf16_t* A, const int* slot_tok,
;                                          const float* W0, const float* W1, bf16_t* OUT, const float* slot_rs  , const int* slot_dst) {
;     ...
;     f32x4 acc[NMU][4];
; #pragma unroll
;     for (int m = 0; m < NMU; ++m)
; #pragma unroll
;         for (int n = 0; n < 4; ++n) acc[m][n] = (f32x4){0.f, 0.f, 0.f, 0.f};
;     f32x2 s0[8], s1[8];
;     float g0[8];
;     MU_GLDS_A(0, 0); MU_B_ISSUE(s0, 0); MU_G_LOAD(g0, 0); MU_B_ISSUE(s1, 1);
;     MU_B_WAIT(s0, 8); MU_B_WRITE(s0, 0, g0); __builtin_amdgcn_sched_barrier(0); MU_B_ISSUE(s0, 2);
;     asm volatile("s_waitcnt vmcnt(16)" ::: "memory");
;     asm volatile("s_waitcnt lgkmcnt(0)" ::: "memory"); __builtin_amdgcn_s_barrier(); asm volatile("" ::: "memory");
; #pragma unroll 1
;     for (int t = 0; t < nt; t += 2) {
;         if (t + 2 < nt) MU_B_WAIT(s1, 8); else MU_B_WAIT(s1, 0);
;         MU_G_LOAD(g0, t + 1); MU_B_WRITE(s1, 1, g0); __builtin_amdgcn_sched_barrier(0); MU_GLDS_A(1, t + 1); __builtin_amdgcn_sched_barrier(0);
;         if (t + 3 < nt) { MU_B_ISSUE(s1, t + 3); }
;         MU_COMPUTE(0);
;         MU_END(t + 3 >= nt);
;         if (t + 2 < nt) { MU_B_WAIT(s0, 8); MU_G_LOAD(g0, t + 2); MU_B_WRITE(s0, 0, g0); __builtin_amdgcn_sched_barrier(0); MU_GLDS_A(0, t + 2); __builtin_amdgcn_sched_barrier(0); }
;         if (t + 4 < nt) { MU_B_ISSUE(s0, t + 4); }
;         MU_COMPUTE(1);
;         MU_END(t + 4 >= nt);
	s_mov_b32 s47, s42
	s_mov_b32 s42, s43
	s_mov_b32 s43, s44
	s_mov_b32 s44, s47
	s_add_i32 s47, s44, s6
	s_add_u32 s30, s30, 0x80
	s_addc_u32 s31, s31, 0
	v_mfma_f32_16x16x32_bf16 v[78:81], v[142:145], v[218:221], v[78:81]
	v_mfma_f32_16x16x32_bf16 v[74:77], v[146:149], v[218:221], v[74:77]
	v_mfma_f32_16x16x32_bf16 v[70:73], v[150:153], v[218:221], v[70:73]
	v_mfma_f32_16x16x32_bf16 v[66:69], v[154:157], v[218:221], v[66:69]
	s_mov_b32 m0, s47
	s_nop 0
	global_load_lds_dwordx4 v86, s[30:31]
	v_mfma_f32_16x16x32_bf16 v[62:65], v[142:145], v[222:225], v[62:65]
	v_mfma_f32_16x16x32_bf16 v[58:61], v[146:149], v[222:225], v[58:61]
	v_mfma_f32_16x16x32_bf16 v[54:57], v[150:153], v[222:225], v[54:57]
	v_mfma_f32_16x16x32_bf16 v[50:53], v[154:157], v[222:225], v[50:53]
	s_add_i32 m0, s47, 0x2000
	s_nop 0
	global_load_lds_dwordx4 v134, s[30:31]
	v_mfma_f32_16x16x32_bf16 v[46:49], v[142:145], v[226:229], v[46:49]
	v_mfma_f32_16x16x32_bf16 v[42:45], v[146:149], v[226:229], v[42:45]
	v_mfma_f32_16x16x32_bf16 v[38:41], v[150:153], v[226:229], v[38:41]
	v_mfma_f32_16x16x32_bf16 v[34:37], v[154:157], v[226:229], v[34:37]
	s_add_i32 m0, s47, 0x4000
	s_nop 0
	global_load_lds_dwordx4 v136, s[30:31]
	v_mfma_f32_16x16x32_bf16 v[18:21], v[142:145], v[230:233], v[18:21]
	v_mfma_f32_16x16x32_bf16 v[22:25], v[146:149], v[230:233], v[22:25]
	v_mfma_f32_16x16x32_bf16 v[26:29], v[150:153], v[230:233], v[26:29]
	v_mfma_f32_16x16x32_bf16 v[30:33], v[154:157], v[230:233], v[30:33]
	s_add_i32 m0, s47, 0x6000
	s_nop 0
	global_load_lds_dwordx4 v138, s[30:31]
	v_mfma_f32_16x16x32_bf16 v[2:5], v[142:145], v[234:237], v[2:5]
	v_mfma_f32_16x16x32_bf16 v[6:9], v[146:149], v[234:237], v[6:9]
	v_mfma_f32_16x16x32_bf16 v[10:13], v[150:153], v[234:237], v[10:13]
	v_mfma_f32_16x16x32_bf16 v[14:17], v[154:157], v[234:237], v[14:17]
	s_add_i32 m0, s47, 0x8000
	s_nop 0
	global_load_lds_dwordx4 v140, s[30:31]
	v_mul_f32_e32 v186, s12, v186
	v_mul_f32_e32 v187, s12, v187
	v_mul_f32_e32 v188, s13, v188
	v_mul_f32_e32 v189, s13, v189
	v_mul_f32_e32 v190, s14, v190
	v_mul_f32_e32 v191, s14, v191
	v_mul_f32_e32 v192, s15, v192
	v_mul_f32_e32 v193, s15, v193
	v_mul_f32_e32 v194, s16, v194
	v_mul_f32_e32 v195, s16, v195
	v_mul_f32_e32 v196, s17, v196
	v_mul_f32_e32 v197, s17, v197
	v_mul_f32_e32 v198, s18, v198
	v_mul_f32_e32 v199, s18, v199
	v_mul_f32_e32 v200, s19, v200
	v_mul_f32_e32 v201, s19, v201
	v_cvt_pk_bf16_f32 v158, v186, v188
	v_cvt_pk_bf16_f32 v159, v190, v192
	v_cvt_pk_bf16_f32 v160, v194, v196
	v_cvt_pk_bf16_f32 v161, v198, v200
	v_cvt_pk_bf16_f32 v162, v187, v189
	v_cvt_pk_bf16_f32 v163, v191, v193
	v_cvt_pk_bf16_f32 v164, v195, v197
	v_cvt_pk_bf16_f32 v165, v199, v201
	ds_write_b128 v1, v[158:161] offset:0
	ds_write_b128 v1, v[162:165] offset:128
	v_add_u32_e32 v91, s42, v135
	v_add_u32_e32 v93, s42, v137
	ds_read_b128 v[238:241], v139 offset:19456
	ds_read_b128 v[242:245], v139 offset:21504
	ds_read_b128 v[246:249], v139 offset:23552
	ds_read_b128 v[250:253], v139 offset:25600
	ds_read_b128 v[218:221], v91 offset:0
	ds_read_b128 v[222:225], v91 offset:2048
	ds_read_b128 v[226:229], v91 offset:4096
	ds_read_b128 v[230:233], v91 offset:6144
	ds_read_b128 v[234:237], v91 offset:8192
	s_waitcnt lgkmcnt(0)
	s_load_dwordx8 s[20:27], s[28:29], 0x0
	s_add_u32 s28, s28, 0x100
	s_addc_u32 s29, s29, 0
	v_mfma_f32_16x16x32_bf16 v[78:81], v[238:241], v[218:221], v[78:81]
	v_mfma_f32_16x16x32_bf16 v[74:77], v[242:245], v[218:221], v[74:77]
	v_mfma_f32_16x16x32_bf16 v[70:73], v[246:249], v[218:221], v[70:73]
	v_mfma_f32_16x16x32_bf16 v[66:69], v[250:253], v[218:221], v[66:69]
	ds_read_b128 v[218:221], v93 offset:0
	ds_read_b128 v[142:145], v141 offset:19456
	v_mfma_f32_16x16x32_bf16 v[62:65], v[238:241], v[222:225], v[62:65]
	v_mfma_f32_16x16x32_bf16 v[58:61], v[242:245], v[222:225], v[58:61]
	v_mfma_f32_16x16x32_bf16 v[54:57], v[246:249], v[222:225], v[54:57]
	v_mfma_f32_16x16x32_bf16 v[50:53], v[250:253], v[222:225], v[50:53]
	ds_read_b128 v[222:225], v93 offset:2048
	ds_read_b128 v[146:149], v141 offset:21504
	v_mfma_f32_16x16x32_bf16 v[46:49], v[238:241], v[226:229], v[46:49]
	v_mfma_f32_16x16x32_bf16 v[42:45], v[242:245], v[226:229], v[42:45]
	v_mfma_f32_16x16x32_bf16 v[38:41], v[246:249], v[226:229], v[38:41]
	v_mfma_f32_16x16x32_bf16 v[34:37], v[250:253], v[226:229], v[34:37]
	ds_read_b128 v[226:229], v93 offset:4096
	ds_read_b128 v[150:153], v141 offset:23552
	v_mfma_f32_16x16x32_bf16 v[18:21], v[238:241], v[230:233], v[18:21]
	v_mfma_f32_16x16x32_bf16 v[22:25], v[242:245], v[230:233], v[22:25]
	v_mfma_f32_16x16x32_bf16 v[26:29], v[246:249], v[230:233], v[26:29]
	v_mfma_f32_16x16x32_bf16 v[30:33], v[250:253], v[230:233], v[30:33]
	ds_read_b128 v[230:233], v93 offset:6144
	ds_read_b128 v[154:157], v141 offset:25600
	v_mfma_f32_16x16x32_bf16 v[2:5], v[238:241], v[234:237], v[2:5]
	v_mfma_f32_16x16x32_bf16 v[6:9], v[242:245], v[234:237], v[6:9]
	v_mfma_f32_16x16x32_bf16 v[10:13], v[246:249], v[234:237], v[10:13]
	v_mfma_f32_16x16x32_bf16 v[14:17], v[250:253], v[234:237], v[14:17]
	ds_read_b128 v[234:237], v93 offset:8192
	s_waitcnt vmcnt(5)
	s_waitcnt lgkmcnt(0)
	s_barrier
; #define MU_GLDS_A(buf, kt) do { _Pragma("unroll") for (int i = 0; i < NMU; ++i) \
;         __builtin_amdgcn_global_load_lds((const unsigned*)((const char*)A + aoff[i] + (size_t)(kt) * 128), (PG8_LAS unsigned*)(MU_SA(buf) + wid * 1024 + i * 8192), 16, 0, 0); } while (0)
; #define MU_B_ISSUE(sb, kt) do { const char* kb_ = Bb + (size_t)(kt) * (64 * (size_t)RB); _Pragma("unroll") for (int j = 0; j < 8; ++j) { const char* p_ = kb_ + (size_t)j * RB; \
;         asm volatile("global_load_dwordx2 %0, %1, off" : "=&v"(sb[j]) : "v"(p_) : "memory"); } } while (0)
; #define MU_B_WAIT(sb, N) asm volatile("s_waitcnt vmcnt(%8)" : "+v"(sb[0]), "+v"(sb[1]), "+v"(sb[2]), "+v"(sb[3]), "+v"(sb[4]), "+v"(sb[5]), "+v"(sb[6]), "+v"(sb[7]) : "n"(N) : "memory")
; #define MU_COMPUTE(buf) MU_COMPUTE_N(buf, NMU)
; template <int MODE>
; __device__ __forceinline__ void moe_unit(PG8_LAS unsigned char* lds, int e, int cb, int slot0  , int nv  , const bf16_t* A, const int* slot_tok,
;                                          const float* W0, const float* W1, bf16_t* OUT, const float* slot_rs  , const int* slot_dst) {
;     ...
;     f32x4 acc[NMU][4];
; #pragma unroll
;     for (int m = 0; m < NMU; ++m)
; #pragma unroll
;         for (int n = 0; n < 4; ++n) acc[m][n] = (f32x4){0.f, 0.f, 0.f, 0.f};
;     f32x2 s0[8], s1[8];
;     float g0[8];
;     MU_GLDS_A(0, 0); MU_B_ISSUE(s0, 0); MU_G_LOAD(g0, 0); MU_B_ISSUE(s1, 1);
;     MU_B_WAIT(s0, 8); MU_B_WRITE(s0, 0, g0); __builtin_amdgcn_sched_barrier(0); MU_B_ISSUE(s0, 2);
;     asm volatile("s_waitcnt vmcnt(16)" ::: "memory");
;     asm volatile("s_waitcnt lgkmcnt(0)" ::: "memory"); __builtin_amdgcn_s_barrier(); asm volatile("" ::: "memory");
; #pragma unroll 1
;     for (int t = 0; t < nt; t += 2) {
;         if (t + 2 < nt) MU_B_WAIT(s1, 8); else MU_B_WAIT(s1, 0);
;         MU_G_LOAD(g0, t + 1); MU_B_WRITE(s1, 1, g0); __builtin_amdgcn_sched_barrier(0); MU_GLDS_A(1, t + 1); __builtin_amdgcn_sched_barrier(0);
;         if (t + 3 < nt) { MU_B_ISSUE(s1, t + 3); }
;         MU_COMPUTE(0);
;         MU_END(t + 3 >= nt);
;         if (t + 2 < nt) { MU_B_WAIT(s0, 8); MU_G_LOAD(g0, t + 2); MU_B_WRITE(s0, 0, g0); __builtin_amdgcn_sched_barrier(0); MU_GLDS_A(0, t + 2); __builtin_amdgcn_sched_barrier(0); }
;         if (t + 4 < nt) { MU_B_ISSUE(s0, t + 4); }
;         MU_COMPUTE(1);
;         MU_END(t + 4 >= nt);
	s_mov_b32 s47, s42
	s_mov_b32 s42, s43
	s_mov_b32 s43, s44
	s_mov_b32 s44, s47
	v_mfma_f32_16x16x32_bf16 v[78:81], v[142:145], v[218:221], v[78:81]
	v_mfma_f32_16x16x32_bf16 v[74:77], v[146:149], v[218:221], v[74:77]
	v_mfma_f32_16x16x32_bf16 v[70:73], v[150:153], v[218:221], v[70:73]
	v_mfma_f32_16x16x32_bf16 v[66:69], v[154:157], v[218:221], v[66:69]
	v_mfma_f32_16x16x32_bf16 v[62:65], v[142:145], v[222:225], v[62:65]
	v_mfma_f32_16x16x32_bf16 v[58:61], v[146:149], v[222:225], v[58:61]
	v_mfma_f32_16x16x32_bf16 v[54:57], v[150:153], v[222:225], v[54:57]
	v_mfma_f32_16x16x32_bf16 v[50:53], v[154:157], v[222:225], v[50:53]
	v_mfma_f32_16x16x32_bf16 v[46:49], v[142:145], v[226:229], v[46:49]
	v_mfma_f32_16x16x32_bf16 v[42:45], v[146:149], v[226:229], v[42:45]
	v_mfma_f32_16x16x32_bf16 v[38:41], v[150:153], v[226:229], v[38:41]
	v_mfma_f32_16x16x32_bf16 v[34:37], v[154:157], v[226:229], v[34:37]
	v_mfma_f32_16x16x32_bf16 v[18:21], v[142:145], v[230:233], v[18:21]
	v_mfma_f32_16x16x32_bf16 v[22:25], v[146:149], v[230:233], v[22:25]
	v_mfma_f32_16x16x32_bf16 v[26:29], v[150:153], v[230:233], v[26:29]
	v_mfma_f32_16x16x32_bf16 v[30:33], v[154:157], v[230:233], v[30:33]
	v_mfma_f32_16x16x32_bf16 v[2:5], v[142:145], v[234:237], v[2:5]
	v_mfma_f32_16x16x32_bf16 v[6:9], v[146:149], v[234:237], v[6:9]
	v_mfma_f32_16x16x32_bf16 v[10:13], v[150:153], v[234:237], v[10:13]
	v_mfma_f32_16x16x32_bf16 v[14:17], v[154:157], v[234:237], v[14:17]
	v_mul_f32_e32 v202, s20, v202
	v_mul_f32_e32 v203, s20, v203
	v_mul_f32_e32 v204, s21, v204
	v_mul_f32_e32 v205, s21, v205
	v_mul_f32_e32 v206, s22, v206
	v_mul_f32_e32 v207, s22, v207
	v_mul_f32_e32 v208, s23, v208
	v_mul_f32_e32 v209, s23, v209
	v_mul_f32_e32 v210, s24, v210
	v_mul_f32_e32 v211, s24, v211
	v_mul_f32_e32 v212, s25, v212
	v_mul_f32_e32 v213, s25, v213
	v_mul_f32_e32 v214, s26, v214
	v_mul_f32_e32 v215, s26, v215
	v_mul_f32_e32 v216, s27, v216
	v_mul_f32_e32 v217, s27, v217
	v_cvt_pk_bf16_f32 v158, v202, v204
	v_cvt_pk_bf16_f32 v159, v206, v208
	v_cvt_pk_bf16_f32 v160, v210, v212
	v_cvt_pk_bf16_f32 v161, v214, v216
	v_cvt_pk_bf16_f32 v162, v203, v205
	v_cvt_pk_bf16_f32 v163, v207, v209
	v_cvt_pk_bf16_f32 v164, v211, v213
	v_cvt_pk_bf16_f32 v165, v215, v217
	ds_write_b128 v1, v[158:161] offset:19456
	ds_write_b128 v1, v[162:165] offset:19584
	v_add_u32_e32 v91, s42, v135
	v_add_u32_e32 v93, s42, v137
	ds_read_b128 v[238:241], v139 offset:0
	ds_read_b128 v[242:245], v139 offset:2048
	ds_read_b128 v[246:249], v139 offset:4096
	ds_read_b128 v[250:253], v139 offset:6144
	ds_read_b128 v[218:221], v91 offset:0
	ds_read_b128 v[222:225], v91 offset:2048
	ds_read_b128 v[226:229], v91 offset:4096
	ds_read_b128 v[230:233], v91 offset:6144
	ds_read_b128 v[234:237], v91 offset:8192
	s_waitcnt lgkmcnt(0)
	v_mfma_f32_16x16x32_bf16 v[78:81], v[238:241], v[218:221], v[78:81]
	v_mfma_f32_16x16x32_bf16 v[74:77], v[242:245], v[218:221], v[74:77]
	v_mfma_f32_16x16x32_bf16 v[70:73], v[246:249], v[218:221], v[70:73]
	v_mfma_f32_16x16x32_bf16 v[66:69], v[250:253], v[218:221], v[66:69]
	ds_read_b128 v[218:221], v93 offset:0
	ds_read_b128 v[142:145], v141 offset:0
	v_mfma_f32_16x16x32_bf16 v[62:65], v[238:241], v[222:225], v[62:65]
	v_mfma_f32_16x16x32_bf16 v[58:61], v[242:245], v[222:225], v[58:61]
	v_mfma_f32_16x16x32_bf16 v[54:57], v[246:249], v[222:225], v[54:57]
	v_mfma_f32_16x16x32_bf16 v[50:53], v[250:253], v[222:225], v[50:53]
	ds_read_b128 v[222:225], v93 offset:2048
	ds_read_b128 v[146:149], v141 offset:2048
	v_mfma_f32_16x16x32_bf16 v[46:49], v[238:241], v[226:229], v[46:49]
	v_mfma_f32_16x16x32_bf16 v[42:45], v[242:245], v[226:229], v[42:45]
	v_mfma_f32_16x16x32_bf16 v[38:41], v[246:249], v[226:229], v[38:41]
	v_mfma_f32_16x16x32_bf16 v[34:37], v[250:253], v[226:229], v[34:37]
	ds_read_b128 v[226:229], v93 offset:4096
	ds_read_b128 v[150:153], v141 offset:4096
	v_mfma_f32_16x16x32_bf16 v[18:21], v[238:241], v[230:233], v[18:21]
	v_mfma_f32_16x16x32_bf16 v[22:25], v[242:245], v[230:233], v[22:25]
	v_mfma_f32_16x16x32_bf16 v[26:29], v[246:249], v[230:233], v[26:29]
	v_mfma_f32_16x16x32_bf16 v[30:33], v[250:253], v[230:233], v[30:33]
	ds_read_b128 v[230:233], v93 offset:6144
	ds_read_b128 v[154:157], v141 offset:6144
	v_mfma_f32_16x16x32_bf16 v[2:5], v[238:241], v[234:237], v[2:5]
	v_mfma_f32_16x16x32_bf16 v[6:9], v[242:245], v[234:237], v[6:9]
	v_mfma_f32_16x16x32_bf16 v[10:13], v[246:249], v[234:237], v[10:13]
	v_mfma_f32_16x16x32_bf16 v[14:17], v[250:253], v[234:237], v[14:17]
	ds_read_b128 v[234:237], v93 offset:8192
	s_waitcnt vmcnt(0)
	s_waitcnt lgkmcnt(0)
	s_barrier
; #define MU_GLDS_A(buf, kt) do { _Pragma("unroll") for (int i = 0; i < NMU; ++i) \
;         __builtin_amdgcn_global_load_lds((const unsigned*)((const char*)A + aoff[i] + (size_t)(kt) * 128), (PG8_LAS unsigned*)(MU_SA(buf) + wid * 1024 + i * 8192), 16, 0, 0); } while (0)
; #define MU_B_ISSUE(sb, kt) do { const char* kb_ = Bb + (size_t)(kt) * (64 * (size_t)RB); _Pragma("unroll") for (int j = 0; j < 8; ++j) { const char* p_ = kb_ + (size_t)j * RB; \
;         asm volatile("global_load_dwordx2 %0, %1, off" : "=&v"(sb[j]) : "v"(p_) : "memory"); } } while (0)
; #define MU_B_WAIT(sb, N) asm volatile("s_waitcnt vmcnt(%8)" : "+v"(sb[0]), "+v"(sb[1]), "+v"(sb[2]), "+v"(sb[3]), "+v"(sb[4]), "+v"(sb[5]), "+v"(sb[6]), "+v"(sb[7]) : "n"(N) : "memory")
; #define MU_COMPUTE(buf) MU_COMPUTE_N(buf, NMU)
; template <int MODE>
; __device__ __forceinline__ void moe_unit(PG8_LAS unsigned char* lds, int e, int cb, int slot0  , int nv  , const bf16_t* A, const int* slot_tok,
;                                          const float* W0, const float* W1, bf16_t* OUT, const float* slot_rs  , const int* slot_dst) {
;     ...
;     f32x4 acc[NMU][4];
; #pragma unroll
;     for (int m = 0; m < NMU; ++m)
; #pragma unroll
;         for (int n = 0; n < 4; ++n) acc[m][n] = (f32x4){0.f, 0.f, 0.f, 0.f};
;     f32x2 s0[8], s1[8];
;     float g0[8];
;     MU_GLDS_A(0, 0); MU_B_ISSUE(s0, 0); MU_G_LOAD(g0, 0); MU_B_ISSUE(s1, 1);
;     MU_B_WAIT(s0, 8); MU_B_WRITE(s0, 0, g0); __builtin_amdgcn_sched_barrier(0); MU_B_ISSUE(s0, 2);
;     asm volatile("s_waitcnt vmcnt(16)" ::: "memory");
;     asm volatile("s_waitcnt lgkmcnt(0)" ::: "memory"); __builtin_amdgcn_s_barrier(); asm volatile("" ::: "memory");
; #pragma unroll 1
;     for (int t = 0; t < nt; t += 2) {
;         if (t + 2 < nt) MU_B_WAIT(s1, 8); else MU_B_WAIT(s1, 0);
;         MU_G_LOAD(g0, t + 1); MU_B_WRITE(s1, 1, g0); __builtin_amdgcn_sched_barrier(0); MU_GLDS_A(1, t + 1); __builtin_amdgcn_sched_barrier(0);
;         if (t + 3 < nt) { MU_B_ISSUE(s1, t + 3); }
;         MU_COMPUTE(0);
;         MU_END(t + 3 >= nt);
;         if (t + 2 < nt) { MU_B_WAIT(s0, 8); MU_G_LOAD(g0, t + 2); MU_B_WRITE(s0, 0, g0); __builtin_amdgcn_sched_barrier(0); MU_GLDS_A(0, t + 2); __builtin_amdgcn_sched_barrier(0); }
;         if (t + 4 < nt) { MU_B_ISSUE(s0, t + 4); }
;         MU_COMPUTE(1);
;         MU_END(t + 4 >= nt);
	s_mov_b32 s47, s42
	s_mov_b32 s42, s43
	s_mov_b32 s43, s44
	s_mov_b32 s44, s47
	v_mfma_f32_16x16x32_bf16 v[78:81], v[142:145], v[218:221], v[78:81]
	v_mfma_f32_16x16x32_bf16 v[74:77], v[146:149], v[218:221], v[74:77]
	v_mfma_f32_16x16x32_bf16 v[70:73], v[150:153], v[218:221], v[70:73]
	v_mfma_f32_16x16x32_bf16 v[66:69], v[154:157], v[218:221], v[66:69]
	v_mfma_f32_16x16x32_bf16 v[62:65], v[142:145], v[222:225], v[62:65]
	v_mfma_f32_16x16x32_bf16 v[58:61], v[146:149], v[222:225], v[58:61]
	v_mfma_f32_16x16x32_bf16 v[54:57], v[150:153], v[222:225], v[54:57]
	v_mfma_f32_16x16x32_bf16 v[50:53], v[154:157], v[222:225], v[50:53]
	v_mfma_f32_16x16x32_bf16 v[46:49], v[142:145], v[226:229], v[46:49]
	v_mfma_f32_16x16x32_bf16 v[42:45], v[146:149], v[226:229], v[42:45]
	v_mfma_f32_16x16x32_bf16 v[38:41], v[150:153], v[226:229], v[38:41]
	v_mfma_f32_16x16x32_bf16 v[34:37], v[154:157], v[226:229], v[34:37]
	v_mfma_f32_16x16x32_bf16 v[18:21], v[142:145], v[230:233], v[18:21]
	v_mfma_f32_16x16x32_bf16 v[22:25], v[146:149], v[230:233], v[22:25]
	v_mfma_f32_16x16x32_bf16 v[26:29], v[150:153], v[230:233], v[26:29]
	v_mfma_f32_16x16x32_bf16 v[30:33], v[154:157], v[230:233], v[30:33]
	v_mfma_f32_16x16x32_bf16 v[2:5], v[142:145], v[234:237], v[2:5]
	v_mfma_f32_16x16x32_bf16 v[6:9], v[146:149], v[234:237], v[6:9]
	v_mfma_f32_16x16x32_bf16 v[10:13], v[150:153], v[234:237], v[10:13]
	v_mfma_f32_16x16x32_bf16 v[14:17], v[154:157], v[234:237], v[14:17]
	v_add_u32_e32 v91, s42, v135
	v_add_u32_e32 v93, s42, v137
	ds_read_b128 v[238:241], v139 offset:19456
	ds_read_b128 v[242:245], v139 offset:21504
	ds_read_b128 v[246:249], v139 offset:23552
	ds_read_b128 v[250:253], v139 offset:25600
	ds_read_b128 v[218:221], v91 offset:0
	ds_read_b128 v[222:225], v91 offset:2048
	ds_read_b128 v[226:229], v91 offset:4096
	ds_read_b128 v[230:233], v91 offset:6144
	ds_read_b128 v[234:237], v91 offset:8192
	s_waitcnt lgkmcnt(0)
	v_mfma_f32_16x16x32_bf16 v[78:81], v[238:241], v[218:221], v[78:81]
	v_mfma_f32_16x16x32_bf16 v[74:77], v[242:245], v[218:221], v[74:77]
	v_mfma_f32_16x16x32_bf16 v[70:73], v[246:249], v[218:221], v[70:73]
	v_mfma_f32_16x16x32_bf16 v[66:69], v[250:253], v[218:221], v[66:69]
	ds_read_b128 v[218:221], v93 offset:0
	ds_read_b128 v[142:145], v141 offset:19456
	v_mfma_f32_16x16x32_bf16 v[62:65], v[238:241], v[222:225], v[62:65]
	v_mfma_f32_16x16x32_bf16 v[58:61], v[242:245], v[222:225], v[58:61]
	v_mfma_f32_16x16x32_bf16 v[54:57], v[246:249], v[222:225], v[54:57]
	v_mfma_f32_16x16x32_bf16 v[50:53], v[250:253], v[222:225], v[50:53]
	ds_read_b128 v[222:225], v93 offset:2048
	ds_read_b128 v[146:149], v141 offset:21504
	v_mfma_f32_16x16x32_bf16 v[46:49], v[238:241], v[226:229], v[46:49]
	v_mfma_f32_16x16x32_bf16 v[42:45], v[242:245], v[226:229], v[42:45]
	v_mfma_f32_16x16x32_bf16 v[38:41], v[246:249], v[226:229], v[38:41]
	v_mfma_f32_16x16x32_bf16 v[34:37], v[250:253], v[226:229], v[34:37]
	ds_read_b128 v[226:229], v93 offset:4096
	ds_read_b128 v[150:153], v141 offset:23552
	v_mfma_f32_16x16x32_bf16 v[18:21], v[238:241], v[230:233], v[18:21]
	v_mfma_f32_16x16x32_bf16 v[22:25], v[242:245], v[230:233], v[22:25]
	v_mfma_f32_16x16x32_bf16 v[26:29], v[246:249], v[230:233], v[26:29]
	v_mfma_f32_16x16x32_bf16 v[30:33], v[250:253], v[230:233], v[30:33]
	ds_read_b128 v[230:233], v93 offset:6144
	ds_read_b128 v[154:157], v141 offset:25600
	v_mfma_f32_16x16x32_bf16 v[2:5], v[238:241], v[234:237], v[2:5]
	v_mfma_f32_16x16x32_bf16 v[6:9], v[242:245], v[234:237], v[6:9]
	v_mfma_f32_16x16x32_bf16 v[10:13], v[246:249], v[234:237], v[10:13]
	v_mfma_f32_16x16x32_bf16 v[14:17], v[250:253], v[234:237], v[14:17]
	ds_read_b128 v[234:237], v93 offset:8192
	s_waitcnt lgkmcnt(0)
	s_barrier
	s_mov_b32 s47, s42
	s_mov_b32 s42, s43
	s_mov_b32 s43, s44
	s_mov_b32 s44, s47
	v_mfma_f32_16x16x32_bf16 v[78:81], v[142:145], v[218:221], v[78:81]
	v_mfma_f32_16x16x32_bf16 v[74:77], v[146:149], v[218:221], v[74:77]
	v_mfma_f32_16x16x32_bf16 v[70:73], v[150:153], v[218:221], v[70:73]
	v_mfma_f32_16x16x32_bf16 v[66:69], v[154:157], v[218:221], v[66:69]
	v_mfma_f32_16x16x32_bf16 v[62:65], v[142:145], v[222:225], v[62:65]
	v_mfma_f32_16x16x32_bf16 v[58:61], v[146:149], v[222:225], v[58:61]
	v_mfma_f32_16x16x32_bf16 v[54:57], v[150:153], v[222:225], v[54:57]
	v_mfma_f32_16x16x32_bf16 v[50:53], v[154:157], v[222:225], v[50:53]
	v_mfma_f32_16x16x32_bf16 v[46:49], v[142:145], v[226:229], v[46:49]
	v_mfma_f32_16x16x32_bf16 v[42:45], v[146:149], v[226:229], v[42:45]
	v_mfma_f32_16x16x32_bf16 v[38:41], v[150:153], v[226:229], v[38:41]
	v_mfma_f32_16x16x32_bf16 v[34:37], v[154:157], v[226:229], v[34:37]
	v_mfma_f32_16x16x32_bf16 v[18:21], v[142:145], v[230:233], v[18:21]
	v_mfma_f32_16x16x32_bf16 v[22:25], v[146:149], v[230:233], v[22:25]
	v_mfma_f32_16x16x32_bf16 v[26:29], v[150:153], v[230:233], v[26:29]
	v_mfma_f32_16x16x32_bf16 v[30:33], v[154:157], v[230:233], v[30:33]
	v_mfma_f32_16x16x32_bf16 v[2:5], v[142:145], v[234:237], v[2:5]
	v_mfma_f32_16x16x32_bf16 v[6:9], v[146:149], v[234:237], v[6:9]
	v_mfma_f32_16x16x32_bf16 v[10:13], v[150:153], v[234:237], v[10:13]
	v_mfma_f32_16x16x32_bf16 v[14:17], v[154:157], v[234:237], v[14:17]
.Lmu_done:

; __device__ __forceinline__ unsigned cvtpk(float lo, float hi) { f32x2 v = {lo, hi}; bf16x2_t b = __builtin_convertvector(v, bf16x2_t); return __builtin_bit_cast(unsigned, b); }
; template <int MODE>
; __device__ __forceinline__ void moe_unit(PG8_LAS unsigned char* lds, int e, int cb, int slot0  , int nv  , const bf16_t* A, const int* slot_tok,
;                                          const float* W0, const float* W1, bf16_t* OUT, const float* slot_rs  , const int* slot_dst) {
;     ...
; #pragma unroll
;     for (int m = 0; m < NMU; ++m) if (m < mcnt) { const int r = 4 * (16 * m + fr) + wr;
;         if (r < nv) { const int slot = slot0 + r; const float rs = slot_rs[slot];
;             if (MODE == 0) {
;                 float h[8];
; #pragma unroll
;                 for (int n = 0; n < 2; ++n)
; #pragma unroll
;                     for (int i = 0; i < 4; ++i) { const float g = acc[m][n][i] * rs, up = acc[m][n + 2][i] * rs; h[4 * n + i] = g * __builtin_amdgcn_rcpf(1.0f + __expf(-g)) * up; }
;                 { u32x4 w; w.x = cvtpk(h[0], h[1]); w.y = cvtpk(h[2], h[3]); w.z = cvtpk(h[4], h[5]); w.w = cvtpk(h[6], h[7]); *(u32x4*)(OUT + (size_t)slot * DFF + 64 * cb + 32 * wc + 8 * fq) = w; }
.LBB0_719:
	s_sub_i32 s6, s69, s33
	s_add_i32 s58, s6, 3
	s_ashr_i32 s6, s58, 2
	s_cmp_gt_i32 s6, 0
	s_cselect_b64 s[56:57], -1, 0
	s_lshl_b64 s[54:55], s[54:55], 1
	s_add_u32 s54, s66, s54
	s_addc_u32 s55, s67, s55
	v_add_u32_e32 v100, s33, v176
	s_lshl_b32 s33, s70, 6
	s_add_u32 s54, s54, s33
	s_addc_u32 s55, s55, 0
	v_mov_b32_e32 v93, v87
	s_cmp_gt_u32 s58, 3
	v_lshl_add_u64 v[98:99], s[10:11], 0, v[96:97]
	v_lshl_add_u64 v[96:97], s[54:55], 0, v[92:93]
	s_cselect_b64 s[54:55], -1, 0
	s_and_b64 s[54:55], s[54:55], s[56:57]
	v_cmp_gt_i32_e32 vcc, s69, v100
	s_and_b64 s[56:57], s[54:55], vcc
	s_and_saveexec_b64 s[54:55], s[56:57]
	s_cbranch_execz .LBB0_721
	v_add_u32_e32 v102, v100, v94
	v_ashrrev_i32_e32 v103, 31, v102
	v_lshl_add_u64 v[104:105], v[102:103], 2, v[98:99]
	v_mov_b32_e32 v86, v178
	v_lshlrev_b64 v[102:103], 10, v[102:103]
	s_nop 0
	v_pk_mul_f32 v[78:79], v[78:79], v[86:87] op_sel_hi:[1,0]
	v_pk_mul_f32 v[80:81], v[80:81], v[86:87] op_sel_hi:[1,0]
	v_pk_mul_f32 v[74:75], v[74:75], v[86:87] op_sel_hi:[1,0]
	v_pk_mul_f32 v[76:77], v[76:77], v[86:87] op_sel_hi:[1,0]
	v_pk_mul_f32 v[70:71], v[70:71], v[86:87] op_sel_hi:[1,0]
	v_pk_mul_f32 v[72:73], v[72:73], v[86:87] op_sel_hi:[1,0]
	v_pk_mul_f32 v[66:67], v[66:67], v[86:87] op_sel_hi:[1,0]
	v_pk_mul_f32 v[68:69], v[68:69], v[86:87] op_sel_hi:[1,0]
	v_mul_f32_e32 v1, 0xbfb8aa3b, v78
	v_mul_f32_e32 v86, 0xbfb8aa3b, v79
	v_mul_f32_e32 v91, 0xbfb8aa3b, v80
	v_mul_f32_e32 v93, 0xbfb8aa3b, v81
	v_mul_f32_e32 v95, 0xbfb8aa3b, v74
	v_mul_f32_e32 v101, 0xbfb8aa3b, v75
	v_mul_f32_e32 v104, 0xbfb8aa3b, v76
	v_mul_f32_e32 v105, 0xbfb8aa3b, v77
	v_exp_f32_e32 v1, v1
	v_exp_f32_e32 v86, v86
	v_exp_f32_e32 v91, v91
	v_exp_f32_e32 v93, v93
	v_exp_f32_e32 v95, v95
	v_exp_f32_e32 v101, v101
	v_exp_f32_e32 v104, v104
	v_exp_f32_e32 v105, v105
	v_add_f32_e32 v1, 1.0, v1
	v_add_f32_e32 v86, 1.0, v86
	v_add_f32_e32 v91, 1.0, v91
	v_add_f32_e32 v93, 1.0, v93
	v_add_f32_e32 v95, 1.0, v95
	v_add_f32_e32 v101, 1.0, v101
	v_add_f32_e32 v110, 1.0, v104
	v_add_f32_e32 v111, 1.0, v105
	v_rcp_f32_e32 v104, v1
	v_rcp_f32_e32 v105, v86
	v_rcp_f32_e32 v106, v91
	v_rcp_f32_e32 v107, v93
	v_rcp_f32_e32 v108, v95
	v_rcp_f32_e32 v109, v101
	v_rcp_f32_e32 v110, v110
	v_rcp_f32_e32 v111, v111
	v_pk_mul_f32 v[78:79], v[78:79], v[104:105]
	v_pk_mul_f32 v[80:81], v[80:81], v[106:107]
	v_pk_mul_f32 v[74:75], v[74:75], v[108:109]
	v_pk_mul_f32 v[76:77], v[76:77], v[110:111]
	v_pk_mul_f32 v[70:71], v[70:71], v[78:79]
	v_pk_mul_f32 v[72:73], v[72:73], v[80:81]
	v_pk_mul_f32 v[74:75], v[66:67], v[74:75]
	v_pk_mul_f32 v[76:77], v[68:69], v[76:77]
	v_cvt_pk_bf16_f32 v66, v70, v71
	v_cvt_pk_bf16_f32 v67, v72, v73
	v_cvt_pk_bf16_f32 v68, v74, v75
	v_cvt_pk_bf16_f32 v69, v76, v77
	v_lshl_add_u64 v[70:71], v[96:97], 0, v[102:103]
	global_store_dwordx4 v[70:71], v[66:69], off
.LBB0_721:
	s_or_b64 exec, exec, s[54:55]
	s_cmp_gt_i32 s6, 16
	v_add_u32_e32 v1, 64, v100
	s_cselect_b64 s[54:55], -1, 0
	v_cmp_gt_i32_e32 vcc, s69, v1
	s_and_b64 s[56:57], s[54:55], vcc
	v_ashrrev_i32_e32 v95, 31, v94
	v_ashrrev_i32_e32 v101, 31, v100
	s_and_saveexec_b64 s[54:55], s[56:57]
	s_cbranch_execz .LBB0_723
	v_lshl_add_u64 v[66:67], v[100:101], 0, v[94:95]
	v_lshl_add_u64 v[66:67], v[66:67], 2, v[98:99]
	v_mov_b32_e32 v66, v179
	v_add_u32_e32 v68, v1, v94
	v_ashrrev_i32_e32 v69, 31, v68
	v_lshlrev_b64 v[68:69], 10, v[68:69]
	s_nop 0
	v_pk_mul_f32 v[62:63], v[62:63], v[66:67] op_sel_hi:[1,0]
	v_pk_mul_f32 v[64:65], v[64:65], v[66:67] op_sel_hi:[1,0]
	v_pk_mul_f32 v[58:59], v[58:59], v[66:67] op_sel_hi:[1,0]
	v_pk_mul_f32 v[60:61], v[60:61], v[66:67] op_sel_hi:[1,0]
	v_pk_mul_f32 v[54:55], v[54:55], v[66:67] op_sel_hi:[1,0]
	v_pk_mul_f32 v[56:57], v[56:57], v[66:67] op_sel_hi:[1,0]
	v_pk_mul_f32 v[50:51], v[50:51], v[66:67] op_sel_hi:[1,0]
	v_pk_mul_f32 v[52:53], v[52:53], v[66:67] op_sel_hi:[1,0]
	v_mul_f32_e32 v1, 0xbfb8aa3b, v62
	v_mul_f32_e32 v66, 0xbfb8aa3b, v63
	v_mul_f32_e32 v67, 0xbfb8aa3b, v64
	v_mul_f32_e32 v70, 0xbfb8aa3b, v65
	v_mul_f32_e32 v71, 0xbfb8aa3b, v58
	v_mul_f32_e32 v72, 0xbfb8aa3b, v59
	v_mul_f32_e32 v73, 0xbfb8aa3b, v60
	v_mul_f32_e32 v74, 0xbfb8aa3b, v61
	v_exp_f32_e32 v1, v1
	v_exp_f32_e32 v66, v66
	v_exp_f32_e32 v67, v67
	v_exp_f32_e32 v70, v70
	v_exp_f32_e32 v71, v71
	v_exp_f32_e32 v72, v72
	v_exp_f32_e32 v73, v73
	v_exp_f32_e32 v74, v74
	v_add_f32_e32 v1, 1.0, v1
	v_add_f32_e32 v75, 1.0, v66
	v_add_f32_e32 v76, 1.0, v67
	v_add_f32_e32 v77, 1.0, v70
	v_add_f32_e32 v78, 1.0, v71
	v_add_f32_e32 v79, 1.0, v72
	v_add_f32_e32 v80, 1.0, v73
	v_add_f32_e32 v81, 1.0, v74
	v_rcp_f32_e32 v66, v1
	v_rcp_f32_e32 v67, v75
	v_rcp_f32_e32 v70, v76
	v_rcp_f32_e32 v71, v77
	v_rcp_f32_e32 v72, v78
	v_rcp_f32_e32 v73, v79
	v_rcp_f32_e32 v74, v80
	v_rcp_f32_e32 v75, v81
	v_pk_mul_f32 v[62:63], v[62:63], v[66:67]
	v_pk_mul_f32 v[64:65], v[64:65], v[70:71]
	v_pk_mul_f32 v[58:59], v[58:59], v[72:73]
	v_pk_mul_f32 v[60:61], v[60:61], v[74:75]
	v_pk_mul_f32 v[54:55], v[54:55], v[62:63]
	v_pk_mul_f32 v[56:57], v[56:57], v[64:65]
	v_pk_mul_f32 v[58:59], v[50:51], v[58:59]
	v_pk_mul_f32 v[60:61], v[52:53], v[60:61]
	v_cvt_pk_bf16_f32 v50, v54, v55
	v_cvt_pk_bf16_f32 v51, v56, v57
	v_cvt_pk_bf16_f32 v52, v58, v59
	v_cvt_pk_bf16_f32 v53, v60, v61
	v_lshl_add_u64 v[54:55], v[96:97], 0, v[68:69]
	global_store_dwordx4 v[54:55], v[50:53], off
; __device__ __forceinline__ unsigned cvtpk(float lo, float hi) { f32x2 v = {lo, hi}; bf16x2_t b = __builtin_convertvector(v, bf16x2_t); return __builtin_bit_cast(unsigned, b); }
; template <int MODE>
; __device__ __forceinline__ void moe_unit(PG8_LAS unsigned char* lds, int e, int cb, int slot0  , int nv  , const bf16_t* A, const int* slot_tok,
;                                          const float* W0, const float* W1, bf16_t* OUT, const float* slot_rs  , const int* slot_dst) {
;     ...
; #pragma unroll
;     for (int m = 0; m < NMU; ++m) if (m < mcnt) { const int r = 4 * (16 * m + fr) + wr;
;         if (r < nv) { const int slot = slot0 + r; const float rs = slot_rs[slot];
;             if (MODE == 0) {
;                 float h[8];
; #pragma unroll
;                 for (int n = 0; n < 2; ++n)
; #pragma unroll
;                     for (int i = 0; i < 4; ++i) { const float g = acc[m][n][i] * rs, up = acc[m][n + 2][i] * rs; h[4 * n + i] = g * __builtin_amdgcn_rcpf(1.0f + __expf(-g)) * up; }
;                 { u32x4 w; w.x = cvtpk(h[0], h[1]); w.y = cvtpk(h[2], h[3]); w.z = cvtpk(h[4], h[5]); w.w = cvtpk(h[6], h[7]); *(u32x4*)(OUT + (size_t)slot * DFF + 64 * cb + 32 * wc + 8 * fq) = w; }
.LBB0_723:
	s_or_b64 exec, exec, s[54:55]
	s_cmp_gt_i32 s6, 32
	v_add_u32_e32 v1, 0x80, v100
	s_cselect_b64 s[54:55], -1, 0
	v_cmp_gt_i32_e32 vcc, s69, v1
	s_and_b64 s[56:57], s[54:55], vcc
	s_and_saveexec_b64 s[54:55], s[56:57]
	s_cbranch_execz .LBB0_725
	v_lshl_add_u64 v[50:51], v[100:101], 0, v[94:95]
	v_lshl_add_u64 v[50:51], v[50:51], 2, v[98:99]
	v_mov_b32_e32 v50, v180
	v_add_u32_e32 v52, v1, v94
	v_ashrrev_i32_e32 v53, 31, v52
	v_lshlrev_b64 v[52:53], 10, v[52:53]
	s_nop 0
	v_pk_mul_f32 v[46:47], v[46:47], v[50:51] op_sel_hi:[1,0]
	v_pk_mul_f32 v[48:49], v[48:49], v[50:51] op_sel_hi:[1,0]
	v_pk_mul_f32 v[42:43], v[42:43], v[50:51] op_sel_hi:[1,0]
	v_pk_mul_f32 v[44:45], v[44:45], v[50:51] op_sel_hi:[1,0]
	v_pk_mul_f32 v[38:39], v[38:39], v[50:51] op_sel_hi:[1,0]
	v_pk_mul_f32 v[40:41], v[40:41], v[50:51] op_sel_hi:[1,0]
	v_pk_mul_f32 v[34:35], v[34:35], v[50:51] op_sel_hi:[1,0]
	v_pk_mul_f32 v[36:37], v[36:37], v[50:51] op_sel_hi:[1,0]
	v_mul_f32_e32 v1, 0xbfb8aa3b, v46
	v_mul_f32_e32 v50, 0xbfb8aa3b, v47
	v_mul_f32_e32 v51, 0xbfb8aa3b, v48
	v_mul_f32_e32 v54, 0xbfb8aa3b, v49
	v_mul_f32_e32 v55, 0xbfb8aa3b, v42
	v_mul_f32_e32 v56, 0xbfb8aa3b, v43
	v_mul_f32_e32 v57, 0xbfb8aa3b, v44
	v_mul_f32_e32 v58, 0xbfb8aa3b, v45
	v_exp_f32_e32 v1, v1
	v_exp_f32_e32 v50, v50
	v_exp_f32_e32 v51, v51
	v_exp_f32_e32 v54, v54
	v_exp_f32_e32 v55, v55
	v_exp_f32_e32 v56, v56
	v_exp_f32_e32 v57, v57
	v_exp_f32_e32 v58, v58
	v_add_f32_e32 v1, 1.0, v1
	v_add_f32_e32 v59, 1.0, v50
	v_add_f32_e32 v60, 1.0, v51
	v_add_f32_e32 v61, 1.0, v54
	v_add_f32_e32 v62, 1.0, v55
	v_add_f32_e32 v63, 1.0, v56
	v_add_f32_e32 v64, 1.0, v57
	v_add_f32_e32 v65, 1.0, v58
	v_rcp_f32_e32 v50, v1
	v_rcp_f32_e32 v51, v59
	v_rcp_f32_e32 v54, v60
	v_rcp_f32_e32 v55, v61
	v_rcp_f32_e32 v56, v62
	v_rcp_f32_e32 v57, v63
	v_rcp_f32_e32 v58, v64
	v_rcp_f32_e32 v59, v65
	v_pk_mul_f32 v[46:47], v[46:47], v[50:51]
	v_pk_mul_f32 v[48:49], v[48:49], v[54:55]
	v_pk_mul_f32 v[42:43], v[42:43], v[56:57]
	v_pk_mul_f32 v[44:45], v[44:45], v[58:59]
	v_pk_mul_f32 v[38:39], v[38:39], v[46:47]
	v_pk_mul_f32 v[40:41], v[40:41], v[48:49]
	v_pk_mul_f32 v[42:43], v[34:35], v[42:43]
	v_pk_mul_f32 v[44:45], v[36:37], v[44:45]
	v_cvt_pk_bf16_f32 v34, v38, v39
	v_cvt_pk_bf16_f32 v35, v40, v41
	v_cvt_pk_bf16_f32 v36, v42, v43
	v_cvt_pk_bf16_f32 v37, v44, v45
	v_lshl_add_u64 v[38:39], v[96:97], 0, v[52:53]
	global_store_dwordx4 v[38:39], v[34:37], off
; __device__ __forceinline__ unsigned cvtpk(float lo, float hi) { f32x2 v = {lo, hi}; bf16x2_t b = __builtin_convertvector(v, bf16x2_t); return __builtin_bit_cast(unsigned, b); }
; template <int MODE>
; __device__ __forceinline__ void moe_unit(PG8_LAS unsigned char* lds, int e, int cb, int slot0  , int nv  , const bf16_t* A, const int* slot_tok,
;                                          const float* W0, const float* W1, bf16_t* OUT, const float* slot_rs  , const int* slot_dst) {
;     ...
; #pragma unroll
;     for (int m = 0; m < NMU; ++m) if (m < mcnt) { const int r = 4 * (16 * m + fr) + wr;
;         if (r < nv) { const int slot = slot0 + r; const float rs = slot_rs[slot];
;             if (MODE == 0) {
;                 float h[8];
; #pragma unroll
;                 for (int n = 0; n < 2; ++n)
; #pragma unroll
;                     for (int i = 0; i < 4; ++i) { const float g = acc[m][n][i] * rs, up = acc[m][n + 2][i] * rs; h[4 * n + i] = g * __builtin_amdgcn_rcpf(1.0f + __expf(-g)) * up; }
;                 { u32x4 w; w.x = cvtpk(h[0], h[1]); w.y = cvtpk(h[2], h[3]); w.z = cvtpk(h[4], h[5]); w.w = cvtpk(h[6], h[7]); *(u32x4*)(OUT + (size_t)slot * DFF + 64 * cb + 32 * wc + 8 * fq) = w; }
.LBB0_725:
	s_or_b64 exec, exec, s[54:55]
	s_cmp_gt_i32 s6, 48
	v_add_u32_e32 v1, 0xc0, v100
	s_cselect_b64 s[54:55], -1, 0
	v_cmp_gt_i32_e32 vcc, s69, v1
	s_and_b64 s[56:57], s[54:55], vcc
	s_and_saveexec_b64 s[54:55], s[56:57]
	s_cbranch_execz .LBB0_727
	v_lshl_add_u64 v[34:35], v[100:101], 0, v[94:95]
	v_lshl_add_u64 v[34:35], v[34:35], 2, v[98:99]
	v_mov_b32_e32 v34, v181
	v_add_u32_e32 v36, v1, v94
	v_ashrrev_i32_e32 v37, 31, v36
	v_lshlrev_b64 v[36:37], 10, v[36:37]
	s_nop 0
	v_pk_mul_f32 v[18:19], v[18:19], v[34:35] op_sel_hi:[1,0]
	v_pk_mul_f32 v[20:21], v[20:21], v[34:35] op_sel_hi:[1,0]
	v_pk_mul_f32 v[22:23], v[22:23], v[34:35] op_sel_hi:[1,0]
	v_pk_mul_f32 v[24:25], v[24:25], v[34:35] op_sel_hi:[1,0]
	v_pk_mul_f32 v[26:27], v[26:27], v[34:35] op_sel_hi:[1,0]
	v_pk_mul_f32 v[28:29], v[28:29], v[34:35] op_sel_hi:[1,0]
	v_pk_mul_f32 v[30:31], v[30:31], v[34:35] op_sel_hi:[1,0]
	v_pk_mul_f32 v[32:33], v[32:33], v[34:35] op_sel_hi:[1,0]
	v_mul_f32_e32 v1, 0xbfb8aa3b, v18
	v_mul_f32_e32 v34, 0xbfb8aa3b, v19
	v_mul_f32_e32 v35, 0xbfb8aa3b, v20
	v_mul_f32_e32 v38, 0xbfb8aa3b, v21
	v_mul_f32_e32 v39, 0xbfb8aa3b, v22
	v_mul_f32_e32 v40, 0xbfb8aa3b, v23
	v_mul_f32_e32 v41, 0xbfb8aa3b, v24
	v_mul_f32_e32 v42, 0xbfb8aa3b, v25
	v_exp_f32_e32 v1, v1
	v_exp_f32_e32 v34, v34
	v_exp_f32_e32 v35, v35
	v_exp_f32_e32 v38, v38
	v_exp_f32_e32 v39, v39
	v_exp_f32_e32 v40, v40
	v_exp_f32_e32 v41, v41
	v_exp_f32_e32 v42, v42
	v_add_f32_e32 v1, 1.0, v1
	v_add_f32_e32 v43, 1.0, v34
	v_add_f32_e32 v44, 1.0, v35
	v_add_f32_e32 v45, 1.0, v38
	v_add_f32_e32 v46, 1.0, v39
	v_add_f32_e32 v47, 1.0, v40
	v_add_f32_e32 v48, 1.0, v41
	v_add_f32_e32 v49, 1.0, v42
	v_rcp_f32_e32 v34, v1
	v_rcp_f32_e32 v35, v43
	v_rcp_f32_e32 v38, v44
	v_rcp_f32_e32 v39, v45
	v_rcp_f32_e32 v40, v46
	v_rcp_f32_e32 v41, v47
	v_rcp_f32_e32 v42, v48
	v_rcp_f32_e32 v43, v49
	v_pk_mul_f32 v[18:19], v[18:19], v[34:35]
	v_pk_mul_f32 v[20:21], v[20:21], v[38:39]
	v_pk_mul_f32 v[22:23], v[22:23], v[40:41]
	v_pk_mul_f32 v[24:25], v[24:25], v[42:43]
	v_pk_mul_f32 v[18:19], v[26:27], v[18:19]
	v_pk_mul_f32 v[20:21], v[28:29], v[20:21]
	v_pk_mul_f32 v[22:23], v[30:31], v[22:23]
	v_pk_mul_f32 v[24:25], v[32:33], v[24:25]
	v_cvt_pk_bf16_f32 v18, v18, v19
	v_cvt_pk_bf16_f32 v19, v20, v21
	v_cvt_pk_bf16_f32 v20, v22, v23
	v_cvt_pk_bf16_f32 v21, v24, v25
	v_lshl_add_u64 v[22:23], v[96:97], 0, v[36:37]
	global_store_dwordx4 v[22:23], v[18:21], off
.LBB0_727:
	s_or_b64 exec, exec, s[54:55]
	s_cmp_gt_i32 s6, 64
	v_add_u32_e32 v1, 0x100, v100
	s_cselect_b64 s[54:55], -1, 0
	v_cmp_gt_i32_e32 vcc, s69, v1
	s_and_b64 s[56:57], s[54:55], vcc
	s_and_saveexec_b64 s[54:55], s[56:57]
	s_cbranch_execz .LBB0_681
	v_lshl_add_u64 v[18:19], v[100:101], 0, v[94:95]
	v_lshl_add_u64 v[18:19], v[18:19], 2, v[98:99]
	v_mov_b32_e32 v18, v182
	v_add_u32_e32 v20, v1, v94
	v_ashrrev_i32_e32 v21, 31, v20
	v_lshlrev_b64 v[20:21], 10, v[20:21]
	s_nop 0
	v_pk_mul_f32 v[2:3], v[2:3], v[18:19] op_sel_hi:[1,0]
	v_pk_mul_f32 v[4:5], v[4:5], v[18:19] op_sel_hi:[1,0]
	v_pk_mul_f32 v[6:7], v[6:7], v[18:19] op_sel_hi:[1,0]
	v_pk_mul_f32 v[8:9], v[8:9], v[18:19] op_sel_hi:[1,0]
	v_pk_mul_f32 v[10:11], v[10:11], v[18:19] op_sel_hi:[1,0]
	v_pk_mul_f32 v[12:13], v[12:13], v[18:19] op_sel_hi:[1,0]
	v_pk_mul_f32 v[14:15], v[14:15], v[18:19] op_sel_hi:[1,0]
	v_pk_mul_f32 v[16:17], v[16:17], v[18:19] op_sel_hi:[1,0]
	v_mul_f32_e32 v1, 0xbfb8aa3b, v2
	v_mul_f32_e32 v18, 0xbfb8aa3b, v3
	v_mul_f32_e32 v19, 0xbfb8aa3b, v4
	v_mul_f32_e32 v22, 0xbfb8aa3b, v5
	v_mul_f32_e32 v23, 0xbfb8aa3b, v6
	v_mul_f32_e32 v24, 0xbfb8aa3b, v7
	v_mul_f32_e32 v25, 0xbfb8aa3b, v8
	v_mul_f32_e32 v26, 0xbfb8aa3b, v9
	v_exp_f32_e32 v1, v1
	v_exp_f32_e32 v18, v18
	v_exp_f32_e32 v19, v19
	v_exp_f32_e32 v22, v22
	v_exp_f32_e32 v23, v23
	v_exp_f32_e32 v24, v24
	v_exp_f32_e32 v25, v25
	v_exp_f32_e32 v26, v26
	v_add_f32_e32 v1, 1.0, v1
	v_add_f32_e32 v27, 1.0, v18
	v_add_f32_e32 v28, 1.0, v19
	v_add_f32_e32 v29, 1.0, v22
	v_add_f32_e32 v30, 1.0, v23
	v_add_f32_e32 v31, 1.0, v24
	v_add_f32_e32 v32, 1.0, v25
	v_add_f32_e32 v33, 1.0, v26
	v_rcp_f32_e32 v18, v1
	v_rcp_f32_e32 v19, v27
	v_rcp_f32_e32 v22, v28
	v_rcp_f32_e32 v23, v29
	v_rcp_f32_e32 v24, v30
	v_rcp_f32_e32 v25, v31
	v_rcp_f32_e32 v26, v32
	v_rcp_f32_e32 v27, v33
	v_pk_mul_f32 v[2:3], v[2:3], v[18:19]
	v_pk_mul_f32 v[4:5], v[4:5], v[22:23]
	v_pk_mul_f32 v[6:7], v[6:7], v[24:25]
	v_pk_mul_f32 v[8:9], v[8:9], v[26:27]
	v_pk_mul_f32 v[2:3], v[10:11], v[2:3]
	v_pk_mul_f32 v[4:5], v[12:13], v[4:5]
	v_pk_mul_f32 v[6:7], v[14:15], v[6:7]
	v_pk_mul_f32 v[8:9], v[16:17], v[8:9]
	v_cvt_pk_bf16_f32 v2, v2, v3
	v_cvt_pk_bf16_f32 v3, v4, v5
	v_cvt_pk_bf16_f32 v4, v6, v7
	v_cvt_pk_bf16_f32 v5, v8, v9
	v_lshl_add_u64 v[6:7], v[96:97], 0, v[20:21]
	global_store_dwordx4 v[6:7], v[2:5], off
	s_branch .LBB0_681
